# dead fp8 dest inits dropped in P0/P4/P6 packs; attention softmax canonicalising v_max x,x removed
# baseline (speedup 1.0000x reference)
.LBB0_16:
	v_readfirstlane_b32 s50, v18
	s_lshl_b32 s51, s8, 12
	s_lshl_b32 s50, s50, 2
	s_add_u32 s50, s50, s51
	s_add_u32 s56, s6, s50
	s_addc_u32 s57, s7, 0
	v_and_b32_e32 v100, 3, v36
	v_lshrrev_b32_e32 v101, 5, v36
	v_lshl_or_b32 v100, v101, 2, v100
	v_bfe_u32 v101, v36, 2, 3
	v_lshlrev_b32_e32 v102, 12, v100
	v_lshl_or_b32 v102, v101, 4, v102
	v_lshlrev_b32_e32 v103, 2, v6
	v_sub_u32_e32 v103, v8, v103
	v_mad_u32_u24 v103, v100, s15, v103
	v_lshl_add_u32 v103, v101, 4, v103
	global_load_dwordx4 v[120:123], v102, s[56:57]
	s_add_u32 s56, s56, 0x8000
	s_addc_u32 s57, s57, 0
	global_load_dwordx4 v[124:127], v102, s[56:57]
	s_add_u32 s56, s56, 0x8000
	s_addc_u32 s57, s57, 0
	s_waitcnt vmcnt(1)
	v_pk_mul_f32 v[120:121], v[120:121], s[10:11] op_sel_hi:[1,0]
	v_pk_mul_f32 v[122:123], v[122:123], s[10:11] op_sel_hi:[1,0]
	ds_write_b32 v103, v120 offset:0
	ds_write_b32 v103, v121 offset:4
	ds_write_b32 v103, v122 offset:8
	ds_write_b32 v103, v123 offset:12
	s_waitcnt vmcnt(0)
	v_pk_mul_f32 v[124:125], v[124:125], s[10:11] op_sel_hi:[1,0]
	v_pk_mul_f32 v[126:127], v[126:127], s[10:11] op_sel_hi:[1,0]
	ds_write_b32 v103, v124 offset:1056
	ds_write_b32 v103, v125 offset:1060
	ds_write_b32 v103, v126 offset:1064
	ds_write_b32 v103, v127 offset:1068
	global_load_dwordx4 v[128:131], v102, s[56:57]
	s_add_u32 s56, s56, 0x8000
	s_addc_u32 s57, s57, 0
	global_load_dwordx4 v[132:135], v102, s[56:57]
	s_add_u32 s56, s56, 0x8000
	s_addc_u32 s57, s57, 0
	s_waitcnt vmcnt(1)
	v_pk_mul_f32 v[128:129], v[128:129], s[10:11] op_sel_hi:[1,0]
	v_pk_mul_f32 v[130:131], v[130:131], s[10:11] op_sel_hi:[1,0]
	ds_write_b32 v103, v128 offset:2112
	ds_write_b32 v103, v129 offset:2116
	ds_write_b32 v103, v130 offset:2120
	ds_write_b32 v103, v131 offset:2124
	s_waitcnt vmcnt(0)
	v_pk_mul_f32 v[132:133], v[132:133], s[10:11] op_sel_hi:[1,0]
	v_pk_mul_f32 v[134:135], v[134:135], s[10:11] op_sel_hi:[1,0]
	ds_write_b32 v103, v132 offset:3168
	ds_write_b32 v103, v133 offset:3172
	ds_write_b32 v103, v134 offset:3176
	ds_write_b32 v103, v135 offset:3180
	global_load_dwordx4 v[136:139], v102, s[56:57]
	s_add_u32 s56, s56, 0x8000
	s_addc_u32 s57, s57, 0
	global_load_dwordx4 v[140:143], v102, s[56:57]
	s_add_u32 s56, s56, 0x8000
	s_addc_u32 s57, s57, 0
	s_waitcnt vmcnt(1)
	v_pk_mul_f32 v[136:137], v[136:137], s[10:11] op_sel_hi:[1,0]
	v_pk_mul_f32 v[138:139], v[138:139], s[10:11] op_sel_hi:[1,0]
	ds_write_b32 v103, v136 offset:4224
	ds_write_b32 v103, v137 offset:4228
	ds_write_b32 v103, v138 offset:4232
	ds_write_b32 v103, v139 offset:4236
	s_waitcnt vmcnt(0)
	v_pk_mul_f32 v[140:141], v[140:141], s[10:11] op_sel_hi:[1,0]
	v_pk_mul_f32 v[142:143], v[142:143], s[10:11] op_sel_hi:[1,0]
	ds_write_b32 v103, v140 offset:5280
	ds_write_b32 v103, v141 offset:5284
	ds_write_b32 v103, v142 offset:5288
	ds_write_b32 v103, v143 offset:5292
	global_load_dwordx4 v[144:147], v102, s[56:57]
	s_add_u32 s56, s56, 0x8000
	s_addc_u32 s57, s57, 0
	global_load_dwordx4 v[148:151], v102, s[56:57]
	s_add_u32 s56, s56, 0x8000
	s_addc_u32 s57, s57, 0
	s_waitcnt vmcnt(1)
	v_pk_mul_f32 v[144:145], v[144:145], s[10:11] op_sel_hi:[1,0]
	v_pk_mul_f32 v[146:147], v[146:147], s[10:11] op_sel_hi:[1,0]
	ds_write_b32 v103, v144 offset:6336
	ds_write_b32 v103, v145 offset:6340
	ds_write_b32 v103, v146 offset:6344
	ds_write_b32 v103, v147 offset:6348
	s_waitcnt vmcnt(0)
	v_pk_mul_f32 v[148:149], v[148:149], s[10:11] op_sel_hi:[1,0]
	v_pk_mul_f32 v[150:151], v[150:151], s[10:11] op_sel_hi:[1,0]
	ds_write_b32 v103, v148 offset:7392
	ds_write_b32 v103, v149 offset:7396
	ds_write_b32 v103, v150 offset:7400
	ds_write_b32 v103, v151 offset:7404
	s_waitcnt lgkmcnt(0)
	v_add_u32_e32 v12, 0x400, v7
	ds_read2_b32 v[22:23], v7 offset1:16
	ds_read2_b32 v[34:35], v7 offset0:33 offset1:49
	ds_read2_b32 v[38:39], v7 offset0:66 offset1:82
	ds_read2_b32 v[40:41], v7 offset0:99 offset1:115
	ds_read2_b32 v[42:43], v7 offset0:132 offset1:148
	ds_read2_b32 v[44:45], v7 offset0:165 offset1:181
	ds_read2_b32 v[46:47], v7 offset0:198 offset1:214
	ds_read2_b32 v[48:49], v7 offset0:231 offset1:247
	ds_read2_b32 v[50:51], v12 offset0:8 offset1:24
	ds_read2_b32 v[52:53], v12 offset0:41 offset1:57
	ds_read2_b32 v[54:55], v12 offset0:74 offset1:90
	ds_read2_b32 v[56:57], v12 offset0:107 offset1:123
	ds_read2_b32 v[58:59], v12 offset0:140 offset1:156
	ds_read2_b32 v[60:61], v12 offset0:173 offset1:189
	s_add_u32 s4, s1, s4
	ds_read2_b32 v[62:63], v12 offset0:206 offset1:222
	ds_read2_b32 v[64:65], v12 offset0:239 offset1:255
	s_addc_u32 s5, s2, s5
	s_lshl_b32 s7, s20, 4
	s_waitcnt lgkmcnt(14)
	v_cvt_pk_fp8_f32 v30, v22, v34
	s_waitcnt lgkmcnt(10)
	v_cvt_pk_fp8_f32 v31, v42, v44
	s_waitcnt lgkmcnt(6)
	v_cvt_pk_fp8_f32 v32, v50, v52
	s_waitcnt lgkmcnt(2)
	v_cvt_pk_fp8_f32 v33, v58, v60
	s_and_b32 s6, s21, 0x300
	s_and_b32 s20, s7, 0x60
	s_add_u32 s4, s4, s8
	v_or_b32_e32 v3, s6, v9
	s_addc_u32 s5, s5, 0
	v_or_b32_e32 v3, s20, v3
	v_lshl_add_u64 v[18:19], s[4:5], 0, v[10:11]
	s_and_b32 s4, s7, 16
	v_cvt_pk_fp8_f32 v30, v38, v40 op_sel:[0,0,1]
	v_cvt_pk_fp8_f32 v31, v46, v48 op_sel:[0,0,1]
	v_cvt_pk_fp8_f32 v32, v54, v56 op_sel:[0,0,1]
	s_waitcnt lgkmcnt(0)
	v_cvt_pk_fp8_f32 v33, v62, v64 op_sel:[0,0,1]
	v_or_b32_e32 v12, s4, v3
	v_lshlrev_b32_e32 v12, 10, v12
	v_lshl_add_u64 v[66:67], v[18:19], 0, v[12:13]
	global_store_dwordx4 v[66:67], v[30:33], off
	v_add_u32_e32 v3, s4, v3
	v_lshl_add_u32 v12, v3, 10, v29
	v_cvt_pk_fp8_f32 v30, v23, v35
	v_cvt_pk_fp8_f32 v31, v43, v45
	v_cvt_pk_fp8_f32 v32, v51, v53
	v_cvt_pk_fp8_f32 v33, v59, v61
	v_cvt_pk_fp8_f32 v30, v39, v41 op_sel:[0,0,1]
	v_cvt_pk_fp8_f32 v31, v47, v49 op_sel:[0,0,1]
	v_cvt_pk_fp8_f32 v32, v55, v57 op_sel:[0,0,1]
	v_cvt_pk_fp8_f32 v33, v63, v65 op_sel:[0,0,1]
	v_lshl_add_u64 v[18:19], v[18:19], 0, v[12:13]
	s_mov_b64 s[4:5], 0
	global_store_dwordx4 v[18:19], v[30:33], off
	s_waitcnt lgkmcnt(0)

.LBB0_20:
	v_readfirstlane_b32 s56, v18
	v_readfirstlane_b32 s57, v19
	s_lshl_b32 s51, s6, 13
	s_add_u32 s56, s56, s51
	s_addc_u32 s57, s57, 0
	s_lshl_b32 s52, s6, 2
	s_add_u32 s52, s4, s52
	s_addc_u32 s53, s5, 0
	v_and_b32_e32 v100, 3, v36
	v_lshrrev_b32_e32 v101, 5, v36
	v_lshl_or_b32 v100, v101, 2, v100
	v_bfe_u32 v101, v36, 2, 3
	v_lshlrev_b32_e32 v102, 13, v100
	v_lshl_or_b32 v102, v101, 4, v102
	v_lshlrev_b32_e32 v104, 2, v100
	v_lshlrev_b32_e32 v103, 2, v6
	v_sub_u32_e32 v103, v8, v103
	v_mad_u32_u24 v103, v100, s15, v103
	v_lshl_add_u32 v103, v101, 4, v103
	global_load_dwordx4 v[120:123], v102, s[56:57]
	s_add_u32 s56, s56, 0x10000
	s_addc_u32 s57, s57, 0
	global_load_dwordx4 v[124:127], v102, s[56:57]
	s_add_u32 s56, s56, 0x10000
	s_addc_u32 s57, s57, 0
	global_load_dword v152, v104, s[52:53] offset:0
	global_load_dword v153, v104, s[52:53] offset:32
	s_waitcnt vmcnt(1)
	v_pk_mul_f32 v[120:121], v[120:121], s[10:11] op_sel_hi:[1,0]
	v_pk_mul_f32 v[122:123], v[122:123], s[10:11] op_sel_hi:[1,0]
	v_mul_f32_e32 v120, v120, v152
	v_mul_f32_e32 v121, v121, v152
	v_mul_f32_e32 v122, v122, v152
	v_mul_f32_e32 v123, v123, v152
	ds_write_b32 v103, v120 offset:0
	ds_write_b32 v103, v121 offset:4
	ds_write_b32 v103, v122 offset:8
	ds_write_b32 v103, v123 offset:12
	s_waitcnt vmcnt(0)
	v_pk_mul_f32 v[124:125], v[124:125], s[10:11] op_sel_hi:[1,0]
	v_pk_mul_f32 v[126:127], v[126:127], s[10:11] op_sel_hi:[1,0]
	v_mul_f32_e32 v124, v124, v153
	v_mul_f32_e32 v125, v125, v153
	v_mul_f32_e32 v126, v126, v153
	v_mul_f32_e32 v127, v127, v153
	ds_write_b32 v103, v124 offset:1056
	ds_write_b32 v103, v125 offset:1060
	ds_write_b32 v103, v126 offset:1064
	ds_write_b32 v103, v127 offset:1068
	global_load_dwordx4 v[128:131], v102, s[56:57]
	s_add_u32 s56, s56, 0x10000
	s_addc_u32 s57, s57, 0
	global_load_dwordx4 v[132:135], v102, s[56:57]
	s_add_u32 s56, s56, 0x10000
	s_addc_u32 s57, s57, 0
	global_load_dword v154, v104, s[52:53] offset:64
	global_load_dword v155, v104, s[52:53] offset:96
	s_waitcnt vmcnt(1)
	v_pk_mul_f32 v[128:129], v[128:129], s[10:11] op_sel_hi:[1,0]
	v_pk_mul_f32 v[130:131], v[130:131], s[10:11] op_sel_hi:[1,0]
	v_mul_f32_e32 v128, v128, v154
	v_mul_f32_e32 v129, v129, v154
	v_mul_f32_e32 v130, v130, v154
	v_mul_f32_e32 v131, v131, v154
	ds_write_b32 v103, v128 offset:2112
	ds_write_b32 v103, v129 offset:2116
	ds_write_b32 v103, v130 offset:2120
	ds_write_b32 v103, v131 offset:2124
	s_waitcnt vmcnt(0)
	v_pk_mul_f32 v[132:133], v[132:133], s[10:11] op_sel_hi:[1,0]
	v_pk_mul_f32 v[134:135], v[134:135], s[10:11] op_sel_hi:[1,0]
	v_mul_f32_e32 v132, v132, v155
	v_mul_f32_e32 v133, v133, v155
	v_mul_f32_e32 v134, v134, v155
	v_mul_f32_e32 v135, v135, v155
	ds_write_b32 v103, v132 offset:3168
	ds_write_b32 v103, v133 offset:3172
	ds_write_b32 v103, v134 offset:3176
	ds_write_b32 v103, v135 offset:3180
	global_load_dwordx4 v[136:139], v102, s[56:57]
	s_add_u32 s56, s56, 0x10000
	s_addc_u32 s57, s57, 0
	global_load_dwordx4 v[140:143], v102, s[56:57]
	s_add_u32 s56, s56, 0x10000
	s_addc_u32 s57, s57, 0
	global_load_dword v156, v104, s[52:53] offset:128
	global_load_dword v157, v104, s[52:53] offset:160
	s_waitcnt vmcnt(1)
	v_pk_mul_f32 v[136:137], v[136:137], s[10:11] op_sel_hi:[1,0]
	v_pk_mul_f32 v[138:139], v[138:139], s[10:11] op_sel_hi:[1,0]
	v_mul_f32_e32 v136, v136, v156
	v_mul_f32_e32 v137, v137, v156
	v_mul_f32_e32 v138, v138, v156
	v_mul_f32_e32 v139, v139, v156
	ds_write_b32 v103, v136 offset:4224
	ds_write_b32 v103, v137 offset:4228
	ds_write_b32 v103, v138 offset:4232
	ds_write_b32 v103, v139 offset:4236
	s_waitcnt vmcnt(0)
	v_pk_mul_f32 v[140:141], v[140:141], s[10:11] op_sel_hi:[1,0]
	v_pk_mul_f32 v[142:143], v[142:143], s[10:11] op_sel_hi:[1,0]
	v_mul_f32_e32 v140, v140, v157
	v_mul_f32_e32 v141, v141, v157
	v_mul_f32_e32 v142, v142, v157
	v_mul_f32_e32 v143, v143, v157
	ds_write_b32 v103, v140 offset:5280
	ds_write_b32 v103, v141 offset:5284
	ds_write_b32 v103, v142 offset:5288
	ds_write_b32 v103, v143 offset:5292
	global_load_dwordx4 v[144:147], v102, s[56:57]
	s_add_u32 s56, s56, 0x10000
	s_addc_u32 s57, s57, 0
	global_load_dwordx4 v[148:151], v102, s[56:57]
	s_add_u32 s56, s56, 0x10000
	s_addc_u32 s57, s57, 0
	global_load_dword v158, v104, s[52:53] offset:192
	global_load_dword v159, v104, s[52:53] offset:224
	s_waitcnt vmcnt(1)
	v_pk_mul_f32 v[144:145], v[144:145], s[10:11] op_sel_hi:[1,0]
	v_pk_mul_f32 v[146:147], v[146:147], s[10:11] op_sel_hi:[1,0]
	v_mul_f32_e32 v144, v144, v158
	v_mul_f32_e32 v145, v145, v158
	v_mul_f32_e32 v146, v146, v158
	v_mul_f32_e32 v147, v147, v158
	ds_write_b32 v103, v144 offset:6336
	ds_write_b32 v103, v145 offset:6340
	ds_write_b32 v103, v146 offset:6344
	ds_write_b32 v103, v147 offset:6348
	s_waitcnt vmcnt(0)
	v_pk_mul_f32 v[148:149], v[148:149], s[10:11] op_sel_hi:[1,0]
	v_pk_mul_f32 v[150:151], v[150:151], s[10:11] op_sel_hi:[1,0]
	v_mul_f32_e32 v148, v148, v159
	v_mul_f32_e32 v149, v149, v159
	v_mul_f32_e32 v150, v150, v159
	v_mul_f32_e32 v151, v151, v159
	ds_write_b32 v103, v148 offset:7392
	ds_write_b32 v103, v149 offset:7396
	ds_write_b32 v103, v150 offset:7400
	ds_write_b32 v103, v151 offset:7404
	s_waitcnt lgkmcnt(0)
	v_add_u32_e32 v12, 0x400, v7
	ds_read2_b32 v[22:23], v7 offset1:16
	ds_read2_b32 v[34:35], v7 offset0:33 offset1:49
	ds_read2_b32 v[38:39], v7 offset0:66 offset1:82
	ds_read2_b32 v[40:41], v7 offset0:99 offset1:115
	ds_read2_b32 v[42:43], v7 offset0:132 offset1:148
	ds_read2_b32 v[44:45], v7 offset0:165 offset1:181
	ds_read2_b32 v[46:47], v7 offset0:198 offset1:214
	ds_read2_b32 v[48:49], v7 offset0:231 offset1:247
	ds_read2_b32 v[50:51], v12 offset0:8 offset1:24
	ds_read2_b32 v[52:53], v12 offset0:41 offset1:57
	ds_read2_b32 v[54:55], v12 offset0:74 offset1:90
	ds_read2_b32 v[56:57], v12 offset0:107 offset1:123
	ds_read2_b32 v[58:59], v12 offset0:140 offset1:156
	ds_read2_b32 v[60:61], v12 offset0:173 offset1:189
	s_lshl_b64 s[4:5], s[8:9], 21
	ds_read2_b32 v[62:63], v12 offset0:206 offset1:222
	ds_read2_b32 v[64:65], v12 offset0:239 offset1:255
	s_add_u32 s4, s3, s4
	s_waitcnt lgkmcnt(14)
	v_cvt_pk_fp8_f32 v30, v22, v34
	s_waitcnt lgkmcnt(10)
	v_cvt_pk_fp8_f32 v31, v42, v44
	s_waitcnt lgkmcnt(6)
	v_cvt_pk_fp8_f32 v32, v50, v52
	s_waitcnt lgkmcnt(2)
	v_cvt_pk_fp8_f32 v33, v58, v60
	s_addc_u32 s5, s11, s5
	s_lshl_b32 s8, s20, 6
	s_lshl_b32 s20, s20, 2
	s_and_b32 s8, s8, 0x700
	s_and_b32 s20, s20, 0x80
	s_or_b32 s8, s8, s20
	s_and_b32 s7, s7, 0x60
	s_add_u32 s4, s4, s6
	v_or_b32_e32 v3, s7, v5
	v_cvt_pk_fp8_f32 v30, v38, v40 op_sel:[0,0,1]
	v_cvt_pk_fp8_f32 v31, v46, v48 op_sel:[0,0,1]
	v_cvt_pk_fp8_f32 v32, v54, v56 op_sel:[0,0,1]
	s_waitcnt lgkmcnt(0)
	v_cvt_pk_fp8_f32 v33, v62, v64 op_sel:[0,0,1]
	s_addc_u32 s5, s5, 0
	v_or_b32_e32 v3, s8, v3
	v_lshl_add_u64 v[18:19], s[4:5], 0, v[10:11]
	v_lshlrev_b32_e32 v12, 10, v3
	v_lshl_add_u64 v[66:67], v[18:19], 0, v[12:13]
	global_store_dwordx4 v[66:67], v[30:33], off
	v_or_b32_e32 v3, s7, v21
	v_or_b32_e32 v3, s8, v3
	v_cvt_pk_fp8_f32 v30, v23, v35
	v_cvt_pk_fp8_f32 v31, v43, v45
	v_cvt_pk_fp8_f32 v32, v51, v53
	v_cvt_pk_fp8_f32 v33, v59, v61
	v_cvt_pk_fp8_f32 v30, v39, v41 op_sel:[0,0,1]
	v_cvt_pk_fp8_f32 v31, v47, v49 op_sel:[0,0,1]
	v_cvt_pk_fp8_f32 v32, v55, v57 op_sel:[0,0,1]
	v_cvt_pk_fp8_f32 v33, v63, v65 op_sel:[0,0,1]
	v_lshlrev_b32_e32 v12, 10, v3
	v_lshl_add_u64 v[18:19], v[18:19], 0, v[12:13]
	global_store_dwordx4 v[18:19], v[30:33], off
	s_waitcnt lgkmcnt(0)

.LBB0_237:
	v_and_b32_e32 v163, 63, v39
	v_lshlrev_b32_e32 v40, 4, v163
	v_lshlrev_b32_e32 v39, 3, v163
	v_and_b32_e32 v40, 0xc0, v40
	v_lshlrev_b32_e32 v41, 1, v163
	s_cmp_lg_u32 0, -1
	v_and_or_b32 v40, v39, 24, v40
	v_and_b32_e32 v41, 32, v41
	v_and_b32_e32 v39, 0x100, v39
	s_cselect_b32 s4, 0, 0
	v_or3_b32 v39, v40, v41, v39
	v_add_u32_e32 v166, s4, v39
	v_max_f32_e32 v39, v18, v19
	v_max3_f32 v39, v39, v20, v21
	v_max3_f32 v39, v39, v22, v23
	v_max3_f32 v39, v39, v24, v25
	v_max3_f32 v39, v39, v26, v27
	v_max3_f32 v39, v39, v28, v29
	v_max3_f32 v39, v39, v30, v31
	v_max3_f32 v39, v39, v32, v33
	v_max3_f32 v39, v39, v2, v3
	v_max3_f32 v39, v39, v4, v5
	v_max3_f32 v39, v39, v6, v7
	v_max3_f32 v39, v39, v8, v9
	v_max3_f32 v39, v39, v10, v11
	v_max3_f32 v39, v39, v12, v13
	v_max3_f32 v39, v39, v14, v15
	v_max3_f32 v39, v39, v16, v17
	v_mov_b32_e32 v40, v39
	s_nop 1
	v_permlane32_swap_b32_e32 v39, v40
	v_max_f32_e32 v39, v39, v40
	v_add_f32_e32 v40, 0x7149f2ca, v39
	s_add_i32 s83, s4, s86
	v_mul_f32_e32 v40, 0x3e000000, v40
	s_add_i32 s85, s83, 0x10000
	v_cmp_ge_f32_e32 vcc, s33, v40
	s_cmp_eq_u64 vcc, exec
	v_max_f32_e32 v39, 0xf149f2ca, v39
	v_sub_f32_e32 v40, 0xf149f2ca, v39
	s_cselect_b64 s[4:5], -1, 0
	v_mul_f32_e32 v40, 0x3e38aa3b, v40
	v_cndmask_b32_e64 v116, v39, v161, s[4:5]
	v_exp_f32_e32 v179, v40
	v_mul_f32_e32 v40, 0xbe38aa3b, v116
	v_pk_fma_f32 v[32:33], v[32:33], s[84:85], v[40:41] op_sel_hi:[1,0,0]
	v_pk_fma_f32 v[30:31], v[30:31], s[84:85], v[40:41] op_sel_hi:[1,0,0]
	v_pk_fma_f32 v[28:29], v[28:29], s[84:85], v[40:41] op_sel_hi:[1,0,0]
	v_pk_fma_f32 v[26:27], v[26:27], s[84:85], v[40:41] op_sel_hi:[1,0,0]
	v_pk_fma_f32 v[24:25], v[24:25], s[84:85], v[40:41] op_sel_hi:[1,0,0]
	v_pk_fma_f32 v[22:23], v[22:23], s[84:85], v[40:41] op_sel_hi:[1,0,0]
	v_pk_fma_f32 v[20:21], v[20:21], s[84:85], v[40:41] op_sel_hi:[1,0,0]
	v_pk_fma_f32 v[18:19], v[18:19], s[84:85], v[40:41] op_sel_hi:[1,0,0]
	v_exp_f32_e32 v58, v20
	v_exp_f32_e32 v56, v18
	v_exp_f32_e32 v57, v19
	v_exp_f32_e32 v59, v21
	v_exp_f32_e32 v60, v22
	v_exp_f32_e32 v61, v23
	v_exp_f32_e32 v62, v24
	v_exp_f32_e32 v63, v25
	v_exp_f32_e32 v26, v26
	v_exp_f32_e32 v27, v27
	v_exp_f32_e32 v28, v28
	v_exp_f32_e32 v29, v29
	v_exp_f32_e32 v30, v30
	v_exp_f32_e32 v31, v31
	v_exp_f32_e32 v32, v32
	v_exp_f32_e32 v33, v33
	s_waitcnt vmcnt(0)
	v_pk_fma_f32 v[42:43], v[16:17], s[84:85], v[40:41] op_sel_hi:[1,0,0]
	v_pk_fma_f32 v[44:45], v[14:15], s[84:85], v[40:41] op_sel_hi:[1,0,0]
	v_pk_fma_f32 v[46:47], v[12:13], s[84:85], v[40:41] op_sel_hi:[1,0,0]
	v_pk_fma_f32 v[48:49], v[10:11], s[84:85], v[40:41] op_sel_hi:[1,0,0]
	v_pk_fma_f32 v[50:51], v[8:9], s[84:85], v[40:41] op_sel_hi:[1,0,0]
	v_pk_fma_f32 v[52:53], v[6:7], s[84:85], v[40:41] op_sel_hi:[1,0,0]
	v_pk_fma_f32 v[54:55], v[4:5], s[84:85], v[40:41] op_sel_hi:[1,0,0]
	v_pk_fma_f32 v[40:41], v[2:3], s[84:85], v[40:41] op_sel_hi:[1,0,0]
	s_barrier
	s_add_u32 s6, s90, 0x80000
	s_addc_u32 s7, s91, 0
	s_mov_b32 m0, s85
	s_nop 0
	global_load_lds_dwordx4 v168, s[6:7] offset:0
	s_add_u32 s6, s92, 0x80000
	s_addc_u32 s7, s93, 0
	s_add_i32 s82, s83, 0x8000
	s_mov_b32 m0, s82
	s_nop 0
	global_load_lds_dwordx4 v169, s[6:7] offset:0
	s_add_i32 s83, s83, 0xa000
	s_mov_b32 m0, s83
	s_nop 0
	global_load_lds_dwordx4 v170, s[6:7] offset:0
	s_add_i32 s6, 0, 0x12000
	v_add_u32_e32 v10, s6, v35
	v_add_u32_e32 v175, v10, v37
	ds_read_b128 v[2:5], v175
	ds_read_b128 v[6:9], v175 offset:4096
	v_add_u32_e32 v176, v10, v38
	v_add_u32_e32 v177, v10, v36
	v_add_u32_e32 v178, v10, v34
	s_waitcnt lgkmcnt(1)
	v_mfma_f32_32x32x16_bf16 v[66:81], v[2:5], v[110:113], 0
	ds_read_b128 v[2:5], v176
	ds_read_b128 v[10:13], v176 offset:4096
	ds_read_b128 v[14:17], v177
	ds_read_b128 v[18:21], v177 offset:4096
	v_exp_f32_e32 v34, v40
	v_exp_f32_e32 v35, v41
	v_exp_f32_e32 v36, v54
	v_exp_f32_e32 v37, v55
	v_exp_f32_e32 v38, v52
	v_exp_f32_e32 v39, v53
	s_waitcnt lgkmcnt(4)
	v_mfma_f32_32x32x16_bf16 v[82:97], v[6:9], v[110:113], 0
	ds_read_b128 v[6:9], v178
	ds_read_b128 v[22:25], v178 offset:4096
	v_exp_f32_e32 v40, v50
	v_exp_f32_e32 v41, v51
	v_exp_f32_e32 v48, v48
	v_exp_f32_e32 v49, v49
	v_exp_f32_e32 v46, v46
	v_exp_f32_e32 v47, v47
	s_waitcnt lgkmcnt(5)
	v_mfma_f32_32x32x16_bf16 v[66:81], v[2:5], v[106:109], v[66:81]
	v_add_f32_e64 v4, v58, v36
	v_add_f32_e64 v5, v59, v37
	v_add_f32_e64 v52, v60, v38
	v_add_f32_e64 v53, v61, v39
	v_add_f32_e64 v2, v28, v46
	v_add_f32_e64 v3, v29, v47
	v_pk_add_f32 v[2:3], v[4:5], v[2:3]
	s_waitcnt lgkmcnt(4)
	v_mfma_f32_32x32x16_bf16 v[82:97], v[10:13], v[106:109], v[82:97]
	v_exp_f32_e32 v10, v44
	v_exp_f32_e32 v12, v42
	v_exp_f32_e32 v13, v43
	v_exp_f32_e32 v11, v45
	v_pk_add_f32 v[44:45], v[56:57], v[34:35]
	v_pk_add_f32 v[42:43], v[32:33], v[12:13]
	s_waitcnt lgkmcnt(3)
	v_mfma_f32_32x32x16_bf16 v[66:81], v[14:17], v[102:105], v[66:81]
	v_add_f32_e64 v14, v62, v40
	v_add_f32_e64 v15, v63, v41
	v_add_f32_e64 v16, v26, v48
	v_add_f32_e64 v17, v27, v49
	v_add_f32_e64 v50, v30, v10
	v_add_f32_e64 v51, v31, v11
	v_pk_add_f32 v[16:17], v[44:45], v[16:17]
	v_pk_add_f32 v[50:51], v[52:53], v[50:51]
	v_pk_add_f32 v[14:15], v[14:15], v[42:43]
	v_pk_add_f32 v[4:5], v[16:17], v[50:51]
	s_waitcnt lgkmcnt(2)
	v_mfma_f32_32x32x16_bf16 v[82:97], v[18:21], v[102:105], v[82:97]
	v_add_f32_e64 v2, v2, v14
	v_add_f32_e64 v3, v3, v15
	v_add_f32_e64 v2, v4, v2
	v_add_f32_e64 v3, v5, v3
	v_add_f32_e64 v114, v2, v3
	v_add_f32_e64 v115, v3, v2
	v_cvt_pk_bf16_f32 v2, v56, v57
	v_cvt_pk_bf16_f32 v3, v58, v59
	s_waitcnt lgkmcnt(1)
	v_mfma_f32_32x32x16_bf16 v[66:81], v[6:9], v[98:101], v[66:81]
	v_mov_b32_e32 v115, v114
	v_cvt_pk_bf16_f32 v4, v60, v61
	v_cvt_pk_bf16_f32 v5, v62, v63
	s_nop 1
	v_permlane32_swap_b32_e32 v114, v115
	v_permlane32_swap_b32_e32 v2, v4
	s_waitcnt lgkmcnt(0)
	v_mfma_f32_32x32x16_bf16 v[82:97], v[22:25], v[98:101], v[82:97]
	v_permlane32_swap_b32_e32 v3, v5
	v_cvt_pk_bf16_f32 v120, v26, v27
	v_cvt_pk_bf16_f32 v121, v28, v29
	v_cvt_pk_bf16_f32 v122, v30, v31
	v_cvt_pk_bf16_f32 v123, v32, v33
	v_cvt_pk_bf16_f32 v124, v34, v35
	v_cvt_pk_bf16_f32 v125, v36, v37
	v_cvt_pk_bf16_f32 v126, v38, v39
	v_cvt_pk_bf16_f32 v127, v40, v41
	v_cvt_pk_bf16_f32 v128, v48, v49
	v_cvt_pk_bf16_f32 v129, v46, v47
	v_cvt_pk_bf16_f32 v130, v10, v11
	v_cvt_pk_bf16_f32 v131, v12, v13
	s_nop 0
	v_permlane32_swap_b32_e32 v120, v122
	v_permlane32_swap_b32_e32 v121, v123
	v_permlane32_swap_b32_e32 v124, v126
	v_permlane32_swap_b32_e32 v125, v127
	v_permlane32_swap_b32_e32 v128, v130
	v_permlane32_swap_b32_e32 v129, v131
	ds_read_b64_tr_b16 v[6:7], v166 offset:0
	ds_read_b64_tr_b16 v[8:9], v166 offset:0x800
	ds_read_b64_tr_b16 v[10:11], v166 offset:0x1000
	ds_read_b64_tr_b16 v[12:13], v166 offset:0x1800
	ds_read_b64_tr_b16 v[14:15], v166 offset:0x2000
	ds_read_b64_tr_b16 v[16:17], v166 offset:0x2800
	ds_read_b64_tr_b16 v[34:35], v166 offset:0x3000
	ds_read_b64_tr_b16 v[36:37], v166 offset:0x3800
	ds_read_b64_tr_b16 v[38:39], v166 offset:0x200
	ds_read_b64_tr_b16 v[40:41], v166 offset:0xa00
	ds_read_b64_tr_b16 v[50:51], v166 offset:0x1200
	ds_read_b64_tr_b16 v[52:53], v166 offset:0x1a00
	ds_read_b64_tr_b16 v[54:55], v166 offset:0x2200
	ds_read_b64_tr_b16 v[56:57], v166 offset:0x2a00
	ds_read_b64_tr_b16 v[58:59], v166 offset:0x3200
	ds_read_b64_tr_b16 v[60:61], v166 offset:0x3a00
	s_waitcnt lgkmcnt(8)
	s_nop 0
	v_mfma_f32_32x32x16_bf16 v[18:33], v[2:5], v[6:9], 0
	v_mfma_f32_32x32x16_bf16 v[18:33], v[120:123], v[10:13], v[18:33]
	v_mfma_f32_32x32x16_bf16 v[18:33], v[124:127], v[14:17], v[18:33]
	v_mfma_f32_32x32x16_bf16 v[18:33], v[128:131], v[34:37], v[18:33]
	ds_read_b64_tr_b16 v[6:7], v166 offset:0x400
	ds_read_b64_tr_b16 v[8:9], v166 offset:0xc00
	ds_read_b64_tr_b16 v[10:11], v166 offset:0x1400
	ds_read_b64_tr_b16 v[12:13], v166 offset:0x1c00
	ds_read_b64_tr_b16 v[14:15], v166 offset:0x2400
	ds_read_b64_tr_b16 v[16:17], v166 offset:0x2c00
	ds_read_b64_tr_b16 v[132:133], v166 offset:0x3400
	ds_read_b64_tr_b16 v[134:135], v166 offset:0x3c00
	s_waitcnt lgkmcnt(8)
	v_mfma_f32_32x32x16_bf16 v[34:49], v[2:5], v[38:41], 0
	v_mfma_f32_32x32x16_bf16 v[34:49], v[120:123], v[50:53], v[34:49]
	v_mfma_f32_32x32x16_bf16 v[34:49], v[124:127], v[54:57], v[34:49]
	v_mfma_f32_32x32x16_bf16 v[34:49], v[128:131], v[58:61], v[34:49]
	ds_read_b64_tr_b16 v[140:141], v166 offset:0x600
	ds_read_b64_tr_b16 v[142:143], v166 offset:0xe00
	ds_read_b64_tr_b16 v[144:145], v166 offset:0x1600
	ds_read_b64_tr_b16 v[146:147], v166 offset:0x1e00
	ds_read_b64_tr_b16 v[148:149], v166 offset:0x2600
	ds_read_b64_tr_b16 v[150:151], v166 offset:0x2e00
	ds_read_b64_tr_b16 v[152:153], v166 offset:0x3600
	ds_read_b64_tr_b16 v[154:155], v166 offset:0x3e00
	s_waitcnt lgkmcnt(8)
	v_mfma_f32_32x32x16_bf16 v[50:65], v[2:5], v[6:9], 0
	v_mfma_f32_32x32x16_bf16 v[50:65], v[120:123], v[10:13], v[50:65]
	v_mfma_f32_32x32x16_bf16 v[50:65], v[124:127], v[14:17], v[50:65]
	v_mfma_f32_32x32x16_bf16 v[50:65], v[128:131], v[132:135], v[50:65]
	s_waitcnt lgkmcnt(0)
	v_mfma_f32_32x32x16_bf16 v[2:17], v[2:5], v[140:143], 0
	s_cmpk_gt_i32 s77, 0x7e
	v_mfma_f32_32x32x16_bf16 v[2:17], v[120:123], v[144:147], v[2:17]
	v_mfma_f32_32x32x16_bf16 v[2:17], v[124:127], v[148:151], v[2:17]
	v_mfma_f32_32x32x16_bf16 v[2:17], v[128:131], v[152:155], v[2:17]
	s_cbranch_scc1 .LBB0_239
	s_movk_i32 s60, 0x5a
	s_movk_i32 s62, 0x5b
	v_cmp_gt_i32_e64 s[60:61], s60, v167
	v_cmp_gt_i32_e64 s[62:63], s62, v167
	s_and_b64 s[60:61], s[62:63], s[60:61]
	s_movk_i32 s28, 0x58
	v_cndmask_b32_e64 v81, v81, v160, s[62:63]
	s_movk_i32 s62, 0x59
	v_cmp_gt_i32_e64 s[62:63], s62, v167
	s_movk_i32 s26, 0x53
	v_cmp_gt_i32_e64 s[58:59], s28, v167
	v_cndmask_b32_e64 v80, v80, v160, s[60:61]
	s_and_b64 s[60:61], s[60:61], s[62:63]
	s_movk_i32 s24, 0x52
	v_cmp_gt_i32_e64 s[56:57], s26, v167
	s_and_b64 s[58:59], s[60:61], s[58:59]
	s_movk_i32 s22, 0x51
	v_cmp_gt_i32_e64 s[54:55], s24, v167
	s_and_b64 s[56:57], s[58:59], s[56:57]
	s_movk_i32 s20, 0x50
	v_cmp_gt_i32_e64 s[52:53], s22, v167
	s_and_b64 s[54:55], s[56:57], s[54:55]
	s_movk_i32 s18, 0x4b
	v_cmp_gt_i32_e64 s[50:51], s20, v167
	s_and_b64 s[52:53], s[54:55], s[52:53]
	s_movk_i32 s16, 0x4a
	v_cmp_gt_i32_e64 s[48:49], s18, v167
	s_and_b64 s[50:51], s[52:53], s[50:51]
	s_movk_i32 s14, 0x49
	v_cmp_gt_i32_e64 s[44:45], s16, v167
	s_and_b64 s[48:49], s[50:51], s[48:49]
	s_movk_i32 s12, 0x48
	v_cmp_gt_i32_e64 s[42:43], s14, v167
	s_and_b64 s[44:45], s[48:49], s[44:45]
	s_movk_i32 s10, 0x43
	v_cmp_gt_i32_e64 s[40:41], s12, v167
	s_and_b64 s[42:43], s[44:45], s[42:43]
	s_movk_i32 s6, 0x60
	s_movk_i32 s8, 0x42
	v_cmp_gt_i32_e64 s[38:39], s10, v167
	s_and_b64 s[40:41], s[42:43], s[40:41]
	v_cmp_gt_i32_e32 vcc, s6, v167
	s_movk_i32 s6, 0x41
	v_cmp_gt_i32_e64 s[36:37], s8, v167
	s_and_b64 s[38:39], s[40:41], s[38:39]
	v_cmp_gt_i32_e64 s[34:35], s6, v167
	s_and_b64 s[36:37], s[38:39], s[36:37]
	v_cmp_gt_i32_e64 s[30:31], 64, v167
	s_and_b64 s[34:35], s[36:37], s[34:35]
	s_and_b64 s[30:31], s[34:35], s[30:31]
	v_cndmask_b32_e64 v79, v79, v160, s[60:61]
	s_movk_i32 s60, 0x7a
	v_cndmask_b32_e64 v66, v66, v160, s[30:31]
	s_movk_i32 s30, 0x7b
	s_movk_i32 s62, 0x79
	v_cmp_gt_i32_e64 s[60:61], s60, v167
	v_cmp_gt_i32_e64 s[30:31], s30, v167
	s_movk_i32 s28, 0x78
	v_cmp_gt_i32_e64 s[62:63], s62, v167
	v_cndmask_b32_e64 v97, v97, v160, s[30:31]
	s_and_b64 s[30:31], s[30:31], s[60:61]
	s_movk_i32 s26, 0x73
	v_cmp_gt_i32_e64 s[28:29], s28, v167
	v_cndmask_b32_e64 v96, v96, v160, s[30:31]
	s_and_b64 s[30:31], s[30:31], s[62:63]
	s_movk_i32 s24, 0x72
	v_cmp_gt_i32_e64 s[26:27], s26, v167
	s_and_b64 s[28:29], s[30:31], s[28:29]
	s_movk_i32 s22, 0x71
	v_cmp_gt_i32_e64 s[24:25], s24, v167
	s_and_b64 s[26:27], s[28:29], s[26:27]
	v_cmp_gt_i32_e64 s[22:23], s22, v167
	s_and_b64 s[24:25], s[26:27], s[24:25]
	s_movk_i32 s18, 0x6b
	v_cmp_gt_i32_e64 s[20:21], s69, v167
	s_and_b64 s[22:23], s[24:25], s[22:23]
	s_movk_i32 s16, 0x6a
	v_cmp_gt_i32_e64 s[18:19], s18, v167
	s_and_b64 s[20:21], s[22:23], s[20:21]
	s_movk_i32 s14, 0x69
	v_cmp_gt_i32_e64 s[16:17], s16, v167
	s_and_b64 s[18:19], s[20:21], s[18:19]
	s_movk_i32 s12, 0x68
	v_cmp_gt_i32_e64 s[14:15], s14, v167
	s_and_b64 s[16:17], s[18:19], s[16:17]
	s_movk_i32 s10, 0x63
	v_cmp_gt_i32_e64 s[12:13], s12, v167
	s_and_b64 s[14:15], s[16:17], s[14:15]
	s_movk_i32 s8, 0x62
	v_cmp_gt_i32_e64 s[10:11], s10, v167
	s_and_b64 s[12:13], s[14:15], s[12:13]
	s_movk_i32 s6, 0x61
	v_cmp_gt_i32_e64 s[8:9], s8, v167
	s_and_b64 s[10:11], s[12:13], s[10:11]
	v_cmp_gt_i32_e64 s[6:7], s6, v167
	s_and_b64 s[8:9], s[10:11], s[8:9]
	s_and_b64 s[6:7], s[8:9], s[6:7]
	s_and_b64 vcc, s[6:7], vcc
	v_cndmask_b32_e64 v78, v78, v160, s[58:59]
	v_cndmask_b32_e64 v77, v77, v160, s[56:57]
	v_cndmask_b32_e64 v76, v76, v160, s[54:55]
	v_cndmask_b32_e64 v75, v75, v160, s[52:53]
	v_cndmask_b32_e64 v74, v74, v160, s[50:51]
	v_cndmask_b32_e64 v73, v73, v160, s[48:49]
	v_cndmask_b32_e64 v72, v72, v160, s[44:45]
	v_cndmask_b32_e64 v71, v71, v160, s[42:43]
	v_cndmask_b32_e64 v70, v70, v160, s[40:41]
	v_cndmask_b32_e64 v69, v69, v160, s[38:39]
	v_cndmask_b32_e64 v68, v68, v160, s[36:37]
	v_cndmask_b32_e64 v67, v67, v160, s[34:35]
	v_cndmask_b32_e64 v95, v95, v160, s[30:31]
	v_cndmask_b32_e64 v94, v94, v160, s[28:29]
	v_cndmask_b32_e64 v93, v93, v160, s[26:27]
	v_cndmask_b32_e64 v92, v92, v160, s[24:25]
	v_cndmask_b32_e64 v91, v91, v160, s[22:23]
	v_cndmask_b32_e64 v90, v90, v160, s[20:21]
	v_cndmask_b32_e64 v89, v89, v160, s[18:19]
	v_cndmask_b32_e64 v88, v88, v160, s[16:17]
	v_cndmask_b32_e64 v87, v87, v160, s[14:15]
	v_cndmask_b32_e64 v86, v86, v160, s[12:13]
	v_cndmask_b32_e64 v85, v85, v160, s[10:11]
	v_cndmask_b32_e64 v84, v84, v160, s[8:9]
	v_cndmask_b32_e64 v83, v83, v160, s[6:7]
	v_cndmask_b32_e32 v82, v82, v160, vcc
.LBB0_239:
	v_max_f32_e32 v117, v66, v67
	v_max3_f32 v117, v117, v68, v69
	v_max3_f32 v117, v117, v70, v71
	v_max3_f32 v117, v117, v72, v73
	v_max3_f32 v117, v117, v74, v75
	v_max3_f32 v117, v117, v76, v77
	v_max3_f32 v117, v117, v78, v79
	v_max3_f32 v117, v117, v80, v81
	v_max3_f32 v117, v117, v82, v83
	v_max3_f32 v117, v117, v84, v85
	v_max3_f32 v117, v117, v86, v87
	v_max3_f32 v117, v117, v88, v89
	v_max3_f32 v117, v117, v90, v91
	v_max3_f32 v117, v117, v92, v93
	v_max3_f32 v117, v117, v94, v95
	v_max3_f32 v117, v117, v96, v97
	v_mov_b32_e32 v120, v117
	s_nop 1
	v_permlane32_swap_b32_e32 v117, v120
	v_max_f32_e32 v117, v117, v120
	v_sub_f32_e32 v120, v117, v116
	v_max_f32_e32 v117, v116, v117
	s_and_b32 s1, s1, 0x3fffffc0
	v_sub_f32_e32 v121, v116, v117
	s_lshl_b32 s1, s1, 2
	v_mul_f32_e32 v121, 0x3e38aa3b, v121
	s_add_i32 s80, s1, 0
	v_mul_f32_e32 v120, 0x3e000000, v120
	v_exp_f32_e32 v121, v121
	s_add_i32 s80, s80, 0x14000
	v_cmp_ge_f32_e32 vcc, s33, v120
	s_cmp_eq_u64 vcc, exec
	s_cselect_b64 s[6:7], -1, 0
	v_cndmask_b32_e64 v182, v121, 1.0, s[6:7]
	v_cmp_gt_f32_e32 vcc, 1.0, v182
	v_cmp_gt_u32_e64 s[8:9], 32, v163
	s_cbranch_vccz .LBB0_243
	s_and_saveexec_b64 s[10:11], s[8:9]
	v_lshl_add_u32 v120, v165, 2, s80
	ds_write_b32 v120, v182 offset:128
	s_or_b64 exec, exec, s[10:11]
	s_waitcnt lgkmcnt(0)
	v_lshl_add_u32 v132, v138, 2, s80
	ds_read_b128 v[120:123], v132 offset:224
	ds_read_b128 v[124:127], v132 offset:192
	ds_read_b128 v[128:131], v132 offset:160
	ds_read_b128 v[132:135], v132 offset:128
	s_waitcnt lgkmcnt(3)
	v_pk_mul_f32 v[32:33], v[32:33], v[122:123]
	s_waitcnt lgkmcnt(2)
	v_pk_mul_f32 v[28:29], v[28:29], v[126:127]
	s_waitcnt lgkmcnt(1)
	v_pk_mul_f32 v[24:25], v[24:25], v[130:131]
	s_waitcnt lgkmcnt(0)
	v_pk_mul_f32 v[20:21], v[20:21], v[134:135]
	v_pk_mul_f32 v[30:31], v[30:31], v[120:121]
	v_pk_mul_f32 v[26:27], v[26:27], v[124:125]
	v_pk_mul_f32 v[22:23], v[22:23], v[128:129]
	v_pk_mul_f32 v[18:19], v[18:19], v[132:133]
	v_pk_mul_f32 v[48:49], v[48:49], v[122:123]
	v_pk_mul_f32 v[44:45], v[44:45], v[126:127]
	v_pk_mul_f32 v[40:41], v[40:41], v[130:131]
	v_pk_mul_f32 v[36:37], v[36:37], v[134:135]
	v_pk_mul_f32 v[46:47], v[46:47], v[120:121]
	v_pk_mul_f32 v[42:43], v[42:43], v[124:125]
	v_pk_mul_f32 v[38:39], v[38:39], v[128:129]
	v_pk_mul_f32 v[34:35], v[34:35], v[132:133]
	v_pk_mul_f32 v[64:65], v[64:65], v[122:123]
	v_pk_mul_f32 v[60:61], v[60:61], v[126:127]
	v_pk_mul_f32 v[56:57], v[56:57], v[130:131]
	v_pk_mul_f32 v[52:53], v[52:53], v[134:135]
	v_pk_mul_f32 v[62:63], v[62:63], v[120:121]
	v_pk_mul_f32 v[58:59], v[58:59], v[124:125]
	v_pk_mul_f32 v[54:55], v[54:55], v[128:129]
	v_pk_mul_f32 v[50:51], v[50:51], v[132:133]
	v_pk_mul_f32 v[16:17], v[16:17], v[122:123]
	v_pk_mul_f32 v[12:13], v[12:13], v[126:127]
	v_pk_mul_f32 v[8:9], v[8:9], v[130:131]
	v_pk_mul_f32 v[4:5], v[4:5], v[134:135]
	v_pk_mul_f32 v[14:15], v[14:15], v[120:121]
	v_pk_mul_f32 v[10:11], v[10:11], v[124:125]
	v_pk_mul_f32 v[6:7], v[6:7], v[128:129]
	v_pk_mul_f32 v[2:3], v[2:3], v[132:133]

.LBB0_245:
	v_max_f32_e32 v121, v82, v83
	v_max3_f32 v121, v121, v84, v85
	v_max3_f32 v121, v121, v86, v87
	v_max3_f32 v121, v121, v88, v89
	v_max3_f32 v121, v121, v90, v91
	v_max3_f32 v121, v121, v92, v93
	v_max3_f32 v121, v121, v94, v95
	v_max3_f32 v121, v121, v96, v97
	v_max3_f32 v121, v121, v66, v67
	v_max3_f32 v121, v121, v68, v69
	v_max3_f32 v121, v121, v70, v71
	v_max3_f32 v121, v121, v72, v73
	v_max3_f32 v121, v121, v74, v75
	v_max3_f32 v121, v121, v76, v77
	v_max3_f32 v121, v121, v78, v79
	v_max3_f32 v121, v121, v80, v81
	v_mov_b32_e32 v122, v121
	s_nop 1
	v_permlane32_swap_b32_e32 v121, v122
	v_max_f32_e32 v121, v121, v122
	v_sub_f32_e32 v122, v121, v120
	v_mul_f32_e32 v122, 0x3e000000, v122
	v_cmp_ge_f32_e32 vcc, s33, v122
	v_max_f32_e32 v121, v120, v121
	v_sub_f32_e32 v122, v120, v121
	v_mul_f32_e32 v122, 0x3e38aa3b, v122
	s_cmp_eq_u64 vcc, exec
	v_exp_f32_e32 v122, v122
	s_cselect_b64 vcc, -1, 0
	v_cndmask_b32_e32 v139, v121, v120, vcc
	v_mul_f32_e32 v120, 0xbe38aa3b, v139
	v_pk_fma_f32 v[96:97], v[96:97], s[84:85], v[120:121] op_sel_hi:[1,0,0]
	v_pk_fma_f32 v[94:95], v[94:95], s[84:85], v[120:121] op_sel_hi:[1,0,0]
	v_pk_fma_f32 v[92:93], v[92:93], s[84:85], v[120:121] op_sel_hi:[1,0,0]
	v_pk_fma_f32 v[90:91], v[90:91], s[84:85], v[120:121] op_sel_hi:[1,0,0]
	v_pk_fma_f32 v[88:89], v[88:89], s[84:85], v[120:121] op_sel_hi:[1,0,0]
	v_pk_fma_f32 v[86:87], v[86:87], s[84:85], v[120:121] op_sel_hi:[1,0,0]
	v_pk_fma_f32 v[84:85], v[84:85], s[84:85], v[120:121] op_sel_hi:[1,0,0]
	v_pk_fma_f32 v[82:83], v[82:83], s[84:85], v[120:121] op_sel_hi:[1,0,0]
	v_cndmask_b32_e64 v181, v122, 1.0, vcc
	v_exp_f32_e32 v136, v82
	v_exp_f32_e32 v137, v83
	v_exp_f32_e32 v134, v84
	v_exp_f32_e32 v135, v85
	v_exp_f32_e32 v132, v86
	v_exp_f32_e32 v133, v87
	v_exp_f32_e32 v130, v88
	v_exp_f32_e32 v131, v89
	v_exp_f32_e32 v128, v90
	v_exp_f32_e32 v129, v91
	v_exp_f32_e32 v126, v92
	v_exp_f32_e32 v127, v93
	v_exp_f32_e32 v124, v94
	v_exp_f32_e32 v125, v95
	v_exp_f32_e32 v122, v96
	v_exp_f32_e32 v123, v97
	v_cmp_gt_f32_e32 vcc, 1.0, v181
	s_cbranch_vccz .LBB0_249
	v_cmp_gt_u32_e32 vcc, 32, v163
	s_and_saveexec_b64 s[6:7], vcc
	v_lshl_add_u32 v82, v165, 2, s80
	ds_write_b32 v82, v181 offset:128
	s_or_b64 exec, exec, s[6:7]
	s_waitcnt lgkmcnt(0)
	v_lshl_add_u32 v94, v138, 2, s80
	ds_read_b128 v[82:85], v94 offset:224
	ds_read_b128 v[86:89], v94 offset:192
	ds_read_b128 v[90:93], v94 offset:160
	ds_read_b128 v[94:97], v94 offset:128
	s_waitcnt lgkmcnt(3)
	v_pk_mul_f32 v[32:33], v[32:33], v[84:85]
	s_waitcnt lgkmcnt(2)
	v_pk_mul_f32 v[28:29], v[28:29], v[88:89]
	s_waitcnt lgkmcnt(1)
	v_pk_mul_f32 v[24:25], v[24:25], v[92:93]
	s_waitcnt lgkmcnt(0)
	v_pk_mul_f32 v[20:21], v[20:21], v[96:97]
	v_pk_mul_f32 v[30:31], v[30:31], v[82:83]
	v_pk_mul_f32 v[26:27], v[26:27], v[86:87]
	v_pk_mul_f32 v[22:23], v[22:23], v[90:91]
	v_pk_mul_f32 v[18:19], v[18:19], v[94:95]
	v_pk_mul_f32 v[48:49], v[48:49], v[84:85]
	v_pk_mul_f32 v[44:45], v[44:45], v[88:89]
	v_pk_mul_f32 v[40:41], v[40:41], v[92:93]
	v_pk_mul_f32 v[36:37], v[36:37], v[96:97]
	v_pk_mul_f32 v[46:47], v[46:47], v[82:83]
	v_pk_mul_f32 v[42:43], v[42:43], v[86:87]
	v_pk_mul_f32 v[38:39], v[38:39], v[90:91]
	v_pk_mul_f32 v[34:35], v[34:35], v[94:95]
	v_pk_mul_f32 v[64:65], v[64:65], v[84:85]
	v_pk_mul_f32 v[60:61], v[60:61], v[88:89]
	v_pk_mul_f32 v[56:57], v[56:57], v[92:93]
	v_pk_mul_f32 v[52:53], v[52:53], v[96:97]
	v_pk_mul_f32 v[62:63], v[62:63], v[82:83]
	v_pk_mul_f32 v[58:59], v[58:59], v[86:87]
	v_pk_mul_f32 v[54:55], v[54:55], v[90:91]
	v_pk_mul_f32 v[50:51], v[50:51], v[94:95]
	v_pk_mul_f32 v[16:17], v[16:17], v[84:85]
	v_pk_mul_f32 v[12:13], v[12:13], v[88:89]
	v_pk_mul_f32 v[8:9], v[8:9], v[92:93]
	v_pk_mul_f32 v[4:5], v[4:5], v[96:97]
	v_pk_mul_f32 v[14:15], v[14:15], v[82:83]
	v_pk_mul_f32 v[10:11], v[10:11], v[86:87]
	v_pk_mul_f32 v[6:7], v[6:7], v[90:91]
	v_pk_mul_f32 v[2:3], v[2:3], v[94:95]

.LBB0_253:
	v_max_f32_e32 v116, v66, v67
	v_max3_f32 v116, v116, v68, v69
	v_max3_f32 v116, v116, v70, v71
	v_max3_f32 v116, v116, v72, v73
	v_max3_f32 v116, v116, v74, v75
	v_max3_f32 v116, v116, v76, v77
	v_max3_f32 v116, v116, v78, v79
	v_max3_f32 v116, v116, v80, v81
	v_max3_f32 v116, v116, v82, v83
	v_max3_f32 v116, v116, v84, v85
	v_max3_f32 v116, v116, v86, v87
	v_max3_f32 v116, v116, v88, v89
	v_max3_f32 v116, v116, v90, v91
	v_max3_f32 v116, v116, v92, v93
	v_max3_f32 v116, v116, v94, v95
	v_max3_f32 v116, v116, v96, v97
	v_mov_b32_e32 v117, v116
	s_nop 1
	v_permlane32_swap_b32_e32 v116, v117
	v_max_f32_e32 v116, v116, v117
	v_sub_f32_e32 v117, v116, v139
	v_max_f32_e32 v116, v139, v116
	v_sub_f32_e32 v120, v139, v116
	v_mul_f32_e32 v120, 0x3e38aa3b, v120
	v_mul_f32_e32 v117, 0x3e000000, v117
	v_exp_f32_e32 v120, v120
	v_cmp_ge_f32_e32 vcc, s33, v117
	s_cmp_eq_u64 vcc, exec
	s_cselect_b64 s[6:7], -1, 0
	v_cndmask_b32_e64 v184, v120, 1.0, s[6:7]
	v_cmp_gt_f32_e32 vcc, 1.0, v184
	s_cbranch_vccz .LBB0_257
	s_and_saveexec_b64 s[8:9], s[4:5]
	ds_write_b32 v182, v184 offset:128
	s_or_b64 exec, exec, s[8:9]
	s_waitcnt lgkmcnt(0)
	ds_read_b128 v[120:123], v179 offset:224
	ds_read_b128 v[124:127], v179 offset:192
	ds_read_b128 v[128:131], v179 offset:160
	ds_read_b128 v[132:135], v179 offset:128
	s_waitcnt lgkmcnt(3)
	v_pk_mul_f32 v[32:33], v[32:33], v[122:123]
	s_waitcnt lgkmcnt(2)
	v_pk_mul_f32 v[28:29], v[28:29], v[126:127]
	s_waitcnt lgkmcnt(1)
	v_pk_mul_f32 v[24:25], v[24:25], v[130:131]
	s_waitcnt lgkmcnt(0)
	v_pk_mul_f32 v[20:21], v[20:21], v[134:135]
	v_pk_mul_f32 v[30:31], v[30:31], v[120:121]
	v_pk_mul_f32 v[26:27], v[26:27], v[124:125]
	v_pk_mul_f32 v[22:23], v[22:23], v[128:129]
	v_pk_mul_f32 v[18:19], v[18:19], v[132:133]
	v_pk_mul_f32 v[48:49], v[48:49], v[122:123]
	v_pk_mul_f32 v[44:45], v[44:45], v[126:127]
	v_pk_mul_f32 v[40:41], v[40:41], v[130:131]
	v_pk_mul_f32 v[36:37], v[36:37], v[134:135]
	v_pk_mul_f32 v[46:47], v[46:47], v[120:121]
	v_pk_mul_f32 v[42:43], v[42:43], v[124:125]
	v_pk_mul_f32 v[38:39], v[38:39], v[128:129]
	v_pk_mul_f32 v[34:35], v[34:35], v[132:133]
	v_pk_mul_f32 v[64:65], v[64:65], v[122:123]
	v_pk_mul_f32 v[60:61], v[60:61], v[126:127]
	v_pk_mul_f32 v[56:57], v[56:57], v[130:131]
	v_pk_mul_f32 v[52:53], v[52:53], v[134:135]
	v_pk_mul_f32 v[62:63], v[62:63], v[120:121]
	v_pk_mul_f32 v[58:59], v[58:59], v[124:125]
	v_pk_mul_f32 v[54:55], v[54:55], v[128:129]
	v_pk_mul_f32 v[50:51], v[50:51], v[132:133]
	v_pk_mul_f32 v[16:17], v[16:17], v[122:123]
	v_pk_mul_f32 v[12:13], v[12:13], v[126:127]
	v_pk_mul_f32 v[8:9], v[8:9], v[130:131]
	v_pk_mul_f32 v[4:5], v[4:5], v[134:135]
	v_pk_mul_f32 v[14:15], v[14:15], v[120:121]
	v_pk_mul_f32 v[10:11], v[10:11], v[124:125]
	v_pk_mul_f32 v[6:7], v[6:7], v[128:129]
	v_pk_mul_f32 v[2:3], v[2:3], v[132:133]

.LBB0_259:
	v_max_f32_e32 v121, v66, v67
	v_max3_f32 v121, v121, v68, v69
	v_max3_f32 v121, v121, v70, v71
	v_max3_f32 v121, v121, v72, v73
	v_max3_f32 v121, v121, v74, v75
	v_max3_f32 v121, v121, v76, v77
	v_max3_f32 v121, v121, v78, v79
	v_max3_f32 v121, v121, v80, v81
	v_max3_f32 v121, v121, v82, v83
	v_max3_f32 v121, v121, v84, v85
	v_max3_f32 v121, v121, v86, v87
	v_max3_f32 v121, v121, v88, v89
	v_max3_f32 v121, v121, v90, v91
	v_max3_f32 v121, v121, v92, v93
	v_max3_f32 v121, v121, v94, v95
	v_max3_f32 v121, v121, v96, v97
	v_mov_b32_e32 v122, v121
	s_nop 1
	v_permlane32_swap_b32_e32 v121, v122
	v_max_f32_e32 v121, v121, v122
	v_sub_f32_e32 v122, v121, v120
	v_max_f32_e32 v121, v120, v121
	v_sub_f32_e32 v123, v120, v121
	v_mul_f32_e32 v123, 0x3e38aa3b, v123
	v_mul_f32_e32 v122, 0x3e000000, v122
	v_exp_f32_e32 v123, v123
	v_cmp_ge_f32_e32 vcc, s33, v122
	s_cmp_eq_u64 vcc, exec
	s_cselect_b64 s[6:7], -1, 0
	v_cndmask_b32_e64 v185, v123, 1.0, s[6:7]
	v_cmp_gt_f32_e32 vcc, 1.0, v185
	s_cbranch_vccz .LBB0_263
	s_and_saveexec_b64 s[8:9], s[4:5]
	ds_write_b32 v182, v185 offset:128
	s_or_b64 exec, exec, s[8:9]
	s_waitcnt lgkmcnt(0)
	ds_read_b128 v[122:125], v179 offset:224
	ds_read_b128 v[126:129], v179 offset:192
	ds_read_b128 v[130:133], v179 offset:160
	ds_read_b128 v[134:137], v179 offset:128
	s_waitcnt lgkmcnt(3)
	v_pk_mul_f32 v[32:33], v[32:33], v[124:125]
	s_waitcnt lgkmcnt(2)
	v_pk_mul_f32 v[28:29], v[28:29], v[128:129]
	s_waitcnt lgkmcnt(1)
	v_pk_mul_f32 v[24:25], v[24:25], v[132:133]
	s_waitcnt lgkmcnt(0)
	v_pk_mul_f32 v[20:21], v[20:21], v[136:137]
	v_pk_mul_f32 v[30:31], v[30:31], v[122:123]
	v_pk_mul_f32 v[26:27], v[26:27], v[126:127]
	v_pk_mul_f32 v[22:23], v[22:23], v[130:131]
	v_pk_mul_f32 v[18:19], v[18:19], v[134:135]
	v_pk_mul_f32 v[48:49], v[48:49], v[124:125]
	v_pk_mul_f32 v[44:45], v[44:45], v[128:129]
	v_pk_mul_f32 v[40:41], v[40:41], v[132:133]
	v_pk_mul_f32 v[36:37], v[36:37], v[136:137]
	v_pk_mul_f32 v[46:47], v[46:47], v[122:123]
	v_pk_mul_f32 v[42:43], v[42:43], v[126:127]
	v_pk_mul_f32 v[38:39], v[38:39], v[130:131]
	v_pk_mul_f32 v[34:35], v[34:35], v[134:135]
	v_pk_mul_f32 v[64:65], v[64:65], v[124:125]
	v_pk_mul_f32 v[60:61], v[60:61], v[128:129]
	v_pk_mul_f32 v[56:57], v[56:57], v[132:133]
	v_pk_mul_f32 v[52:53], v[52:53], v[136:137]
	v_pk_mul_f32 v[62:63], v[62:63], v[122:123]
	v_pk_mul_f32 v[58:59], v[58:59], v[126:127]
	v_pk_mul_f32 v[54:55], v[54:55], v[130:131]
	v_pk_mul_f32 v[50:51], v[50:51], v[134:135]
	v_pk_mul_f32 v[16:17], v[16:17], v[124:125]
	v_pk_mul_f32 v[12:13], v[12:13], v[128:129]
	v_pk_mul_f32 v[8:9], v[8:9], v[132:133]
	v_pk_mul_f32 v[4:5], v[4:5], v[136:137]
	v_pk_mul_f32 v[14:15], v[14:15], v[122:123]
	v_pk_mul_f32 v[10:11], v[10:11], v[126:127]
	v_pk_mul_f32 v[6:7], v[6:7], v[130:131]
	v_pk_mul_f32 v[2:3], v[2:3], v[134:135]

.LBB0_265:
	v_max_f32_e32 v121, v66, v67
	v_max3_f32 v121, v121, v68, v69
	v_max3_f32 v121, v121, v70, v71
	v_max3_f32 v121, v121, v72, v73
	v_max3_f32 v121, v121, v74, v75
	v_max3_f32 v121, v121, v76, v77
	v_max3_f32 v121, v121, v78, v79
	v_max3_f32 v121, v121, v80, v81
	v_max3_f32 v121, v121, v82, v83
	v_max3_f32 v121, v121, v84, v85
	v_max3_f32 v121, v121, v86, v87
	v_max3_f32 v121, v121, v88, v89
	v_max3_f32 v121, v121, v90, v91
	v_max3_f32 v121, v121, v92, v93
	v_max3_f32 v121, v121, v94, v95
	v_max3_f32 v121, v121, v96, v97
	v_mov_b32_e32 v123, v121
	s_nop 1
	v_permlane32_swap_b32_e32 v121, v123
	v_max_f32_e32 v121, v121, v123
	v_sub_f32_e32 v123, v121, v122
	v_max_f32_e32 v121, v122, v121
	v_sub_f32_e32 v124, v122, v121
	v_mul_f32_e32 v124, 0x3e38aa3b, v124
	v_mul_f32_e32 v123, 0x3e000000, v123
	v_exp_f32_e32 v124, v124
	v_cmp_ge_f32_e32 vcc, s33, v123
	s_cmp_eq_u64 vcc, exec
	s_cselect_b64 s[6:7], -1, 0
	v_cndmask_b32_e64 v187, v124, 1.0, s[6:7]
	v_cmp_gt_f32_e32 vcc, 1.0, v187
	s_cbranch_vccz .LBB0_269
	s_and_saveexec_b64 s[8:9], s[4:5]
	ds_write_b32 v182, v187 offset:128
	s_or_b64 exec, exec, s[8:9]
	s_waitcnt lgkmcnt(0)
	ds_read_b128 v[124:127], v179 offset:224
	ds_read_b128 v[128:131], v179 offset:192
	ds_read_b128 v[132:135], v179 offset:160
	ds_read_b128 v[136:139], v179 offset:128
	s_waitcnt lgkmcnt(3)
	v_pk_mul_f32 v[32:33], v[32:33], v[126:127]
	s_waitcnt lgkmcnt(2)
	v_pk_mul_f32 v[28:29], v[28:29], v[130:131]
	s_waitcnt lgkmcnt(1)
	v_pk_mul_f32 v[24:25], v[24:25], v[134:135]
	s_waitcnt lgkmcnt(0)
	v_pk_mul_f32 v[20:21], v[20:21], v[138:139]
	v_pk_mul_f32 v[30:31], v[30:31], v[124:125]
	v_pk_mul_f32 v[26:27], v[26:27], v[128:129]
	v_pk_mul_f32 v[22:23], v[22:23], v[132:133]
	v_pk_mul_f32 v[18:19], v[18:19], v[136:137]
	v_pk_mul_f32 v[48:49], v[48:49], v[126:127]
	v_pk_mul_f32 v[44:45], v[44:45], v[130:131]
	v_pk_mul_f32 v[40:41], v[40:41], v[134:135]
	v_pk_mul_f32 v[36:37], v[36:37], v[138:139]
	v_pk_mul_f32 v[46:47], v[46:47], v[124:125]
	v_pk_mul_f32 v[42:43], v[42:43], v[128:129]
	v_pk_mul_f32 v[38:39], v[38:39], v[132:133]
	v_pk_mul_f32 v[34:35], v[34:35], v[136:137]
	v_pk_mul_f32 v[64:65], v[64:65], v[126:127]
	v_pk_mul_f32 v[60:61], v[60:61], v[130:131]
	v_pk_mul_f32 v[56:57], v[56:57], v[134:135]
	v_pk_mul_f32 v[52:53], v[52:53], v[138:139]
	v_pk_mul_f32 v[62:63], v[62:63], v[124:125]
	v_pk_mul_f32 v[58:59], v[58:59], v[128:129]
	v_pk_mul_f32 v[54:55], v[54:55], v[132:133]
	v_pk_mul_f32 v[50:51], v[50:51], v[136:137]
	v_pk_mul_f32 v[16:17], v[16:17], v[126:127]
	v_pk_mul_f32 v[12:13], v[12:13], v[130:131]
	v_pk_mul_f32 v[8:9], v[8:9], v[134:135]
	v_pk_mul_f32 v[4:5], v[4:5], v[138:139]
	v_pk_mul_f32 v[14:15], v[14:15], v[124:125]
	v_pk_mul_f32 v[10:11], v[10:11], v[128:129]
	v_pk_mul_f32 v[6:7], v[6:7], v[132:133]
	v_pk_mul_f32 v[2:3], v[2:3], v[136:137]

.LBB0_271:
	v_max_f32_e32 v122, v82, v83
	v_max3_f32 v122, v122, v84, v85
	v_max3_f32 v122, v122, v86, v87
	v_max3_f32 v122, v122, v88, v89
	v_max3_f32 v122, v122, v90, v91
	v_max3_f32 v122, v122, v92, v93
	v_max3_f32 v122, v122, v94, v95
	v_max3_f32 v122, v122, v96, v97
	v_max3_f32 v122, v122, v66, v67
	v_max3_f32 v122, v122, v68, v69
	v_max3_f32 v122, v122, v70, v71
	v_max3_f32 v122, v122, v72, v73
	v_max3_f32 v122, v122, v74, v75
	v_max3_f32 v122, v122, v76, v77
	v_max3_f32 v122, v122, v78, v79
	v_max3_f32 v122, v122, v80, v81
	v_mov_b32_e32 v123, v122
	s_nop 1
	v_permlane32_swap_b32_e32 v122, v123
	v_max_f32_e32 v122, v122, v123
	v_sub_f32_e32 v123, v122, v121
	v_mul_f32_e32 v123, 0x3e000000, v123
	v_cmp_ge_f32_e32 vcc, s33, v123
	v_max_f32_e32 v122, v121, v122
	v_sub_f32_e32 v123, v121, v122
	v_mul_f32_e32 v123, 0x3e38aa3b, v123
	s_cmp_eq_u64 vcc, exec
	v_exp_f32_e32 v123, v123
	s_cselect_b64 vcc, -1, 0
	v_cndmask_b32_e32 v139, v122, v121, vcc
	v_mul_f32_e32 v154, 0xbe38aa3b, v139
	v_pk_fma_f32 v[96:97], v[96:97], s[84:85], v[154:155] op_sel_hi:[1,0,0]
	v_pk_fma_f32 v[94:95], v[94:95], s[84:85], v[154:155] op_sel_hi:[1,0,0]
	v_pk_fma_f32 v[92:93], v[92:93], s[84:85], v[154:155] op_sel_hi:[1,0,0]
	v_pk_fma_f32 v[90:91], v[90:91], s[84:85], v[154:155] op_sel_hi:[1,0,0]
	v_pk_fma_f32 v[88:89], v[88:89], s[84:85], v[154:155] op_sel_hi:[1,0,0]
	v_pk_fma_f32 v[86:87], v[86:87], s[84:85], v[154:155] op_sel_hi:[1,0,0]
	v_pk_fma_f32 v[84:85], v[84:85], s[84:85], v[154:155] op_sel_hi:[1,0,0]
	v_pk_fma_f32 v[82:83], v[82:83], s[84:85], v[154:155] op_sel_hi:[1,0,0]
	v_cndmask_b32_e64 v121, v123, 1.0, vcc
	v_exp_f32_e32 v136, v82
	v_exp_f32_e32 v137, v83
	v_exp_f32_e32 v134, v84
	v_exp_f32_e32 v135, v85
	v_exp_f32_e32 v132, v86
	v_exp_f32_e32 v133, v87
	v_exp_f32_e32 v130, v88
	v_exp_f32_e32 v131, v89
	v_exp_f32_e32 v128, v90
	v_exp_f32_e32 v129, v91
	v_exp_f32_e32 v126, v92
	v_exp_f32_e32 v127, v93
	v_exp_f32_e32 v124, v94
	v_exp_f32_e32 v125, v95
	v_exp_f32_e32 v122, v96
	v_exp_f32_e32 v123, v97
	v_cmp_gt_f32_e32 vcc, 1.0, v121
	s_cbranch_vccz .LBB0_275
	s_and_saveexec_b64 s[6:7], s[4:5]
	ds_write_b32 v182, v121 offset:128
	s_or_b64 exec, exec, s[6:7]
	s_waitcnt lgkmcnt(0)
	ds_read_b128 v[82:85], v179 offset:224
	ds_read_b128 v[86:89], v179 offset:192
	ds_read_b128 v[90:93], v179 offset:160
	ds_read_b128 v[94:97], v179 offset:128
	s_waitcnt lgkmcnt(3)
	v_pk_mul_f32 v[32:33], v[32:33], v[84:85]
	s_waitcnt lgkmcnt(2)
	v_pk_mul_f32 v[28:29], v[28:29], v[88:89]
	s_waitcnt lgkmcnt(1)
	v_pk_mul_f32 v[24:25], v[24:25], v[92:93]
	s_waitcnt lgkmcnt(0)
	v_pk_mul_f32 v[20:21], v[20:21], v[96:97]
	v_pk_mul_f32 v[30:31], v[30:31], v[82:83]
	v_pk_mul_f32 v[26:27], v[26:27], v[86:87]
	v_pk_mul_f32 v[22:23], v[22:23], v[90:91]
	v_pk_mul_f32 v[18:19], v[18:19], v[94:95]
	v_pk_mul_f32 v[48:49], v[48:49], v[84:85]
	v_pk_mul_f32 v[44:45], v[44:45], v[88:89]
	v_pk_mul_f32 v[40:41], v[40:41], v[92:93]
	v_pk_mul_f32 v[36:37], v[36:37], v[96:97]
	v_pk_mul_f32 v[46:47], v[46:47], v[82:83]
	v_pk_mul_f32 v[42:43], v[42:43], v[86:87]
	v_pk_mul_f32 v[38:39], v[38:39], v[90:91]
	v_pk_mul_f32 v[34:35], v[34:35], v[94:95]
	v_pk_mul_f32 v[64:65], v[64:65], v[84:85]
	v_pk_mul_f32 v[60:61], v[60:61], v[88:89]
	v_pk_mul_f32 v[56:57], v[56:57], v[92:93]
	v_pk_mul_f32 v[52:53], v[52:53], v[96:97]
	v_pk_mul_f32 v[62:63], v[62:63], v[82:83]
	v_pk_mul_f32 v[58:59], v[58:59], v[86:87]
	v_pk_mul_f32 v[54:55], v[54:55], v[90:91]
	v_pk_mul_f32 v[50:51], v[50:51], v[94:95]
	v_pk_mul_f32 v[16:17], v[16:17], v[84:85]
	v_pk_mul_f32 v[12:13], v[12:13], v[88:89]
	v_pk_mul_f32 v[8:9], v[8:9], v[92:93]
	v_pk_mul_f32 v[4:5], v[4:5], v[96:97]
	v_pk_mul_f32 v[14:15], v[14:15], v[82:83]
	v_pk_mul_f32 v[10:11], v[10:11], v[86:87]
	v_pk_mul_f32 v[6:7], v[6:7], v[90:91]
	v_pk_mul_f32 v[2:3], v[2:3], v[94:95]

.LBB0_281:
	v_max_f32_e32 v100, v66, v67
	v_max3_f32 v100, v100, v68, v69
	v_max3_f32 v100, v100, v70, v71
	v_max3_f32 v100, v100, v72, v73
	v_max3_f32 v100, v100, v74, v75
	v_max3_f32 v100, v100, v76, v77
	v_max3_f32 v100, v100, v78, v79
	v_max3_f32 v100, v100, v80, v81
	v_max3_f32 v100, v100, v82, v83
	v_max3_f32 v100, v100, v84, v85
	v_max3_f32 v100, v100, v86, v87
	v_max3_f32 v100, v100, v88, v89
	v_max3_f32 v100, v100, v90, v91
	v_max3_f32 v100, v100, v92, v93
	v_max3_f32 v100, v100, v94, v95
	v_max3_f32 v100, v100, v96, v97
	v_mov_b32_e32 v101, v100
	s_nop 1
	v_permlane32_swap_b32_e32 v100, v101
	v_max_f32_e32 v100, v100, v101
	v_sub_f32_e32 v101, v100, v139
	v_mul_f32_e32 v118, 0x3e000000, v101
	v_max_f32_e32 v101, v139, v100
	v_sub_f32_e32 v100, v139, v101
	v_mul_f32_e32 v100, 0x3e38aa3b, v100
	v_exp_f32_e32 v100, v100
	v_cmp_ge_f32_e32 vcc, s33, v118
	s_cmp_eq_u64 vcc, exec
	s_cselect_b64 s[4:5], -1, 0
	v_readlane_b32 s10, v254, 24
	v_readlane_b32 s12, v254, 31
	v_cndmask_b32_e64 v100, v100, 1.0, s[4:5]
	v_readlane_b32 s86, v254, 19
	v_readlane_b32 s8, v254, 23
	v_readlane_b32 s11, v254, 25
	v_readlane_b32 s9, v254, 30
	v_readlane_b32 s68, v254, 33
	v_readlane_b32 s13, v254, 32
	v_cmp_gt_f32_e32 vcc, 1.0, v100
	v_readlane_b32 s87, v254, 20
	s_cbranch_vccz .LBB0_285
	v_cmp_gt_u32_e32 vcc, 32, v163
	s_and_saveexec_b64 s[6:7], vcc
	v_lshl_add_u32 v118, v165, 2, s80
	ds_write_b32 v118, v100 offset:128
	s_or_b64 exec, exec, s[6:7]
	s_waitcnt lgkmcnt(0)
	ds_read_b128 v[122:125], v179 offset:224
	ds_read_b128 v[126:129], v179 offset:192
	ds_read_b128 v[130:133], v179 offset:160
	ds_read_b128 v[134:137], v179 offset:128
	s_waitcnt lgkmcnt(3)
	v_pk_mul_f32 v[32:33], v[32:33], v[124:125]
	s_waitcnt lgkmcnt(2)
	v_pk_mul_f32 v[28:29], v[28:29], v[128:129]
	s_waitcnt lgkmcnt(1)
	v_pk_mul_f32 v[24:25], v[24:25], v[132:133]
	s_waitcnt lgkmcnt(0)
	v_pk_mul_f32 v[20:21], v[20:21], v[136:137]
	v_pk_mul_f32 v[30:31], v[30:31], v[122:123]
	v_pk_mul_f32 v[26:27], v[26:27], v[126:127]
	v_pk_mul_f32 v[22:23], v[22:23], v[130:131]
	v_pk_mul_f32 v[18:19], v[18:19], v[134:135]
	v_pk_mul_f32 v[48:49], v[48:49], v[124:125]
	v_pk_mul_f32 v[44:45], v[44:45], v[128:129]
	v_pk_mul_f32 v[40:41], v[40:41], v[132:133]
	v_pk_mul_f32 v[36:37], v[36:37], v[136:137]
	v_pk_mul_f32 v[46:47], v[46:47], v[122:123]
	v_pk_mul_f32 v[42:43], v[42:43], v[126:127]
	v_pk_mul_f32 v[38:39], v[38:39], v[130:131]
	v_pk_mul_f32 v[34:35], v[34:35], v[134:135]
	v_pk_mul_f32 v[64:65], v[64:65], v[124:125]
	v_pk_mul_f32 v[60:61], v[60:61], v[128:129]
	v_pk_mul_f32 v[56:57], v[56:57], v[132:133]
	v_pk_mul_f32 v[52:53], v[52:53], v[136:137]
	v_pk_mul_f32 v[62:63], v[62:63], v[122:123]
	v_pk_mul_f32 v[58:59], v[58:59], v[126:127]
	v_pk_mul_f32 v[54:55], v[54:55], v[130:131]
	v_pk_mul_f32 v[50:51], v[50:51], v[134:135]
	v_pk_mul_f32 v[16:17], v[16:17], v[124:125]
	v_pk_mul_f32 v[12:13], v[12:13], v[128:129]
	v_pk_mul_f32 v[8:9], v[8:9], v[132:133]
	v_pk_mul_f32 v[4:5], v[4:5], v[136:137]
	v_pk_mul_f32 v[14:15], v[14:15], v[122:123]
	v_pk_mul_f32 v[10:11], v[10:11], v[126:127]
	v_pk_mul_f32 v[6:7], v[6:7], v[130:131]
	v_pk_mul_f32 v[2:3], v[2:3], v[134:135]

.LBB0_435:
	v_add_u32_e32 v166, s3, v171
	v_ashrrev_i32_e32 v167, 31, v166
	v_lshlrev_b64 v[2:3], 11, v[166:167]
	v_lshl_add_u64 v[2:3], v[140:141], 0, v[2:3]
	global_load_dwordx4 v[126:129], v[2:3], off
	global_load_dwordx4 v[122:125], v[2:3], off offset:64
	global_load_dwordx4 v[118:121], v[2:3], off offset:128
	global_load_dwordx4 v[114:117], v[2:3], off offset:192
	global_load_dwordx4 v[110:113], v[2:3], off offset:256
	global_load_dwordx4 v[106:109], v[2:3], off offset:320
	global_load_dwordx4 v[102:105], v[2:3], off offset:384
	global_load_dwordx4 v[98:101], v[2:3], off offset:448
	global_load_dwordx4 v[94:97], v[2:3], off offset:512
	global_load_dwordx4 v[90:93], v[2:3], off offset:576
	global_load_dwordx4 v[86:89], v[2:3], off offset:640
	global_load_dwordx4 v[82:85], v[2:3], off offset:704
	global_load_dwordx4 v[78:81], v[2:3], off offset:768
	global_load_dwordx4 v[74:77], v[2:3], off offset:832
	global_load_dwordx4 v[70:73], v[2:3], off offset:896
	global_load_dwordx4 v[66:69], v[2:3], off offset:960
	global_load_dwordx4 v[62:65], v[2:3], off offset:1024
	global_load_dwordx4 v[58:61], v[2:3], off offset:1088
	global_load_dwordx4 v[54:57], v[2:3], off offset:1152
	global_load_dwordx4 v[50:53], v[2:3], off offset:1216
	global_load_dwordx4 v[46:49], v[2:3], off offset:1280
	global_load_dwordx4 v[42:45], v[2:3], off offset:1344
	global_load_dwordx4 v[38:41], v[2:3], off offset:1408
	global_load_dwordx4 v[34:37], v[2:3], off offset:1472
	global_load_dwordx4 v[30:33], v[2:3], off offset:1536
	global_load_dwordx4 v[26:29], v[2:3], off offset:1600
	global_load_dwordx4 v[22:25], v[2:3], off offset:1664
	global_load_dwordx4 v[18:21], v[2:3], off offset:1728
	global_load_dwordx4 v[14:17], v[2:3], off offset:1792
	global_load_dwordx4 v[10:13], v[2:3], off offset:1856
	global_load_dwordx4 v[6:9], v[2:3], off offset:1920
	s_nop 0
	global_load_dwordx4 v[2:5], v[2:3], off offset:1984
	ds_read_b128 v[130:133], v175 offset:33024
	ds_read_b128 v[134:137], v175 offset:33088
	ds_read_b128 v[210:213], v175
	ds_read_b128 v[214:217], v175 offset:64
	ds_read_b128 v[218:221], v174 offset:33024
	ds_read_b128 v[222:225], v174 offset:33088
	ds_read_b128 v[226:229], v174
	ds_read_b128 v[230:233], v174 offset:64
	v_lshlrev_b64 v[168:169], 10, v[166:167]
	s_waitcnt vmcnt(31) lgkmcnt(1)
	v_mfma_f32_16x16x32_bf16 v[226:229], v[126:129], v[226:229], 0
	v_and_b32_e32 v147, 0xffff0000, v126
	v_and_b32_e32 v151, 0xffff0000, v127
	v_lshlrev_b32_e32 v145, 16, v126
	v_mfma_f32_16x16x32_bf16 v[218:221], v[126:129], v[218:221], 0
	v_lshlrev_b32_e32 v149, 16, v127
	v_and_b32_e32 v155, 0xffff0000, v128
	v_mul_f32_e32 v147, v147, v147
	v_mul_f32_e32 v151, v151, v151
	v_mfma_f32_16x16x32_bf16 v[210:213], v[126:129], v[210:213], v[226:229]
	v_lshlrev_b32_e32 v153, 16, v128
	v_and_b32_e32 v159, 0xffff0000, v129
	v_mul_f32_e32 v155, v155, v155
	v_mfma_f32_16x16x32_bf16 v[130:133], v[126:129], v[130:133], v[218:221]
	v_fmac_f32_e32 v147, v145, v145
	v_fmac_f32_e32 v151, v149, v149
	v_lshlrev_b32_e32 v157, 16, v129
	s_waitcnt vmcnt(30)
	v_and_b32_e32 v234, 0xffff0000, v122
	v_mul_f32_e32 v159, v159, v159
	v_fmac_f32_e32 v155, v153, v153
	v_add_f32_e32 v145, v147, v151
	v_lshlrev_b32_e32 v167, 16, v122
	v_and_b32_e32 v236, 0xffff0000, v123
	v_mul_f32_e32 v234, v234, v234
	v_fmac_f32_e32 v159, v157, v157
	v_add_f32_e32 v145, v155, v145
	v_lshlrev_b32_e32 v235, 16, v123
	v_and_b32_e32 v238, 0xffff0000, v124
	v_mul_f32_e32 v236, v236, v236
	v_fmac_f32_e32 v234, v167, v167
	s_waitcnt lgkmcnt(0)
	v_mfma_f32_16x16x32_bf16 v[210:213], v[122:125], v[230:233], v[210:213]
	v_add_f32_e32 v145, v159, v145
	v_lshlrev_b32_e32 v237, 16, v124
	v_and_b32_e32 v240, 0xffff0000, v125
	v_mfma_f32_16x16x32_bf16 v[130:133], v[122:125], v[222:225], v[130:133]
	v_mul_f32_e32 v238, v238, v238
	v_fmac_f32_e32 v236, v235, v235
	v_add_f32_e32 v145, v234, v145
	v_lshlrev_b32_e32 v239, 16, v125
	v_mul_f32_e32 v240, v240, v240
	v_fmac_f32_e32 v238, v237, v237
	v_add_f32_e32 v145, v236, v145
	v_fmac_f32_e32 v240, v239, v239
	v_add_f32_e32 v145, v238, v145
	v_mfma_f32_16x16x32_bf16 v[210:213], v[122:125], v[214:217], v[210:213]
	v_add_f32_e32 v145, v240, v145
	v_mfma_f32_16x16x32_bf16 v[130:133], v[122:125], v[134:137], v[130:133]
	s_waitcnt vmcnt(29)
	v_and_b32_e32 v149, 0xffff0000, v118
	v_lshlrev_b32_e32 v147, 16, v118
	v_mul_f32_e32 v149, v149, v149
	v_fmac_f32_e32 v149, v147, v147
	v_add_f32_e32 v145, v149, v145
	v_and_b32_e32 v149, 0xffff0000, v119
	v_lshlrev_b32_e32 v147, 16, v119
	v_mul_f32_e32 v149, v149, v149
	v_fmac_f32_e32 v149, v147, v147
	v_add_f32_e32 v145, v149, v145
	v_and_b32_e32 v149, 0xffff0000, v120
	v_lshlrev_b32_e32 v147, 16, v120
	v_mul_f32_e32 v149, v149, v149
	v_fmac_f32_e32 v149, v147, v147
	v_add_f32_e32 v145, v149, v145
	v_and_b32_e32 v149, 0xffff0000, v121
	ds_read_b128 v[134:137], v174 offset:128
	ds_read_b128 v[214:217], v174 offset:33152
	ds_read_b128 v[218:221], v175 offset:128
	ds_read_b128 v[222:225], v175 offset:33152
	ds_read_b128 v[226:229], v174 offset:192
	v_lshlrev_b32_e32 v147, 16, v121
	v_mul_f32_e32 v149, v149, v149
	s_waitcnt lgkmcnt(4)
	v_mfma_f32_16x16x32_bf16 v[134:137], v[118:121], v[134:137], v[210:213]
	v_fmac_f32_e32 v149, v147, v147
	v_add_f32_e32 v145, v149, v145
	s_waitcnt vmcnt(28)
	v_and_b32_e32 v149, 0xffff0000, v114
	s_waitcnt lgkmcnt(3)
	v_mfma_f32_16x16x32_bf16 v[130:133], v[118:121], v[214:217], v[130:133]
	v_lshlrev_b32_e32 v147, 16, v114
	v_mul_f32_e32 v149, v149, v149
	v_fmac_f32_e32 v149, v147, v147
	s_waitcnt lgkmcnt(2)
	v_mfma_f32_16x16x32_bf16 v[134:137], v[118:121], v[218:221], v[134:137]
	ds_read_b128 v[218:221], v174 offset:33216
	ds_read_b128 v[214:217], v175 offset:33216
	v_add_f32_e32 v145, v149, v145
	v_and_b32_e32 v149, 0xffff0000, v115
	s_waitcnt lgkmcnt(3)
	v_mfma_f32_16x16x32_bf16 v[130:133], v[118:121], v[222:225], v[130:133]
	v_lshlrev_b32_e32 v147, 16, v115
	v_mul_f32_e32 v149, v149, v149
	v_fmac_f32_e32 v149, v147, v147
	v_add_f32_e32 v145, v149, v145
	v_and_b32_e32 v149, 0xffff0000, v116
	ds_read_b128 v[210:213], v175 offset:192
	v_lshlrev_b32_e32 v147, 16, v116
	v_mul_f32_e32 v149, v149, v149
	s_waitcnt lgkmcnt(3)
	v_mfma_f32_16x16x32_bf16 v[134:137], v[114:117], v[226:229], v[134:137]
	v_fmac_f32_e32 v149, v147, v147
	v_add_f32_e32 v145, v149, v145
	v_and_b32_e32 v149, 0xffff0000, v117
	s_waitcnt lgkmcnt(2)
	v_mfma_f32_16x16x32_bf16 v[130:133], v[114:117], v[218:221], v[130:133]
	v_lshlrev_b32_e32 v147, 16, v117
	v_mul_f32_e32 v149, v149, v149
	v_fmac_f32_e32 v149, v147, v147
	s_waitcnt lgkmcnt(0)
	v_mfma_f32_16x16x32_bf16 v[134:137], v[114:117], v[210:213], v[134:137]
	v_add_f32_e32 v145, v149, v145
	v_mfma_f32_16x16x32_bf16 v[130:133], v[114:117], v[214:217], v[130:133]
	s_waitcnt vmcnt(27)
	v_and_b32_e32 v149, 0xffff0000, v110
	v_lshlrev_b32_e32 v147, 16, v110
	v_mul_f32_e32 v149, v149, v149
	v_fmac_f32_e32 v149, v147, v147
	v_add_f32_e32 v145, v149, v145
	v_and_b32_e32 v149, 0xffff0000, v111
	v_lshlrev_b32_e32 v147, 16, v111
	v_mul_f32_e32 v149, v149, v149
	v_fmac_f32_e32 v149, v147, v147
	v_add_f32_e32 v145, v149, v145
	v_and_b32_e32 v149, 0xffff0000, v112
	v_lshlrev_b32_e32 v147, 16, v112
	v_mul_f32_e32 v149, v149, v149
	v_fmac_f32_e32 v149, v147, v147
	v_add_f32_e32 v145, v149, v145
	v_and_b32_e32 v149, 0xffff0000, v113
	ds_read_b128 v[210:213], v174 offset:256
	ds_read_b128 v[214:217], v174 offset:33280
	ds_read_b128 v[218:221], v175 offset:256
	ds_read_b128 v[222:225], v175 offset:33280
	ds_read_b128 v[226:229], v174 offset:320
	v_lshlrev_b32_e32 v147, 16, v113
	v_mul_f32_e32 v149, v149, v149
	s_waitcnt lgkmcnt(4)
	v_mfma_f32_16x16x32_bf16 v[134:137], v[110:113], v[210:213], v[134:137]
	v_fmac_f32_e32 v149, v147, v147
	v_add_f32_e32 v145, v149, v145
	s_waitcnt vmcnt(26)
	v_and_b32_e32 v149, 0xffff0000, v106
	s_waitcnt lgkmcnt(3)
	v_mfma_f32_16x16x32_bf16 v[130:133], v[110:113], v[214:217], v[130:133]
	v_lshlrev_b32_e32 v147, 16, v106
	v_mul_f32_e32 v149, v149, v149
	v_fmac_f32_e32 v149, v147, v147
	s_waitcnt lgkmcnt(2)
	v_mfma_f32_16x16x32_bf16 v[134:137], v[110:113], v[218:221], v[134:137]
	ds_read_b128 v[218:221], v174 offset:33344
	ds_read_b128 v[214:217], v175 offset:33344
	v_add_f32_e32 v145, v149, v145
	v_and_b32_e32 v149, 0xffff0000, v107
	s_waitcnt lgkmcnt(3)
	v_mfma_f32_16x16x32_bf16 v[130:133], v[110:113], v[222:225], v[130:133]
	v_lshlrev_b32_e32 v147, 16, v107
	v_mul_f32_e32 v149, v149, v149
	v_fmac_f32_e32 v149, v147, v147
	v_add_f32_e32 v145, v149, v145
	v_and_b32_e32 v149, 0xffff0000, v108
	ds_read_b128 v[210:213], v175 offset:320
	v_lshlrev_b32_e32 v147, 16, v108
	v_mul_f32_e32 v149, v149, v149
	s_waitcnt lgkmcnt(3)
	v_mfma_f32_16x16x32_bf16 v[134:137], v[106:109], v[226:229], v[134:137]
	v_fmac_f32_e32 v149, v147, v147
	v_add_f32_e32 v145, v149, v145
	v_and_b32_e32 v149, 0xffff0000, v109
	s_waitcnt lgkmcnt(2)
	v_mfma_f32_16x16x32_bf16 v[130:133], v[106:109], v[218:221], v[130:133]
	v_lshlrev_b32_e32 v147, 16, v109
	v_mul_f32_e32 v149, v149, v149
	v_fmac_f32_e32 v149, v147, v147
	s_waitcnt lgkmcnt(0)
	v_mfma_f32_16x16x32_bf16 v[134:137], v[106:109], v[210:213], v[134:137]
	v_add_f32_e32 v145, v149, v145
	v_mfma_f32_16x16x32_bf16 v[130:133], v[106:109], v[214:217], v[130:133]
	s_waitcnt vmcnt(25)
	v_and_b32_e32 v149, 0xffff0000, v102
	v_lshlrev_b32_e32 v147, 16, v102
	v_mul_f32_e32 v149, v149, v149
	v_fmac_f32_e32 v149, v147, v147
	v_add_f32_e32 v145, v149, v145
	v_and_b32_e32 v149, 0xffff0000, v103
	v_lshlrev_b32_e32 v147, 16, v103
	v_mul_f32_e32 v149, v149, v149
	v_fmac_f32_e32 v149, v147, v147
	v_add_f32_e32 v145, v149, v145
	v_and_b32_e32 v149, 0xffff0000, v104
	v_lshlrev_b32_e32 v147, 16, v104
	v_mul_f32_e32 v149, v149, v149
	v_fmac_f32_e32 v149, v147, v147
	v_add_f32_e32 v145, v149, v145
	v_and_b32_e32 v149, 0xffff0000, v105
	ds_read_b128 v[210:213], v174 offset:384
	ds_read_b128 v[214:217], v174 offset:33408
	ds_read_b128 v[218:221], v175 offset:384
	ds_read_b128 v[222:225], v175 offset:33408
	ds_read_b128 v[226:229], v174 offset:448
	v_lshlrev_b32_e32 v147, 16, v105
	v_mul_f32_e32 v149, v149, v149
	s_waitcnt lgkmcnt(4)
	v_mfma_f32_16x16x32_bf16 v[134:137], v[102:105], v[210:213], v[134:137]
	v_fmac_f32_e32 v149, v147, v147
	v_add_f32_e32 v145, v149, v145
	s_waitcnt vmcnt(24)
	v_and_b32_e32 v149, 0xffff0000, v98
	s_waitcnt lgkmcnt(3)
	v_mfma_f32_16x16x32_bf16 v[130:133], v[102:105], v[214:217], v[130:133]
	v_lshlrev_b32_e32 v147, 16, v98
	v_mul_f32_e32 v149, v149, v149
	v_fmac_f32_e32 v149, v147, v147
	s_waitcnt lgkmcnt(2)
	v_mfma_f32_16x16x32_bf16 v[134:137], v[102:105], v[218:221], v[134:137]
	ds_read_b128 v[218:221], v174 offset:33472
	ds_read_b128 v[214:217], v175 offset:33472
	v_add_f32_e32 v145, v149, v145
	v_and_b32_e32 v149, 0xffff0000, v99
	s_waitcnt lgkmcnt(3)
	v_mfma_f32_16x16x32_bf16 v[130:133], v[102:105], v[222:225], v[130:133]
	v_lshlrev_b32_e32 v147, 16, v99
	v_mul_f32_e32 v149, v149, v149
	v_fmac_f32_e32 v149, v147, v147
	v_add_f32_e32 v145, v149, v145
	v_and_b32_e32 v149, 0xffff0000, v100
	ds_read_b128 v[210:213], v175 offset:448
	v_lshlrev_b32_e32 v147, 16, v100
	v_mul_f32_e32 v149, v149, v149
	s_waitcnt lgkmcnt(3)
	v_mfma_f32_16x16x32_bf16 v[134:137], v[98:101], v[226:229], v[134:137]
	v_fmac_f32_e32 v149, v147, v147
	v_add_f32_e32 v145, v149, v145
	v_and_b32_e32 v149, 0xffff0000, v101
	s_waitcnt lgkmcnt(2)
	v_mfma_f32_16x16x32_bf16 v[130:133], v[98:101], v[218:221], v[130:133]
	v_lshlrev_b32_e32 v147, 16, v101
	v_mul_f32_e32 v149, v149, v149
	v_fmac_f32_e32 v149, v147, v147
	s_waitcnt lgkmcnt(0)
	v_mfma_f32_16x16x32_bf16 v[134:137], v[98:101], v[210:213], v[134:137]
	v_add_f32_e32 v145, v149, v145
	v_mfma_f32_16x16x32_bf16 v[130:133], v[98:101], v[214:217], v[130:133]
	s_waitcnt vmcnt(23)
	v_and_b32_e32 v149, 0xffff0000, v94
	v_lshlrev_b32_e32 v147, 16, v94
	v_mul_f32_e32 v149, v149, v149
	v_fmac_f32_e32 v149, v147, v147
	v_add_f32_e32 v145, v149, v145
	v_and_b32_e32 v149, 0xffff0000, v95
	v_lshlrev_b32_e32 v147, 16, v95
	v_mul_f32_e32 v149, v149, v149
	v_fmac_f32_e32 v149, v147, v147
	v_add_f32_e32 v145, v149, v145
	v_and_b32_e32 v149, 0xffff0000, v96
	v_lshlrev_b32_e32 v147, 16, v96
	v_mul_f32_e32 v149, v149, v149
	v_fmac_f32_e32 v149, v147, v147
	v_add_f32_e32 v145, v149, v145
	v_and_b32_e32 v149, 0xffff0000, v97
	ds_read_b128 v[210:213], v174 offset:512
	ds_read_b128 v[214:217], v174 offset:33536
	ds_read_b128 v[218:221], v175 offset:512
	ds_read_b128 v[222:225], v175 offset:33536
	ds_read_b128 v[226:229], v174 offset:576
	v_lshlrev_b32_e32 v147, 16, v97
	v_mul_f32_e32 v149, v149, v149
	s_waitcnt lgkmcnt(4)
	v_mfma_f32_16x16x32_bf16 v[134:137], v[94:97], v[210:213], v[134:137]
	v_fmac_f32_e32 v149, v147, v147
	v_add_f32_e32 v145, v149, v145
	s_waitcnt vmcnt(22)
	v_and_b32_e32 v149, 0xffff0000, v90
	s_waitcnt lgkmcnt(3)
	v_mfma_f32_16x16x32_bf16 v[130:133], v[94:97], v[214:217], v[130:133]
	v_lshlrev_b32_e32 v147, 16, v90
	v_mul_f32_e32 v149, v149, v149
	v_fmac_f32_e32 v149, v147, v147
	s_waitcnt lgkmcnt(2)
	v_mfma_f32_16x16x32_bf16 v[134:137], v[94:97], v[218:221], v[134:137]
	ds_read_b128 v[218:221], v174 offset:33600
	ds_read_b128 v[214:217], v175 offset:33600
	v_add_f32_e32 v145, v149, v145
	v_and_b32_e32 v149, 0xffff0000, v91
	s_waitcnt lgkmcnt(3)
	v_mfma_f32_16x16x32_bf16 v[130:133], v[94:97], v[222:225], v[130:133]
	v_lshlrev_b32_e32 v147, 16, v91
	v_mul_f32_e32 v149, v149, v149
	v_fmac_f32_e32 v149, v147, v147
	v_add_f32_e32 v145, v149, v145
	v_and_b32_e32 v149, 0xffff0000, v92
	ds_read_b128 v[210:213], v175 offset:576
	v_lshlrev_b32_e32 v147, 16, v92
	v_mul_f32_e32 v149, v149, v149
	s_waitcnt lgkmcnt(3)
	v_mfma_f32_16x16x32_bf16 v[134:137], v[90:93], v[226:229], v[134:137]
	v_fmac_f32_e32 v149, v147, v147
	v_add_f32_e32 v145, v149, v145
	v_and_b32_e32 v149, 0xffff0000, v93
	s_waitcnt lgkmcnt(2)
	v_mfma_f32_16x16x32_bf16 v[130:133], v[90:93], v[218:221], v[130:133]
	v_lshlrev_b32_e32 v147, 16, v93
	v_mul_f32_e32 v149, v149, v149
	v_fmac_f32_e32 v149, v147, v147
	s_waitcnt lgkmcnt(0)
	v_mfma_f32_16x16x32_bf16 v[134:137], v[90:93], v[210:213], v[134:137]
	v_add_f32_e32 v145, v149, v145
	v_mfma_f32_16x16x32_bf16 v[130:133], v[90:93], v[214:217], v[130:133]
	s_waitcnt vmcnt(21)
	v_and_b32_e32 v149, 0xffff0000, v86
	v_lshlrev_b32_e32 v147, 16, v86
	v_mul_f32_e32 v149, v149, v149
	v_fmac_f32_e32 v149, v147, v147
	v_add_f32_e32 v145, v149, v145
	v_and_b32_e32 v149, 0xffff0000, v87
	v_lshlrev_b32_e32 v147, 16, v87
	v_mul_f32_e32 v149, v149, v149
	v_fmac_f32_e32 v149, v147, v147
	v_add_f32_e32 v145, v149, v145
	v_and_b32_e32 v149, 0xffff0000, v88
	v_lshlrev_b32_e32 v147, 16, v88
	v_mul_f32_e32 v149, v149, v149
	v_fmac_f32_e32 v149, v147, v147
	v_add_f32_e32 v145, v149, v145
	v_and_b32_e32 v149, 0xffff0000, v89
	ds_read_b128 v[210:213], v174 offset:640
	ds_read_b128 v[214:217], v174 offset:33664
	ds_read_b128 v[218:221], v175 offset:640
	ds_read_b128 v[222:225], v175 offset:33664
	ds_read_b128 v[226:229], v174 offset:704
	v_lshlrev_b32_e32 v147, 16, v89
	v_mul_f32_e32 v149, v149, v149
	s_waitcnt lgkmcnt(4)
	v_mfma_f32_16x16x32_bf16 v[134:137], v[86:89], v[210:213], v[134:137]
	v_fmac_f32_e32 v149, v147, v147
	v_add_f32_e32 v145, v149, v145
	s_waitcnt vmcnt(20)
	v_and_b32_e32 v149, 0xffff0000, v82
	s_waitcnt lgkmcnt(3)
	v_mfma_f32_16x16x32_bf16 v[130:133], v[86:89], v[214:217], v[130:133]
	v_lshlrev_b32_e32 v147, 16, v82
	v_mul_f32_e32 v149, v149, v149
	v_fmac_f32_e32 v149, v147, v147
	s_waitcnt lgkmcnt(2)
	v_mfma_f32_16x16x32_bf16 v[134:137], v[86:89], v[218:221], v[134:137]
	ds_read_b128 v[218:221], v174 offset:33728
	ds_read_b128 v[214:217], v175 offset:33728
	v_add_f32_e32 v145, v149, v145
	v_and_b32_e32 v149, 0xffff0000, v83
	s_waitcnt lgkmcnt(3)
	v_mfma_f32_16x16x32_bf16 v[130:133], v[86:89], v[222:225], v[130:133]
	v_lshlrev_b32_e32 v147, 16, v83
	v_mul_f32_e32 v149, v149, v149
	v_fmac_f32_e32 v149, v147, v147
	v_add_f32_e32 v145, v149, v145
	v_and_b32_e32 v149, 0xffff0000, v84
	ds_read_b128 v[210:213], v175 offset:704
	v_lshlrev_b32_e32 v147, 16, v84
	v_mul_f32_e32 v149, v149, v149
	s_waitcnt lgkmcnt(3)
	v_mfma_f32_16x16x32_bf16 v[134:137], v[82:85], v[226:229], v[134:137]
	v_fmac_f32_e32 v149, v147, v147
	v_add_f32_e32 v145, v149, v145
	v_and_b32_e32 v149, 0xffff0000, v85
	s_waitcnt lgkmcnt(2)
	v_mfma_f32_16x16x32_bf16 v[130:133], v[82:85], v[218:221], v[130:133]
	v_lshlrev_b32_e32 v147, 16, v85
	v_mul_f32_e32 v149, v149, v149
	v_fmac_f32_e32 v149, v147, v147
	s_waitcnt lgkmcnt(0)
	v_mfma_f32_16x16x32_bf16 v[134:137], v[82:85], v[210:213], v[134:137]
	v_add_f32_e32 v145, v149, v145
	v_mfma_f32_16x16x32_bf16 v[130:133], v[82:85], v[214:217], v[130:133]
	s_waitcnt vmcnt(19)
	v_and_b32_e32 v149, 0xffff0000, v78
	v_lshlrev_b32_e32 v147, 16, v78
	v_mul_f32_e32 v149, v149, v149
	v_fmac_f32_e32 v149, v147, v147
	v_add_f32_e32 v145, v149, v145
	v_and_b32_e32 v149, 0xffff0000, v79
	v_lshlrev_b32_e32 v147, 16, v79
	v_mul_f32_e32 v149, v149, v149
	v_fmac_f32_e32 v149, v147, v147
	v_add_f32_e32 v145, v149, v145
	v_and_b32_e32 v149, 0xffff0000, v80
	v_lshlrev_b32_e32 v147, 16, v80
	v_mul_f32_e32 v149, v149, v149
	v_fmac_f32_e32 v149, v147, v147
	v_add_f32_e32 v145, v149, v145
	v_and_b32_e32 v149, 0xffff0000, v81
	ds_read_b128 v[210:213], v174 offset:768
	ds_read_b128 v[214:217], v174 offset:33792
	ds_read_b128 v[218:221], v175 offset:768
	ds_read_b128 v[222:225], v175 offset:33792
	ds_read_b128 v[226:229], v174 offset:832
	v_lshlrev_b32_e32 v147, 16, v81
	v_mul_f32_e32 v149, v149, v149
	s_waitcnt lgkmcnt(4)
	v_mfma_f32_16x16x32_bf16 v[134:137], v[78:81], v[210:213], v[134:137]
	v_fmac_f32_e32 v149, v147, v147
	v_add_f32_e32 v145, v149, v145
	s_waitcnt vmcnt(18)
	v_and_b32_e32 v149, 0xffff0000, v74
	s_waitcnt lgkmcnt(3)
	v_mfma_f32_16x16x32_bf16 v[130:133], v[78:81], v[214:217], v[130:133]
	v_lshlrev_b32_e32 v147, 16, v74
	v_mul_f32_e32 v149, v149, v149
	v_fmac_f32_e32 v149, v147, v147
	s_waitcnt lgkmcnt(2)
	v_mfma_f32_16x16x32_bf16 v[134:137], v[78:81], v[218:221], v[134:137]
	ds_read_b128 v[218:221], v174 offset:33856
	ds_read_b128 v[214:217], v175 offset:33856
	v_add_f32_e32 v145, v149, v145
	v_and_b32_e32 v149, 0xffff0000, v75
	s_waitcnt lgkmcnt(3)
	v_mfma_f32_16x16x32_bf16 v[130:133], v[78:81], v[222:225], v[130:133]
	v_lshlrev_b32_e32 v147, 16, v75
	v_mul_f32_e32 v149, v149, v149
	v_fmac_f32_e32 v149, v147, v147
	v_add_f32_e32 v145, v149, v145
	v_and_b32_e32 v149, 0xffff0000, v76
	ds_read_b128 v[210:213], v175 offset:832
	v_lshlrev_b32_e32 v147, 16, v76
	v_mul_f32_e32 v149, v149, v149
	s_waitcnt lgkmcnt(3)
	v_mfma_f32_16x16x32_bf16 v[134:137], v[74:77], v[226:229], v[134:137]
	v_fmac_f32_e32 v149, v147, v147
	v_add_f32_e32 v145, v149, v145
	v_and_b32_e32 v149, 0xffff0000, v77
	s_waitcnt lgkmcnt(2)
	v_mfma_f32_16x16x32_bf16 v[130:133], v[74:77], v[218:221], v[130:133]
	v_lshlrev_b32_e32 v147, 16, v77
	v_mul_f32_e32 v149, v149, v149
	v_fmac_f32_e32 v149, v147, v147
	s_waitcnt lgkmcnt(0)
	v_mfma_f32_16x16x32_bf16 v[134:137], v[74:77], v[210:213], v[134:137]
	v_add_f32_e32 v145, v149, v145
	v_mfma_f32_16x16x32_bf16 v[130:133], v[74:77], v[214:217], v[130:133]
	s_waitcnt vmcnt(17)
	v_and_b32_e32 v149, 0xffff0000, v70
	v_lshlrev_b32_e32 v147, 16, v70
	v_mul_f32_e32 v149, v149, v149
	v_fmac_f32_e32 v149, v147, v147
	v_add_f32_e32 v145, v149, v145
	v_and_b32_e32 v149, 0xffff0000, v71
	v_lshlrev_b32_e32 v147, 16, v71
	v_mul_f32_e32 v149, v149, v149
	v_fmac_f32_e32 v149, v147, v147
	v_add_f32_e32 v145, v149, v145
	v_and_b32_e32 v149, 0xffff0000, v72
	v_lshlrev_b32_e32 v147, 16, v72
	v_mul_f32_e32 v149, v149, v149
	v_fmac_f32_e32 v149, v147, v147
	v_add_f32_e32 v145, v149, v145
	v_and_b32_e32 v149, 0xffff0000, v73
	ds_read_b128 v[210:213], v174 offset:896
	ds_read_b128 v[214:217], v174 offset:33920
	ds_read_b128 v[218:221], v175 offset:896
	ds_read_b128 v[222:225], v175 offset:33920
	ds_read_b128 v[226:229], v174 offset:960
	v_lshlrev_b32_e32 v147, 16, v73
	v_mul_f32_e32 v149, v149, v149
	s_waitcnt lgkmcnt(4)
	v_mfma_f32_16x16x32_bf16 v[134:137], v[70:73], v[210:213], v[134:137]
	v_fmac_f32_e32 v149, v147, v147
	v_add_f32_e32 v145, v149, v145
	s_waitcnt vmcnt(16)
	v_and_b32_e32 v149, 0xffff0000, v66
	s_waitcnt lgkmcnt(3)
	v_mfma_f32_16x16x32_bf16 v[130:133], v[70:73], v[214:217], v[130:133]
	v_lshlrev_b32_e32 v147, 16, v66
	v_mul_f32_e32 v149, v149, v149
	v_fmac_f32_e32 v149, v147, v147
	s_waitcnt lgkmcnt(2)
	v_mfma_f32_16x16x32_bf16 v[134:137], v[70:73], v[218:221], v[134:137]
	ds_read_b128 v[218:221], v174 offset:33984
	ds_read_b128 v[214:217], v175 offset:33984
	v_add_f32_e32 v145, v149, v145
	v_and_b32_e32 v149, 0xffff0000, v67
	s_waitcnt lgkmcnt(3)
	v_mfma_f32_16x16x32_bf16 v[130:133], v[70:73], v[222:225], v[130:133]
	v_lshlrev_b32_e32 v147, 16, v67
	v_mul_f32_e32 v149, v149, v149
	v_fmac_f32_e32 v149, v147, v147
	v_add_f32_e32 v145, v149, v145
	v_and_b32_e32 v149, 0xffff0000, v68
	ds_read_b128 v[210:213], v175 offset:960
	v_lshlrev_b32_e32 v147, 16, v68
	v_mul_f32_e32 v149, v149, v149
	s_waitcnt lgkmcnt(3)
	v_mfma_f32_16x16x32_bf16 v[134:137], v[66:69], v[226:229], v[134:137]
	v_fmac_f32_e32 v149, v147, v147
	v_add_f32_e32 v145, v149, v145
	v_and_b32_e32 v149, 0xffff0000, v69
	s_waitcnt lgkmcnt(2)
	v_mfma_f32_16x16x32_bf16 v[130:133], v[66:69], v[218:221], v[130:133]
	v_lshlrev_b32_e32 v147, 16, v69
	v_mul_f32_e32 v149, v149, v149
	v_fmac_f32_e32 v149, v147, v147
	s_waitcnt lgkmcnt(0)
	v_mfma_f32_16x16x32_bf16 v[134:137], v[66:69], v[210:213], v[134:137]
	v_add_f32_e32 v145, v149, v145
	v_mfma_f32_16x16x32_bf16 v[130:133], v[66:69], v[214:217], v[130:133]
	s_waitcnt vmcnt(15)
	v_and_b32_e32 v149, 0xffff0000, v62
	v_lshlrev_b32_e32 v147, 16, v62
	v_mul_f32_e32 v149, v149, v149
	v_fmac_f32_e32 v149, v147, v147
	v_add_f32_e32 v145, v149, v145
	v_and_b32_e32 v149, 0xffff0000, v63
	v_lshlrev_b32_e32 v147, 16, v63
	v_mul_f32_e32 v149, v149, v149
	v_fmac_f32_e32 v149, v147, v147
	v_add_f32_e32 v145, v149, v145
	v_and_b32_e32 v149, 0xffff0000, v64
	v_lshlrev_b32_e32 v147, 16, v64
	v_mul_f32_e32 v149, v149, v149
	v_fmac_f32_e32 v149, v147, v147
	v_add_f32_e32 v145, v149, v145
	v_and_b32_e32 v149, 0xffff0000, v65
	ds_read_b128 v[210:213], v174 offset:1024
	ds_read_b128 v[214:217], v174 offset:34048
	ds_read_b128 v[218:221], v175 offset:1024
	ds_read_b128 v[222:225], v175 offset:34048
	ds_read_b128 v[226:229], v174 offset:1088
	v_lshlrev_b32_e32 v147, 16, v65
	v_mul_f32_e32 v149, v149, v149
	s_waitcnt lgkmcnt(4)
	v_mfma_f32_16x16x32_bf16 v[134:137], v[62:65], v[210:213], v[134:137]
	v_fmac_f32_e32 v149, v147, v147
	v_add_f32_e32 v145, v149, v145
	s_waitcnt vmcnt(14)
	v_and_b32_e32 v149, 0xffff0000, v58
	s_waitcnt lgkmcnt(3)
	v_mfma_f32_16x16x32_bf16 v[130:133], v[62:65], v[214:217], v[130:133]
	v_lshlrev_b32_e32 v147, 16, v58
	v_mul_f32_e32 v149, v149, v149
	v_fmac_f32_e32 v149, v147, v147
	s_waitcnt lgkmcnt(2)
	v_mfma_f32_16x16x32_bf16 v[134:137], v[62:65], v[218:221], v[134:137]
	ds_read_b128 v[218:221], v174 offset:34112
	ds_read_b128 v[214:217], v175 offset:34112
	v_add_f32_e32 v145, v149, v145
	v_and_b32_e32 v149, 0xffff0000, v59
	s_waitcnt lgkmcnt(3)
	v_mfma_f32_16x16x32_bf16 v[130:133], v[62:65], v[222:225], v[130:133]
	v_lshlrev_b32_e32 v147, 16, v59
	v_mul_f32_e32 v149, v149, v149
	v_fmac_f32_e32 v149, v147, v147
	v_add_f32_e32 v145, v149, v145
	v_and_b32_e32 v149, 0xffff0000, v60
	ds_read_b128 v[210:213], v175 offset:1088
	v_lshlrev_b32_e32 v147, 16, v60
	v_mul_f32_e32 v149, v149, v149
	s_waitcnt lgkmcnt(3)
	v_mfma_f32_16x16x32_bf16 v[134:137], v[58:61], v[226:229], v[134:137]
	v_fmac_f32_e32 v149, v147, v147
	v_add_f32_e32 v145, v149, v145
	v_and_b32_e32 v149, 0xffff0000, v61
	s_waitcnt lgkmcnt(2)
	v_mfma_f32_16x16x32_bf16 v[130:133], v[58:61], v[218:221], v[130:133]
	v_lshlrev_b32_e32 v147, 16, v61
	v_mul_f32_e32 v149, v149, v149
	v_fmac_f32_e32 v149, v147, v147
	s_waitcnt lgkmcnt(0)
	v_mfma_f32_16x16x32_bf16 v[134:137], v[58:61], v[210:213], v[134:137]
	v_add_f32_e32 v145, v149, v145
	v_mfma_f32_16x16x32_bf16 v[130:133], v[58:61], v[214:217], v[130:133]
	s_waitcnt vmcnt(13)
	v_and_b32_e32 v149, 0xffff0000, v54
	v_lshlrev_b32_e32 v147, 16, v54
	v_mul_f32_e32 v149, v149, v149
	v_fmac_f32_e32 v149, v147, v147
	v_add_f32_e32 v145, v149, v145
	v_and_b32_e32 v149, 0xffff0000, v55
	v_lshlrev_b32_e32 v147, 16, v55
	v_mul_f32_e32 v149, v149, v149
	v_fmac_f32_e32 v149, v147, v147
	v_add_f32_e32 v145, v149, v145
	v_and_b32_e32 v149, 0xffff0000, v56
	v_lshlrev_b32_e32 v147, 16, v56
	v_mul_f32_e32 v149, v149, v149
	v_fmac_f32_e32 v149, v147, v147
	v_add_f32_e32 v145, v149, v145
	v_and_b32_e32 v149, 0xffff0000, v57
	ds_read_b128 v[210:213], v174 offset:1152
	ds_read_b128 v[214:217], v174 offset:34176
	ds_read_b128 v[218:221], v175 offset:1152
	ds_read_b128 v[222:225], v175 offset:34176
	ds_read_b128 v[226:229], v174 offset:1216
	v_lshlrev_b32_e32 v147, 16, v57
	v_mul_f32_e32 v149, v149, v149
	s_waitcnt lgkmcnt(4)
	v_mfma_f32_16x16x32_bf16 v[134:137], v[54:57], v[210:213], v[134:137]
	v_fmac_f32_e32 v149, v147, v147
	v_add_f32_e32 v145, v149, v145
	s_waitcnt vmcnt(12)
	v_and_b32_e32 v149, 0xffff0000, v50
	s_waitcnt lgkmcnt(3)
	v_mfma_f32_16x16x32_bf16 v[130:133], v[54:57], v[214:217], v[130:133]
	v_lshlrev_b32_e32 v147, 16, v50
	v_mul_f32_e32 v149, v149, v149
	v_fmac_f32_e32 v149, v147, v147
	s_waitcnt lgkmcnt(2)
	v_mfma_f32_16x16x32_bf16 v[134:137], v[54:57], v[218:221], v[134:137]
	ds_read_b128 v[218:221], v174 offset:34240
	ds_read_b128 v[214:217], v175 offset:34240
	v_add_f32_e32 v145, v149, v145
	v_and_b32_e32 v149, 0xffff0000, v51
	s_waitcnt lgkmcnt(3)
	v_mfma_f32_16x16x32_bf16 v[130:133], v[54:57], v[222:225], v[130:133]
	v_lshlrev_b32_e32 v147, 16, v51
	v_mul_f32_e32 v149, v149, v149
	v_fmac_f32_e32 v149, v147, v147
	v_add_f32_e32 v145, v149, v145
	v_and_b32_e32 v149, 0xffff0000, v52
	ds_read_b128 v[210:213], v175 offset:1216
	v_lshlrev_b32_e32 v147, 16, v52
	v_mul_f32_e32 v149, v149, v149
	s_waitcnt lgkmcnt(3)
	v_mfma_f32_16x16x32_bf16 v[134:137], v[50:53], v[226:229], v[134:137]
	v_fmac_f32_e32 v149, v147, v147
	v_add_f32_e32 v145, v149, v145
	v_and_b32_e32 v149, 0xffff0000, v53
	s_waitcnt lgkmcnt(2)
	v_mfma_f32_16x16x32_bf16 v[130:133], v[50:53], v[218:221], v[130:133]
	v_lshlrev_b32_e32 v147, 16, v53
	v_mul_f32_e32 v149, v149, v149
	v_fmac_f32_e32 v149, v147, v147
	s_waitcnt lgkmcnt(0)
	v_mfma_f32_16x16x32_bf16 v[134:137], v[50:53], v[210:213], v[134:137]
	v_add_f32_e32 v145, v149, v145
	v_mfma_f32_16x16x32_bf16 v[130:133], v[50:53], v[214:217], v[130:133]
	s_waitcnt vmcnt(11)
	v_and_b32_e32 v149, 0xffff0000, v46
	v_lshlrev_b32_e32 v147, 16, v46
	v_mul_f32_e32 v149, v149, v149
	v_fmac_f32_e32 v149, v147, v147
	v_add_f32_e32 v145, v149, v145
	v_and_b32_e32 v149, 0xffff0000, v47
	v_lshlrev_b32_e32 v147, 16, v47
	v_mul_f32_e32 v149, v149, v149
	v_fmac_f32_e32 v149, v147, v147
	v_add_f32_e32 v145, v149, v145
	v_and_b32_e32 v149, 0xffff0000, v48
	v_lshlrev_b32_e32 v147, 16, v48
	v_mul_f32_e32 v149, v149, v149
	v_fmac_f32_e32 v149, v147, v147
	v_add_f32_e32 v145, v149, v145
	v_and_b32_e32 v149, 0xffff0000, v49
	ds_read_b128 v[210:213], v174 offset:1280
	ds_read_b128 v[214:217], v174 offset:34304
	ds_read_b128 v[218:221], v175 offset:1280
	ds_read_b128 v[222:225], v175 offset:34304
	ds_read_b128 v[226:229], v174 offset:1344
	v_lshlrev_b32_e32 v147, 16, v49
	v_mul_f32_e32 v149, v149, v149
	s_waitcnt lgkmcnt(4)
	v_mfma_f32_16x16x32_bf16 v[134:137], v[46:49], v[210:213], v[134:137]
	v_fmac_f32_e32 v149, v147, v147
	v_add_f32_e32 v145, v149, v145
	s_waitcnt vmcnt(10)
	v_and_b32_e32 v149, 0xffff0000, v42
	s_waitcnt lgkmcnt(3)
	v_mfma_f32_16x16x32_bf16 v[130:133], v[46:49], v[214:217], v[130:133]
	v_lshlrev_b32_e32 v147, 16, v42
	v_mul_f32_e32 v149, v149, v149
	v_fmac_f32_e32 v149, v147, v147
	s_waitcnt lgkmcnt(2)
	v_mfma_f32_16x16x32_bf16 v[134:137], v[46:49], v[218:221], v[134:137]
	ds_read_b128 v[218:221], v174 offset:34368
	ds_read_b128 v[214:217], v175 offset:34368
	v_add_f32_e32 v145, v149, v145
	v_and_b32_e32 v149, 0xffff0000, v43
	s_waitcnt lgkmcnt(3)
	v_mfma_f32_16x16x32_bf16 v[130:133], v[46:49], v[222:225], v[130:133]
	v_lshlrev_b32_e32 v147, 16, v43
	v_mul_f32_e32 v149, v149, v149
	v_fmac_f32_e32 v149, v147, v147
	v_add_f32_e32 v145, v149, v145
	v_and_b32_e32 v149, 0xffff0000, v44
	ds_read_b128 v[210:213], v175 offset:1344
	v_lshlrev_b32_e32 v147, 16, v44
	v_mul_f32_e32 v149, v149, v149
	s_waitcnt lgkmcnt(3)
	v_mfma_f32_16x16x32_bf16 v[134:137], v[42:45], v[226:229], v[134:137]
	v_fmac_f32_e32 v149, v147, v147
	v_add_f32_e32 v145, v149, v145
	v_and_b32_e32 v149, 0xffff0000, v45
	s_waitcnt lgkmcnt(2)
	v_mfma_f32_16x16x32_bf16 v[130:133], v[42:45], v[218:221], v[130:133]
	v_lshlrev_b32_e32 v147, 16, v45
	v_mul_f32_e32 v149, v149, v149
	v_fmac_f32_e32 v149, v147, v147
	s_waitcnt lgkmcnt(0)
	v_mfma_f32_16x16x32_bf16 v[134:137], v[42:45], v[210:213], v[134:137]
	v_add_f32_e32 v145, v149, v145
	v_mfma_f32_16x16x32_bf16 v[130:133], v[42:45], v[214:217], v[130:133]
	s_waitcnt vmcnt(9)
	v_and_b32_e32 v149, 0xffff0000, v38
	v_lshlrev_b32_e32 v147, 16, v38
	v_mul_f32_e32 v149, v149, v149
	v_fmac_f32_e32 v149, v147, v147
	v_add_f32_e32 v145, v149, v145
	v_and_b32_e32 v149, 0xffff0000, v39
	v_lshlrev_b32_e32 v147, 16, v39
	v_mul_f32_e32 v149, v149, v149
	v_fmac_f32_e32 v149, v147, v147
	v_add_f32_e32 v145, v149, v145
	v_and_b32_e32 v149, 0xffff0000, v40
	v_lshlrev_b32_e32 v147, 16, v40
	v_mul_f32_e32 v149, v149, v149
	v_fmac_f32_e32 v149, v147, v147
	v_add_f32_e32 v145, v149, v145
	v_and_b32_e32 v149, 0xffff0000, v41
	ds_read_b128 v[210:213], v174 offset:1408
	ds_read_b128 v[214:217], v174 offset:34432
	ds_read_b128 v[218:221], v175 offset:1408
	ds_read_b128 v[222:225], v175 offset:34432
	ds_read_b128 v[226:229], v174 offset:1472
	v_lshlrev_b32_e32 v147, 16, v41
	v_mul_f32_e32 v149, v149, v149
	s_waitcnt lgkmcnt(4)
	v_mfma_f32_16x16x32_bf16 v[134:137], v[38:41], v[210:213], v[134:137]
	v_fmac_f32_e32 v149, v147, v147
	v_add_f32_e32 v145, v149, v145
	s_waitcnt vmcnt(8)
	v_and_b32_e32 v149, 0xffff0000, v34
	s_waitcnt lgkmcnt(3)
	v_mfma_f32_16x16x32_bf16 v[130:133], v[38:41], v[214:217], v[130:133]
	v_lshlrev_b32_e32 v147, 16, v34
	v_mul_f32_e32 v149, v149, v149
	v_fmac_f32_e32 v149, v147, v147
	s_waitcnt lgkmcnt(2)
	v_mfma_f32_16x16x32_bf16 v[134:137], v[38:41], v[218:221], v[134:137]
	ds_read_b128 v[218:221], v174 offset:34496
	ds_read_b128 v[214:217], v175 offset:34496
	v_add_f32_e32 v145, v149, v145
	v_and_b32_e32 v149, 0xffff0000, v35
	s_waitcnt lgkmcnt(3)
	v_mfma_f32_16x16x32_bf16 v[130:133], v[38:41], v[222:225], v[130:133]
	v_lshlrev_b32_e32 v147, 16, v35
	v_mul_f32_e32 v149, v149, v149
	v_fmac_f32_e32 v149, v147, v147
	v_add_f32_e32 v145, v149, v145
	v_and_b32_e32 v149, 0xffff0000, v36
	ds_read_b128 v[210:213], v175 offset:1472
	v_lshlrev_b32_e32 v147, 16, v36
	v_mul_f32_e32 v149, v149, v149
	s_waitcnt lgkmcnt(3)
	v_mfma_f32_16x16x32_bf16 v[134:137], v[34:37], v[226:229], v[134:137]
	v_fmac_f32_e32 v149, v147, v147
	v_add_f32_e32 v145, v149, v145
	v_and_b32_e32 v149, 0xffff0000, v37
	s_waitcnt lgkmcnt(2)
	v_mfma_f32_16x16x32_bf16 v[130:133], v[34:37], v[218:221], v[130:133]
	v_lshlrev_b32_e32 v147, 16, v37
	v_mul_f32_e32 v149, v149, v149
	v_fmac_f32_e32 v149, v147, v147
	s_waitcnt lgkmcnt(0)
	v_mfma_f32_16x16x32_bf16 v[134:137], v[34:37], v[210:213], v[134:137]
	v_add_f32_e32 v145, v149, v145
	v_mfma_f32_16x16x32_bf16 v[130:133], v[34:37], v[214:217], v[130:133]
	s_waitcnt vmcnt(7)
	v_and_b32_e32 v149, 0xffff0000, v30
	v_lshlrev_b32_e32 v147, 16, v30
	v_mul_f32_e32 v149, v149, v149
	v_fmac_f32_e32 v149, v147, v147
	v_add_f32_e32 v145, v149, v145
	v_and_b32_e32 v149, 0xffff0000, v31
	v_lshlrev_b32_e32 v147, 16, v31
	v_mul_f32_e32 v149, v149, v149
	v_fmac_f32_e32 v149, v147, v147
	v_add_f32_e32 v145, v149, v145
	v_and_b32_e32 v149, 0xffff0000, v32
	v_lshlrev_b32_e32 v147, 16, v32
	v_mul_f32_e32 v149, v149, v149
	v_fmac_f32_e32 v149, v147, v147
	v_add_f32_e32 v145, v149, v145
	v_and_b32_e32 v149, 0xffff0000, v33
	ds_read_b128 v[210:213], v174 offset:1536
	ds_read_b128 v[214:217], v174 offset:34560
	ds_read_b128 v[218:221], v175 offset:1536
	ds_read_b128 v[222:225], v175 offset:34560
	ds_read_b128 v[226:229], v174 offset:1600
	v_lshlrev_b32_e32 v147, 16, v33
	v_mul_f32_e32 v149, v149, v149
	s_waitcnt lgkmcnt(4)
	v_mfma_f32_16x16x32_bf16 v[134:137], v[30:33], v[210:213], v[134:137]
	v_fmac_f32_e32 v149, v147, v147
	v_add_f32_e32 v145, v149, v145
	s_waitcnt vmcnt(6)
	v_and_b32_e32 v149, 0xffff0000, v26
	s_waitcnt lgkmcnt(3)
	v_mfma_f32_16x16x32_bf16 v[130:133], v[30:33], v[214:217], v[130:133]
	v_lshlrev_b32_e32 v147, 16, v26
	v_mul_f32_e32 v149, v149, v149
	v_fmac_f32_e32 v149, v147, v147
	s_waitcnt lgkmcnt(2)
	v_mfma_f32_16x16x32_bf16 v[134:137], v[30:33], v[218:221], v[134:137]
	ds_read_b128 v[218:221], v174 offset:34624
	ds_read_b128 v[214:217], v175 offset:34624
	v_add_f32_e32 v145, v149, v145
	v_and_b32_e32 v149, 0xffff0000, v27
	s_waitcnt lgkmcnt(3)
	v_mfma_f32_16x16x32_bf16 v[130:133], v[30:33], v[222:225], v[130:133]
	v_lshlrev_b32_e32 v147, 16, v27
	v_mul_f32_e32 v149, v149, v149
	v_fmac_f32_e32 v149, v147, v147
	v_add_f32_e32 v145, v149, v145
	v_and_b32_e32 v149, 0xffff0000, v28
	ds_read_b128 v[210:213], v175 offset:1600
	v_lshlrev_b32_e32 v147, 16, v28
	v_mul_f32_e32 v149, v149, v149
	s_waitcnt lgkmcnt(3)
	v_mfma_f32_16x16x32_bf16 v[134:137], v[26:29], v[226:229], v[134:137]
	v_fmac_f32_e32 v149, v147, v147
	v_add_f32_e32 v145, v149, v145
	v_and_b32_e32 v149, 0xffff0000, v29
	s_waitcnt lgkmcnt(2)
	v_mfma_f32_16x16x32_bf16 v[130:133], v[26:29], v[218:221], v[130:133]
	v_lshlrev_b32_e32 v147, 16, v29
	v_mul_f32_e32 v149, v149, v149
	v_fmac_f32_e32 v149, v147, v147
	s_waitcnt lgkmcnt(0)
	v_mfma_f32_16x16x32_bf16 v[134:137], v[26:29], v[210:213], v[134:137]
	v_add_f32_e32 v145, v149, v145
	v_mfma_f32_16x16x32_bf16 v[130:133], v[26:29], v[214:217], v[130:133]
	s_waitcnt vmcnt(5)
	v_and_b32_e32 v149, 0xffff0000, v22
	v_lshlrev_b32_e32 v147, 16, v22
	v_mul_f32_e32 v149, v149, v149
	v_fmac_f32_e32 v149, v147, v147
	v_add_f32_e32 v145, v149, v145
	v_and_b32_e32 v149, 0xffff0000, v23
	v_lshlrev_b32_e32 v147, 16, v23
	v_mul_f32_e32 v149, v149, v149
	v_fmac_f32_e32 v149, v147, v147
	v_add_f32_e32 v145, v149, v145
	v_and_b32_e32 v149, 0xffff0000, v24
	v_lshlrev_b32_e32 v147, 16, v24
	v_mul_f32_e32 v149, v149, v149
	v_fmac_f32_e32 v149, v147, v147
	v_add_f32_e32 v145, v149, v145
	v_and_b32_e32 v149, 0xffff0000, v25
	ds_read_b128 v[210:213], v174 offset:1664
	ds_read_b128 v[214:217], v174 offset:34688
	ds_read_b128 v[218:221], v175 offset:1664
	ds_read_b128 v[222:225], v175 offset:34688
	ds_read_b128 v[226:229], v174 offset:1728
	v_lshlrev_b32_e32 v147, 16, v25
	v_mul_f32_e32 v149, v149, v149
	s_waitcnt lgkmcnt(4)
	v_mfma_f32_16x16x32_bf16 v[134:137], v[22:25], v[210:213], v[134:137]
	v_fmac_f32_e32 v149, v147, v147
	v_add_f32_e32 v145, v149, v145
	s_waitcnt vmcnt(4)
	v_and_b32_e32 v149, 0xffff0000, v18
	s_waitcnt lgkmcnt(3)
	v_mfma_f32_16x16x32_bf16 v[130:133], v[22:25], v[214:217], v[130:133]
	v_lshlrev_b32_e32 v147, 16, v18
	v_mul_f32_e32 v149, v149, v149
	v_fmac_f32_e32 v149, v147, v147
	s_waitcnt lgkmcnt(2)
	v_mfma_f32_16x16x32_bf16 v[134:137], v[22:25], v[218:221], v[134:137]
	ds_read_b128 v[218:221], v174 offset:34752
	ds_read_b128 v[214:217], v175 offset:34752
	v_add_f32_e32 v145, v149, v145
	v_and_b32_e32 v149, 0xffff0000, v19
	s_waitcnt lgkmcnt(3)
	v_mfma_f32_16x16x32_bf16 v[130:133], v[22:25], v[222:225], v[130:133]
	v_lshlrev_b32_e32 v147, 16, v19
	v_mul_f32_e32 v149, v149, v149
	v_fmac_f32_e32 v149, v147, v147
	v_add_f32_e32 v145, v149, v145
	v_and_b32_e32 v149, 0xffff0000, v20
	ds_read_b128 v[210:213], v175 offset:1728
	v_lshlrev_b32_e32 v147, 16, v20
	v_mul_f32_e32 v149, v149, v149
	s_waitcnt lgkmcnt(3)
	v_mfma_f32_16x16x32_bf16 v[134:137], v[18:21], v[226:229], v[134:137]
	v_fmac_f32_e32 v149, v147, v147
	v_add_f32_e32 v145, v149, v145
	v_and_b32_e32 v149, 0xffff0000, v21
	s_waitcnt lgkmcnt(2)
	v_mfma_f32_16x16x32_bf16 v[130:133], v[18:21], v[218:221], v[130:133]
	v_lshlrev_b32_e32 v147, 16, v21
	v_mul_f32_e32 v149, v149, v149
	v_fmac_f32_e32 v149, v147, v147
	s_waitcnt lgkmcnt(0)
	v_mfma_f32_16x16x32_bf16 v[134:137], v[18:21], v[210:213], v[134:137]
	v_add_f32_e32 v145, v149, v145
	v_mfma_f32_16x16x32_bf16 v[130:133], v[18:21], v[214:217], v[130:133]
	s_waitcnt vmcnt(3)
	v_and_b32_e32 v149, 0xffff0000, v14
	v_lshlrev_b32_e32 v147, 16, v14
	v_mul_f32_e32 v149, v149, v149
	v_fmac_f32_e32 v149, v147, v147
	v_add_f32_e32 v145, v149, v145
	v_and_b32_e32 v149, 0xffff0000, v15
	v_lshlrev_b32_e32 v147, 16, v15
	v_mul_f32_e32 v149, v149, v149
	v_fmac_f32_e32 v149, v147, v147
	v_add_f32_e32 v145, v149, v145
	v_and_b32_e32 v149, 0xffff0000, v16
	v_lshlrev_b32_e32 v147, 16, v16
	v_mul_f32_e32 v149, v149, v149
	v_fmac_f32_e32 v149, v147, v147
	v_add_f32_e32 v145, v149, v145
	v_and_b32_e32 v149, 0xffff0000, v17
	ds_read_b128 v[210:213], v174 offset:1792
	ds_read_b128 v[214:217], v174 offset:34816
	ds_read_b128 v[218:221], v175 offset:1792
	ds_read_b128 v[222:225], v175 offset:34816
	ds_read_b128 v[226:229], v174 offset:1856
	v_lshlrev_b32_e32 v147, 16, v17
	v_mul_f32_e32 v149, v149, v149
	s_waitcnt lgkmcnt(4)
	v_mfma_f32_16x16x32_bf16 v[134:137], v[14:17], v[210:213], v[134:137]
	v_fmac_f32_e32 v149, v147, v147
	v_add_f32_e32 v145, v149, v145
	s_waitcnt vmcnt(2)
	v_and_b32_e32 v149, 0xffff0000, v10
	s_waitcnt lgkmcnt(3)
	v_mfma_f32_16x16x32_bf16 v[130:133], v[14:17], v[214:217], v[130:133]
	v_lshlrev_b32_e32 v147, 16, v10
	v_mul_f32_e32 v149, v149, v149
	v_fmac_f32_e32 v149, v147, v147
	s_waitcnt lgkmcnt(2)
	v_mfma_f32_16x16x32_bf16 v[134:137], v[14:17], v[218:221], v[134:137]
	ds_read_b128 v[218:221], v174 offset:34880
	ds_read_b128 v[214:217], v175 offset:34880
	v_add_f32_e32 v145, v149, v145
	v_and_b32_e32 v149, 0xffff0000, v11
	s_waitcnt lgkmcnt(3)
	v_mfma_f32_16x16x32_bf16 v[130:133], v[14:17], v[222:225], v[130:133]
	v_lshlrev_b32_e32 v147, 16, v11
	v_mul_f32_e32 v149, v149, v149
	v_fmac_f32_e32 v149, v147, v147
	v_add_f32_e32 v145, v149, v145
	v_and_b32_e32 v149, 0xffff0000, v12
	ds_read_b128 v[210:213], v175 offset:1856
	v_lshlrev_b32_e32 v147, 16, v12
	v_mul_f32_e32 v149, v149, v149
	s_waitcnt lgkmcnt(3)
	v_mfma_f32_16x16x32_bf16 v[134:137], v[10:13], v[226:229], v[134:137]
	v_fmac_f32_e32 v149, v147, v147
	v_add_f32_e32 v145, v149, v145
	v_and_b32_e32 v149, 0xffff0000, v13
	s_waitcnt lgkmcnt(2)
	v_mfma_f32_16x16x32_bf16 v[130:133], v[10:13], v[218:221], v[130:133]
	v_lshlrev_b32_e32 v147, 16, v13
	v_mul_f32_e32 v149, v149, v149
	v_fmac_f32_e32 v149, v147, v147
	s_waitcnt lgkmcnt(0)
	v_mfma_f32_16x16x32_bf16 v[134:137], v[10:13], v[210:213], v[134:137]
	v_add_f32_e32 v145, v149, v145
	v_mfma_f32_16x16x32_bf16 v[130:133], v[10:13], v[214:217], v[130:133]
	s_waitcnt vmcnt(1)
	v_and_b32_e32 v149, 0xffff0000, v6
	ds_read_b128 v[210:213], v174 offset:1920
	ds_read_b128 v[214:217], v174 offset:34944
	ds_read_b128 v[218:221], v175 offset:1920
	ds_read_b128 v[222:225], v175 offset:34944
	ds_read_b128 v[226:229], v174 offset:1984
	v_lshlrev_b32_e32 v147, 16, v6
	v_mul_f32_e32 v149, v149, v149
	s_waitcnt lgkmcnt(4)
	v_mfma_f32_16x16x32_bf16 v[134:137], v[6:9], v[210:213], v[134:137]
	v_fmac_f32_e32 v149, v147, v147
	v_add_f32_e32 v145, v149, v145
	v_and_b32_e32 v149, 0xffff0000, v7
	v_lshlrev_b32_e32 v147, 16, v7
	v_mul_f32_e32 v149, v149, v149
	v_fmac_f32_e32 v149, v147, v147
	s_waitcnt lgkmcnt(2)
	v_mfma_f32_16x16x32_bf16 v[134:137], v[6:9], v[218:221], v[134:137]
	v_add_f32_e32 v145, v149, v145
	v_and_b32_e32 v149, 0xffff0000, v8
	v_lshlrev_b32_e32 v147, 16, v8
	v_mfma_f32_16x16x32_bf16 v[130:133], v[6:9], v[214:217], v[130:133]
	v_mul_f32_e32 v149, v149, v149
	v_fmac_f32_e32 v149, v147, v147
	v_add_f32_e32 v145, v149, v145
	v_and_b32_e32 v149, 0xffff0000, v9
	s_waitcnt lgkmcnt(1)
	v_mfma_f32_16x16x32_bf16 v[222:225], v[6:9], v[222:225], v[130:133]
	v_lshlrev_b32_e32 v147, 16, v9
	ds_read_b128 v[218:221], v174 offset:35008
	ds_read_b128 v[214:217], v175 offset:35008
	s_waitcnt vmcnt(0) lgkmcnt(2)
	v_mfma_f32_16x16x32_bf16 v[130:133], v[2:5], v[226:229], v[134:137]
	ds_read_b128 v[210:213], v175 offset:1984
	s_nop 1
	v_mul_f32_e32 v134, v149, v149
	v_and_b32_e32 v136, 0xffff0000, v2
	v_fmac_f32_e32 v134, v147, v147
	v_lshlrev_b32_e32 v135, 16, v2
	v_mul_f32_e32 v136, v136, v136
	v_add_f32_e32 v134, v134, v145
	v_fmac_f32_e32 v136, v135, v135
	v_add_f32_e32 v134, v136, v134
	v_and_b32_e32 v136, 0xffff0000, v3
	v_lshlrev_b32_e32 v135, 16, v3
	v_mul_f32_e32 v136, v136, v136
	v_fmac_f32_e32 v136, v135, v135
	v_add_f32_e32 v134, v136, v134
	v_and_b32_e32 v136, 0xffff0000, v4
	v_lshlrev_b32_e32 v135, 16, v4
	v_mul_f32_e32 v136, v136, v136
	v_fmac_f32_e32 v136, v135, v135
	v_add_f32_e32 v145, v136, v134
	s_waitcnt lgkmcnt(2)
	v_mfma_f32_16x16x32_bf16 v[134:137], v[2:5], v[218:221], v[222:225]
	v_and_b32_e32 v149, 0xffff0000, v5
	v_lshlrev_b32_e32 v147, 16, v5
	v_mul_f32_e32 v149, v149, v149
	v_fmac_f32_e32 v149, v147, v147
	s_waitcnt lgkmcnt(0)
	v_mfma_f32_16x16x32_bf16 v[130:133], v[2:5], v[210:213], v[130:133]
	v_add_f32_e32 v145, v149, v145
	v_mfma_f32_16x16x32_bf16 v[134:137], v[2:5], v[214:217], v[134:137]
	ds_bpermute_b32 v147, v192, v145
	v_lshlrev_b32_e32 v149, 16, v126
	v_and_b32_e32 v126, 0xffff0000, v126
	s_waitcnt lgkmcnt(0)
	v_add_f32_e32 v145, v145, v147
	ds_bpermute_b32 v147, v193, v145
	s_waitcnt lgkmcnt(0)
	v_add_f32_e32 v145, v145, v147
	v_fmamk_f32 v145, v145, 0x3a800000, v195
	v_mul_f32_e32 v147, 0x4f800000, v145
	v_cmp_gt_f32_e32 vcc, s25, v145
	s_nop 1
	v_cndmask_b32_e32 v145, v145, v147, vcc
	v_sqrt_f32_e32 v147, v145
	s_nop 0
	v_add_u32_e32 v151, -1, v147
	v_add_u32_e32 v153, 1, v147
	v_fma_f32 v155, -v151, v147, v145
	v_fma_f32 v157, -v153, v147, v145
	v_cmp_ge_f32_e64 s[8:9], 0, v155
	s_nop 1
	v_cndmask_b32_e64 v147, v147, v151, s[8:9]
	v_cmp_lt_f32_e64 s[8:9], 0, v157
	s_nop 1
	v_cndmask_b32_e64 v147, v147, v153, s[8:9]
	v_mul_f32_e32 v151, 0x37800000, v147
	v_cndmask_b32_e32 v147, v147, v151, vcc
	v_cmp_class_f32_e32 vcc, v145, v196
	s_nop 1
	v_cndmask_b32_e32 v145, v147, v145, vcc
	v_div_scale_f32 v147, s[8:9], v145, v145, 1.0
	v_rcp_f32_e32 v151, v147
	v_div_scale_f32 v153, vcc, 1.0, v145, 1.0
	v_fma_f32 v155, -v147, v151, 1.0
	v_fmac_f32_e32 v151, v155, v151
	v_mul_f32_e32 v155, v153, v151
	v_fma_f32 v157, -v147, v155, v153
	v_fmac_f32_e32 v155, v157, v151
	v_fma_f32 v147, -v147, v155, v153
	v_div_fmas_f32 v147, v147, v151, v155
	v_div_fixup_f32 v145, v147, v145, 1.0
	v_mul_f32_e32 v147, 0x41800000, v145
	v_mul_f32_e32 v149, v147, v149
	v_mul_f32_e32 v126, v147, v126
	v_cvt_pk_fp8_f32 v210, v149, v126
	v_lshlrev_b32_e32 v151, 16, v127
	v_and_b32_e32 v127, 0xffff0000, v127
	v_mul_f32_e32 v126, v147, v151
	v_mul_f32_e32 v127, v147, v127
	v_cvt_pk_fp8_f32 v210, v126, v127 op_sel:[0,0,1]
	v_lshlrev_b32_e32 v126, 16, v128
	v_and_b32_e32 v127, 0xffff0000, v128
	v_mul_f32_e32 v126, v147, v126
	v_mul_f32_e32 v127, v147, v127
	v_cvt_pk_fp8_f32 v211, v126, v127
	v_lshlrev_b32_e32 v128, 16, v129
	v_and_b32_e32 v127, 0xffff0000, v129
	v_mul_f32_e32 v126, v147, v128
	v_mul_f32_e32 v127, v147, v127
	v_cvt_pk_fp8_f32 v211, v126, v127 op_sel:[0,0,1]
	v_lshl_add_u64 v[126:127], v[142:143], 0, v[168:169]
	global_store_dwordx2 v[126:127], v[210:211], off
	s_nop 0
	v_lshlrev_b32_e32 v128, 16, v122
	v_and_b32_e32 v122, 0xffff0000, v122
	v_mul_f32_e32 v128, v147, v128
	v_mul_f32_e32 v129, v147, v122
	v_cvt_pk_fp8_f32 v122, v128, v129
	v_lshlrev_b32_e32 v149, 16, v123
	v_and_b32_e32 v123, 0xffff0000, v123
	v_mul_f32_e32 v128, v147, v149
	v_mul_f32_e32 v123, v147, v123
	v_cvt_pk_fp8_f32 v122, v128, v123 op_sel:[0,0,1]
	v_lshlrev_b32_e32 v123, 16, v124
	v_mul_f32_e32 v128, v147, v123
	v_and_b32_e32 v123, 0xffff0000, v124
	v_mul_f32_e32 v124, v147, v123
	v_cvt_pk_fp8_f32 v123, v128, v124
	v_lshlrev_b32_e32 v129, 16, v125
	v_and_b32_e32 v125, 0xffff0000, v125
	v_mul_f32_e32 v124, v147, v129
	v_mul_f32_e32 v125, v147, v125
	v_cvt_pk_fp8_f32 v123, v124, v125 op_sel:[0,0,1]
	global_store_dwordx2 v[126:127], v[122:123], off offset:32
	s_nop 0
	v_lshlrev_b32_e32 v122, 16, v118
	v_and_b32_e32 v118, 0xffff0000, v118
	v_mul_f32_e32 v122, v147, v122
	v_mul_f32_e32 v123, v147, v118
	v_cvt_pk_fp8_f32 v118, v122, v123
	v_lshlrev_b32_e32 v124, 16, v119
	v_and_b32_e32 v119, 0xffff0000, v119
	v_mul_f32_e32 v122, v147, v124
	v_mul_f32_e32 v119, v147, v119
	v_cvt_pk_fp8_f32 v118, v122, v119 op_sel:[0,0,1]
	v_lshlrev_b32_e32 v119, 16, v120
	v_mul_f32_e32 v122, v147, v119
	v_and_b32_e32 v119, 0xffff0000, v120
	v_mul_f32_e32 v120, v147, v119
	v_cvt_pk_fp8_f32 v119, v122, v120
	v_lshlrev_b32_e32 v123, 16, v121
	v_and_b32_e32 v121, 0xffff0000, v121
	v_mul_f32_e32 v120, v147, v123
	v_mul_f32_e32 v121, v147, v121
	v_cvt_pk_fp8_f32 v119, v120, v121 op_sel:[0,0,1]
	global_store_dwordx2 v[126:127], v[118:119], off offset:64
	s_nop 0
	v_lshlrev_b32_e32 v118, 16, v114
	v_and_b32_e32 v114, 0xffff0000, v114
	v_mul_f32_e32 v118, v147, v118
	v_mul_f32_e32 v119, v147, v114
	v_cvt_pk_fp8_f32 v114, v118, v119
	v_lshlrev_b32_e32 v120, 16, v115
	v_and_b32_e32 v115, 0xffff0000, v115
	v_mul_f32_e32 v118, v147, v120
	v_mul_f32_e32 v115, v147, v115
	v_cvt_pk_fp8_f32 v114, v118, v115 op_sel:[0,0,1]
	v_lshlrev_b32_e32 v115, 16, v116
	v_mul_f32_e32 v118, v147, v115
	v_and_b32_e32 v115, 0xffff0000, v116
	v_mul_f32_e32 v116, v147, v115
	v_cvt_pk_fp8_f32 v115, v118, v116
	v_lshlrev_b32_e32 v119, 16, v117
	v_and_b32_e32 v117, 0xffff0000, v117
	v_mul_f32_e32 v116, v147, v119
	v_mul_f32_e32 v117, v147, v117
	v_cvt_pk_fp8_f32 v115, v116, v117 op_sel:[0,0,1]
	global_store_dwordx2 v[126:127], v[114:115], off offset:96
	s_nop 0
	v_lshlrev_b32_e32 v114, 16, v110
	v_and_b32_e32 v110, 0xffff0000, v110
	v_mul_f32_e32 v114, v147, v114
	v_mul_f32_e32 v115, v147, v110
	v_cvt_pk_fp8_f32 v110, v114, v115
	v_lshlrev_b32_e32 v116, 16, v111
	v_and_b32_e32 v111, 0xffff0000, v111
	v_mul_f32_e32 v114, v147, v116
	v_mul_f32_e32 v111, v147, v111
	v_cvt_pk_fp8_f32 v110, v114, v111 op_sel:[0,0,1]
	v_lshlrev_b32_e32 v111, 16, v112
	v_mul_f32_e32 v114, v147, v111
	v_and_b32_e32 v111, 0xffff0000, v112
	v_mul_f32_e32 v112, v147, v111
	v_cvt_pk_fp8_f32 v111, v114, v112
	v_lshlrev_b32_e32 v115, 16, v113
	v_and_b32_e32 v113, 0xffff0000, v113
	v_mul_f32_e32 v112, v147, v115
	v_mul_f32_e32 v113, v147, v113
	v_cvt_pk_fp8_f32 v111, v112, v113 op_sel:[0,0,1]
	global_store_dwordx2 v[126:127], v[110:111], off offset:128
	s_nop 0
	v_lshlrev_b32_e32 v110, 16, v106
	v_and_b32_e32 v106, 0xffff0000, v106
	v_mul_f32_e32 v110, v147, v110
	v_mul_f32_e32 v111, v147, v106
	v_cvt_pk_fp8_f32 v106, v110, v111
	v_lshlrev_b32_e32 v112, 16, v107
	v_and_b32_e32 v107, 0xffff0000, v107
	v_mul_f32_e32 v110, v147, v112
	v_mul_f32_e32 v107, v147, v107
	v_cvt_pk_fp8_f32 v106, v110, v107 op_sel:[0,0,1]
	v_lshlrev_b32_e32 v107, 16, v108
	v_mul_f32_e32 v110, v147, v107
	v_and_b32_e32 v107, 0xffff0000, v108
	v_mul_f32_e32 v108, v147, v107
	v_cvt_pk_fp8_f32 v107, v110, v108
	v_lshlrev_b32_e32 v111, 16, v109
	v_and_b32_e32 v109, 0xffff0000, v109
	v_mul_f32_e32 v108, v147, v111
	v_mul_f32_e32 v109, v147, v109
	v_cvt_pk_fp8_f32 v107, v108, v109 op_sel:[0,0,1]
	global_store_dwordx2 v[126:127], v[106:107], off offset:160
	s_nop 0
	v_lshlrev_b32_e32 v106, 16, v102
	v_and_b32_e32 v102, 0xffff0000, v102
	v_mul_f32_e32 v106, v147, v106
	v_mul_f32_e32 v107, v147, v102
	v_cvt_pk_fp8_f32 v102, v106, v107
	v_lshlrev_b32_e32 v108, 16, v103
	v_and_b32_e32 v103, 0xffff0000, v103
	v_mul_f32_e32 v106, v147, v108
	v_mul_f32_e32 v103, v147, v103
	v_cvt_pk_fp8_f32 v102, v106, v103 op_sel:[0,0,1]
	v_lshlrev_b32_e32 v103, 16, v104
	v_mul_f32_e32 v106, v147, v103
	v_and_b32_e32 v103, 0xffff0000, v104
	v_mul_f32_e32 v104, v147, v103
	v_cvt_pk_fp8_f32 v103, v106, v104
	v_lshlrev_b32_e32 v107, 16, v105
	v_and_b32_e32 v105, 0xffff0000, v105
	v_mul_f32_e32 v104, v147, v107
	v_mul_f32_e32 v105, v147, v105
	v_cvt_pk_fp8_f32 v103, v104, v105 op_sel:[0,0,1]
	global_store_dwordx2 v[126:127], v[102:103], off offset:192
	s_nop 0
	v_lshlrev_b32_e32 v102, 16, v98
	v_and_b32_e32 v98, 0xffff0000, v98
	v_mul_f32_e32 v102, v147, v102
	v_mul_f32_e32 v103, v147, v98
	v_cvt_pk_fp8_f32 v98, v102, v103
	v_lshlrev_b32_e32 v104, 16, v99
	v_and_b32_e32 v99, 0xffff0000, v99
	v_mul_f32_e32 v102, v147, v104
	v_mul_f32_e32 v99, v147, v99
	v_cvt_pk_fp8_f32 v98, v102, v99 op_sel:[0,0,1]
	v_lshlrev_b32_e32 v99, 16, v100
	v_mul_f32_e32 v102, v147, v99
	v_and_b32_e32 v99, 0xffff0000, v100
	v_mul_f32_e32 v100, v147, v99
	v_cvt_pk_fp8_f32 v99, v102, v100
	v_lshlrev_b32_e32 v103, 16, v101
	v_and_b32_e32 v101, 0xffff0000, v101
	v_mul_f32_e32 v100, v147, v103
	v_mul_f32_e32 v101, v147, v101
	v_cvt_pk_fp8_f32 v99, v100, v101 op_sel:[0,0,1]
	global_store_dwordx2 v[126:127], v[98:99], off offset:224
	s_nop 0
	v_lshlrev_b32_e32 v98, 16, v94
	v_and_b32_e32 v94, 0xffff0000, v94
	v_mul_f32_e32 v98, v147, v98
	v_mul_f32_e32 v99, v147, v94
	v_cvt_pk_fp8_f32 v94, v98, v99
	v_lshlrev_b32_e32 v100, 16, v95
	v_and_b32_e32 v95, 0xffff0000, v95
	v_mul_f32_e32 v98, v147, v100
	v_mul_f32_e32 v95, v147, v95
	v_cvt_pk_fp8_f32 v94, v98, v95 op_sel:[0,0,1]
	v_lshlrev_b32_e32 v95, 16, v96
	v_mul_f32_e32 v98, v147, v95
	v_and_b32_e32 v95, 0xffff0000, v96
	v_mul_f32_e32 v96, v147, v95
	v_cvt_pk_fp8_f32 v95, v98, v96
	v_lshlrev_b32_e32 v99, 16, v97
	v_and_b32_e32 v97, 0xffff0000, v97
	v_mul_f32_e32 v96, v147, v99
	v_mul_f32_e32 v97, v147, v97
	v_cvt_pk_fp8_f32 v95, v96, v97 op_sel:[0,0,1]
	global_store_dwordx2 v[126:127], v[94:95], off offset:256
	s_nop 0
	v_lshlrev_b32_e32 v94, 16, v90
	v_and_b32_e32 v90, 0xffff0000, v90
	v_mul_f32_e32 v94, v147, v94
	v_mul_f32_e32 v95, v147, v90
	v_cvt_pk_fp8_f32 v90, v94, v95
	v_lshlrev_b32_e32 v96, 16, v91
	v_and_b32_e32 v91, 0xffff0000, v91
	v_mul_f32_e32 v94, v147, v96
	v_mul_f32_e32 v91, v147, v91
	v_cvt_pk_fp8_f32 v90, v94, v91 op_sel:[0,0,1]
	v_lshlrev_b32_e32 v91, 16, v92
	v_mul_f32_e32 v94, v147, v91
	v_and_b32_e32 v91, 0xffff0000, v92
	v_mul_f32_e32 v92, v147, v91
	v_cvt_pk_fp8_f32 v91, v94, v92
	v_lshlrev_b32_e32 v95, 16, v93
	v_and_b32_e32 v93, 0xffff0000, v93
	v_mul_f32_e32 v92, v147, v95
	v_mul_f32_e32 v93, v147, v93
	v_cvt_pk_fp8_f32 v91, v92, v93 op_sel:[0,0,1]
	global_store_dwordx2 v[126:127], v[90:91], off offset:288
	s_nop 0
	v_lshlrev_b32_e32 v90, 16, v86
	v_and_b32_e32 v86, 0xffff0000, v86
	v_mul_f32_e32 v90, v147, v90
	v_mul_f32_e32 v91, v147, v86
	v_cvt_pk_fp8_f32 v86, v90, v91
	v_lshlrev_b32_e32 v92, 16, v87
	v_and_b32_e32 v87, 0xffff0000, v87
	v_mul_f32_e32 v90, v147, v92
	v_mul_f32_e32 v87, v147, v87
	v_cvt_pk_fp8_f32 v86, v90, v87 op_sel:[0,0,1]
	v_lshlrev_b32_e32 v87, 16, v88
	v_mul_f32_e32 v90, v147, v87
	v_and_b32_e32 v87, 0xffff0000, v88
	v_mul_f32_e32 v88, v147, v87
	v_cvt_pk_fp8_f32 v87, v90, v88
	v_lshlrev_b32_e32 v91, 16, v89
	v_and_b32_e32 v89, 0xffff0000, v89
	v_mul_f32_e32 v88, v147, v91
	v_mul_f32_e32 v89, v147, v89
	v_cvt_pk_fp8_f32 v87, v88, v89 op_sel:[0,0,1]
	global_store_dwordx2 v[126:127], v[86:87], off offset:320
	s_nop 0
	v_lshlrev_b32_e32 v86, 16, v82
	v_and_b32_e32 v82, 0xffff0000, v82
	v_mul_f32_e32 v86, v147, v86
	v_mul_f32_e32 v87, v147, v82
	v_cvt_pk_fp8_f32 v82, v86, v87
	v_lshlrev_b32_e32 v88, 16, v83
	v_and_b32_e32 v83, 0xffff0000, v83
	v_mul_f32_e32 v86, v147, v88
	v_mul_f32_e32 v83, v147, v83
	v_cvt_pk_fp8_f32 v82, v86, v83 op_sel:[0,0,1]
	v_lshlrev_b32_e32 v83, 16, v84
	v_mul_f32_e32 v86, v147, v83
	v_and_b32_e32 v83, 0xffff0000, v84
	v_mul_f32_e32 v84, v147, v83
	v_cvt_pk_fp8_f32 v83, v86, v84
	v_lshlrev_b32_e32 v87, 16, v85
	v_and_b32_e32 v85, 0xffff0000, v85
	v_mul_f32_e32 v84, v147, v87
	v_mul_f32_e32 v85, v147, v85
	v_cvt_pk_fp8_f32 v83, v84, v85 op_sel:[0,0,1]
	global_store_dwordx2 v[126:127], v[82:83], off offset:352
	s_nop 0
	v_lshlrev_b32_e32 v82, 16, v78
	v_and_b32_e32 v78, 0xffff0000, v78
	v_mul_f32_e32 v82, v147, v82
	v_mul_f32_e32 v83, v147, v78
	v_cvt_pk_fp8_f32 v78, v82, v83
	v_lshlrev_b32_e32 v84, 16, v79
	v_and_b32_e32 v79, 0xffff0000, v79
	v_mul_f32_e32 v82, v147, v84
	v_mul_f32_e32 v79, v147, v79
	v_cvt_pk_fp8_f32 v78, v82, v79 op_sel:[0,0,1]
	v_lshlrev_b32_e32 v79, 16, v80
	v_mul_f32_e32 v82, v147, v79
	v_and_b32_e32 v79, 0xffff0000, v80
	v_mul_f32_e32 v80, v147, v79
	v_cvt_pk_fp8_f32 v79, v82, v80
	v_lshlrev_b32_e32 v83, 16, v81
	v_and_b32_e32 v81, 0xffff0000, v81
	v_mul_f32_e32 v80, v147, v83
	v_mul_f32_e32 v81, v147, v81
	v_cvt_pk_fp8_f32 v79, v80, v81 op_sel:[0,0,1]
	global_store_dwordx2 v[126:127], v[78:79], off offset:384
	s_nop 0
	v_lshlrev_b32_e32 v78, 16, v74
	v_and_b32_e32 v74, 0xffff0000, v74
	v_mul_f32_e32 v78, v147, v78
	v_mul_f32_e32 v79, v147, v74
	v_cvt_pk_fp8_f32 v74, v78, v79
	v_lshlrev_b32_e32 v80, 16, v75
	v_and_b32_e32 v75, 0xffff0000, v75
	v_mul_f32_e32 v78, v147, v80
	v_mul_f32_e32 v75, v147, v75
	v_cvt_pk_fp8_f32 v74, v78, v75 op_sel:[0,0,1]
	v_lshlrev_b32_e32 v75, 16, v76
	v_mul_f32_e32 v78, v147, v75
	v_and_b32_e32 v75, 0xffff0000, v76
	v_mul_f32_e32 v76, v147, v75
	v_cvt_pk_fp8_f32 v75, v78, v76
	v_lshlrev_b32_e32 v79, 16, v77
	v_and_b32_e32 v77, 0xffff0000, v77
	v_mul_f32_e32 v76, v147, v79
	v_mul_f32_e32 v77, v147, v77
	v_cvt_pk_fp8_f32 v75, v76, v77 op_sel:[0,0,1]
	global_store_dwordx2 v[126:127], v[74:75], off offset:416
	s_nop 0
	v_lshlrev_b32_e32 v74, 16, v70
	v_and_b32_e32 v70, 0xffff0000, v70
	v_mul_f32_e32 v74, v147, v74
	v_mul_f32_e32 v75, v147, v70
	v_cvt_pk_fp8_f32 v70, v74, v75
	v_lshlrev_b32_e32 v76, 16, v71
	v_and_b32_e32 v71, 0xffff0000, v71
	v_mul_f32_e32 v74, v147, v76
	v_mul_f32_e32 v71, v147, v71
	v_cvt_pk_fp8_f32 v70, v74, v71 op_sel:[0,0,1]
	v_lshlrev_b32_e32 v71, 16, v72
	v_mul_f32_e32 v74, v147, v71
	v_and_b32_e32 v71, 0xffff0000, v72
	v_mul_f32_e32 v72, v147, v71
	v_cvt_pk_fp8_f32 v71, v74, v72
	v_lshlrev_b32_e32 v75, 16, v73
	v_and_b32_e32 v73, 0xffff0000, v73
	v_mul_f32_e32 v72, v147, v75
	v_mul_f32_e32 v73, v147, v73
	v_cvt_pk_fp8_f32 v71, v72, v73 op_sel:[0,0,1]
	global_store_dwordx2 v[126:127], v[70:71], off offset:448
	s_nop 0
	v_lshlrev_b32_e32 v70, 16, v66
	v_and_b32_e32 v66, 0xffff0000, v66
	v_mul_f32_e32 v70, v147, v70
	v_mul_f32_e32 v71, v147, v66
	v_cvt_pk_fp8_f32 v66, v70, v71
	v_lshlrev_b32_e32 v72, 16, v67
	v_and_b32_e32 v67, 0xffff0000, v67
	v_mul_f32_e32 v70, v147, v72
	v_mul_f32_e32 v67, v147, v67
	v_cvt_pk_fp8_f32 v66, v70, v67 op_sel:[0,0,1]
	v_lshlrev_b32_e32 v67, 16, v68
	v_mul_f32_e32 v70, v147, v67
	v_and_b32_e32 v67, 0xffff0000, v68
	v_mul_f32_e32 v68, v147, v67
	v_cvt_pk_fp8_f32 v67, v70, v68
	v_lshlrev_b32_e32 v71, 16, v69
	v_and_b32_e32 v69, 0xffff0000, v69
	v_mul_f32_e32 v68, v147, v71
	v_mul_f32_e32 v69, v147, v69
	v_cvt_pk_fp8_f32 v67, v68, v69 op_sel:[0,0,1]
	global_store_dwordx2 v[126:127], v[66:67], off offset:480
	s_nop 0
	v_lshlrev_b32_e32 v66, 16, v62
	v_and_b32_e32 v62, 0xffff0000, v62
	v_mul_f32_e32 v66, v147, v66
	v_mul_f32_e32 v67, v147, v62
	v_cvt_pk_fp8_f32 v62, v66, v67
	v_lshlrev_b32_e32 v68, 16, v63
	v_and_b32_e32 v63, 0xffff0000, v63
	v_mul_f32_e32 v66, v147, v68
	v_mul_f32_e32 v63, v147, v63
	v_cvt_pk_fp8_f32 v62, v66, v63 op_sel:[0,0,1]
	v_lshlrev_b32_e32 v63, 16, v64
	v_mul_f32_e32 v66, v147, v63
	v_and_b32_e32 v63, 0xffff0000, v64
	v_mul_f32_e32 v64, v147, v63
	v_cvt_pk_fp8_f32 v63, v66, v64
	v_lshlrev_b32_e32 v67, 16, v65
	v_and_b32_e32 v65, 0xffff0000, v65
	v_mul_f32_e32 v64, v147, v67
	v_mul_f32_e32 v65, v147, v65
	v_cvt_pk_fp8_f32 v63, v64, v65 op_sel:[0,0,1]
	global_store_dwordx2 v[126:127], v[62:63], off offset:512
	s_nop 0
	v_lshlrev_b32_e32 v62, 16, v58
	v_and_b32_e32 v58, 0xffff0000, v58
	v_mul_f32_e32 v62, v147, v62
	v_mul_f32_e32 v63, v147, v58
	v_cvt_pk_fp8_f32 v58, v62, v63
	v_lshlrev_b32_e32 v64, 16, v59
	v_and_b32_e32 v59, 0xffff0000, v59
	v_mul_f32_e32 v62, v147, v64
	v_mul_f32_e32 v59, v147, v59
	v_cvt_pk_fp8_f32 v58, v62, v59 op_sel:[0,0,1]
	v_lshlrev_b32_e32 v59, 16, v60
	v_mul_f32_e32 v62, v147, v59
	v_and_b32_e32 v59, 0xffff0000, v60
	v_mul_f32_e32 v60, v147, v59
	v_cvt_pk_fp8_f32 v59, v62, v60
	v_lshlrev_b32_e32 v63, 16, v61
	v_and_b32_e32 v61, 0xffff0000, v61
	v_mul_f32_e32 v60, v147, v63
	v_mul_f32_e32 v61, v147, v61
	v_cvt_pk_fp8_f32 v59, v60, v61 op_sel:[0,0,1]
	global_store_dwordx2 v[126:127], v[58:59], off offset:544
	s_nop 0
	v_lshlrev_b32_e32 v58, 16, v54
	v_and_b32_e32 v54, 0xffff0000, v54
	v_mul_f32_e32 v58, v147, v58
	v_mul_f32_e32 v59, v147, v54
	v_cvt_pk_fp8_f32 v54, v58, v59
	v_lshlrev_b32_e32 v60, 16, v55
	v_and_b32_e32 v55, 0xffff0000, v55
	v_mul_f32_e32 v58, v147, v60
	v_mul_f32_e32 v55, v147, v55
	v_cvt_pk_fp8_f32 v54, v58, v55 op_sel:[0,0,1]
	v_lshlrev_b32_e32 v55, 16, v56
	v_mul_f32_e32 v58, v147, v55
	v_and_b32_e32 v55, 0xffff0000, v56
	v_mul_f32_e32 v56, v147, v55
	v_cvt_pk_fp8_f32 v55, v58, v56
	v_lshlrev_b32_e32 v59, 16, v57
	v_and_b32_e32 v57, 0xffff0000, v57
	v_mul_f32_e32 v56, v147, v59
	v_mul_f32_e32 v57, v147, v57
	v_cvt_pk_fp8_f32 v55, v56, v57 op_sel:[0,0,1]
	global_store_dwordx2 v[126:127], v[54:55], off offset:576
	s_nop 0
	v_lshlrev_b32_e32 v54, 16, v50
	v_and_b32_e32 v50, 0xffff0000, v50
	v_mul_f32_e32 v54, v147, v54
	v_mul_f32_e32 v55, v147, v50
	v_cvt_pk_fp8_f32 v50, v54, v55
	v_lshlrev_b32_e32 v56, 16, v51
	v_and_b32_e32 v51, 0xffff0000, v51
	v_mul_f32_e32 v54, v147, v56
	v_mul_f32_e32 v51, v147, v51
	v_cvt_pk_fp8_f32 v50, v54, v51 op_sel:[0,0,1]
	v_lshlrev_b32_e32 v51, 16, v52
	v_mul_f32_e32 v54, v147, v51
	v_and_b32_e32 v51, 0xffff0000, v52
	v_mul_f32_e32 v52, v147, v51
	v_cvt_pk_fp8_f32 v51, v54, v52
	v_lshlrev_b32_e32 v55, 16, v53
	v_and_b32_e32 v53, 0xffff0000, v53
	v_mul_f32_e32 v52, v147, v55
	v_mul_f32_e32 v53, v147, v53
	v_cvt_pk_fp8_f32 v51, v52, v53 op_sel:[0,0,1]
	global_store_dwordx2 v[126:127], v[50:51], off offset:608
	s_nop 0
	v_lshlrev_b32_e32 v50, 16, v46
	v_and_b32_e32 v46, 0xffff0000, v46
	v_mul_f32_e32 v50, v147, v50
	v_mul_f32_e32 v51, v147, v46
	v_cvt_pk_fp8_f32 v46, v50, v51
	v_lshlrev_b32_e32 v52, 16, v47
	v_and_b32_e32 v47, 0xffff0000, v47
	v_mul_f32_e32 v50, v147, v52
	v_mul_f32_e32 v47, v147, v47
	v_cvt_pk_fp8_f32 v46, v50, v47 op_sel:[0,0,1]
	v_lshlrev_b32_e32 v47, 16, v48
	v_mul_f32_e32 v50, v147, v47
	v_and_b32_e32 v47, 0xffff0000, v48
	v_mul_f32_e32 v48, v147, v47
	v_cvt_pk_fp8_f32 v47, v50, v48
	v_lshlrev_b32_e32 v51, 16, v49
	v_and_b32_e32 v49, 0xffff0000, v49
	v_mul_f32_e32 v48, v147, v51
	v_mul_f32_e32 v49, v147, v49
	v_cvt_pk_fp8_f32 v47, v48, v49 op_sel:[0,0,1]
	global_store_dwordx2 v[126:127], v[46:47], off offset:640
	s_nop 0
	v_lshlrev_b32_e32 v46, 16, v42
	v_and_b32_e32 v42, 0xffff0000, v42
	v_mul_f32_e32 v46, v147, v46
	v_mul_f32_e32 v47, v147, v42
	v_cvt_pk_fp8_f32 v42, v46, v47
	v_lshlrev_b32_e32 v48, 16, v43
	v_and_b32_e32 v43, 0xffff0000, v43
	v_mul_f32_e32 v46, v147, v48
	v_mul_f32_e32 v43, v147, v43
	v_cvt_pk_fp8_f32 v42, v46, v43 op_sel:[0,0,1]
	v_lshlrev_b32_e32 v43, 16, v44
	v_mul_f32_e32 v46, v147, v43
	v_and_b32_e32 v43, 0xffff0000, v44
	v_mul_f32_e32 v44, v147, v43
	v_cvt_pk_fp8_f32 v43, v46, v44
	v_lshlrev_b32_e32 v47, 16, v45
	v_and_b32_e32 v45, 0xffff0000, v45
	v_mul_f32_e32 v44, v147, v47
	v_mul_f32_e32 v45, v147, v45
	v_cvt_pk_fp8_f32 v43, v44, v45 op_sel:[0,0,1]
	global_store_dwordx2 v[126:127], v[42:43], off offset:672
	s_nop 0
	v_lshlrev_b32_e32 v42, 16, v38
	v_and_b32_e32 v38, 0xffff0000, v38
	v_mul_f32_e32 v42, v147, v42
	v_mul_f32_e32 v43, v147, v38
	v_cvt_pk_fp8_f32 v38, v42, v43
	v_lshlrev_b32_e32 v44, 16, v39
	v_and_b32_e32 v39, 0xffff0000, v39
	v_mul_f32_e32 v42, v147, v44
	v_mul_f32_e32 v39, v147, v39
	v_cvt_pk_fp8_f32 v38, v42, v39 op_sel:[0,0,1]
	v_lshlrev_b32_e32 v39, 16, v40
	v_mul_f32_e32 v42, v147, v39
	v_and_b32_e32 v39, 0xffff0000, v40
	v_mul_f32_e32 v40, v147, v39
	v_cvt_pk_fp8_f32 v39, v42, v40
	v_lshlrev_b32_e32 v43, 16, v41
	v_and_b32_e32 v41, 0xffff0000, v41
	v_mul_f32_e32 v40, v147, v43
	v_mul_f32_e32 v41, v147, v41
	v_cvt_pk_fp8_f32 v39, v40, v41 op_sel:[0,0,1]
	global_store_dwordx2 v[126:127], v[38:39], off offset:704
	s_nop 0
	v_lshlrev_b32_e32 v38, 16, v34
	v_and_b32_e32 v34, 0xffff0000, v34
	v_mul_f32_e32 v38, v147, v38
	v_mul_f32_e32 v39, v147, v34
	v_cvt_pk_fp8_f32 v34, v38, v39
	v_lshlrev_b32_e32 v40, 16, v35
	v_and_b32_e32 v35, 0xffff0000, v35
	v_mul_f32_e32 v38, v147, v40
	v_mul_f32_e32 v35, v147, v35
	v_cvt_pk_fp8_f32 v34, v38, v35 op_sel:[0,0,1]
	v_lshlrev_b32_e32 v35, 16, v36
	v_mul_f32_e32 v38, v147, v35
	v_and_b32_e32 v35, 0xffff0000, v36
	v_mul_f32_e32 v36, v147, v35
	v_cvt_pk_fp8_f32 v35, v38, v36
	v_lshlrev_b32_e32 v39, 16, v37
	v_and_b32_e32 v37, 0xffff0000, v37
	v_mul_f32_e32 v36, v147, v39
	v_mul_f32_e32 v37, v147, v37
	v_cvt_pk_fp8_f32 v35, v36, v37 op_sel:[0,0,1]
	global_store_dwordx2 v[126:127], v[34:35], off offset:736
	s_nop 0
	v_lshlrev_b32_e32 v34, 16, v30
	v_and_b32_e32 v30, 0xffff0000, v30
	v_mul_f32_e32 v34, v147, v34
	v_mul_f32_e32 v35, v147, v30
	v_cvt_pk_fp8_f32 v30, v34, v35
	v_lshlrev_b32_e32 v36, 16, v31
	v_and_b32_e32 v31, 0xffff0000, v31
	v_mul_f32_e32 v34, v147, v36
	v_mul_f32_e32 v31, v147, v31
	v_cvt_pk_fp8_f32 v30, v34, v31 op_sel:[0,0,1]
	v_lshlrev_b32_e32 v31, 16, v32
	v_mul_f32_e32 v34, v147, v31
	v_and_b32_e32 v31, 0xffff0000, v32
	v_mul_f32_e32 v32, v147, v31
	v_cvt_pk_fp8_f32 v31, v34, v32
	v_lshlrev_b32_e32 v35, 16, v33
	v_and_b32_e32 v33, 0xffff0000, v33
	v_mul_f32_e32 v32, v147, v35
	v_mul_f32_e32 v33, v147, v33
	v_cvt_pk_fp8_f32 v31, v32, v33 op_sel:[0,0,1]
	global_store_dwordx2 v[126:127], v[30:31], off offset:768
	s_nop 0
	v_lshlrev_b32_e32 v30, 16, v26
	v_and_b32_e32 v26, 0xffff0000, v26
	v_mul_f32_e32 v30, v147, v30
	v_mul_f32_e32 v31, v147, v26
	v_cvt_pk_fp8_f32 v26, v30, v31
	v_lshlrev_b32_e32 v32, 16, v27
	v_and_b32_e32 v27, 0xffff0000, v27
	v_mul_f32_e32 v30, v147, v32
	v_mul_f32_e32 v27, v147, v27
	v_cvt_pk_fp8_f32 v26, v30, v27 op_sel:[0,0,1]
	v_lshlrev_b32_e32 v27, 16, v28
	v_mul_f32_e32 v30, v147, v27
	v_and_b32_e32 v27, 0xffff0000, v28
	v_mul_f32_e32 v28, v147, v27
	v_cvt_pk_fp8_f32 v27, v30, v28
	v_lshlrev_b32_e32 v31, 16, v29
	v_and_b32_e32 v29, 0xffff0000, v29
	v_mul_f32_e32 v28, v147, v31
	v_mul_f32_e32 v29, v147, v29
	v_cvt_pk_fp8_f32 v27, v28, v29 op_sel:[0,0,1]
	global_store_dwordx2 v[126:127], v[26:27], off offset:800
	s_nop 0
	v_lshlrev_b32_e32 v26, 16, v22
	v_and_b32_e32 v22, 0xffff0000, v22
	v_mul_f32_e32 v26, v147, v26
	v_mul_f32_e32 v27, v147, v22
	v_cvt_pk_fp8_f32 v22, v26, v27
	v_lshlrev_b32_e32 v28, 16, v23
	v_and_b32_e32 v23, 0xffff0000, v23
	v_mul_f32_e32 v26, v147, v28
	v_mul_f32_e32 v23, v147, v23
	v_cvt_pk_fp8_f32 v22, v26, v23 op_sel:[0,0,1]
	v_lshlrev_b32_e32 v23, 16, v24
	v_mul_f32_e32 v26, v147, v23
	v_and_b32_e32 v23, 0xffff0000, v24
	v_mul_f32_e32 v24, v147, v23
	v_cvt_pk_fp8_f32 v23, v26, v24
	v_lshlrev_b32_e32 v27, 16, v25
	v_and_b32_e32 v25, 0xffff0000, v25
	v_mul_f32_e32 v24, v147, v27
	v_mul_f32_e32 v25, v147, v25
	v_cvt_pk_fp8_f32 v23, v24, v25 op_sel:[0,0,1]
	global_store_dwordx2 v[126:127], v[22:23], off offset:832
	s_nop 0
	v_lshlrev_b32_e32 v22, 16, v18
	v_and_b32_e32 v18, 0xffff0000, v18
	v_mul_f32_e32 v22, v147, v22
	v_mul_f32_e32 v23, v147, v18
	v_cvt_pk_fp8_f32 v18, v22, v23
	v_lshlrev_b32_e32 v24, 16, v19
	v_and_b32_e32 v19, 0xffff0000, v19
	v_mul_f32_e32 v22, v147, v24
	v_mul_f32_e32 v19, v147, v19
	v_cvt_pk_fp8_f32 v18, v22, v19 op_sel:[0,0,1]
	v_lshlrev_b32_e32 v19, 16, v20
	v_mul_f32_e32 v22, v147, v19
	v_and_b32_e32 v19, 0xffff0000, v20
	v_mul_f32_e32 v20, v147, v19
	v_cvt_pk_fp8_f32 v19, v22, v20
	v_lshlrev_b32_e32 v23, 16, v21
	v_and_b32_e32 v21, 0xffff0000, v21
	v_mul_f32_e32 v20, v147, v23
	v_mul_f32_e32 v21, v147, v21
	v_cvt_pk_fp8_f32 v19, v20, v21 op_sel:[0,0,1]
	global_store_dwordx2 v[126:127], v[18:19], off offset:864
	s_nop 0
	v_lshlrev_b32_e32 v18, 16, v14
	v_and_b32_e32 v14, 0xffff0000, v14
	v_mul_f32_e32 v18, v147, v18
	v_mul_f32_e32 v19, v147, v14
	v_cvt_pk_fp8_f32 v14, v18, v19
	v_lshlrev_b32_e32 v20, 16, v15
	v_and_b32_e32 v15, 0xffff0000, v15
	v_mul_f32_e32 v18, v147, v20
	v_mul_f32_e32 v15, v147, v15
	v_cvt_pk_fp8_f32 v14, v18, v15 op_sel:[0,0,1]
	v_lshlrev_b32_e32 v15, 16, v16
	v_mul_f32_e32 v18, v147, v15
	v_and_b32_e32 v15, 0xffff0000, v16
	v_mul_f32_e32 v16, v147, v15
	v_cvt_pk_fp8_f32 v15, v18, v16
	v_lshlrev_b32_e32 v19, 16, v17
	v_and_b32_e32 v17, 0xffff0000, v17
	v_mul_f32_e32 v16, v147, v19
	v_mul_f32_e32 v17, v147, v17
	v_cvt_pk_fp8_f32 v15, v16, v17 op_sel:[0,0,1]
	global_store_dwordx2 v[126:127], v[14:15], off offset:896
	s_nop 0
	v_lshlrev_b32_e32 v14, 16, v10
	v_and_b32_e32 v10, 0xffff0000, v10
	v_mul_f32_e32 v14, v147, v14
	v_mul_f32_e32 v15, v147, v10
	v_cvt_pk_fp8_f32 v10, v14, v15
	v_lshlrev_b32_e32 v16, 16, v11
	v_and_b32_e32 v11, 0xffff0000, v11
	v_mul_f32_e32 v14, v147, v16
	v_mul_f32_e32 v11, v147, v11
	v_cvt_pk_fp8_f32 v10, v14, v11 op_sel:[0,0,1]
	v_lshlrev_b32_e32 v11, 16, v12
	v_mul_f32_e32 v14, v147, v11
	v_and_b32_e32 v11, 0xffff0000, v12
	v_mul_f32_e32 v12, v147, v11
	v_cvt_pk_fp8_f32 v11, v14, v12
	v_lshlrev_b32_e32 v15, 16, v13
	v_and_b32_e32 v13, 0xffff0000, v13
	v_mul_f32_e32 v12, v147, v15
	v_mul_f32_e32 v13, v147, v13
	v_cvt_pk_fp8_f32 v11, v12, v13 op_sel:[0,0,1]
	global_store_dwordx2 v[126:127], v[10:11], off offset:928
	s_nop 0
	v_lshlrev_b32_e32 v10, 16, v6
	v_and_b32_e32 v6, 0xffff0000, v6
	v_mul_f32_e32 v10, v147, v10
	v_mul_f32_e32 v11, v147, v6
	v_cvt_pk_fp8_f32 v6, v10, v11
	v_lshlrev_b32_e32 v12, 16, v7
	v_and_b32_e32 v7, 0xffff0000, v7
	v_mul_f32_e32 v10, v147, v12
	v_mul_f32_e32 v7, v147, v7
	v_cvt_pk_fp8_f32 v6, v10, v7 op_sel:[0,0,1]
	v_lshlrev_b32_e32 v7, 16, v8
	v_mul_f32_e32 v10, v147, v7
	v_and_b32_e32 v7, 0xffff0000, v8
	v_mul_f32_e32 v8, v147, v7
	v_cvt_pk_fp8_f32 v7, v10, v8
	v_lshlrev_b32_e32 v11, 16, v9
	v_and_b32_e32 v9, 0xffff0000, v9
	v_mul_f32_e32 v8, v147, v11
	v_mul_f32_e32 v9, v147, v9
	v_cvt_pk_fp8_f32 v7, v8, v9 op_sel:[0,0,1]
	global_store_dwordx2 v[126:127], v[6:7], off offset:960
	s_nop 0
	v_lshlrev_b32_e32 v6, 16, v2
	v_and_b32_e32 v2, 0xffff0000, v2
	v_mul_f32_e32 v6, v147, v6
	v_mul_f32_e32 v7, v147, v2
	v_cvt_pk_fp8_f32 v2, v6, v7
	v_lshlrev_b32_e32 v8, 16, v3
	v_and_b32_e32 v3, 0xffff0000, v3
	v_mul_f32_e32 v6, v147, v8
	v_mul_f32_e32 v3, v147, v3
	v_cvt_pk_fp8_f32 v2, v6, v3 op_sel:[0,0,1]
	v_lshlrev_b32_e32 v3, 16, v4
	v_mul_f32_e32 v6, v147, v3
	v_and_b32_e32 v3, 0xffff0000, v4
	v_mul_f32_e32 v4, v147, v3
	v_cvt_pk_fp8_f32 v3, v6, v4
	v_lshlrev_b32_e32 v7, 16, v5
	v_and_b32_e32 v5, 0xffff0000, v5
	v_mul_f32_e32 v4, v147, v7
	v_mul_f32_e32 v5, v147, v5
	v_cvt_pk_fp8_f32 v3, v4, v5 op_sel:[0,0,1]
	ds_bpermute_b32 v4, v179, v145
	ds_bpermute_b32 v5, v185, v145
	global_store_dwordx2 v[126:127], v[2:3], off offset:992
	ds_bpermute_b32 v2, v181, v145
	s_waitcnt lgkmcnt(2)
	v_fma_f32 v3, v130, v4, v172
	v_fma_f32 v4, v134, v4, v173
	s_waitcnt lgkmcnt(0)
	ds_write2_b32 v180, v3, v4 offset1:16
	ds_bpermute_b32 v3, v183, v145
	s_waitcnt lgkmcnt(2)
	v_fma_f32 v4, v131, v2, v172
	v_fma_f32 v2, v135, v2, v173
	ds_write2_b32 v182, v4, v2 offset1:16
	s_waitcnt lgkmcnt(1)
	v_fma_f32 v2, v132, v3, v172
	v_fma_f32 v3, v136, v3, v173
	ds_write2_b32 v184, v2, v3 offset1:16
	v_fma_f32 v2, v133, v5, v172
	v_fma_f32 v3, v137, v5, v173
	ds_write2_b32 v186, v2, v3 offset1:16
	s_waitcnt lgkmcnt(0)
	s_and_saveexec_b64 s[20:21], s[6:7]
	s_cbranch_execz .LBB0_437
	v_add_u32_e32 v2, s0, v176
	ds_read2_b32 v[32:33], v2 offset1:1
	ds_read2_b32 v[30:31], v2 offset0:2 offset1:3
	ds_read2_b32 v[28:29], v2 offset0:4 offset1:5
	ds_read2_b32 v[26:27], v2 offset0:6 offset1:7
	ds_read2_b32 v[24:25], v2 offset0:8 offset1:9
	ds_read2_b32 v[22:23], v2 offset0:10 offset1:11
	ds_read2_b32 v[20:21], v2 offset0:12 offset1:13
	ds_read2_b32 v[18:19], v2 offset0:14 offset1:15
	ds_read2_b32 v[16:17], v2 offset0:16 offset1:17
	ds_read2_b32 v[14:15], v2 offset0:18 offset1:19
	ds_read2_b32 v[12:13], v2 offset0:20 offset1:21
	ds_read2_b32 v[10:11], v2 offset0:22 offset1:23
	ds_read2_b32 v[8:9], v2 offset0:24 offset1:25
	ds_read2_b32 v[6:7], v2 offset0:26 offset1:27
	ds_read2_b32 v[4:5], v2 offset0:28 offset1:29
	ds_read2_b32 v[2:3], v2 offset0:30 offset1:31
	s_waitcnt lgkmcnt(14)
	v_cmp_gt_f32_e32 vcc, v33, v32
	s_nop 1
	v_cndmask_b32_e32 v35, v32, v33, vcc
	v_cndmask_b32_e64 v34, 0, 1, vcc
	v_cmp_gt_f32_e32 vcc, v30, v35
	s_nop 1
	v_cndmask_b32_e32 v35, v35, v30, vcc
	v_cndmask_b32_e64 v34, v34, 2, vcc
	v_cmp_gt_f32_e32 vcc, v31, v35
	s_nop 1
	v_cndmask_b32_e32 v35, v35, v31, vcc
	v_cndmask_b32_e64 v34, v34, 3, vcc
	s_waitcnt lgkmcnt(13)
	v_cmp_gt_f32_e32 vcc, v28, v35
	s_nop 1
	v_cndmask_b32_e32 v35, v35, v28, vcc
	v_cndmask_b32_e64 v34, v34, 4, vcc
	v_cmp_gt_f32_e32 vcc, v29, v35
	s_nop 1
	v_cndmask_b32_e32 v35, v35, v29, vcc
	v_cndmask_b32_e64 v34, v34, 5, vcc
	s_waitcnt lgkmcnt(12)
	v_cmp_gt_f32_e32 vcc, v26, v35
	s_nop 1
	v_cndmask_b32_e32 v35, v35, v26, vcc
	v_cndmask_b32_e64 v34, v34, 6, vcc
	v_cmp_gt_f32_e32 vcc, v27, v35
	s_nop 1
	v_cndmask_b32_e32 v35, v35, v27, vcc
	v_cndmask_b32_e64 v34, v34, 7, vcc
	s_waitcnt lgkmcnt(11)
	v_cmp_gt_f32_e32 vcc, v24, v35
	s_nop 1
	v_cndmask_b32_e32 v35, v35, v24, vcc
	v_cndmask_b32_e64 v34, v34, 8, vcc
	v_cmp_gt_f32_e32 vcc, v25, v35
	s_nop 1
	v_cndmask_b32_e32 v35, v35, v25, vcc
	v_cndmask_b32_e64 v34, v34, 9, vcc
	s_waitcnt lgkmcnt(10)
	v_cmp_gt_f32_e32 vcc, v22, v35
	s_nop 1
	v_cndmask_b32_e32 v35, v35, v22, vcc
	v_cndmask_b32_e64 v34, v34, 10, vcc
	v_cmp_gt_f32_e32 vcc, v23, v35
	s_nop 1
	v_cndmask_b32_e32 v35, v35, v23, vcc
	v_cndmask_b32_e64 v34, v34, 11, vcc
	s_waitcnt lgkmcnt(9)
	v_cmp_gt_f32_e32 vcc, v20, v35
	s_nop 1
	v_cndmask_b32_e32 v35, v35, v20, vcc
	v_cndmask_b32_e64 v34, v34, 12, vcc
	v_cmp_gt_f32_e32 vcc, v21, v35
	s_nop 1
	v_cndmask_b32_e32 v35, v35, v21, vcc
	v_cndmask_b32_e64 v34, v34, 13, vcc
	s_waitcnt lgkmcnt(8)
	v_cmp_gt_f32_e32 vcc, v18, v35
	s_nop 1
	v_cndmask_b32_e32 v35, v35, v18, vcc
	v_cndmask_b32_e64 v34, v34, 14, vcc
	v_cmp_gt_f32_e32 vcc, v19, v35
	s_nop 1
	v_cndmask_b32_e32 v35, v35, v19, vcc
	v_cndmask_b32_e64 v34, v34, 15, vcc
	s_waitcnt lgkmcnt(7)
	v_cmp_gt_f32_e32 vcc, v16, v35
	s_nop 1
	v_cndmask_b32_e32 v35, v35, v16, vcc
	v_cndmask_b32_e64 v34, v34, 16, vcc
	v_cmp_gt_f32_e32 vcc, v17, v35
	s_nop 1
	v_cndmask_b32_e32 v35, v35, v17, vcc
	v_cndmask_b32_e64 v34, v34, 17, vcc
	s_waitcnt lgkmcnt(6)
	v_cmp_gt_f32_e32 vcc, v14, v35
	s_nop 1
	v_cndmask_b32_e32 v35, v35, v14, vcc
	v_cndmask_b32_e64 v34, v34, 18, vcc
	v_cmp_gt_f32_e32 vcc, v15, v35
	s_nop 1
	v_cndmask_b32_e32 v35, v35, v15, vcc
	v_cndmask_b32_e64 v34, v34, 19, vcc
	s_waitcnt lgkmcnt(5)
	v_cmp_gt_f32_e32 vcc, v12, v35
	s_nop 1
	v_cndmask_b32_e32 v35, v35, v12, vcc
	v_cndmask_b32_e64 v34, v34, 20, vcc
	v_cmp_gt_f32_e32 vcc, v13, v35
	s_nop 1
	v_cndmask_b32_e32 v35, v35, v13, vcc
	v_cndmask_b32_e64 v34, v34, 21, vcc
	s_waitcnt lgkmcnt(4)
	v_cmp_gt_f32_e32 vcc, v10, v35
	s_nop 1
	v_cndmask_b32_e32 v35, v35, v10, vcc
	v_cndmask_b32_e64 v34, v34, 22, vcc
	v_cmp_gt_f32_e32 vcc, v11, v35
	s_nop 1
	v_cndmask_b32_e32 v35, v35, v11, vcc
	v_cndmask_b32_e64 v34, v34, 23, vcc
	s_waitcnt lgkmcnt(3)
	v_cmp_gt_f32_e32 vcc, v8, v35
	s_nop 1
	v_cndmask_b32_e32 v35, v35, v8, vcc
	v_cndmask_b32_e64 v34, v34, 24, vcc
	v_cmp_gt_f32_e32 vcc, v9, v35
	s_nop 1
	v_cndmask_b32_e32 v35, v35, v9, vcc
	v_cndmask_b32_e64 v34, v34, 25, vcc
	s_waitcnt lgkmcnt(2)
	v_cmp_gt_f32_e32 vcc, v6, v35
	s_nop 1
	v_cndmask_b32_e32 v35, v35, v6, vcc
	v_cndmask_b32_e64 v34, v34, 26, vcc
	v_cmp_gt_f32_e32 vcc, v7, v35
	s_nop 1
	v_cndmask_b32_e32 v35, v35, v7, vcc
	v_cndmask_b32_e64 v34, v34, 27, vcc
	s_waitcnt lgkmcnt(1)
	v_cmp_gt_f32_e32 vcc, v4, v35
	s_nop 1
	v_cndmask_b32_e32 v35, v35, v4, vcc
	v_cndmask_b32_e64 v34, v34, 28, vcc
	v_cmp_gt_f32_e32 vcc, v5, v35
	s_nop 1
	v_cndmask_b32_e32 v35, v35, v5, vcc
	v_cndmask_b32_e64 v34, v34, 29, vcc
	s_waitcnt lgkmcnt(0)
	v_cmp_gt_f32_e32 vcc, v2, v35
	s_nop 1
	v_cndmask_b32_e32 v35, v35, v2, vcc
	v_cndmask_b32_e64 v34, v34, 30, vcc
	v_cmp_gt_f32_e32 vcc, v3, v35
	s_nop 1
	v_cndmask_b32_e64 v146, v34, 31, vcc
	v_cndmask_b32_e32 v34, v35, v3, vcc
	v_cmp_eq_u32_e32 vcc, 0, v146
	v_lshlrev_b32_e64 v36, v146, 1
	v_and_b32_e32 v38, 2, v36
	v_cndmask_b32_e32 v37, v32, v198, vcc
	v_cmp_gt_f32_e64 s[8:9], v33, v37
	v_cndmask_b32_e64 v35, 0, -1, vcc
	s_or_b64 vcc, vcc, s[8:9]
	v_cndmask_b32_e64 v39, 0, 1, vcc
	v_cndmask_b32_e32 v40, v32, v33, vcc
	v_cmp_eq_u32_e32 vcc, 0, v38
	v_and_b32_e32 v38, 4, v36
	s_nop 0
	v_cndmask_b32_e32 v37, v37, v40, vcc
	v_cndmask_b32_e32 v35, v35, v39, vcc
	v_cmp_eq_u32_e32 vcc, 0, v38
	v_cmp_gt_f32_e64 s[8:9], v30, v37
	s_and_b64 vcc, vcc, s[8:9]
	v_cndmask_b32_e64 v35, v35, 2, vcc
	v_cndmask_b32_e32 v37, v37, v30, vcc
	v_and_b32_e32 v38, 8, v36
	v_cmp_gt_i32_e64 s[8:9], 0, v35
	v_cmp_gt_f32_e64 s[10:11], v31, v37
	v_cmp_eq_u32_e32 vcc, 0, v38
	s_or_b64 s[8:9], s[8:9], s[10:11]
	s_and_b64 vcc, vcc, s[8:9]
	v_cndmask_b32_e64 v35, v35, 3, vcc
	v_cndmask_b32_e32 v37, v37, v31, vcc
	v_and_b32_e32 v38, 16, v36
	v_cmp_gt_i32_e64 s[8:9], 0, v35
	v_cmp_gt_f32_e64 s[10:11], v28, v37
	v_cmp_eq_u32_e32 vcc, 0, v38
	s_or_b64 s[8:9], s[8:9], s[10:11]
	s_and_b64 vcc, vcc, s[8:9]
	v_cndmask_b32_e64 v35, v35, 4, vcc
	v_cndmask_b32_e32 v37, v37, v28, vcc
	v_and_b32_e32 v38, 32, v36
	v_cmp_gt_i32_e64 s[8:9], 0, v35
	v_cmp_gt_f32_e64 s[10:11], v29, v37
	v_cmp_eq_u32_e32 vcc, 0, v38
	s_or_b64 s[8:9], s[8:9], s[10:11]
	s_and_b64 vcc, vcc, s[8:9]
	v_cndmask_b32_e64 v35, v35, 5, vcc
	v_cndmask_b32_e32 v37, v37, v29, vcc
	v_and_b32_e32 v38, 64, v36
	v_cmp_gt_i32_e64 s[8:9], 0, v35
	v_cmp_gt_f32_e64 s[10:11], v26, v37
	v_cmp_eq_u32_e32 vcc, 0, v38
	s_or_b64 s[8:9], s[8:9], s[10:11]
	s_and_b64 vcc, vcc, s[8:9]
	v_cndmask_b32_e64 v35, v35, 6, vcc
	v_cndmask_b32_e32 v37, v37, v26, vcc
	v_and_b32_e32 v38, 0x80, v36
	v_cmp_gt_i32_e64 s[8:9], 0, v35
	v_cmp_gt_f32_e64 s[10:11], v27, v37
	v_cmp_eq_u32_e32 vcc, 0, v38
	s_or_b64 s[8:9], s[8:9], s[10:11]
	s_and_b64 vcc, vcc, s[8:9]
	v_cndmask_b32_e64 v35, v35, 7, vcc
	v_cndmask_b32_e32 v37, v37, v27, vcc
	v_and_b32_e32 v38, 0x100, v36
	v_cmp_gt_i32_e64 s[8:9], 0, v35
	v_cmp_gt_f32_e64 s[10:11], v24, v37
	v_cmp_eq_u32_e32 vcc, 0, v38
	s_or_b64 s[8:9], s[8:9], s[10:11]
	s_and_b64 vcc, vcc, s[8:9]
	v_cndmask_b32_e64 v35, v35, 8, vcc
	v_cndmask_b32_e32 v37, v37, v24, vcc
	v_and_b32_e32 v38, 0x200, v36
	v_cmp_gt_i32_e64 s[8:9], 0, v35
	v_cmp_gt_f32_e64 s[10:11], v25, v37
	v_cmp_eq_u32_e32 vcc, 0, v38
	s_or_b64 s[8:9], s[8:9], s[10:11]
	s_and_b64 vcc, vcc, s[8:9]
	v_cndmask_b32_e64 v35, v35, 9, vcc
	v_cndmask_b32_e32 v37, v37, v25, vcc
	v_and_b32_e32 v38, 0x400, v36
	v_cmp_gt_i32_e64 s[8:9], 0, v35
	v_cmp_gt_f32_e64 s[10:11], v22, v37
	v_cmp_eq_u32_e32 vcc, 0, v38
	s_or_b64 s[8:9], s[8:9], s[10:11]
	s_and_b64 vcc, vcc, s[8:9]
	v_cndmask_b32_e64 v35, v35, 10, vcc
	v_cndmask_b32_e32 v37, v37, v22, vcc
	v_and_b32_e32 v38, 0x800, v36
	v_cmp_gt_i32_e64 s[8:9], 0, v35
	v_cmp_gt_f32_e64 s[10:11], v23, v37
	v_cmp_eq_u32_e32 vcc, 0, v38
	s_or_b64 s[8:9], s[8:9], s[10:11]
	s_and_b64 vcc, vcc, s[8:9]
	v_cndmask_b32_e64 v35, v35, 11, vcc
	v_cndmask_b32_e32 v37, v37, v23, vcc
	v_and_b32_e32 v38, 0x1000, v36
	v_cmp_gt_i32_e64 s[8:9], 0, v35
	v_cmp_gt_f32_e64 s[10:11], v20, v37
	v_cmp_eq_u32_e32 vcc, 0, v38
	s_or_b64 s[8:9], s[8:9], s[10:11]
	s_and_b64 vcc, vcc, s[8:9]
	v_cndmask_b32_e64 v35, v35, 12, vcc
	v_cndmask_b32_e32 v37, v37, v20, vcc
	v_and_b32_e32 v38, 0x2000, v36
	v_cmp_gt_i32_e64 s[8:9], 0, v35
	v_cmp_gt_f32_e64 s[10:11], v21, v37
	v_cmp_eq_u32_e32 vcc, 0, v38
	s_or_b64 s[8:9], s[8:9], s[10:11]
	s_and_b64 vcc, vcc, s[8:9]
	v_cndmask_b32_e64 v35, v35, 13, vcc
	v_cndmask_b32_e32 v37, v37, v21, vcc
	v_and_b32_e32 v38, 0x4000, v36
	v_cmp_gt_i32_e64 s[8:9], 0, v35
	v_cmp_gt_f32_e64 s[10:11], v18, v37
	v_cmp_eq_u32_e32 vcc, 0, v38
	s_or_b64 s[8:9], s[8:9], s[10:11]
	s_and_b64 vcc, vcc, s[8:9]
	v_cndmask_b32_e64 v35, v35, 14, vcc
	v_cndmask_b32_e32 v37, v37, v18, vcc
	v_and_b32_e32 v38, 0x8000, v36
	v_cmp_gt_i32_e64 s[8:9], 0, v35
	v_cmp_gt_f32_e64 s[10:11], v19, v37
	v_cmp_eq_u32_e32 vcc, 0, v38
	s_or_b64 s[8:9], s[8:9], s[10:11]
	s_and_b64 vcc, vcc, s[8:9]
	v_cndmask_b32_e64 v35, v35, 15, vcc
	v_cndmask_b32_e32 v37, v37, v19, vcc
	v_and_b32_e32 v38, 0x10000, v36
	v_cmp_gt_i32_e64 s[8:9], 0, v35
	v_cmp_gt_f32_e64 s[10:11], v16, v37
	v_cmp_eq_u32_e32 vcc, 0, v38
	s_or_b64 s[8:9], s[8:9], s[10:11]
	s_and_b64 vcc, vcc, s[8:9]
	v_cndmask_b32_e64 v35, v35, 16, vcc
	v_cndmask_b32_e32 v37, v37, v16, vcc
	v_and_b32_e32 v38, 0x20000, v36
	v_cmp_gt_i32_e64 s[8:9], 0, v35
	v_cmp_gt_f32_e64 s[10:11], v17, v37
	v_cmp_eq_u32_e32 vcc, 0, v38
	s_or_b64 s[8:9], s[8:9], s[10:11]
	s_and_b64 vcc, vcc, s[8:9]
	v_cndmask_b32_e64 v35, v35, 17, vcc
	v_cndmask_b32_e32 v37, v37, v17, vcc
	v_and_b32_e32 v38, 0x40000, v36
	v_cmp_gt_i32_e64 s[8:9], 0, v35
	v_cmp_gt_f32_e64 s[10:11], v14, v37
	v_cmp_eq_u32_e32 vcc, 0, v38
	s_or_b64 s[8:9], s[8:9], s[10:11]
	s_and_b64 vcc, vcc, s[8:9]
	v_cndmask_b32_e64 v35, v35, 18, vcc
	v_cndmask_b32_e32 v37, v37, v14, vcc
	v_and_b32_e32 v38, 0x80000, v36
	v_cmp_gt_i32_e64 s[8:9], 0, v35
	v_cmp_gt_f32_e64 s[10:11], v15, v37
	v_cmp_eq_u32_e32 vcc, 0, v38
	s_or_b64 s[8:9], s[8:9], s[10:11]
	s_and_b64 vcc, vcc, s[8:9]
	v_cndmask_b32_e64 v35, v35, 19, vcc
	v_cndmask_b32_e32 v37, v37, v15, vcc
	v_and_b32_e32 v38, 0x100000, v36
	v_cmp_gt_i32_e64 s[8:9], 0, v35
	v_cmp_gt_f32_e64 s[10:11], v12, v37
	v_cmp_eq_u32_e32 vcc, 0, v38
	s_or_b64 s[8:9], s[8:9], s[10:11]
	s_and_b64 vcc, vcc, s[8:9]
	v_cndmask_b32_e64 v35, v35, 20, vcc
	v_cndmask_b32_e32 v37, v37, v12, vcc
	v_and_b32_e32 v38, 0x200000, v36
	v_cmp_gt_i32_e64 s[8:9], 0, v35
	v_cmp_gt_f32_e64 s[10:11], v13, v37
	v_cmp_eq_u32_e32 vcc, 0, v38
	s_or_b64 s[8:9], s[8:9], s[10:11]
	s_and_b64 vcc, vcc, s[8:9]
	v_cndmask_b32_e64 v35, v35, 21, vcc
	v_cndmask_b32_e32 v37, v37, v13, vcc
	v_and_b32_e32 v38, 0x400000, v36
	v_cmp_gt_i32_e64 s[8:9], 0, v35
	v_cmp_gt_f32_e64 s[10:11], v10, v37
	v_cmp_eq_u32_e32 vcc, 0, v38
	s_or_b64 s[8:9], s[8:9], s[10:11]
	s_and_b64 vcc, vcc, s[8:9]
	v_cndmask_b32_e64 v35, v35, 22, vcc
	v_cndmask_b32_e32 v37, v37, v10, vcc
	v_and_b32_e32 v38, 0x800000, v36
	v_cmp_gt_i32_e64 s[8:9], 0, v35
	v_cmp_gt_f32_e64 s[10:11], v11, v37
	v_cmp_eq_u32_e32 vcc, 0, v38
	s_or_b64 s[8:9], s[8:9], s[10:11]
	s_and_b64 vcc, vcc, s[8:9]
	v_cndmask_b32_e64 v35, v35, 23, vcc
	v_cndmask_b32_e32 v37, v37, v11, vcc
	v_and_b32_e32 v38, 0x1000000, v36
	v_cmp_gt_i32_e64 s[8:9], 0, v35
	v_cmp_gt_f32_e64 s[10:11], v8, v37
	v_cmp_eq_u32_e32 vcc, 0, v38
	s_or_b64 s[8:9], s[8:9], s[10:11]
	s_and_b64 vcc, vcc, s[8:9]
	v_cndmask_b32_e64 v35, v35, 24, vcc
	v_cndmask_b32_e32 v37, v37, v8, vcc
	v_and_b32_e32 v38, 0x2000000, v36
	v_cmp_gt_i32_e64 s[8:9], 0, v35
	v_cmp_gt_f32_e64 s[10:11], v9, v37
	v_cmp_eq_u32_e32 vcc, 0, v38
	s_or_b64 s[8:9], s[8:9], s[10:11]
	s_and_b64 vcc, vcc, s[8:9]
	v_cndmask_b32_e64 v35, v35, 25, vcc
	v_cndmask_b32_e32 v37, v37, v9, vcc
	v_and_b32_e32 v38, 0x4000000, v36
	v_cmp_gt_i32_e64 s[8:9], 0, v35
	v_cmp_gt_f32_e64 s[10:11], v6, v37
	v_cmp_eq_u32_e32 vcc, 0, v38
	s_or_b64 s[8:9], s[8:9], s[10:11]
	s_and_b64 vcc, vcc, s[8:9]
	v_cndmask_b32_e64 v35, v35, 26, vcc
	v_cndmask_b32_e32 v37, v37, v6, vcc
	v_and_b32_e32 v38, 0x8000000, v36
	v_cmp_gt_i32_e64 s[8:9], 0, v35
	v_cmp_gt_f32_e64 s[10:11], v7, v37
	v_cmp_eq_u32_e32 vcc, 0, v38
	s_or_b64 s[8:9], s[8:9], s[10:11]
	s_and_b64 vcc, vcc, s[8:9]
	v_cndmask_b32_e64 v35, v35, 27, vcc
	v_cndmask_b32_e32 v37, v37, v7, vcc
	v_and_b32_e32 v38, 0x10000000, v36
	v_cmp_gt_i32_e64 s[8:9], 0, v35
	v_cmp_gt_f32_e64 s[10:11], v4, v37
	v_cmp_eq_u32_e32 vcc, 0, v38
	s_or_b64 s[8:9], s[8:9], s[10:11]
	s_and_b64 vcc, vcc, s[8:9]
	v_cndmask_b32_e64 v35, v35, 28, vcc
	v_cndmask_b32_e32 v37, v37, v4, vcc
	v_and_b32_e32 v38, 0x20000000, v36
	v_cmp_gt_i32_e64 s[8:9], 0, v35
	v_cmp_gt_f32_e64 s[10:11], v5, v37
	v_cmp_eq_u32_e32 vcc, 0, v38
	s_or_b64 s[8:9], s[8:9], s[10:11]
	s_and_b64 vcc, vcc, s[8:9]
	v_cndmask_b32_e64 v35, v35, 29, vcc
	v_cndmask_b32_e32 v37, v37, v5, vcc
	v_and_b32_e32 v38, 2.0, v36
	v_cmp_gt_i32_e64 s[8:9], 0, v35
	v_cmp_gt_f32_e64 s[10:11], v2, v37
	v_cmp_eq_u32_e32 vcc, 0, v38
	s_or_b64 s[8:9], s[8:9], s[10:11]
	s_and_b64 vcc, vcc, s[8:9]
	v_cndmask_b32_e64 v35, v35, 30, vcc
	v_cndmask_b32_e32 v37, v37, v2, vcc
	v_cmp_gt_i32_e32 vcc, 0, v35
	v_cmp_gt_f32_e64 s[8:9], v3, v37
	s_or_b64 vcc, vcc, s[8:9]
	v_cndmask_b32_e64 v38, v35, 31, vcc
	v_cndmask_b32_e32 v39, v37, v3, vcc
	v_cmp_eq_u32_e32 vcc, 31, v146
	s_nop 1
	v_cndmask_b32_e32 v150, v38, v35, vcc
	v_lshl_or_b32 v36, 1, v150, v36
	v_cndmask_b32_e32 v35, v39, v37, vcc
	v_and_b32_e32 v37, 1, v36
	v_cmp_eq_u32_e32 vcc, 1, v37
	v_and_b32_e32 v39, 2, v36
	v_bfe_i32 v38, v36, 0, 1
	v_cndmask_b32_e32 v37, v32, v198, vcc
	v_cmp_gt_f32_e64 s[8:9], v33, v37
	s_or_b64 vcc, vcc, s[8:9]
	v_cndmask_b32_e64 v40, 0, 1, vcc
	v_cndmask_b32_e32 v41, v32, v33, vcc
	v_cmp_eq_u32_e32 vcc, 0, v39
	v_and_b32_e32 v39, 4, v36
	s_nop 0
	v_cndmask_b32_e32 v38, v38, v40, vcc
	v_cndmask_b32_e32 v37, v37, v41, vcc
	v_cmp_eq_u32_e32 vcc, 0, v39
	v_and_b32_e32 v39, 3, v36
	v_cmp_eq_u32_e64 s[8:9], 3, v39
	v_cmp_gt_f32_e64 s[10:11], v30, v37
	s_or_b64 s[8:9], s[8:9], s[10:11]
	s_and_b64 vcc, vcc, s[8:9]
	v_cndmask_b32_e64 v38, v38, 2, vcc
	v_cndmask_b32_e32 v37, v37, v30, vcc
	v_and_b32_e32 v39, 8, v36
	v_cmp_gt_i32_e64 s[8:9], 0, v38
	v_cmp_gt_f32_e64 s[10:11], v31, v37
	v_cmp_eq_u32_e32 vcc, 0, v39
	s_or_b64 s[8:9], s[8:9], s[10:11]
	s_and_b64 vcc, vcc, s[8:9]
	v_cndmask_b32_e64 v38, v38, 3, vcc
	v_cndmask_b32_e32 v37, v37, v31, vcc
	v_and_b32_e32 v39, 16, v36
	v_cmp_gt_i32_e64 s[8:9], 0, v38
	v_cmp_gt_f32_e64 s[10:11], v28, v37
	v_cmp_eq_u32_e32 vcc, 0, v39
	s_or_b64 s[8:9], s[8:9], s[10:11]
	s_and_b64 vcc, vcc, s[8:9]
	v_cndmask_b32_e64 v38, v38, 4, vcc
	v_cndmask_b32_e32 v37, v37, v28, vcc
	v_and_b32_e32 v39, 32, v36
	v_cmp_gt_i32_e64 s[8:9], 0, v38
	v_cmp_gt_f32_e64 s[10:11], v29, v37
	v_cmp_eq_u32_e32 vcc, 0, v39
	s_or_b64 s[8:9], s[8:9], s[10:11]
	s_and_b64 vcc, vcc, s[8:9]
	v_cndmask_b32_e64 v38, v38, 5, vcc
	v_cndmask_b32_e32 v37, v37, v29, vcc
	v_and_b32_e32 v39, 64, v36
	v_cmp_gt_i32_e64 s[8:9], 0, v38
	v_cmp_gt_f32_e64 s[10:11], v26, v37
	v_cmp_eq_u32_e32 vcc, 0, v39
	s_or_b64 s[8:9], s[8:9], s[10:11]
	s_and_b64 vcc, vcc, s[8:9]
	v_cndmask_b32_e64 v38, v38, 6, vcc
	v_cndmask_b32_e32 v37, v37, v26, vcc
	v_and_b32_e32 v39, 0x80, v36
	v_cmp_gt_i32_e64 s[8:9], 0, v38
	v_cmp_gt_f32_e64 s[10:11], v27, v37
	v_cmp_eq_u32_e32 vcc, 0, v39
	s_or_b64 s[8:9], s[8:9], s[10:11]
	s_and_b64 vcc, vcc, s[8:9]
	v_cndmask_b32_e64 v38, v38, 7, vcc
	v_cndmask_b32_e32 v37, v37, v27, vcc
	v_and_b32_e32 v39, 0x100, v36
	v_cmp_gt_i32_e64 s[8:9], 0, v38
	v_cmp_gt_f32_e64 s[10:11], v24, v37
	v_cmp_eq_u32_e32 vcc, 0, v39
	s_or_b64 s[8:9], s[8:9], s[10:11]
	s_and_b64 vcc, vcc, s[8:9]
	v_cndmask_b32_e64 v38, v38, 8, vcc
	v_cndmask_b32_e32 v37, v37, v24, vcc
	v_and_b32_e32 v39, 0x200, v36
	v_cmp_gt_i32_e64 s[8:9], 0, v38
	v_cmp_gt_f32_e64 s[10:11], v25, v37
	v_cmp_eq_u32_e32 vcc, 0, v39
	s_or_b64 s[8:9], s[8:9], s[10:11]
	s_and_b64 vcc, vcc, s[8:9]
	v_cndmask_b32_e64 v38, v38, 9, vcc
	v_cndmask_b32_e32 v37, v37, v25, vcc
	v_and_b32_e32 v39, 0x400, v36
	v_cmp_gt_i32_e64 s[8:9], 0, v38
	v_cmp_gt_f32_e64 s[10:11], v22, v37
	v_cmp_eq_u32_e32 vcc, 0, v39
	s_or_b64 s[8:9], s[8:9], s[10:11]
	s_and_b64 vcc, vcc, s[8:9]
	v_cndmask_b32_e64 v38, v38, 10, vcc
	v_cndmask_b32_e32 v37, v37, v22, vcc
	v_and_b32_e32 v39, 0x800, v36
	v_cmp_gt_i32_e64 s[8:9], 0, v38
	v_cmp_gt_f32_e64 s[10:11], v23, v37
	v_cmp_eq_u32_e32 vcc, 0, v39
	s_or_b64 s[8:9], s[8:9], s[10:11]
	s_and_b64 vcc, vcc, s[8:9]
	v_cndmask_b32_e64 v38, v38, 11, vcc
	v_cndmask_b32_e32 v37, v37, v23, vcc
	v_and_b32_e32 v39, 0x1000, v36
	v_cmp_gt_i32_e64 s[8:9], 0, v38
	v_cmp_gt_f32_e64 s[10:11], v20, v37
	v_cmp_eq_u32_e32 vcc, 0, v39
	s_or_b64 s[8:9], s[8:9], s[10:11]
	s_and_b64 vcc, vcc, s[8:9]
	v_cndmask_b32_e64 v38, v38, 12, vcc
	v_cndmask_b32_e32 v37, v37, v20, vcc
	v_and_b32_e32 v39, 0x2000, v36
	v_cmp_gt_i32_e64 s[8:9], 0, v38
	v_cmp_gt_f32_e64 s[10:11], v21, v37
	v_cmp_eq_u32_e32 vcc, 0, v39
	s_or_b64 s[8:9], s[8:9], s[10:11]
	s_and_b64 vcc, vcc, s[8:9]
	v_cndmask_b32_e64 v38, v38, 13, vcc
	v_cndmask_b32_e32 v37, v37, v21, vcc
	v_and_b32_e32 v39, 0x4000, v36
	v_cmp_gt_i32_e64 s[8:9], 0, v38
	v_cmp_gt_f32_e64 s[10:11], v18, v37
	v_cmp_eq_u32_e32 vcc, 0, v39
	s_or_b64 s[8:9], s[8:9], s[10:11]
	s_and_b64 vcc, vcc, s[8:9]
	v_cndmask_b32_e64 v38, v38, 14, vcc
	v_cndmask_b32_e32 v37, v37, v18, vcc
	v_and_b32_e32 v39, 0x8000, v36
	v_cmp_gt_i32_e64 s[8:9], 0, v38
	v_cmp_gt_f32_e64 s[10:11], v19, v37
	v_cmp_eq_u32_e32 vcc, 0, v39
	s_or_b64 s[8:9], s[8:9], s[10:11]
	s_and_b64 vcc, vcc, s[8:9]
	v_cndmask_b32_e64 v38, v38, 15, vcc
	v_cndmask_b32_e32 v37, v37, v19, vcc
	v_and_b32_e32 v39, 0x10000, v36
	v_cmp_gt_i32_e64 s[8:9], 0, v38
	v_cmp_gt_f32_e64 s[10:11], v16, v37
	v_cmp_eq_u32_e32 vcc, 0, v39
	s_or_b64 s[8:9], s[8:9], s[10:11]
	s_and_b64 vcc, vcc, s[8:9]
	v_cndmask_b32_e64 v38, v38, 16, vcc
	v_cndmask_b32_e32 v37, v37, v16, vcc
	v_and_b32_e32 v39, 0x20000, v36
	v_cmp_gt_i32_e64 s[8:9], 0, v38
	v_cmp_gt_f32_e64 s[10:11], v17, v37
	v_cmp_eq_u32_e32 vcc, 0, v39
	s_or_b64 s[8:9], s[8:9], s[10:11]
	s_and_b64 vcc, vcc, s[8:9]
	v_cndmask_b32_e64 v38, v38, 17, vcc
	v_cndmask_b32_e32 v37, v37, v17, vcc
	v_and_b32_e32 v39, 0x40000, v36
	v_cmp_gt_i32_e64 s[8:9], 0, v38
	v_cmp_gt_f32_e64 s[10:11], v14, v37
	v_cmp_eq_u32_e32 vcc, 0, v39
	s_or_b64 s[8:9], s[8:9], s[10:11]
	s_and_b64 vcc, vcc, s[8:9]
	v_cndmask_b32_e64 v38, v38, 18, vcc
	v_cndmask_b32_e32 v37, v37, v14, vcc
	v_and_b32_e32 v39, 0x80000, v36
	v_cmp_gt_i32_e64 s[8:9], 0, v38
	v_cmp_gt_f32_e64 s[10:11], v15, v37
	v_cmp_eq_u32_e32 vcc, 0, v39
	s_or_b64 s[8:9], s[8:9], s[10:11]
	s_and_b64 vcc, vcc, s[8:9]
	v_cndmask_b32_e64 v38, v38, 19, vcc
	v_cndmask_b32_e32 v37, v37, v15, vcc
	v_and_b32_e32 v39, 0x100000, v36
	v_cmp_gt_i32_e64 s[8:9], 0, v38
	v_cmp_gt_f32_e64 s[10:11], v12, v37
	v_cmp_eq_u32_e32 vcc, 0, v39
	s_or_b64 s[8:9], s[8:9], s[10:11]
	s_and_b64 vcc, vcc, s[8:9]
	v_cndmask_b32_e64 v38, v38, 20, vcc
	v_cndmask_b32_e32 v37, v37, v12, vcc
	v_and_b32_e32 v39, 0x200000, v36
	v_cmp_gt_i32_e64 s[8:9], 0, v38
	v_cmp_gt_f32_e64 s[10:11], v13, v37
	v_cmp_eq_u32_e32 vcc, 0, v39
	s_or_b64 s[8:9], s[8:9], s[10:11]
	s_and_b64 vcc, vcc, s[8:9]
	v_cndmask_b32_e64 v38, v38, 21, vcc
	v_cndmask_b32_e32 v37, v37, v13, vcc
	v_and_b32_e32 v39, 0x400000, v36
	v_cmp_gt_i32_e64 s[8:9], 0, v38
	v_cmp_gt_f32_e64 s[10:11], v10, v37
	v_cmp_eq_u32_e32 vcc, 0, v39
	s_or_b64 s[8:9], s[8:9], s[10:11]
	s_and_b64 vcc, vcc, s[8:9]
	v_cndmask_b32_e64 v38, v38, 22, vcc
	v_cndmask_b32_e32 v37, v37, v10, vcc
	v_and_b32_e32 v39, 0x800000, v36
	v_cmp_gt_i32_e64 s[8:9], 0, v38
	v_cmp_gt_f32_e64 s[10:11], v11, v37
	v_cmp_eq_u32_e32 vcc, 0, v39
	s_or_b64 s[8:9], s[8:9], s[10:11]
	s_and_b64 vcc, vcc, s[8:9]
	v_cndmask_b32_e64 v38, v38, 23, vcc
	v_cndmask_b32_e32 v37, v37, v11, vcc
	v_and_b32_e32 v39, 0x1000000, v36
	v_cmp_gt_i32_e64 s[8:9], 0, v38
	v_cmp_gt_f32_e64 s[10:11], v8, v37
	v_cmp_eq_u32_e32 vcc, 0, v39
	s_or_b64 s[8:9], s[8:9], s[10:11]
	s_and_b64 vcc, vcc, s[8:9]
	v_cndmask_b32_e64 v38, v38, 24, vcc
	v_cndmask_b32_e32 v37, v37, v8, vcc
	v_and_b32_e32 v39, 0x2000000, v36
	v_cmp_gt_i32_e64 s[8:9], 0, v38
	v_cmp_gt_f32_e64 s[10:11], v9, v37
	v_cmp_eq_u32_e32 vcc, 0, v39
	s_or_b64 s[8:9], s[8:9], s[10:11]
	s_and_b64 vcc, vcc, s[8:9]
	v_cndmask_b32_e64 v38, v38, 25, vcc
	v_cndmask_b32_e32 v37, v37, v9, vcc
	v_and_b32_e32 v39, 0x4000000, v36
	v_cmp_gt_i32_e64 s[8:9], 0, v38
	v_cmp_gt_f32_e64 s[10:11], v6, v37
	v_cmp_eq_u32_e32 vcc, 0, v39
	s_or_b64 s[8:9], s[8:9], s[10:11]
	s_and_b64 vcc, vcc, s[8:9]
	v_cndmask_b32_e64 v38, v38, 26, vcc
	v_cndmask_b32_e32 v37, v37, v6, vcc
	v_and_b32_e32 v39, 0x8000000, v36
	v_cmp_gt_i32_e64 s[8:9], 0, v38
	v_cmp_gt_f32_e64 s[10:11], v7, v37
	v_cmp_eq_u32_e32 vcc, 0, v39
	s_or_b64 s[8:9], s[8:9], s[10:11]
	s_and_b64 vcc, vcc, s[8:9]
	v_cndmask_b32_e64 v38, v38, 27, vcc
	v_cndmask_b32_e32 v37, v37, v7, vcc
	v_and_b32_e32 v39, 0x10000000, v36
	v_cmp_gt_i32_e64 s[8:9], 0, v38
	v_cmp_gt_f32_e64 s[10:11], v4, v37
	v_cmp_eq_u32_e32 vcc, 0, v39
	s_or_b64 s[8:9], s[8:9], s[10:11]
	s_and_b64 vcc, vcc, s[8:9]
	v_cndmask_b32_e64 v38, v38, 28, vcc
	v_cndmask_b32_e32 v37, v37, v4, vcc
	v_and_b32_e32 v39, 0x20000000, v36
	v_cmp_gt_i32_e64 s[8:9], 0, v38
	v_cmp_gt_f32_e64 s[10:11], v5, v37
	v_cmp_eq_u32_e32 vcc, 0, v39
	s_or_b64 s[8:9], s[8:9], s[10:11]
	s_and_b64 vcc, vcc, s[8:9]
	v_cndmask_b32_e64 v38, v38, 29, vcc
	v_cndmask_b32_e32 v37, v37, v5, vcc
	v_and_b32_e32 v39, 2.0, v36
	v_cmp_gt_i32_e64 s[8:9], 0, v38
	v_cmp_gt_f32_e64 s[10:11], v2, v37
	v_cmp_eq_u32_e32 vcc, 0, v39
	s_or_b64 s[8:9], s[8:9], s[10:11]
	s_and_b64 vcc, vcc, s[8:9]
	v_cndmask_b32_e64 v38, v38, 30, vcc
	v_cndmask_b32_e32 v37, v37, v2, vcc
	v_cmp_gt_i32_e64 s[8:9], 0, v38
	v_cmp_gt_f32_e64 s[10:11], v3, v37
	v_cmp_lt_i32_e32 vcc, -1, v36
	s_or_b64 s[8:9], s[8:9], s[10:11]
	s_and_b64 vcc, vcc, s[8:9]
	v_cndmask_b32_e64 v154, v38, 31, vcc
	v_lshlrev_b32_e64 v38, v154, 1
	v_or_b32_e32 v39, v38, v36
	v_and_b32_e32 v40, 1, v39
	v_cndmask_b32_e32 v37, v37, v3, vcc
	v_cmp_eq_u32_e32 vcc, 1, v40
	v_bitop3_b32 v42, v38, 2, v36 bitop3:0xc8
	v_bfe_i32 v41, v39, 0, 1
	v_cndmask_b32_e32 v40, v32, v198, vcc
	v_cmp_gt_f32_e64 s[8:9], v33, v40
	s_or_b64 vcc, vcc, s[8:9]
	v_cndmask_b32_e64 v43, 0, 1, vcc
	v_cndmask_b32_e32 v32, v32, v33, vcc
	v_cmp_eq_u32_e32 vcc, 0, v42
	s_nop 1
	v_cndmask_b32_e32 v32, v40, v32, vcc
	v_bitop3_b32 v40, v38, 4, v36 bitop3:0xc8
	v_cndmask_b32_e32 v33, v41, v43, vcc
	v_cmp_eq_u32_e32 vcc, 0, v40
	v_bitop3_b32 v40, v38, 3, v36 bitop3:0xc8
	v_cmp_eq_u32_e64 s[8:9], 3, v40
	v_cmp_gt_f32_e64 s[10:11], v30, v32
	s_or_b64 s[8:9], s[8:9], s[10:11]
	s_and_b64 vcc, vcc, s[8:9]
	v_cndmask_b32_e64 v33, v33, 2, vcc
	v_cndmask_b32_e32 v30, v32, v30, vcc
	v_bitop3_b32 v32, v38, 8, v36 bitop3:0xc8
	v_cmp_gt_i32_e64 s[8:9], 0, v33
	v_cmp_gt_f32_e64 s[10:11], v31, v30
	v_cmp_eq_u32_e32 vcc, 0, v32
	s_or_b64 s[8:9], s[8:9], s[10:11]
	s_and_b64 vcc, vcc, s[8:9]
	v_cndmask_b32_e64 v32, v33, 3, vcc
	v_cndmask_b32_e32 v30, v30, v31, vcc
	v_bitop3_b32 v31, v38, 16, v36 bitop3:0xc8
	v_cmp_gt_i32_e64 s[8:9], 0, v32
	v_cmp_gt_f32_e64 s[10:11], v28, v30
	v_cmp_eq_u32_e32 vcc, 0, v31
	s_or_b64 s[8:9], s[8:9], s[10:11]
	s_and_b64 vcc, vcc, s[8:9]
	v_cndmask_b32_e64 v31, v32, 4, vcc
	v_cndmask_b32_e32 v28, v30, v28, vcc
	v_bitop3_b32 v30, v38, 32, v36 bitop3:0xc8
	v_cmp_gt_i32_e64 s[8:9], 0, v31
	v_cmp_gt_f32_e64 s[10:11], v29, v28
	v_cmp_eq_u32_e32 vcc, 0, v30
	s_or_b64 s[8:9], s[8:9], s[10:11]
	s_and_b64 vcc, vcc, s[8:9]
	v_cndmask_b32_e64 v30, v31, 5, vcc
	v_cndmask_b32_e32 v28, v28, v29, vcc
	v_bitop3_b32 v29, v38, 64, v36 bitop3:0xc8
	v_cmp_gt_i32_e64 s[8:9], 0, v30
	v_cmp_gt_f32_e64 s[10:11], v26, v28
	v_cmp_eq_u32_e32 vcc, 0, v29
	s_or_b64 s[8:9], s[8:9], s[10:11]
	s_and_b64 vcc, vcc, s[8:9]
	v_cndmask_b32_e64 v29, v30, 6, vcc
	v_cndmask_b32_e32 v26, v28, v26, vcc
	v_bitop3_b32 v28, v38, s26, v36 bitop3:0xc8
	v_cmp_gt_i32_e64 s[8:9], 0, v29
	v_cmp_gt_f32_e64 s[10:11], v27, v26
	v_cmp_eq_u32_e32 vcc, 0, v28
	s_or_b64 s[8:9], s[8:9], s[10:11]
	s_and_b64 vcc, vcc, s[8:9]
	v_cndmask_b32_e64 v28, v29, 7, vcc
	v_cndmask_b32_e32 v26, v26, v27, vcc
	v_bitop3_b32 v27, v38, s27, v36 bitop3:0xc8
	v_cmp_gt_i32_e64 s[8:9], 0, v28
	v_cmp_gt_f32_e64 s[10:11], v24, v26
	v_cmp_eq_u32_e32 vcc, 0, v27
	s_or_b64 s[8:9], s[8:9], s[10:11]
	s_and_b64 vcc, vcc, s[8:9]
	v_cndmask_b32_e64 v27, v28, 8, vcc
	v_cndmask_b32_e32 v24, v26, v24, vcc
	v_bitop3_b32 v26, v38, s28, v36 bitop3:0xc8
	v_cmp_gt_i32_e64 s[8:9], 0, v27
	v_cmp_gt_f32_e64 s[10:11], v25, v24
	v_cmp_eq_u32_e32 vcc, 0, v26
	s_or_b64 s[8:9], s[8:9], s[10:11]
	s_and_b64 vcc, vcc, s[8:9]
	v_cndmask_b32_e64 v26, v27, 9, vcc
	v_cndmask_b32_e32 v24, v24, v25, vcc
	v_bitop3_b32 v25, v38, s29, v36 bitop3:0xc8
	v_cmp_gt_i32_e64 s[8:9], 0, v26
	v_cmp_gt_f32_e64 s[10:11], v22, v24
	v_cmp_eq_u32_e32 vcc, 0, v25
	s_or_b64 s[8:9], s[8:9], s[10:11]
	s_and_b64 vcc, vcc, s[8:9]
	v_cndmask_b32_e64 v25, v26, 10, vcc
	v_cndmask_b32_e32 v22, v24, v22, vcc
	v_bitop3_b32 v24, v38, s30, v36 bitop3:0xc8
	v_cmp_gt_i32_e64 s[8:9], 0, v25
	v_cmp_gt_f32_e64 s[10:11], v23, v22
	v_cmp_eq_u32_e32 vcc, 0, v24
	s_or_b64 s[8:9], s[8:9], s[10:11]
	s_and_b64 vcc, vcc, s[8:9]
	v_cndmask_b32_e64 v24, v25, 11, vcc
	v_cndmask_b32_e32 v22, v22, v23, vcc
	v_bitop3_b32 v23, v38, s31, v36 bitop3:0xc8
	v_cmp_gt_i32_e64 s[8:9], 0, v24
	v_cmp_gt_f32_e64 s[10:11], v20, v22
	v_cmp_eq_u32_e32 vcc, 0, v23
	s_or_b64 s[8:9], s[8:9], s[10:11]
	s_and_b64 vcc, vcc, s[8:9]
	v_cndmask_b32_e64 v23, v24, 12, vcc
	v_cndmask_b32_e32 v20, v22, v20, vcc
	v_bitop3_b32 v22, v38, s33, v36 bitop3:0xc8
	v_cmp_gt_i32_e64 s[8:9], 0, v23
	v_cmp_gt_f32_e64 s[10:11], v21, v20
	v_cmp_eq_u32_e32 vcc, 0, v22
	s_or_b64 s[8:9], s[8:9], s[10:11]
	s_and_b64 vcc, vcc, s[8:9]
	v_cndmask_b32_e64 v22, v23, 13, vcc
	v_cndmask_b32_e32 v20, v20, v21, vcc
	v_bitop3_b32 v21, v38, s34, v36 bitop3:0xc8
	v_cmp_gt_i32_e64 s[8:9], 0, v22
	v_cmp_gt_f32_e64 s[10:11], v18, v20
	v_cmp_eq_u32_e32 vcc, 0, v21
	s_or_b64 s[8:9], s[8:9], s[10:11]
	s_and_b64 vcc, vcc, s[8:9]
	v_cndmask_b32_e64 v21, v22, 14, vcc
	v_cndmask_b32_e32 v18, v20, v18, vcc
	v_bitop3_b32 v20, v38, s35, v36 bitop3:0xc8
	v_cmp_gt_i32_e64 s[8:9], 0, v21
	v_cmp_gt_f32_e64 s[10:11], v19, v18
	v_cmp_eq_u32_e32 vcc, 0, v20
	s_or_b64 s[8:9], s[8:9], s[10:11]
	s_and_b64 vcc, vcc, s[8:9]
	v_cndmask_b32_e64 v20, v21, 15, vcc
	v_cndmask_b32_e32 v18, v18, v19, vcc
	v_bitop3_b32 v19, v38, s36, v36 bitop3:0xc8
	v_cmp_gt_i32_e64 s[8:9], 0, v20
	v_cmp_gt_f32_e64 s[10:11], v16, v18
	v_cmp_eq_u32_e32 vcc, 0, v19
	s_or_b64 s[8:9], s[8:9], s[10:11]
	s_and_b64 vcc, vcc, s[8:9]
	v_cndmask_b32_e64 v19, v20, 16, vcc
	v_cndmask_b32_e32 v16, v18, v16, vcc
	v_bitop3_b32 v18, v38, s37, v36 bitop3:0xc8
	v_cmp_gt_i32_e64 s[8:9], 0, v19
	v_cmp_gt_f32_e64 s[10:11], v17, v16
	v_cmp_eq_u32_e32 vcc, 0, v18
	s_or_b64 s[8:9], s[8:9], s[10:11]
	s_and_b64 vcc, vcc, s[8:9]
	v_cndmask_b32_e64 v18, v19, 17, vcc
	v_cndmask_b32_e32 v16, v16, v17, vcc
	v_bitop3_b32 v17, v38, s38, v36 bitop3:0xc8
	v_cmp_gt_i32_e64 s[8:9], 0, v18
	v_cmp_gt_f32_e64 s[10:11], v14, v16
	v_cmp_eq_u32_e32 vcc, 0, v17
	s_or_b64 s[8:9], s[8:9], s[10:11]
	s_and_b64 vcc, vcc, s[8:9]
	v_cndmask_b32_e64 v17, v18, 18, vcc
	v_cndmask_b32_e32 v14, v16, v14, vcc
	v_bitop3_b32 v16, v38, s39, v36 bitop3:0xc8
	v_cmp_gt_i32_e64 s[8:9], 0, v17
	v_cmp_gt_f32_e64 s[10:11], v15, v14
	v_cmp_eq_u32_e32 vcc, 0, v16
	s_or_b64 s[8:9], s[8:9], s[10:11]
	s_and_b64 vcc, vcc, s[8:9]
	v_cndmask_b32_e64 v16, v17, 19, vcc
	v_cndmask_b32_e32 v14, v14, v15, vcc
	v_bitop3_b32 v15, v38, s40, v36 bitop3:0xc8
	v_cmp_gt_i32_e64 s[8:9], 0, v16
	v_cmp_gt_f32_e64 s[10:11], v12, v14
	v_cmp_eq_u32_e32 vcc, 0, v15
	s_or_b64 s[8:9], s[8:9], s[10:11]
	s_and_b64 vcc, vcc, s[8:9]
	v_cndmask_b32_e64 v15, v16, 20, vcc
	v_cndmask_b32_e32 v12, v14, v12, vcc
	v_bitop3_b32 v14, v38, s41, v36 bitop3:0xc8
	v_cmp_gt_i32_e64 s[8:9], 0, v15
	v_cmp_gt_f32_e64 s[10:11], v13, v12
	v_cmp_eq_u32_e32 vcc, 0, v14
	s_or_b64 s[8:9], s[8:9], s[10:11]
	s_and_b64 vcc, vcc, s[8:9]
	v_cndmask_b32_e64 v14, v15, 21, vcc
	v_cndmask_b32_e32 v12, v12, v13, vcc
	v_bitop3_b32 v13, v38, s42, v36 bitop3:0xc8
	v_cmp_gt_i32_e64 s[8:9], 0, v14
	v_cmp_gt_f32_e64 s[10:11], v10, v12
	v_cmp_eq_u32_e32 vcc, 0, v13
	s_or_b64 s[8:9], s[8:9], s[10:11]
	s_and_b64 vcc, vcc, s[8:9]
	v_cndmask_b32_e64 v13, v14, 22, vcc
	v_cndmask_b32_e32 v10, v12, v10, vcc
	v_bitop3_b32 v12, v38, s43, v36 bitop3:0xc8
	v_cmp_gt_i32_e64 s[8:9], 0, v13
	v_cmp_gt_f32_e64 s[10:11], v11, v10
	v_cmp_eq_u32_e32 vcc, 0, v12
	s_or_b64 s[8:9], s[8:9], s[10:11]
	s_and_b64 vcc, vcc, s[8:9]
	v_cndmask_b32_e64 v12, v13, 23, vcc
	v_cndmask_b32_e32 v10, v10, v11, vcc
	v_bitop3_b32 v11, v38, s44, v36 bitop3:0xc8
	v_cmp_gt_i32_e64 s[8:9], 0, v12
	v_cmp_gt_f32_e64 s[10:11], v8, v10
	v_cmp_eq_u32_e32 vcc, 0, v11
	s_or_b64 s[8:9], s[8:9], s[10:11]
	s_and_b64 vcc, vcc, s[8:9]
	v_cndmask_b32_e64 v11, v12, 24, vcc
	v_cndmask_b32_e32 v8, v10, v8, vcc
	v_bitop3_b32 v10, v38, s45, v36 bitop3:0xc8
	v_cmp_gt_i32_e64 s[8:9], 0, v11
	v_cmp_gt_f32_e64 s[10:11], v9, v8
	v_cmp_eq_u32_e32 vcc, 0, v10
	s_or_b64 s[8:9], s[8:9], s[10:11]
	s_and_b64 vcc, vcc, s[8:9]
	v_cndmask_b32_e64 v10, v11, 25, vcc
	v_cndmask_b32_e32 v8, v8, v9, vcc
	v_bitop3_b32 v9, v38, s46, v36 bitop3:0xc8
	v_cmp_gt_i32_e64 s[8:9], 0, v10
	v_cmp_gt_f32_e64 s[10:11], v6, v8
	v_cmp_eq_u32_e32 vcc, 0, v9
	s_or_b64 s[8:9], s[8:9], s[10:11]
	s_and_b64 vcc, vcc, s[8:9]
	v_cndmask_b32_e64 v9, v10, 26, vcc
	v_cndmask_b32_e32 v6, v8, v6, vcc
	v_bitop3_b32 v8, v38, s47, v36 bitop3:0xc8
	v_cmp_gt_i32_e64 s[8:9], 0, v9
	v_cmp_gt_f32_e64 s[10:11], v7, v6
	v_cmp_eq_u32_e32 vcc, 0, v8
	s_or_b64 s[8:9], s[8:9], s[10:11]
	s_and_b64 vcc, vcc, s[8:9]
	v_cndmask_b32_e64 v8, v9, 27, vcc
	v_cndmask_b32_e32 v6, v6, v7, vcc
	v_bitop3_b32 v7, v38, s48, v36 bitop3:0xc8
	v_cmp_gt_i32_e64 s[8:9], 0, v8
	v_cmp_gt_f32_e64 s[10:11], v4, v6
	v_cmp_eq_u32_e32 vcc, 0, v7
	s_or_b64 s[8:9], s[8:9], s[10:11]
	s_and_b64 vcc, vcc, s[8:9]
	v_cndmask_b32_e64 v7, v8, 28, vcc
	v_cndmask_b32_e32 v4, v6, v4, vcc
	v_bitop3_b32 v6, v38, s49, v36 bitop3:0xc8
	v_cmp_gt_i32_e64 s[8:9], 0, v7
	v_cmp_gt_f32_e64 s[10:11], v5, v4
	v_cmp_eq_u32_e32 vcc, 0, v6
	s_or_b64 s[8:9], s[8:9], s[10:11]
	s_and_b64 vcc, vcc, s[8:9]
	v_cndmask_b32_e64 v6, v7, 29, vcc
	v_cndmask_b32_e32 v4, v4, v5, vcc
	v_bitop3_b32 v5, v38, 2.0, v36 bitop3:0xc8
	v_cmp_gt_i32_e64 s[8:9], 0, v6
	v_cmp_gt_f32_e64 s[10:11], v2, v4
	v_cmp_eq_u32_e32 vcc, 0, v5
	s_or_b64 s[8:9], s[8:9], s[10:11]
	s_and_b64 vcc, vcc, s[8:9]
	v_cndmask_b32_e32 v2, v4, v2, vcc
	v_sub_f32_e32 v4, v35, v34
	v_cndmask_b32_e64 v5, v6, 30, vcc
	v_mul_f32_e32 v6, 0x3fb8aa3b, v4
	v_fma_f32 v7, v4, s50, -v6
	v_rndne_f32_e32 v8, v6
	v_fmac_f32_e32 v7, 0x32a5705f, v4
	v_sub_f32_e32 v6, v6, v8
	v_add_f32_e32 v6, v6, v7
	v_cmp_gt_i32_e64 s[8:9], 0, v5
	v_cmp_gt_f32_e64 s[10:11], v3, v2
	v_exp_f32_e32 v6, v6
	v_cvt_i32_f32_e32 v7, v8
	v_cmp_lt_i32_e32 vcc, -1, v39
	s_or_b64 s[8:9], s[8:9], s[10:11]
	s_and_b64 vcc, vcc, s[8:9]
	v_cndmask_b32_e64 v158, v5, 31, vcc
	v_sub_f32_e32 v5, v37, v34
	v_cndmask_b32_e32 v2, v2, v3, vcc
	v_ldexp_f32 v3, v6, v7
	v_mul_f32_e32 v6, 0x3fb8aa3b, v5
	v_fma_f32 v7, v5, s50, -v6
	v_rndne_f32_e32 v8, v6
	v_fmac_f32_e32 v7, 0x32a5705f, v5
	v_sub_f32_e32 v6, v6, v8
	v_add_f32_e32 v6, v6, v7
	v_exp_f32_e32 v6, v6
	v_cvt_i32_f32_e32 v7, v8
	v_cmp_ngt_f32_e32 vcc, s51, v4
	v_sub_f32_e32 v2, v2, v34
	s_nop 0
	v_cndmask_b32_e32 v3, 0, v3, vcc
	v_cmp_nlt_f32_e32 vcc, s52, v4
	s_nop 1
	v_cndmask_b32_e32 v4, v199, v3, vcc
	v_ldexp_f32 v3, v6, v7
	v_mul_f32_e32 v6, 0x3fb8aa3b, v2
	v_fma_f32 v7, v2, s50, -v6
	v_rndne_f32_e32 v8, v6
	v_fmac_f32_e32 v7, 0x32a5705f, v2
	v_sub_f32_e32 v6, v6, v8
	v_add_f32_e32 v6, v6, v7
	v_exp_f32_e32 v6, v6
	v_cvt_i32_f32_e32 v7, v8
	v_cmp_ngt_f32_e32 vcc, s51, v5
	s_nop 1
	v_cndmask_b32_e32 v3, 0, v3, vcc
	v_cmp_nlt_f32_e32 vcc, s52, v5
	v_ldexp_f32 v5, v6, v7
	s_nop 0
	v_cndmask_b32_e32 v3, v199, v3, vcc
	v_cmp_ngt_f32_e32 vcc, s51, v2
	s_nop 1
	v_cndmask_b32_e32 v5, 0, v5, vcc
	v_cmp_nlt_f32_e32 vcc, s52, v2
	s_nop 1
	v_cndmask_b32_e32 v2, v199, v5, vcc
	v_add_f32_e32 v5, 1.0, v4
	v_add_f32_e32 v5, v5, v3
	v_add_f32_e32 v5, v5, v2
	v_div_scale_f32 v6, s[8:9], v5, v5, 1.0
	v_rcp_f32_e32 v7, v6
	s_nop 0
	v_fma_f32 v8, -v6, v7, 1.0
	v_fmac_f32_e32 v7, v8, v7
	v_div_scale_f32 v8, vcc, 1.0, v5, 1.0
	v_mul_f32_e32 v9, v8, v7
	v_fma_f32 v10, -v6, v9, v8
	v_fmac_f32_e32 v9, v10, v7
	v_fma_f32 v6, -v6, v9, v8
	v_lshl_add_u32 v8, v146, 2, s1
	ds_add_rtn_u32 v205, v8, v197
	v_lshl_add_u32 v8, v150, 2, s1
	ds_add_rtn_u32 v207, v8, v197
	v_lshl_add_u32 v8, v154, 2, s1
	ds_add_rtn_u32 v208, v8, v197
	v_lshl_add_u32 v8, v158, 2, s1
	ds_add_rtn_u32 v209, v8, v197
	v_div_fmas_f32 v6, v6, v7, v9
	v_div_fixup_f32 v160, v6, v5, 1.0
	v_mul_f32_e32 v206, v4, v160
	v_pk_mul_f32 v[164:165], v[2:3], v[160:161] op_sel_hi:[1,0]
.LBB0_437:
	s_or_b64 exec, exec, s[20:21]
	s_waitcnt lgkmcnt(0)
	v_add_u32_e32 v166, 16, v166
	v_ashrrev_i32_e32 v167, 31, v166
	v_lshlrev_b64 v[2:3], 11, v[166:167]
	v_lshl_add_u64 v[2:3], v[140:141], 0, v[2:3]
	global_load_dwordx4 v[126:129], v[2:3], off
	global_load_dwordx4 v[122:125], v[2:3], off offset:64
	global_load_dwordx4 v[118:121], v[2:3], off offset:128
	global_load_dwordx4 v[114:117], v[2:3], off offset:192
	global_load_dwordx4 v[110:113], v[2:3], off offset:256
	global_load_dwordx4 v[106:109], v[2:3], off offset:320
	global_load_dwordx4 v[102:105], v[2:3], off offset:384
	global_load_dwordx4 v[98:101], v[2:3], off offset:448
	global_load_dwordx4 v[94:97], v[2:3], off offset:512
	global_load_dwordx4 v[90:93], v[2:3], off offset:576
	global_load_dwordx4 v[86:89], v[2:3], off offset:640
	global_load_dwordx4 v[82:85], v[2:3], off offset:704
	global_load_dwordx4 v[78:81], v[2:3], off offset:768
	global_load_dwordx4 v[74:77], v[2:3], off offset:832
	global_load_dwordx4 v[70:73], v[2:3], off offset:896
	global_load_dwordx4 v[66:69], v[2:3], off offset:960
	global_load_dwordx4 v[62:65], v[2:3], off offset:1024
	global_load_dwordx4 v[58:61], v[2:3], off offset:1088
	global_load_dwordx4 v[54:57], v[2:3], off offset:1152
	global_load_dwordx4 v[50:53], v[2:3], off offset:1216
	global_load_dwordx4 v[46:49], v[2:3], off offset:1280
	global_load_dwordx4 v[42:45], v[2:3], off offset:1344
	global_load_dwordx4 v[38:41], v[2:3], off offset:1408
	global_load_dwordx4 v[34:37], v[2:3], off offset:1472
	global_load_dwordx4 v[30:33], v[2:3], off offset:1536
	global_load_dwordx4 v[26:29], v[2:3], off offset:1600
	global_load_dwordx4 v[22:25], v[2:3], off offset:1664
	global_load_dwordx4 v[18:21], v[2:3], off offset:1728
	global_load_dwordx4 v[14:17], v[2:3], off offset:1792
	global_load_dwordx4 v[10:13], v[2:3], off offset:1856
	global_load_dwordx4 v[6:9], v[2:3], off offset:1920
	s_nop 0
	global_load_dwordx4 v[2:5], v[2:3], off offset:1984
	ds_read_b128 v[130:133], v175 offset:33024
	ds_read_b128 v[134:137], v175 offset:33088
	ds_read_b128 v[210:213], v175
	ds_read_b128 v[214:217], v175 offset:64
	ds_read_b128 v[218:221], v174 offset:33024
	ds_read_b128 v[222:225], v174 offset:33088
	ds_read_b128 v[226:229], v174
	ds_read_b128 v[230:233], v174 offset:64
	v_lshlrev_b64 v[166:167], 10, v[166:167]
	s_waitcnt vmcnt(31) lgkmcnt(1)
	v_mfma_f32_16x16x32_bf16 v[226:229], v[126:129], v[226:229], 0
	v_and_b32_e32 v147, 0xffff0000, v126
	v_and_b32_e32 v151, 0xffff0000, v127
	v_lshlrev_b32_e32 v145, 16, v126
	v_mfma_f32_16x16x32_bf16 v[218:221], v[126:129], v[218:221], 0
	v_lshlrev_b32_e32 v149, 16, v127
	v_and_b32_e32 v155, 0xffff0000, v128
	v_mul_f32_e32 v147, v147, v147
	v_mul_f32_e32 v151, v151, v151
	v_mfma_f32_16x16x32_bf16 v[210:213], v[126:129], v[210:213], v[226:229]
	v_lshlrev_b32_e32 v153, 16, v128
	v_and_b32_e32 v159, 0xffff0000, v129
	v_mul_f32_e32 v155, v155, v155
	v_mfma_f32_16x16x32_bf16 v[130:133], v[126:129], v[130:133], v[218:221]
	v_fmac_f32_e32 v147, v145, v145
	v_fmac_f32_e32 v151, v149, v149
	v_lshlrev_b32_e32 v157, 16, v129
	s_waitcnt vmcnt(30)
	v_and_b32_e32 v169, 0xffff0000, v122
	v_mul_f32_e32 v159, v159, v159
	v_fmac_f32_e32 v155, v153, v153
	v_add_f32_e32 v145, v147, v151
	v_lshlrev_b32_e32 v168, 16, v122
	v_and_b32_e32 v235, 0xffff0000, v123
	v_mul_f32_e32 v169, v169, v169
	v_fmac_f32_e32 v159, v157, v157
	v_add_f32_e32 v145, v155, v145
	v_lshlrev_b32_e32 v234, 16, v123
	v_and_b32_e32 v237, 0xffff0000, v124
	v_mul_f32_e32 v235, v235, v235
	v_fmac_f32_e32 v169, v168, v168
	s_waitcnt lgkmcnt(0)
	v_mfma_f32_16x16x32_bf16 v[210:213], v[122:125], v[230:233], v[210:213]
	v_add_f32_e32 v145, v159, v145
	v_lshlrev_b32_e32 v236, 16, v124
	v_and_b32_e32 v239, 0xffff0000, v125
	v_mfma_f32_16x16x32_bf16 v[130:133], v[122:125], v[222:225], v[130:133]
	v_mul_f32_e32 v237, v237, v237
	v_fmac_f32_e32 v235, v234, v234
	v_add_f32_e32 v145, v169, v145
	v_lshlrev_b32_e32 v238, 16, v125
	v_mul_f32_e32 v239, v239, v239
	v_fmac_f32_e32 v237, v236, v236
	v_add_f32_e32 v145, v235, v145
	v_fmac_f32_e32 v239, v238, v238
	v_add_f32_e32 v145, v237, v145
	v_mfma_f32_16x16x32_bf16 v[210:213], v[122:125], v[214:217], v[210:213]
	v_add_f32_e32 v145, v239, v145
	v_mfma_f32_16x16x32_bf16 v[130:133], v[122:125], v[134:137], v[130:133]
	s_waitcnt vmcnt(29)
	v_and_b32_e32 v149, 0xffff0000, v118
	v_lshlrev_b32_e32 v147, 16, v118
	v_mul_f32_e32 v149, v149, v149
	v_fmac_f32_e32 v149, v147, v147
	v_add_f32_e32 v145, v149, v145
	v_and_b32_e32 v149, 0xffff0000, v119
	v_lshlrev_b32_e32 v147, 16, v119
	v_mul_f32_e32 v149, v149, v149
	v_fmac_f32_e32 v149, v147, v147
	v_add_f32_e32 v145, v149, v145
	v_and_b32_e32 v149, 0xffff0000, v120
	v_lshlrev_b32_e32 v147, 16, v120
	v_mul_f32_e32 v149, v149, v149
	v_fmac_f32_e32 v149, v147, v147
	v_add_f32_e32 v145, v149, v145
	v_and_b32_e32 v149, 0xffff0000, v121
	ds_read_b128 v[134:137], v174 offset:128
	ds_read_b128 v[214:217], v174 offset:33152
	ds_read_b128 v[218:221], v175 offset:128
	ds_read_b128 v[222:225], v175 offset:33152
	ds_read_b128 v[226:229], v174 offset:192
	v_lshlrev_b32_e32 v147, 16, v121
	v_mul_f32_e32 v149, v149, v149
	s_waitcnt lgkmcnt(4)
	v_mfma_f32_16x16x32_bf16 v[134:137], v[118:121], v[134:137], v[210:213]
	v_fmac_f32_e32 v149, v147, v147
	v_add_f32_e32 v145, v149, v145
	s_waitcnt vmcnt(28)
	v_and_b32_e32 v149, 0xffff0000, v114
	s_waitcnt lgkmcnt(3)
	v_mfma_f32_16x16x32_bf16 v[130:133], v[118:121], v[214:217], v[130:133]
	v_lshlrev_b32_e32 v147, 16, v114
	v_mul_f32_e32 v149, v149, v149
	v_fmac_f32_e32 v149, v147, v147
	s_waitcnt lgkmcnt(2)
	v_mfma_f32_16x16x32_bf16 v[134:137], v[118:121], v[218:221], v[134:137]
	ds_read_b128 v[218:221], v174 offset:33216
	ds_read_b128 v[214:217], v175 offset:33216
	v_add_f32_e32 v145, v149, v145
	v_and_b32_e32 v149, 0xffff0000, v115
	s_waitcnt lgkmcnt(3)
	v_mfma_f32_16x16x32_bf16 v[130:133], v[118:121], v[222:225], v[130:133]
	v_lshlrev_b32_e32 v147, 16, v115
	v_mul_f32_e32 v149, v149, v149
	v_fmac_f32_e32 v149, v147, v147
	v_add_f32_e32 v145, v149, v145
	v_and_b32_e32 v149, 0xffff0000, v116
	ds_read_b128 v[210:213], v175 offset:192
	v_lshlrev_b32_e32 v147, 16, v116
	v_mul_f32_e32 v149, v149, v149
	s_waitcnt lgkmcnt(3)
	v_mfma_f32_16x16x32_bf16 v[134:137], v[114:117], v[226:229], v[134:137]
	v_fmac_f32_e32 v149, v147, v147
	v_add_f32_e32 v145, v149, v145
	v_and_b32_e32 v149, 0xffff0000, v117
	s_waitcnt lgkmcnt(2)
	v_mfma_f32_16x16x32_bf16 v[130:133], v[114:117], v[218:221], v[130:133]
	v_lshlrev_b32_e32 v147, 16, v117
	v_mul_f32_e32 v149, v149, v149
	v_fmac_f32_e32 v149, v147, v147
	s_waitcnt lgkmcnt(0)
	v_mfma_f32_16x16x32_bf16 v[134:137], v[114:117], v[210:213], v[134:137]
	v_add_f32_e32 v145, v149, v145
	v_mfma_f32_16x16x32_bf16 v[130:133], v[114:117], v[214:217], v[130:133]
	s_waitcnt vmcnt(27)
	v_and_b32_e32 v149, 0xffff0000, v110
	v_lshlrev_b32_e32 v147, 16, v110
	v_mul_f32_e32 v149, v149, v149
	v_fmac_f32_e32 v149, v147, v147
	v_add_f32_e32 v145, v149, v145
	v_and_b32_e32 v149, 0xffff0000, v111
	v_lshlrev_b32_e32 v147, 16, v111
	v_mul_f32_e32 v149, v149, v149
	v_fmac_f32_e32 v149, v147, v147
	v_add_f32_e32 v145, v149, v145
	v_and_b32_e32 v149, 0xffff0000, v112
	v_lshlrev_b32_e32 v147, 16, v112
	v_mul_f32_e32 v149, v149, v149
	v_fmac_f32_e32 v149, v147, v147
	v_add_f32_e32 v145, v149, v145
	v_and_b32_e32 v149, 0xffff0000, v113
	ds_read_b128 v[210:213], v174 offset:256
	ds_read_b128 v[214:217], v174 offset:33280
	ds_read_b128 v[218:221], v175 offset:256
	ds_read_b128 v[222:225], v175 offset:33280
	ds_read_b128 v[226:229], v174 offset:320
	v_lshlrev_b32_e32 v147, 16, v113
	v_mul_f32_e32 v149, v149, v149
	s_waitcnt lgkmcnt(4)
	v_mfma_f32_16x16x32_bf16 v[134:137], v[110:113], v[210:213], v[134:137]
	v_fmac_f32_e32 v149, v147, v147
	v_add_f32_e32 v145, v149, v145
	s_waitcnt vmcnt(26)
	v_and_b32_e32 v149, 0xffff0000, v106
	s_waitcnt lgkmcnt(3)
	v_mfma_f32_16x16x32_bf16 v[130:133], v[110:113], v[214:217], v[130:133]
	v_lshlrev_b32_e32 v147, 16, v106
	v_mul_f32_e32 v149, v149, v149
	v_fmac_f32_e32 v149, v147, v147
	s_waitcnt lgkmcnt(2)
	v_mfma_f32_16x16x32_bf16 v[134:137], v[110:113], v[218:221], v[134:137]
	ds_read_b128 v[218:221], v174 offset:33344
	ds_read_b128 v[214:217], v175 offset:33344
	v_add_f32_e32 v145, v149, v145
	v_and_b32_e32 v149, 0xffff0000, v107
	s_waitcnt lgkmcnt(3)
	v_mfma_f32_16x16x32_bf16 v[130:133], v[110:113], v[222:225], v[130:133]
	v_lshlrev_b32_e32 v147, 16, v107
	v_mul_f32_e32 v149, v149, v149
	v_fmac_f32_e32 v149, v147, v147
	v_add_f32_e32 v145, v149, v145
	v_and_b32_e32 v149, 0xffff0000, v108
	ds_read_b128 v[210:213], v175 offset:320
	v_lshlrev_b32_e32 v147, 16, v108
	v_mul_f32_e32 v149, v149, v149
	s_waitcnt lgkmcnt(3)
	v_mfma_f32_16x16x32_bf16 v[134:137], v[106:109], v[226:229], v[134:137]
	v_fmac_f32_e32 v149, v147, v147
	v_add_f32_e32 v145, v149, v145
	v_and_b32_e32 v149, 0xffff0000, v109
	s_waitcnt lgkmcnt(2)
	v_mfma_f32_16x16x32_bf16 v[130:133], v[106:109], v[218:221], v[130:133]
	v_lshlrev_b32_e32 v147, 16, v109
	v_mul_f32_e32 v149, v149, v149
	v_fmac_f32_e32 v149, v147, v147
	s_waitcnt lgkmcnt(0)
	v_mfma_f32_16x16x32_bf16 v[134:137], v[106:109], v[210:213], v[134:137]
	v_add_f32_e32 v145, v149, v145
	v_mfma_f32_16x16x32_bf16 v[130:133], v[106:109], v[214:217], v[130:133]
	s_waitcnt vmcnt(25)
	v_and_b32_e32 v149, 0xffff0000, v102
	v_lshlrev_b32_e32 v147, 16, v102
	v_mul_f32_e32 v149, v149, v149
	v_fmac_f32_e32 v149, v147, v147
	v_add_f32_e32 v145, v149, v145
	v_and_b32_e32 v149, 0xffff0000, v103
	v_lshlrev_b32_e32 v147, 16, v103
	v_mul_f32_e32 v149, v149, v149
	v_fmac_f32_e32 v149, v147, v147
	v_add_f32_e32 v145, v149, v145
	v_and_b32_e32 v149, 0xffff0000, v104
	v_lshlrev_b32_e32 v147, 16, v104
	v_mul_f32_e32 v149, v149, v149
	v_fmac_f32_e32 v149, v147, v147
	v_add_f32_e32 v145, v149, v145
	v_and_b32_e32 v149, 0xffff0000, v105
	ds_read_b128 v[210:213], v174 offset:384
	ds_read_b128 v[214:217], v174 offset:33408
	ds_read_b128 v[218:221], v175 offset:384
	ds_read_b128 v[222:225], v175 offset:33408
	ds_read_b128 v[226:229], v174 offset:448
	v_lshlrev_b32_e32 v147, 16, v105
	v_mul_f32_e32 v149, v149, v149
	s_waitcnt lgkmcnt(4)
	v_mfma_f32_16x16x32_bf16 v[134:137], v[102:105], v[210:213], v[134:137]
	v_fmac_f32_e32 v149, v147, v147
	v_add_f32_e32 v145, v149, v145
	s_waitcnt vmcnt(24)
	v_and_b32_e32 v149, 0xffff0000, v98
	s_waitcnt lgkmcnt(3)
	v_mfma_f32_16x16x32_bf16 v[130:133], v[102:105], v[214:217], v[130:133]
	v_lshlrev_b32_e32 v147, 16, v98
	v_mul_f32_e32 v149, v149, v149
	v_fmac_f32_e32 v149, v147, v147
	s_waitcnt lgkmcnt(2)
	v_mfma_f32_16x16x32_bf16 v[134:137], v[102:105], v[218:221], v[134:137]
	ds_read_b128 v[218:221], v174 offset:33472
	ds_read_b128 v[214:217], v175 offset:33472
	v_add_f32_e32 v145, v149, v145
	v_and_b32_e32 v149, 0xffff0000, v99
	s_waitcnt lgkmcnt(3)
	v_mfma_f32_16x16x32_bf16 v[130:133], v[102:105], v[222:225], v[130:133]
	v_lshlrev_b32_e32 v147, 16, v99
	v_mul_f32_e32 v149, v149, v149
	v_fmac_f32_e32 v149, v147, v147
	v_add_f32_e32 v145, v149, v145
	v_and_b32_e32 v149, 0xffff0000, v100
	ds_read_b128 v[210:213], v175 offset:448
	v_lshlrev_b32_e32 v147, 16, v100
	v_mul_f32_e32 v149, v149, v149
	s_waitcnt lgkmcnt(3)
	v_mfma_f32_16x16x32_bf16 v[134:137], v[98:101], v[226:229], v[134:137]
	v_fmac_f32_e32 v149, v147, v147
	v_add_f32_e32 v145, v149, v145
	v_and_b32_e32 v149, 0xffff0000, v101
	s_waitcnt lgkmcnt(2)
	v_mfma_f32_16x16x32_bf16 v[130:133], v[98:101], v[218:221], v[130:133]
	v_lshlrev_b32_e32 v147, 16, v101
	v_mul_f32_e32 v149, v149, v149
	v_fmac_f32_e32 v149, v147, v147
	s_waitcnt lgkmcnt(0)
	v_mfma_f32_16x16x32_bf16 v[134:137], v[98:101], v[210:213], v[134:137]
	v_add_f32_e32 v145, v149, v145
	v_mfma_f32_16x16x32_bf16 v[130:133], v[98:101], v[214:217], v[130:133]
	s_waitcnt vmcnt(23)
	v_and_b32_e32 v149, 0xffff0000, v94
	v_lshlrev_b32_e32 v147, 16, v94
	v_mul_f32_e32 v149, v149, v149
	v_fmac_f32_e32 v149, v147, v147
	v_add_f32_e32 v145, v149, v145
	v_and_b32_e32 v149, 0xffff0000, v95
	v_lshlrev_b32_e32 v147, 16, v95
	v_mul_f32_e32 v149, v149, v149
	v_fmac_f32_e32 v149, v147, v147
	v_add_f32_e32 v145, v149, v145
	v_and_b32_e32 v149, 0xffff0000, v96
	v_lshlrev_b32_e32 v147, 16, v96
	v_mul_f32_e32 v149, v149, v149
	v_fmac_f32_e32 v149, v147, v147
	v_add_f32_e32 v145, v149, v145
	v_and_b32_e32 v149, 0xffff0000, v97
	ds_read_b128 v[210:213], v174 offset:512
	ds_read_b128 v[214:217], v174 offset:33536
	ds_read_b128 v[218:221], v175 offset:512
	ds_read_b128 v[222:225], v175 offset:33536
	ds_read_b128 v[226:229], v174 offset:576
	v_lshlrev_b32_e32 v147, 16, v97
	v_mul_f32_e32 v149, v149, v149
	s_waitcnt lgkmcnt(4)
	v_mfma_f32_16x16x32_bf16 v[134:137], v[94:97], v[210:213], v[134:137]
	v_fmac_f32_e32 v149, v147, v147
	v_add_f32_e32 v145, v149, v145
	s_waitcnt vmcnt(22)
	v_and_b32_e32 v149, 0xffff0000, v90
	s_waitcnt lgkmcnt(3)
	v_mfma_f32_16x16x32_bf16 v[130:133], v[94:97], v[214:217], v[130:133]
	v_lshlrev_b32_e32 v147, 16, v90
	v_mul_f32_e32 v149, v149, v149
	v_fmac_f32_e32 v149, v147, v147
	s_waitcnt lgkmcnt(2)
	v_mfma_f32_16x16x32_bf16 v[134:137], v[94:97], v[218:221], v[134:137]
	ds_read_b128 v[218:221], v174 offset:33600
	ds_read_b128 v[214:217], v175 offset:33600
	v_add_f32_e32 v145, v149, v145
	v_and_b32_e32 v149, 0xffff0000, v91
	s_waitcnt lgkmcnt(3)
	v_mfma_f32_16x16x32_bf16 v[130:133], v[94:97], v[222:225], v[130:133]
	v_lshlrev_b32_e32 v147, 16, v91
	v_mul_f32_e32 v149, v149, v149
	v_fmac_f32_e32 v149, v147, v147
	v_add_f32_e32 v145, v149, v145
	v_and_b32_e32 v149, 0xffff0000, v92
	ds_read_b128 v[210:213], v175 offset:576
	v_lshlrev_b32_e32 v147, 16, v92
	v_mul_f32_e32 v149, v149, v149
	s_waitcnt lgkmcnt(3)
	v_mfma_f32_16x16x32_bf16 v[134:137], v[90:93], v[226:229], v[134:137]
	v_fmac_f32_e32 v149, v147, v147
	v_add_f32_e32 v145, v149, v145
	v_and_b32_e32 v149, 0xffff0000, v93
	s_waitcnt lgkmcnt(2)
	v_mfma_f32_16x16x32_bf16 v[130:133], v[90:93], v[218:221], v[130:133]
	v_lshlrev_b32_e32 v147, 16, v93
	v_mul_f32_e32 v149, v149, v149
	v_fmac_f32_e32 v149, v147, v147
	s_waitcnt lgkmcnt(0)
	v_mfma_f32_16x16x32_bf16 v[134:137], v[90:93], v[210:213], v[134:137]
	v_add_f32_e32 v145, v149, v145
	v_mfma_f32_16x16x32_bf16 v[130:133], v[90:93], v[214:217], v[130:133]
	s_waitcnt vmcnt(21)
	v_and_b32_e32 v149, 0xffff0000, v86
	v_lshlrev_b32_e32 v147, 16, v86
	v_mul_f32_e32 v149, v149, v149
	v_fmac_f32_e32 v149, v147, v147
	v_add_f32_e32 v145, v149, v145
	v_and_b32_e32 v149, 0xffff0000, v87
	v_lshlrev_b32_e32 v147, 16, v87
	v_mul_f32_e32 v149, v149, v149
	v_fmac_f32_e32 v149, v147, v147
	v_add_f32_e32 v145, v149, v145
	v_and_b32_e32 v149, 0xffff0000, v88
	v_lshlrev_b32_e32 v147, 16, v88
	v_mul_f32_e32 v149, v149, v149
	v_fmac_f32_e32 v149, v147, v147
	v_add_f32_e32 v145, v149, v145
	v_and_b32_e32 v149, 0xffff0000, v89
	ds_read_b128 v[210:213], v174 offset:640
	ds_read_b128 v[214:217], v174 offset:33664
	ds_read_b128 v[218:221], v175 offset:640
	ds_read_b128 v[222:225], v175 offset:33664
	ds_read_b128 v[226:229], v174 offset:704
	v_lshlrev_b32_e32 v147, 16, v89
	v_mul_f32_e32 v149, v149, v149
	s_waitcnt lgkmcnt(4)
	v_mfma_f32_16x16x32_bf16 v[134:137], v[86:89], v[210:213], v[134:137]
	v_fmac_f32_e32 v149, v147, v147
	v_add_f32_e32 v145, v149, v145
	s_waitcnt vmcnt(20)
	v_and_b32_e32 v149, 0xffff0000, v82
	s_waitcnt lgkmcnt(3)
	v_mfma_f32_16x16x32_bf16 v[130:133], v[86:89], v[214:217], v[130:133]
	v_lshlrev_b32_e32 v147, 16, v82
	v_mul_f32_e32 v149, v149, v149
	v_fmac_f32_e32 v149, v147, v147
	s_waitcnt lgkmcnt(2)
	v_mfma_f32_16x16x32_bf16 v[134:137], v[86:89], v[218:221], v[134:137]
	ds_read_b128 v[218:221], v174 offset:33728
	ds_read_b128 v[214:217], v175 offset:33728
	v_add_f32_e32 v145, v149, v145
	v_and_b32_e32 v149, 0xffff0000, v83
	s_waitcnt lgkmcnt(3)
	v_mfma_f32_16x16x32_bf16 v[130:133], v[86:89], v[222:225], v[130:133]
	v_lshlrev_b32_e32 v147, 16, v83
	v_mul_f32_e32 v149, v149, v149
	v_fmac_f32_e32 v149, v147, v147
	v_add_f32_e32 v145, v149, v145
	v_and_b32_e32 v149, 0xffff0000, v84
	ds_read_b128 v[210:213], v175 offset:704
	v_lshlrev_b32_e32 v147, 16, v84
	v_mul_f32_e32 v149, v149, v149
	s_waitcnt lgkmcnt(3)
	v_mfma_f32_16x16x32_bf16 v[134:137], v[82:85], v[226:229], v[134:137]
	v_fmac_f32_e32 v149, v147, v147
	v_add_f32_e32 v145, v149, v145
	v_and_b32_e32 v149, 0xffff0000, v85
	s_waitcnt lgkmcnt(2)
	v_mfma_f32_16x16x32_bf16 v[130:133], v[82:85], v[218:221], v[130:133]
	v_lshlrev_b32_e32 v147, 16, v85
	v_mul_f32_e32 v149, v149, v149
	v_fmac_f32_e32 v149, v147, v147
	s_waitcnt lgkmcnt(0)
	v_mfma_f32_16x16x32_bf16 v[134:137], v[82:85], v[210:213], v[134:137]
	v_add_f32_e32 v145, v149, v145
	v_mfma_f32_16x16x32_bf16 v[130:133], v[82:85], v[214:217], v[130:133]
	s_waitcnt vmcnt(19)
	v_and_b32_e32 v149, 0xffff0000, v78
	v_lshlrev_b32_e32 v147, 16, v78
	v_mul_f32_e32 v149, v149, v149
	v_fmac_f32_e32 v149, v147, v147
	v_add_f32_e32 v145, v149, v145
	v_and_b32_e32 v149, 0xffff0000, v79
	v_lshlrev_b32_e32 v147, 16, v79
	v_mul_f32_e32 v149, v149, v149
	v_fmac_f32_e32 v149, v147, v147
	v_add_f32_e32 v145, v149, v145
	v_and_b32_e32 v149, 0xffff0000, v80
	v_lshlrev_b32_e32 v147, 16, v80
	v_mul_f32_e32 v149, v149, v149
	v_fmac_f32_e32 v149, v147, v147
	v_add_f32_e32 v145, v149, v145
	v_and_b32_e32 v149, 0xffff0000, v81
	ds_read_b128 v[210:213], v174 offset:768
	ds_read_b128 v[214:217], v174 offset:33792
	ds_read_b128 v[218:221], v175 offset:768
	ds_read_b128 v[222:225], v175 offset:33792
	ds_read_b128 v[226:229], v174 offset:832
	v_lshlrev_b32_e32 v147, 16, v81
	v_mul_f32_e32 v149, v149, v149
	s_waitcnt lgkmcnt(4)
	v_mfma_f32_16x16x32_bf16 v[134:137], v[78:81], v[210:213], v[134:137]
	v_fmac_f32_e32 v149, v147, v147
	v_add_f32_e32 v145, v149, v145
	s_waitcnt vmcnt(18)
	v_and_b32_e32 v149, 0xffff0000, v74
	s_waitcnt lgkmcnt(3)
	v_mfma_f32_16x16x32_bf16 v[130:133], v[78:81], v[214:217], v[130:133]
	v_lshlrev_b32_e32 v147, 16, v74
	v_mul_f32_e32 v149, v149, v149
	v_fmac_f32_e32 v149, v147, v147
	s_waitcnt lgkmcnt(2)
	v_mfma_f32_16x16x32_bf16 v[134:137], v[78:81], v[218:221], v[134:137]
	ds_read_b128 v[218:221], v174 offset:33856
	ds_read_b128 v[214:217], v175 offset:33856
	v_add_f32_e32 v145, v149, v145
	v_and_b32_e32 v149, 0xffff0000, v75
	s_waitcnt lgkmcnt(3)
	v_mfma_f32_16x16x32_bf16 v[130:133], v[78:81], v[222:225], v[130:133]
	v_lshlrev_b32_e32 v147, 16, v75
	v_mul_f32_e32 v149, v149, v149
	v_fmac_f32_e32 v149, v147, v147
	v_add_f32_e32 v145, v149, v145
	v_and_b32_e32 v149, 0xffff0000, v76
	ds_read_b128 v[210:213], v175 offset:832
	v_lshlrev_b32_e32 v147, 16, v76
	v_mul_f32_e32 v149, v149, v149
	s_waitcnt lgkmcnt(3)
	v_mfma_f32_16x16x32_bf16 v[134:137], v[74:77], v[226:229], v[134:137]
	v_fmac_f32_e32 v149, v147, v147
	v_add_f32_e32 v145, v149, v145
	v_and_b32_e32 v149, 0xffff0000, v77
	s_waitcnt lgkmcnt(2)
	v_mfma_f32_16x16x32_bf16 v[130:133], v[74:77], v[218:221], v[130:133]
	v_lshlrev_b32_e32 v147, 16, v77
	v_mul_f32_e32 v149, v149, v149
	v_fmac_f32_e32 v149, v147, v147
	s_waitcnt lgkmcnt(0)
	v_mfma_f32_16x16x32_bf16 v[134:137], v[74:77], v[210:213], v[134:137]
	v_add_f32_e32 v145, v149, v145
	v_mfma_f32_16x16x32_bf16 v[130:133], v[74:77], v[214:217], v[130:133]
	s_waitcnt vmcnt(17)
	v_and_b32_e32 v149, 0xffff0000, v70
	v_lshlrev_b32_e32 v147, 16, v70
	v_mul_f32_e32 v149, v149, v149
	v_fmac_f32_e32 v149, v147, v147
	v_add_f32_e32 v145, v149, v145
	v_and_b32_e32 v149, 0xffff0000, v71
	v_lshlrev_b32_e32 v147, 16, v71
	v_mul_f32_e32 v149, v149, v149
	v_fmac_f32_e32 v149, v147, v147
	v_add_f32_e32 v145, v149, v145
	v_and_b32_e32 v149, 0xffff0000, v72
	v_lshlrev_b32_e32 v147, 16, v72
	v_mul_f32_e32 v149, v149, v149
	v_fmac_f32_e32 v149, v147, v147
	v_add_f32_e32 v145, v149, v145
	v_and_b32_e32 v149, 0xffff0000, v73
	ds_read_b128 v[210:213], v174 offset:896
	ds_read_b128 v[214:217], v174 offset:33920
	ds_read_b128 v[218:221], v175 offset:896
	ds_read_b128 v[222:225], v175 offset:33920
	ds_read_b128 v[226:229], v174 offset:960
	v_lshlrev_b32_e32 v147, 16, v73
	v_mul_f32_e32 v149, v149, v149
	s_waitcnt lgkmcnt(4)
	v_mfma_f32_16x16x32_bf16 v[134:137], v[70:73], v[210:213], v[134:137]
	v_fmac_f32_e32 v149, v147, v147
	v_add_f32_e32 v145, v149, v145
	s_waitcnt vmcnt(16)
	v_and_b32_e32 v149, 0xffff0000, v66
	s_waitcnt lgkmcnt(3)
	v_mfma_f32_16x16x32_bf16 v[130:133], v[70:73], v[214:217], v[130:133]
	v_lshlrev_b32_e32 v147, 16, v66
	v_mul_f32_e32 v149, v149, v149
	v_fmac_f32_e32 v149, v147, v147
	s_waitcnt lgkmcnt(2)
	v_mfma_f32_16x16x32_bf16 v[134:137], v[70:73], v[218:221], v[134:137]
	ds_read_b128 v[218:221], v174 offset:33984
	ds_read_b128 v[214:217], v175 offset:33984
	v_add_f32_e32 v145, v149, v145
	v_and_b32_e32 v149, 0xffff0000, v67
	s_waitcnt lgkmcnt(3)
	v_mfma_f32_16x16x32_bf16 v[130:133], v[70:73], v[222:225], v[130:133]
	v_lshlrev_b32_e32 v147, 16, v67
	v_mul_f32_e32 v149, v149, v149
	v_fmac_f32_e32 v149, v147, v147
	v_add_f32_e32 v145, v149, v145
	v_and_b32_e32 v149, 0xffff0000, v68
	ds_read_b128 v[210:213], v175 offset:960
	v_lshlrev_b32_e32 v147, 16, v68
	v_mul_f32_e32 v149, v149, v149
	s_waitcnt lgkmcnt(3)
	v_mfma_f32_16x16x32_bf16 v[134:137], v[66:69], v[226:229], v[134:137]
	v_fmac_f32_e32 v149, v147, v147
	v_add_f32_e32 v145, v149, v145
	v_and_b32_e32 v149, 0xffff0000, v69
	s_waitcnt lgkmcnt(2)
	v_mfma_f32_16x16x32_bf16 v[130:133], v[66:69], v[218:221], v[130:133]
	v_lshlrev_b32_e32 v147, 16, v69
	v_mul_f32_e32 v149, v149, v149
	v_fmac_f32_e32 v149, v147, v147
	s_waitcnt lgkmcnt(0)
	v_mfma_f32_16x16x32_bf16 v[134:137], v[66:69], v[210:213], v[134:137]
	v_add_f32_e32 v145, v149, v145
	v_mfma_f32_16x16x32_bf16 v[130:133], v[66:69], v[214:217], v[130:133]
	s_waitcnt vmcnt(15)
	v_and_b32_e32 v149, 0xffff0000, v62
	v_lshlrev_b32_e32 v147, 16, v62
	v_mul_f32_e32 v149, v149, v149
	v_fmac_f32_e32 v149, v147, v147
	v_add_f32_e32 v145, v149, v145
	v_and_b32_e32 v149, 0xffff0000, v63
	v_lshlrev_b32_e32 v147, 16, v63
	v_mul_f32_e32 v149, v149, v149
	v_fmac_f32_e32 v149, v147, v147
	v_add_f32_e32 v145, v149, v145
	v_and_b32_e32 v149, 0xffff0000, v64
	v_lshlrev_b32_e32 v147, 16, v64
	v_mul_f32_e32 v149, v149, v149
	v_fmac_f32_e32 v149, v147, v147
	v_add_f32_e32 v145, v149, v145
	v_and_b32_e32 v149, 0xffff0000, v65
	ds_read_b128 v[210:213], v174 offset:1024
	ds_read_b128 v[214:217], v174 offset:34048
	ds_read_b128 v[218:221], v175 offset:1024
	ds_read_b128 v[222:225], v175 offset:34048
	ds_read_b128 v[226:229], v174 offset:1088
	v_lshlrev_b32_e32 v147, 16, v65
	v_mul_f32_e32 v149, v149, v149
	s_waitcnt lgkmcnt(4)
	v_mfma_f32_16x16x32_bf16 v[134:137], v[62:65], v[210:213], v[134:137]
	v_fmac_f32_e32 v149, v147, v147
	v_add_f32_e32 v145, v149, v145
	s_waitcnt vmcnt(14)
	v_and_b32_e32 v149, 0xffff0000, v58
	s_waitcnt lgkmcnt(3)
	v_mfma_f32_16x16x32_bf16 v[130:133], v[62:65], v[214:217], v[130:133]
	v_lshlrev_b32_e32 v147, 16, v58
	v_mul_f32_e32 v149, v149, v149
	v_fmac_f32_e32 v149, v147, v147
	s_waitcnt lgkmcnt(2)
	v_mfma_f32_16x16x32_bf16 v[134:137], v[62:65], v[218:221], v[134:137]
	ds_read_b128 v[218:221], v174 offset:34112
	ds_read_b128 v[214:217], v175 offset:34112
	v_add_f32_e32 v145, v149, v145
	v_and_b32_e32 v149, 0xffff0000, v59
	s_waitcnt lgkmcnt(3)
	v_mfma_f32_16x16x32_bf16 v[130:133], v[62:65], v[222:225], v[130:133]
	v_lshlrev_b32_e32 v147, 16, v59
	v_mul_f32_e32 v149, v149, v149
	v_fmac_f32_e32 v149, v147, v147
	v_add_f32_e32 v145, v149, v145
	v_and_b32_e32 v149, 0xffff0000, v60
	ds_read_b128 v[210:213], v175 offset:1088
	v_lshlrev_b32_e32 v147, 16, v60
	v_mul_f32_e32 v149, v149, v149
	s_waitcnt lgkmcnt(3)
	v_mfma_f32_16x16x32_bf16 v[134:137], v[58:61], v[226:229], v[134:137]
	v_fmac_f32_e32 v149, v147, v147
	v_add_f32_e32 v145, v149, v145
	v_and_b32_e32 v149, 0xffff0000, v61
	s_waitcnt lgkmcnt(2)
	v_mfma_f32_16x16x32_bf16 v[130:133], v[58:61], v[218:221], v[130:133]
	v_lshlrev_b32_e32 v147, 16, v61
	v_mul_f32_e32 v149, v149, v149
	v_fmac_f32_e32 v149, v147, v147
	s_waitcnt lgkmcnt(0)
	v_mfma_f32_16x16x32_bf16 v[134:137], v[58:61], v[210:213], v[134:137]
	v_add_f32_e32 v145, v149, v145
	v_mfma_f32_16x16x32_bf16 v[130:133], v[58:61], v[214:217], v[130:133]
	s_waitcnt vmcnt(13)
	v_and_b32_e32 v149, 0xffff0000, v54
	v_lshlrev_b32_e32 v147, 16, v54
	v_mul_f32_e32 v149, v149, v149
	v_fmac_f32_e32 v149, v147, v147
	v_add_f32_e32 v145, v149, v145
	v_and_b32_e32 v149, 0xffff0000, v55
	v_lshlrev_b32_e32 v147, 16, v55
	v_mul_f32_e32 v149, v149, v149
	v_fmac_f32_e32 v149, v147, v147
	v_add_f32_e32 v145, v149, v145
	v_and_b32_e32 v149, 0xffff0000, v56
	v_lshlrev_b32_e32 v147, 16, v56
	v_mul_f32_e32 v149, v149, v149
	v_fmac_f32_e32 v149, v147, v147
	v_add_f32_e32 v145, v149, v145
	v_and_b32_e32 v149, 0xffff0000, v57
	ds_read_b128 v[210:213], v174 offset:1152
	ds_read_b128 v[214:217], v174 offset:34176
	ds_read_b128 v[218:221], v175 offset:1152
	ds_read_b128 v[222:225], v175 offset:34176
	ds_read_b128 v[226:229], v174 offset:1216
	v_lshlrev_b32_e32 v147, 16, v57
	v_mul_f32_e32 v149, v149, v149
	s_waitcnt lgkmcnt(4)
	v_mfma_f32_16x16x32_bf16 v[134:137], v[54:57], v[210:213], v[134:137]
	v_fmac_f32_e32 v149, v147, v147
	v_add_f32_e32 v145, v149, v145
	s_waitcnt vmcnt(12)
	v_and_b32_e32 v149, 0xffff0000, v50
	s_waitcnt lgkmcnt(3)
	v_mfma_f32_16x16x32_bf16 v[130:133], v[54:57], v[214:217], v[130:133]
	v_lshlrev_b32_e32 v147, 16, v50
	v_mul_f32_e32 v149, v149, v149
	v_fmac_f32_e32 v149, v147, v147
	s_waitcnt lgkmcnt(2)
	v_mfma_f32_16x16x32_bf16 v[134:137], v[54:57], v[218:221], v[134:137]
	ds_read_b128 v[218:221], v174 offset:34240
	ds_read_b128 v[214:217], v175 offset:34240
	v_add_f32_e32 v145, v149, v145
	v_and_b32_e32 v149, 0xffff0000, v51
	s_waitcnt lgkmcnt(3)
	v_mfma_f32_16x16x32_bf16 v[130:133], v[54:57], v[222:225], v[130:133]
	v_lshlrev_b32_e32 v147, 16, v51
	v_mul_f32_e32 v149, v149, v149
	v_fmac_f32_e32 v149, v147, v147
	v_add_f32_e32 v145, v149, v145
	v_and_b32_e32 v149, 0xffff0000, v52
	ds_read_b128 v[210:213], v175 offset:1216
	v_lshlrev_b32_e32 v147, 16, v52
	v_mul_f32_e32 v149, v149, v149
	s_waitcnt lgkmcnt(3)
	v_mfma_f32_16x16x32_bf16 v[134:137], v[50:53], v[226:229], v[134:137]
	v_fmac_f32_e32 v149, v147, v147
	v_add_f32_e32 v145, v149, v145
	v_and_b32_e32 v149, 0xffff0000, v53
	s_waitcnt lgkmcnt(2)
	v_mfma_f32_16x16x32_bf16 v[130:133], v[50:53], v[218:221], v[130:133]
	v_lshlrev_b32_e32 v147, 16, v53
	v_mul_f32_e32 v149, v149, v149
	v_fmac_f32_e32 v149, v147, v147
	s_waitcnt lgkmcnt(0)
	v_mfma_f32_16x16x32_bf16 v[134:137], v[50:53], v[210:213], v[134:137]
	v_add_f32_e32 v145, v149, v145
	v_mfma_f32_16x16x32_bf16 v[130:133], v[50:53], v[214:217], v[130:133]
	s_waitcnt vmcnt(11)
	v_and_b32_e32 v149, 0xffff0000, v46
	v_lshlrev_b32_e32 v147, 16, v46
	v_mul_f32_e32 v149, v149, v149
	v_fmac_f32_e32 v149, v147, v147
	v_add_f32_e32 v145, v149, v145
	v_and_b32_e32 v149, 0xffff0000, v47
	v_lshlrev_b32_e32 v147, 16, v47
	v_mul_f32_e32 v149, v149, v149
	v_fmac_f32_e32 v149, v147, v147
	v_add_f32_e32 v145, v149, v145
	v_and_b32_e32 v149, 0xffff0000, v48
	v_lshlrev_b32_e32 v147, 16, v48
	v_mul_f32_e32 v149, v149, v149
	v_fmac_f32_e32 v149, v147, v147
	v_add_f32_e32 v145, v149, v145
	v_and_b32_e32 v149, 0xffff0000, v49
	ds_read_b128 v[210:213], v174 offset:1280
	ds_read_b128 v[214:217], v174 offset:34304
	ds_read_b128 v[218:221], v175 offset:1280
	ds_read_b128 v[222:225], v175 offset:34304
	ds_read_b128 v[226:229], v174 offset:1344
	v_lshlrev_b32_e32 v147, 16, v49
	v_mul_f32_e32 v149, v149, v149
	s_waitcnt lgkmcnt(4)
	v_mfma_f32_16x16x32_bf16 v[134:137], v[46:49], v[210:213], v[134:137]
	v_fmac_f32_e32 v149, v147, v147
	v_add_f32_e32 v145, v149, v145
	s_waitcnt vmcnt(10)
	v_and_b32_e32 v149, 0xffff0000, v42
	s_waitcnt lgkmcnt(3)
	v_mfma_f32_16x16x32_bf16 v[130:133], v[46:49], v[214:217], v[130:133]
	v_lshlrev_b32_e32 v147, 16, v42
	v_mul_f32_e32 v149, v149, v149
	v_fmac_f32_e32 v149, v147, v147
	s_waitcnt lgkmcnt(2)
	v_mfma_f32_16x16x32_bf16 v[134:137], v[46:49], v[218:221], v[134:137]
	ds_read_b128 v[218:221], v174 offset:34368
	ds_read_b128 v[214:217], v175 offset:34368
	v_add_f32_e32 v145, v149, v145
	v_and_b32_e32 v149, 0xffff0000, v43
	s_waitcnt lgkmcnt(3)
	v_mfma_f32_16x16x32_bf16 v[130:133], v[46:49], v[222:225], v[130:133]
	v_lshlrev_b32_e32 v147, 16, v43
	v_mul_f32_e32 v149, v149, v149
	v_fmac_f32_e32 v149, v147, v147
	v_add_f32_e32 v145, v149, v145
	v_and_b32_e32 v149, 0xffff0000, v44
	ds_read_b128 v[210:213], v175 offset:1344
	v_lshlrev_b32_e32 v147, 16, v44
	v_mul_f32_e32 v149, v149, v149
	s_waitcnt lgkmcnt(3)
	v_mfma_f32_16x16x32_bf16 v[134:137], v[42:45], v[226:229], v[134:137]
	v_fmac_f32_e32 v149, v147, v147
	v_add_f32_e32 v145, v149, v145
	v_and_b32_e32 v149, 0xffff0000, v45
	s_waitcnt lgkmcnt(2)
	v_mfma_f32_16x16x32_bf16 v[130:133], v[42:45], v[218:221], v[130:133]
	v_lshlrev_b32_e32 v147, 16, v45
	v_mul_f32_e32 v149, v149, v149
	v_fmac_f32_e32 v149, v147, v147
	s_waitcnt lgkmcnt(0)
	v_mfma_f32_16x16x32_bf16 v[134:137], v[42:45], v[210:213], v[134:137]
	v_add_f32_e32 v145, v149, v145
	v_mfma_f32_16x16x32_bf16 v[130:133], v[42:45], v[214:217], v[130:133]
	s_waitcnt vmcnt(9)
	v_and_b32_e32 v149, 0xffff0000, v38
	v_lshlrev_b32_e32 v147, 16, v38
	v_mul_f32_e32 v149, v149, v149
	v_fmac_f32_e32 v149, v147, v147
	v_add_f32_e32 v145, v149, v145
	v_and_b32_e32 v149, 0xffff0000, v39
	v_lshlrev_b32_e32 v147, 16, v39
	v_mul_f32_e32 v149, v149, v149
	v_fmac_f32_e32 v149, v147, v147
	v_add_f32_e32 v145, v149, v145
	v_and_b32_e32 v149, 0xffff0000, v40
	v_lshlrev_b32_e32 v147, 16, v40
	v_mul_f32_e32 v149, v149, v149
	v_fmac_f32_e32 v149, v147, v147
	v_add_f32_e32 v145, v149, v145
	v_and_b32_e32 v149, 0xffff0000, v41
	ds_read_b128 v[210:213], v174 offset:1408
	ds_read_b128 v[214:217], v174 offset:34432
	ds_read_b128 v[218:221], v175 offset:1408
	ds_read_b128 v[222:225], v175 offset:34432
	ds_read_b128 v[226:229], v174 offset:1472
	v_lshlrev_b32_e32 v147, 16, v41
	v_mul_f32_e32 v149, v149, v149
	s_waitcnt lgkmcnt(4)
	v_mfma_f32_16x16x32_bf16 v[134:137], v[38:41], v[210:213], v[134:137]
	v_fmac_f32_e32 v149, v147, v147
	v_add_f32_e32 v145, v149, v145
	s_waitcnt vmcnt(8)
	v_and_b32_e32 v149, 0xffff0000, v34
	s_waitcnt lgkmcnt(3)
	v_mfma_f32_16x16x32_bf16 v[130:133], v[38:41], v[214:217], v[130:133]
	v_lshlrev_b32_e32 v147, 16, v34
	v_mul_f32_e32 v149, v149, v149
	v_fmac_f32_e32 v149, v147, v147
	s_waitcnt lgkmcnt(2)
	v_mfma_f32_16x16x32_bf16 v[134:137], v[38:41], v[218:221], v[134:137]
	ds_read_b128 v[218:221], v174 offset:34496
	ds_read_b128 v[214:217], v175 offset:34496
	v_add_f32_e32 v145, v149, v145
	v_and_b32_e32 v149, 0xffff0000, v35
	s_waitcnt lgkmcnt(3)
	v_mfma_f32_16x16x32_bf16 v[130:133], v[38:41], v[222:225], v[130:133]
	v_lshlrev_b32_e32 v147, 16, v35
	v_mul_f32_e32 v149, v149, v149
	v_fmac_f32_e32 v149, v147, v147
	v_add_f32_e32 v145, v149, v145
	v_and_b32_e32 v149, 0xffff0000, v36
	ds_read_b128 v[210:213], v175 offset:1472
	v_lshlrev_b32_e32 v147, 16, v36
	v_mul_f32_e32 v149, v149, v149
	s_waitcnt lgkmcnt(3)
	v_mfma_f32_16x16x32_bf16 v[134:137], v[34:37], v[226:229], v[134:137]
	v_fmac_f32_e32 v149, v147, v147
	v_add_f32_e32 v145, v149, v145
	v_and_b32_e32 v149, 0xffff0000, v37
	s_waitcnt lgkmcnt(2)
	v_mfma_f32_16x16x32_bf16 v[130:133], v[34:37], v[218:221], v[130:133]
	v_lshlrev_b32_e32 v147, 16, v37
	v_mul_f32_e32 v149, v149, v149
	v_fmac_f32_e32 v149, v147, v147
	s_waitcnt lgkmcnt(0)
	v_mfma_f32_16x16x32_bf16 v[134:137], v[34:37], v[210:213], v[134:137]
	v_add_f32_e32 v145, v149, v145
	v_mfma_f32_16x16x32_bf16 v[130:133], v[34:37], v[214:217], v[130:133]
	s_waitcnt vmcnt(7)
	v_and_b32_e32 v149, 0xffff0000, v30
	v_lshlrev_b32_e32 v147, 16, v30
	v_mul_f32_e32 v149, v149, v149
	v_fmac_f32_e32 v149, v147, v147
	v_add_f32_e32 v145, v149, v145
	v_and_b32_e32 v149, 0xffff0000, v31
	v_lshlrev_b32_e32 v147, 16, v31
	v_mul_f32_e32 v149, v149, v149
	v_fmac_f32_e32 v149, v147, v147
	v_add_f32_e32 v145, v149, v145
	v_and_b32_e32 v149, 0xffff0000, v32
	v_lshlrev_b32_e32 v147, 16, v32
	v_mul_f32_e32 v149, v149, v149
	v_fmac_f32_e32 v149, v147, v147
	v_add_f32_e32 v145, v149, v145
	v_and_b32_e32 v149, 0xffff0000, v33
	ds_read_b128 v[210:213], v174 offset:1536
	ds_read_b128 v[214:217], v174 offset:34560
	ds_read_b128 v[218:221], v175 offset:1536
	ds_read_b128 v[222:225], v175 offset:34560
	ds_read_b128 v[226:229], v174 offset:1600
	v_lshlrev_b32_e32 v147, 16, v33
	v_mul_f32_e32 v149, v149, v149
	s_waitcnt lgkmcnt(4)
	v_mfma_f32_16x16x32_bf16 v[134:137], v[30:33], v[210:213], v[134:137]
	v_fmac_f32_e32 v149, v147, v147
	v_add_f32_e32 v145, v149, v145
	s_waitcnt vmcnt(6)
	v_and_b32_e32 v149, 0xffff0000, v26
	s_waitcnt lgkmcnt(3)
	v_mfma_f32_16x16x32_bf16 v[130:133], v[30:33], v[214:217], v[130:133]
	v_lshlrev_b32_e32 v147, 16, v26
	v_mul_f32_e32 v149, v149, v149
	v_fmac_f32_e32 v149, v147, v147
	s_waitcnt lgkmcnt(2)
	v_mfma_f32_16x16x32_bf16 v[134:137], v[30:33], v[218:221], v[134:137]
	ds_read_b128 v[218:221], v174 offset:34624
	ds_read_b128 v[214:217], v175 offset:34624
	v_add_f32_e32 v145, v149, v145
	v_and_b32_e32 v149, 0xffff0000, v27
	s_waitcnt lgkmcnt(3)
	v_mfma_f32_16x16x32_bf16 v[130:133], v[30:33], v[222:225], v[130:133]
	v_lshlrev_b32_e32 v147, 16, v27
	v_mul_f32_e32 v149, v149, v149
	v_fmac_f32_e32 v149, v147, v147
	v_add_f32_e32 v145, v149, v145
	v_and_b32_e32 v149, 0xffff0000, v28
	ds_read_b128 v[210:213], v175 offset:1600
	v_lshlrev_b32_e32 v147, 16, v28
	v_mul_f32_e32 v149, v149, v149
	s_waitcnt lgkmcnt(3)
	v_mfma_f32_16x16x32_bf16 v[134:137], v[26:29], v[226:229], v[134:137]
	v_fmac_f32_e32 v149, v147, v147
	v_add_f32_e32 v145, v149, v145
	v_and_b32_e32 v149, 0xffff0000, v29
	s_waitcnt lgkmcnt(2)
	v_mfma_f32_16x16x32_bf16 v[130:133], v[26:29], v[218:221], v[130:133]
	v_lshlrev_b32_e32 v147, 16, v29
	v_mul_f32_e32 v149, v149, v149
	v_fmac_f32_e32 v149, v147, v147
	s_waitcnt lgkmcnt(0)
	v_mfma_f32_16x16x32_bf16 v[134:137], v[26:29], v[210:213], v[134:137]
	v_add_f32_e32 v145, v149, v145
	v_mfma_f32_16x16x32_bf16 v[130:133], v[26:29], v[214:217], v[130:133]
	s_waitcnt vmcnt(5)
	v_and_b32_e32 v149, 0xffff0000, v22
	v_lshlrev_b32_e32 v147, 16, v22
	v_mul_f32_e32 v149, v149, v149
	v_fmac_f32_e32 v149, v147, v147
	v_add_f32_e32 v145, v149, v145
	v_and_b32_e32 v149, 0xffff0000, v23
	v_lshlrev_b32_e32 v147, 16, v23
	v_mul_f32_e32 v149, v149, v149
	v_fmac_f32_e32 v149, v147, v147
	v_add_f32_e32 v145, v149, v145
	v_and_b32_e32 v149, 0xffff0000, v24
	v_lshlrev_b32_e32 v147, 16, v24
	v_mul_f32_e32 v149, v149, v149
	v_fmac_f32_e32 v149, v147, v147
	v_add_f32_e32 v145, v149, v145
	v_and_b32_e32 v149, 0xffff0000, v25
	ds_read_b128 v[210:213], v174 offset:1664
	ds_read_b128 v[214:217], v174 offset:34688
	ds_read_b128 v[218:221], v175 offset:1664
	ds_read_b128 v[222:225], v175 offset:34688
	ds_read_b128 v[226:229], v174 offset:1728
	v_lshlrev_b32_e32 v147, 16, v25
	v_mul_f32_e32 v149, v149, v149
	s_waitcnt lgkmcnt(4)
	v_mfma_f32_16x16x32_bf16 v[134:137], v[22:25], v[210:213], v[134:137]
	v_fmac_f32_e32 v149, v147, v147
	v_add_f32_e32 v145, v149, v145
	s_waitcnt vmcnt(4)
	v_and_b32_e32 v149, 0xffff0000, v18
	s_waitcnt lgkmcnt(3)
	v_mfma_f32_16x16x32_bf16 v[130:133], v[22:25], v[214:217], v[130:133]
	v_lshlrev_b32_e32 v147, 16, v18
	v_mul_f32_e32 v149, v149, v149
	v_fmac_f32_e32 v149, v147, v147
	s_waitcnt lgkmcnt(2)
	v_mfma_f32_16x16x32_bf16 v[134:137], v[22:25], v[218:221], v[134:137]
	ds_read_b128 v[218:221], v174 offset:34752
	ds_read_b128 v[214:217], v175 offset:34752
	v_add_f32_e32 v145, v149, v145
	v_and_b32_e32 v149, 0xffff0000, v19
	s_waitcnt lgkmcnt(3)
	v_mfma_f32_16x16x32_bf16 v[130:133], v[22:25], v[222:225], v[130:133]
	v_lshlrev_b32_e32 v147, 16, v19
	v_mul_f32_e32 v149, v149, v149
	v_fmac_f32_e32 v149, v147, v147
	v_add_f32_e32 v145, v149, v145
	v_and_b32_e32 v149, 0xffff0000, v20
	ds_read_b128 v[210:213], v175 offset:1728
	v_lshlrev_b32_e32 v147, 16, v20
	v_mul_f32_e32 v149, v149, v149
	s_waitcnt lgkmcnt(3)
	v_mfma_f32_16x16x32_bf16 v[134:137], v[18:21], v[226:229], v[134:137]
	v_fmac_f32_e32 v149, v147, v147
	v_add_f32_e32 v145, v149, v145
	v_and_b32_e32 v149, 0xffff0000, v21
	s_waitcnt lgkmcnt(2)
	v_mfma_f32_16x16x32_bf16 v[130:133], v[18:21], v[218:221], v[130:133]
	v_lshlrev_b32_e32 v147, 16, v21
	v_mul_f32_e32 v149, v149, v149
	v_fmac_f32_e32 v149, v147, v147
	s_waitcnt lgkmcnt(0)
	v_mfma_f32_16x16x32_bf16 v[134:137], v[18:21], v[210:213], v[134:137]
	v_add_f32_e32 v145, v149, v145
	v_mfma_f32_16x16x32_bf16 v[130:133], v[18:21], v[214:217], v[130:133]
	s_waitcnt vmcnt(3)
	v_and_b32_e32 v149, 0xffff0000, v14
	v_lshlrev_b32_e32 v147, 16, v14
	v_mul_f32_e32 v149, v149, v149
	v_fmac_f32_e32 v149, v147, v147
	v_add_f32_e32 v145, v149, v145
	v_and_b32_e32 v149, 0xffff0000, v15
	v_lshlrev_b32_e32 v147, 16, v15
	v_mul_f32_e32 v149, v149, v149
	v_fmac_f32_e32 v149, v147, v147
	v_add_f32_e32 v145, v149, v145
	v_and_b32_e32 v149, 0xffff0000, v16
	v_lshlrev_b32_e32 v147, 16, v16
	v_mul_f32_e32 v149, v149, v149
	v_fmac_f32_e32 v149, v147, v147
	v_add_f32_e32 v145, v149, v145
	v_and_b32_e32 v149, 0xffff0000, v17
	ds_read_b128 v[210:213], v174 offset:1792
	ds_read_b128 v[214:217], v174 offset:34816
	ds_read_b128 v[218:221], v175 offset:1792
	ds_read_b128 v[222:225], v175 offset:34816
	ds_read_b128 v[226:229], v174 offset:1856
	v_lshlrev_b32_e32 v147, 16, v17
	v_mul_f32_e32 v149, v149, v149
	s_waitcnt lgkmcnt(4)
	v_mfma_f32_16x16x32_bf16 v[134:137], v[14:17], v[210:213], v[134:137]
	v_fmac_f32_e32 v149, v147, v147
	v_add_f32_e32 v145, v149, v145
	s_waitcnt vmcnt(2)
	v_and_b32_e32 v149, 0xffff0000, v10
	s_waitcnt lgkmcnt(3)
	v_mfma_f32_16x16x32_bf16 v[130:133], v[14:17], v[214:217], v[130:133]
	v_lshlrev_b32_e32 v147, 16, v10
	v_mul_f32_e32 v149, v149, v149
	v_fmac_f32_e32 v149, v147, v147
	s_waitcnt lgkmcnt(2)
	v_mfma_f32_16x16x32_bf16 v[134:137], v[14:17], v[218:221], v[134:137]
	ds_read_b128 v[218:221], v174 offset:34880
	ds_read_b128 v[214:217], v175 offset:34880
	v_add_f32_e32 v145, v149, v145
	v_and_b32_e32 v149, 0xffff0000, v11
	s_waitcnt lgkmcnt(3)
	v_mfma_f32_16x16x32_bf16 v[130:133], v[14:17], v[222:225], v[130:133]
	v_lshlrev_b32_e32 v147, 16, v11
	v_mul_f32_e32 v149, v149, v149
	v_fmac_f32_e32 v149, v147, v147
	v_add_f32_e32 v145, v149, v145
	v_and_b32_e32 v149, 0xffff0000, v12
	ds_read_b128 v[210:213], v175 offset:1856
	v_lshlrev_b32_e32 v147, 16, v12
	v_mul_f32_e32 v149, v149, v149
	s_waitcnt lgkmcnt(3)
	v_mfma_f32_16x16x32_bf16 v[134:137], v[10:13], v[226:229], v[134:137]
	v_fmac_f32_e32 v149, v147, v147
	v_add_f32_e32 v145, v149, v145
	v_and_b32_e32 v149, 0xffff0000, v13
	s_waitcnt lgkmcnt(2)
	v_mfma_f32_16x16x32_bf16 v[130:133], v[10:13], v[218:221], v[130:133]
	v_lshlrev_b32_e32 v147, 16, v13
	v_mul_f32_e32 v149, v149, v149
	v_fmac_f32_e32 v149, v147, v147
	s_waitcnt lgkmcnt(0)
	v_mfma_f32_16x16x32_bf16 v[134:137], v[10:13], v[210:213], v[134:137]
	v_add_f32_e32 v145, v149, v145
	v_mfma_f32_16x16x32_bf16 v[130:133], v[10:13], v[214:217], v[130:133]
	s_waitcnt vmcnt(1)
	v_and_b32_e32 v149, 0xffff0000, v6
	ds_read_b128 v[210:213], v174 offset:1920
	ds_read_b128 v[214:217], v174 offset:34944
	ds_read_b128 v[218:221], v175 offset:1920
	ds_read_b128 v[222:225], v175 offset:34944
	ds_read_b128 v[226:229], v174 offset:1984
	v_lshlrev_b32_e32 v147, 16, v6
	v_mul_f32_e32 v149, v149, v149
	s_waitcnt lgkmcnt(4)
	v_mfma_f32_16x16x32_bf16 v[134:137], v[6:9], v[210:213], v[134:137]
	v_fmac_f32_e32 v149, v147, v147
	v_add_f32_e32 v145, v149, v145
	v_and_b32_e32 v149, 0xffff0000, v7
	v_lshlrev_b32_e32 v147, 16, v7
	v_mul_f32_e32 v149, v149, v149
	v_fmac_f32_e32 v149, v147, v147
	s_waitcnt lgkmcnt(2)
	v_mfma_f32_16x16x32_bf16 v[134:137], v[6:9], v[218:221], v[134:137]
	v_add_f32_e32 v145, v149, v145
	v_and_b32_e32 v149, 0xffff0000, v8
	v_lshlrev_b32_e32 v147, 16, v8
	v_mfma_f32_16x16x32_bf16 v[130:133], v[6:9], v[214:217], v[130:133]
	v_mul_f32_e32 v149, v149, v149
	v_fmac_f32_e32 v149, v147, v147
	v_add_f32_e32 v145, v149, v145
	v_and_b32_e32 v149, 0xffff0000, v9
	s_waitcnt lgkmcnt(1)
	v_mfma_f32_16x16x32_bf16 v[222:225], v[6:9], v[222:225], v[130:133]
	v_lshlrev_b32_e32 v147, 16, v9
	ds_read_b128 v[218:221], v174 offset:35008
	ds_read_b128 v[214:217], v175 offset:35008
	s_waitcnt vmcnt(0) lgkmcnt(2)
	v_mfma_f32_16x16x32_bf16 v[130:133], v[2:5], v[226:229], v[134:137]
	ds_read_b128 v[210:213], v175 offset:1984
	s_nop 1
	v_mul_f32_e32 v134, v149, v149
	v_and_b32_e32 v136, 0xffff0000, v2
	v_fmac_f32_e32 v134, v147, v147
	v_lshlrev_b32_e32 v135, 16, v2
	v_mul_f32_e32 v136, v136, v136
	v_add_f32_e32 v134, v134, v145
	v_fmac_f32_e32 v136, v135, v135
	v_add_f32_e32 v134, v136, v134
	v_and_b32_e32 v136, 0xffff0000, v3
	v_lshlrev_b32_e32 v135, 16, v3
	v_mul_f32_e32 v136, v136, v136
	v_fmac_f32_e32 v136, v135, v135
	v_add_f32_e32 v134, v136, v134
	v_and_b32_e32 v136, 0xffff0000, v4
	v_lshlrev_b32_e32 v135, 16, v4
	v_mul_f32_e32 v136, v136, v136
	v_fmac_f32_e32 v136, v135, v135
	v_add_f32_e32 v145, v136, v134
	s_waitcnt lgkmcnt(2)
	v_mfma_f32_16x16x32_bf16 v[134:137], v[2:5], v[218:221], v[222:225]
	v_and_b32_e32 v149, 0xffff0000, v5
	v_lshlrev_b32_e32 v147, 16, v5
	v_mul_f32_e32 v149, v149, v149
	v_fmac_f32_e32 v149, v147, v147
	s_waitcnt lgkmcnt(0)
	v_mfma_f32_16x16x32_bf16 v[130:133], v[2:5], v[210:213], v[130:133]
	v_add_f32_e32 v145, v149, v145
	v_mfma_f32_16x16x32_bf16 v[134:137], v[2:5], v[214:217], v[134:137]
	ds_bpermute_b32 v147, v192, v145
	v_lshlrev_b32_e32 v149, 16, v126
	v_and_b32_e32 v126, 0xffff0000, v126
	s_waitcnt lgkmcnt(0)
	v_add_f32_e32 v145, v145, v147
	ds_bpermute_b32 v147, v193, v145
	s_waitcnt lgkmcnt(0)
	v_add_f32_e32 v145, v145, v147
	v_fmamk_f32 v145, v145, 0x3a800000, v195
	v_mul_f32_e32 v147, 0x4f800000, v145
	v_cmp_gt_f32_e32 vcc, s25, v145
	s_nop 1
	v_cndmask_b32_e32 v145, v145, v147, vcc
	v_sqrt_f32_e32 v147, v145
	s_nop 0
	v_add_u32_e32 v151, -1, v147
	v_add_u32_e32 v153, 1, v147
	v_fma_f32 v155, -v151, v147, v145
	v_fma_f32 v157, -v153, v147, v145
	v_cmp_ge_f32_e64 s[8:9], 0, v155
	s_nop 1
	v_cndmask_b32_e64 v147, v147, v151, s[8:9]
	v_cmp_lt_f32_e64 s[8:9], 0, v157
	s_nop 1
	v_cndmask_b32_e64 v147, v147, v153, s[8:9]
	v_mul_f32_e32 v151, 0x37800000, v147
	v_cndmask_b32_e32 v147, v147, v151, vcc
	v_cmp_class_f32_e32 vcc, v145, v196
	s_nop 1
	v_cndmask_b32_e32 v145, v147, v145, vcc
	v_div_scale_f32 v147, s[8:9], v145, v145, 1.0
	v_rcp_f32_e32 v151, v147
	v_div_scale_f32 v153, vcc, 1.0, v145, 1.0
	v_fma_f32 v155, -v147, v151, 1.0
	v_fmac_f32_e32 v151, v155, v151
	v_mul_f32_e32 v155, v153, v151
	v_fma_f32 v157, -v147, v155, v153
	v_fmac_f32_e32 v155, v157, v151
	v_fma_f32 v147, -v147, v155, v153
	v_div_fmas_f32 v147, v147, v151, v155
	v_div_fixup_f32 v145, v147, v145, 1.0
	v_mul_f32_e32 v147, 0x41800000, v145
	v_mul_f32_e32 v149, v147, v149
	v_mul_f32_e32 v126, v147, v126
	v_cvt_pk_fp8_f32 v168, v149, v126
	v_lshlrev_b32_e32 v151, 16, v127
	v_and_b32_e32 v127, 0xffff0000, v127
	v_mul_f32_e32 v126, v147, v151
	v_mul_f32_e32 v127, v147, v127
	v_cvt_pk_fp8_f32 v168, v126, v127 op_sel:[0,0,1]
	v_lshlrev_b32_e32 v126, 16, v128
	v_and_b32_e32 v127, 0xffff0000, v128
	v_mul_f32_e32 v126, v147, v126
	v_mul_f32_e32 v127, v147, v127
	v_cvt_pk_fp8_f32 v169, v126, v127
	v_lshlrev_b32_e32 v128, 16, v129
	v_and_b32_e32 v127, 0xffff0000, v129
	v_mul_f32_e32 v126, v147, v128
	v_mul_f32_e32 v127, v147, v127
	v_cvt_pk_fp8_f32 v169, v126, v127 op_sel:[0,0,1]
	v_lshl_add_u64 v[126:127], v[142:143], 0, v[166:167]
	global_store_dwordx2 v[126:127], v[168:169], off
	s_nop 0
	v_lshlrev_b32_e32 v128, 16, v122
	v_and_b32_e32 v122, 0xffff0000, v122
	v_mul_f32_e32 v128, v147, v128
	v_mul_f32_e32 v129, v147, v122
	v_cvt_pk_fp8_f32 v122, v128, v129
	v_lshlrev_b32_e32 v149, 16, v123
	v_and_b32_e32 v123, 0xffff0000, v123
	v_mul_f32_e32 v128, v147, v149
	v_mul_f32_e32 v123, v147, v123
	v_cvt_pk_fp8_f32 v122, v128, v123 op_sel:[0,0,1]
	v_lshlrev_b32_e32 v123, 16, v124
	v_mul_f32_e32 v128, v147, v123
	v_and_b32_e32 v123, 0xffff0000, v124
	v_mul_f32_e32 v124, v147, v123
	v_cvt_pk_fp8_f32 v123, v128, v124
	v_lshlrev_b32_e32 v129, 16, v125
	v_and_b32_e32 v125, 0xffff0000, v125
	v_mul_f32_e32 v124, v147, v129
	v_mul_f32_e32 v125, v147, v125
	v_cvt_pk_fp8_f32 v123, v124, v125 op_sel:[0,0,1]
	global_store_dwordx2 v[126:127], v[122:123], off offset:32
	s_nop 0
	v_lshlrev_b32_e32 v122, 16, v118
	v_and_b32_e32 v118, 0xffff0000, v118
	v_mul_f32_e32 v122, v147, v122
	v_mul_f32_e32 v123, v147, v118
	v_cvt_pk_fp8_f32 v118, v122, v123
	v_lshlrev_b32_e32 v124, 16, v119
	v_and_b32_e32 v119, 0xffff0000, v119
	v_mul_f32_e32 v122, v147, v124
	v_mul_f32_e32 v119, v147, v119
	v_cvt_pk_fp8_f32 v118, v122, v119 op_sel:[0,0,1]
	v_lshlrev_b32_e32 v119, 16, v120
	v_mul_f32_e32 v122, v147, v119
	v_and_b32_e32 v119, 0xffff0000, v120
	v_mul_f32_e32 v120, v147, v119
	v_cvt_pk_fp8_f32 v119, v122, v120
	v_lshlrev_b32_e32 v123, 16, v121
	v_and_b32_e32 v121, 0xffff0000, v121
	v_mul_f32_e32 v120, v147, v123
	v_mul_f32_e32 v121, v147, v121
	v_cvt_pk_fp8_f32 v119, v120, v121 op_sel:[0,0,1]
	global_store_dwordx2 v[126:127], v[118:119], off offset:64
	s_nop 0
	v_lshlrev_b32_e32 v118, 16, v114
	v_and_b32_e32 v114, 0xffff0000, v114
	v_mul_f32_e32 v118, v147, v118
	v_mul_f32_e32 v119, v147, v114
	v_cvt_pk_fp8_f32 v114, v118, v119
	v_lshlrev_b32_e32 v120, 16, v115
	v_and_b32_e32 v115, 0xffff0000, v115
	v_mul_f32_e32 v118, v147, v120
	v_mul_f32_e32 v115, v147, v115
	v_cvt_pk_fp8_f32 v114, v118, v115 op_sel:[0,0,1]
	v_lshlrev_b32_e32 v115, 16, v116
	v_mul_f32_e32 v118, v147, v115
	v_and_b32_e32 v115, 0xffff0000, v116
	v_mul_f32_e32 v116, v147, v115
	v_cvt_pk_fp8_f32 v115, v118, v116
	v_lshlrev_b32_e32 v119, 16, v117
	v_and_b32_e32 v117, 0xffff0000, v117
	v_mul_f32_e32 v116, v147, v119
	v_mul_f32_e32 v117, v147, v117
	v_cvt_pk_fp8_f32 v115, v116, v117 op_sel:[0,0,1]
	global_store_dwordx2 v[126:127], v[114:115], off offset:96
	s_nop 0
	v_lshlrev_b32_e32 v114, 16, v110
	v_and_b32_e32 v110, 0xffff0000, v110
	v_mul_f32_e32 v114, v147, v114
	v_mul_f32_e32 v115, v147, v110
	v_cvt_pk_fp8_f32 v110, v114, v115
	v_lshlrev_b32_e32 v116, 16, v111
	v_and_b32_e32 v111, 0xffff0000, v111
	v_mul_f32_e32 v114, v147, v116
	v_mul_f32_e32 v111, v147, v111
	v_cvt_pk_fp8_f32 v110, v114, v111 op_sel:[0,0,1]
	v_lshlrev_b32_e32 v111, 16, v112
	v_mul_f32_e32 v114, v147, v111
	v_and_b32_e32 v111, 0xffff0000, v112
	v_mul_f32_e32 v112, v147, v111
	v_cvt_pk_fp8_f32 v111, v114, v112
	v_lshlrev_b32_e32 v115, 16, v113
	v_and_b32_e32 v113, 0xffff0000, v113
	v_mul_f32_e32 v112, v147, v115
	v_mul_f32_e32 v113, v147, v113
	v_cvt_pk_fp8_f32 v111, v112, v113 op_sel:[0,0,1]
	global_store_dwordx2 v[126:127], v[110:111], off offset:128
	s_nop 0
	v_lshlrev_b32_e32 v110, 16, v106
	v_and_b32_e32 v106, 0xffff0000, v106
	v_mul_f32_e32 v110, v147, v110
	v_mul_f32_e32 v111, v147, v106
	v_cvt_pk_fp8_f32 v106, v110, v111
	v_lshlrev_b32_e32 v112, 16, v107
	v_and_b32_e32 v107, 0xffff0000, v107
	v_mul_f32_e32 v110, v147, v112
	v_mul_f32_e32 v107, v147, v107
	v_cvt_pk_fp8_f32 v106, v110, v107 op_sel:[0,0,1]
	v_lshlrev_b32_e32 v107, 16, v108
	v_mul_f32_e32 v110, v147, v107
	v_and_b32_e32 v107, 0xffff0000, v108
	v_mul_f32_e32 v108, v147, v107
	v_cvt_pk_fp8_f32 v107, v110, v108
	v_lshlrev_b32_e32 v111, 16, v109
	v_and_b32_e32 v109, 0xffff0000, v109
	v_mul_f32_e32 v108, v147, v111
	v_mul_f32_e32 v109, v147, v109
	v_cvt_pk_fp8_f32 v107, v108, v109 op_sel:[0,0,1]
	global_store_dwordx2 v[126:127], v[106:107], off offset:160
	s_nop 0
	v_lshlrev_b32_e32 v106, 16, v102
	v_and_b32_e32 v102, 0xffff0000, v102
	v_mul_f32_e32 v106, v147, v106
	v_mul_f32_e32 v107, v147, v102
	v_cvt_pk_fp8_f32 v102, v106, v107
	v_lshlrev_b32_e32 v108, 16, v103
	v_and_b32_e32 v103, 0xffff0000, v103
	v_mul_f32_e32 v106, v147, v108
	v_mul_f32_e32 v103, v147, v103
	v_cvt_pk_fp8_f32 v102, v106, v103 op_sel:[0,0,1]
	v_lshlrev_b32_e32 v103, 16, v104
	v_mul_f32_e32 v106, v147, v103
	v_and_b32_e32 v103, 0xffff0000, v104
	v_mul_f32_e32 v104, v147, v103
	v_cvt_pk_fp8_f32 v103, v106, v104
	v_lshlrev_b32_e32 v107, 16, v105
	v_and_b32_e32 v105, 0xffff0000, v105
	v_mul_f32_e32 v104, v147, v107
	v_mul_f32_e32 v105, v147, v105
	v_cvt_pk_fp8_f32 v103, v104, v105 op_sel:[0,0,1]
	global_store_dwordx2 v[126:127], v[102:103], off offset:192
	s_nop 0
	v_lshlrev_b32_e32 v102, 16, v98
	v_and_b32_e32 v98, 0xffff0000, v98
	v_mul_f32_e32 v102, v147, v102
	v_mul_f32_e32 v103, v147, v98
	v_cvt_pk_fp8_f32 v98, v102, v103
	v_lshlrev_b32_e32 v104, 16, v99
	v_and_b32_e32 v99, 0xffff0000, v99
	v_mul_f32_e32 v102, v147, v104
	v_mul_f32_e32 v99, v147, v99
	v_cvt_pk_fp8_f32 v98, v102, v99 op_sel:[0,0,1]
	v_lshlrev_b32_e32 v99, 16, v100
	v_mul_f32_e32 v102, v147, v99
	v_and_b32_e32 v99, 0xffff0000, v100
	v_mul_f32_e32 v100, v147, v99
	v_cvt_pk_fp8_f32 v99, v102, v100
	v_lshlrev_b32_e32 v103, 16, v101
	v_and_b32_e32 v101, 0xffff0000, v101
	v_mul_f32_e32 v100, v147, v103
	v_mul_f32_e32 v101, v147, v101
	v_cvt_pk_fp8_f32 v99, v100, v101 op_sel:[0,0,1]
	global_store_dwordx2 v[126:127], v[98:99], off offset:224
	s_nop 0
	v_lshlrev_b32_e32 v98, 16, v94
	v_and_b32_e32 v94, 0xffff0000, v94
	v_mul_f32_e32 v98, v147, v98
	v_mul_f32_e32 v99, v147, v94
	v_cvt_pk_fp8_f32 v94, v98, v99
	v_lshlrev_b32_e32 v100, 16, v95
	v_and_b32_e32 v95, 0xffff0000, v95
	v_mul_f32_e32 v98, v147, v100
	v_mul_f32_e32 v95, v147, v95
	v_cvt_pk_fp8_f32 v94, v98, v95 op_sel:[0,0,1]
	v_lshlrev_b32_e32 v95, 16, v96
	v_mul_f32_e32 v98, v147, v95
	v_and_b32_e32 v95, 0xffff0000, v96
	v_mul_f32_e32 v96, v147, v95
	v_cvt_pk_fp8_f32 v95, v98, v96
	v_lshlrev_b32_e32 v99, 16, v97
	v_and_b32_e32 v97, 0xffff0000, v97
	v_mul_f32_e32 v96, v147, v99
	v_mul_f32_e32 v97, v147, v97
	v_cvt_pk_fp8_f32 v95, v96, v97 op_sel:[0,0,1]
	global_store_dwordx2 v[126:127], v[94:95], off offset:256
	s_nop 0
	v_lshlrev_b32_e32 v94, 16, v90
	v_and_b32_e32 v90, 0xffff0000, v90
	v_mul_f32_e32 v94, v147, v94
	v_mul_f32_e32 v95, v147, v90
	v_cvt_pk_fp8_f32 v90, v94, v95
	v_lshlrev_b32_e32 v96, 16, v91
	v_and_b32_e32 v91, 0xffff0000, v91
	v_mul_f32_e32 v94, v147, v96
	v_mul_f32_e32 v91, v147, v91
	v_cvt_pk_fp8_f32 v90, v94, v91 op_sel:[0,0,1]
	v_lshlrev_b32_e32 v91, 16, v92
	v_mul_f32_e32 v94, v147, v91
	v_and_b32_e32 v91, 0xffff0000, v92
	v_mul_f32_e32 v92, v147, v91
	v_cvt_pk_fp8_f32 v91, v94, v92
	v_lshlrev_b32_e32 v95, 16, v93
	v_and_b32_e32 v93, 0xffff0000, v93
	v_mul_f32_e32 v92, v147, v95
	v_mul_f32_e32 v93, v147, v93
	v_cvt_pk_fp8_f32 v91, v92, v93 op_sel:[0,0,1]
	global_store_dwordx2 v[126:127], v[90:91], off offset:288
	s_nop 0
	v_lshlrev_b32_e32 v90, 16, v86
	v_and_b32_e32 v86, 0xffff0000, v86
	v_mul_f32_e32 v90, v147, v90
	v_mul_f32_e32 v91, v147, v86
	v_cvt_pk_fp8_f32 v86, v90, v91
	v_lshlrev_b32_e32 v92, 16, v87
	v_and_b32_e32 v87, 0xffff0000, v87
	v_mul_f32_e32 v90, v147, v92
	v_mul_f32_e32 v87, v147, v87
	v_cvt_pk_fp8_f32 v86, v90, v87 op_sel:[0,0,1]
	v_lshlrev_b32_e32 v87, 16, v88
	v_mul_f32_e32 v90, v147, v87
	v_and_b32_e32 v87, 0xffff0000, v88
	v_mul_f32_e32 v88, v147, v87
	v_cvt_pk_fp8_f32 v87, v90, v88
	v_lshlrev_b32_e32 v91, 16, v89
	v_and_b32_e32 v89, 0xffff0000, v89
	v_mul_f32_e32 v88, v147, v91
	v_mul_f32_e32 v89, v147, v89
	v_cvt_pk_fp8_f32 v87, v88, v89 op_sel:[0,0,1]
	global_store_dwordx2 v[126:127], v[86:87], off offset:320
	s_nop 0
	v_lshlrev_b32_e32 v86, 16, v82
	v_and_b32_e32 v82, 0xffff0000, v82
	v_mul_f32_e32 v86, v147, v86
	v_mul_f32_e32 v87, v147, v82
	v_cvt_pk_fp8_f32 v82, v86, v87
	v_lshlrev_b32_e32 v88, 16, v83
	v_and_b32_e32 v83, 0xffff0000, v83
	v_mul_f32_e32 v86, v147, v88
	v_mul_f32_e32 v83, v147, v83
	v_cvt_pk_fp8_f32 v82, v86, v83 op_sel:[0,0,1]
	v_lshlrev_b32_e32 v83, 16, v84
	v_mul_f32_e32 v86, v147, v83
	v_and_b32_e32 v83, 0xffff0000, v84
	v_mul_f32_e32 v84, v147, v83
	v_cvt_pk_fp8_f32 v83, v86, v84
	v_lshlrev_b32_e32 v87, 16, v85
	v_and_b32_e32 v85, 0xffff0000, v85
	v_mul_f32_e32 v84, v147, v87
	v_mul_f32_e32 v85, v147, v85
	v_cvt_pk_fp8_f32 v83, v84, v85 op_sel:[0,0,1]
	global_store_dwordx2 v[126:127], v[82:83], off offset:352
	s_nop 0
	v_lshlrev_b32_e32 v82, 16, v78
	v_and_b32_e32 v78, 0xffff0000, v78
	v_mul_f32_e32 v82, v147, v82
	v_mul_f32_e32 v83, v147, v78
	v_cvt_pk_fp8_f32 v78, v82, v83
	v_lshlrev_b32_e32 v84, 16, v79
	v_and_b32_e32 v79, 0xffff0000, v79
	v_mul_f32_e32 v82, v147, v84
	v_mul_f32_e32 v79, v147, v79
	v_cvt_pk_fp8_f32 v78, v82, v79 op_sel:[0,0,1]
	v_lshlrev_b32_e32 v79, 16, v80
	v_mul_f32_e32 v82, v147, v79
	v_and_b32_e32 v79, 0xffff0000, v80
	v_mul_f32_e32 v80, v147, v79
	v_cvt_pk_fp8_f32 v79, v82, v80
	v_lshlrev_b32_e32 v83, 16, v81
	v_and_b32_e32 v81, 0xffff0000, v81
	v_mul_f32_e32 v80, v147, v83
	v_mul_f32_e32 v81, v147, v81
	v_cvt_pk_fp8_f32 v79, v80, v81 op_sel:[0,0,1]
	global_store_dwordx2 v[126:127], v[78:79], off offset:384
	s_nop 0
	v_lshlrev_b32_e32 v78, 16, v74
	v_and_b32_e32 v74, 0xffff0000, v74
	v_mul_f32_e32 v78, v147, v78
	v_mul_f32_e32 v79, v147, v74
	v_cvt_pk_fp8_f32 v74, v78, v79
	v_lshlrev_b32_e32 v80, 16, v75
	v_and_b32_e32 v75, 0xffff0000, v75
	v_mul_f32_e32 v78, v147, v80
	v_mul_f32_e32 v75, v147, v75
	v_cvt_pk_fp8_f32 v74, v78, v75 op_sel:[0,0,1]
	v_lshlrev_b32_e32 v75, 16, v76
	v_mul_f32_e32 v78, v147, v75
	v_and_b32_e32 v75, 0xffff0000, v76
	v_mul_f32_e32 v76, v147, v75
	v_cvt_pk_fp8_f32 v75, v78, v76
	v_lshlrev_b32_e32 v79, 16, v77
	v_and_b32_e32 v77, 0xffff0000, v77
	v_mul_f32_e32 v76, v147, v79
	v_mul_f32_e32 v77, v147, v77
	v_cvt_pk_fp8_f32 v75, v76, v77 op_sel:[0,0,1]
	global_store_dwordx2 v[126:127], v[74:75], off offset:416
	s_nop 0
	v_lshlrev_b32_e32 v74, 16, v70
	v_and_b32_e32 v70, 0xffff0000, v70
	v_mul_f32_e32 v74, v147, v74
	v_mul_f32_e32 v75, v147, v70
	v_cvt_pk_fp8_f32 v70, v74, v75
	v_lshlrev_b32_e32 v76, 16, v71
	v_and_b32_e32 v71, 0xffff0000, v71
	v_mul_f32_e32 v74, v147, v76
	v_mul_f32_e32 v71, v147, v71
	v_cvt_pk_fp8_f32 v70, v74, v71 op_sel:[0,0,1]
	v_lshlrev_b32_e32 v71, 16, v72
	v_mul_f32_e32 v74, v147, v71
	v_and_b32_e32 v71, 0xffff0000, v72
	v_mul_f32_e32 v72, v147, v71
	v_cvt_pk_fp8_f32 v71, v74, v72
	v_lshlrev_b32_e32 v75, 16, v73
	v_and_b32_e32 v73, 0xffff0000, v73
	v_mul_f32_e32 v72, v147, v75
	v_mul_f32_e32 v73, v147, v73
	v_cvt_pk_fp8_f32 v71, v72, v73 op_sel:[0,0,1]
	global_store_dwordx2 v[126:127], v[70:71], off offset:448
	s_nop 0
	v_lshlrev_b32_e32 v70, 16, v66
	v_and_b32_e32 v66, 0xffff0000, v66
	v_mul_f32_e32 v70, v147, v70
	v_mul_f32_e32 v71, v147, v66
	v_cvt_pk_fp8_f32 v66, v70, v71
	v_lshlrev_b32_e32 v72, 16, v67
	v_and_b32_e32 v67, 0xffff0000, v67
	v_mul_f32_e32 v70, v147, v72
	v_mul_f32_e32 v67, v147, v67
	v_cvt_pk_fp8_f32 v66, v70, v67 op_sel:[0,0,1]
	v_lshlrev_b32_e32 v67, 16, v68
	v_mul_f32_e32 v70, v147, v67
	v_and_b32_e32 v67, 0xffff0000, v68
	v_mul_f32_e32 v68, v147, v67
	v_cvt_pk_fp8_f32 v67, v70, v68
	v_lshlrev_b32_e32 v71, 16, v69
	v_and_b32_e32 v69, 0xffff0000, v69
	v_mul_f32_e32 v68, v147, v71
	v_mul_f32_e32 v69, v147, v69
	v_cvt_pk_fp8_f32 v67, v68, v69 op_sel:[0,0,1]
	global_store_dwordx2 v[126:127], v[66:67], off offset:480
	s_nop 0
	v_lshlrev_b32_e32 v66, 16, v62
	v_and_b32_e32 v62, 0xffff0000, v62
	v_mul_f32_e32 v66, v147, v66
	v_mul_f32_e32 v67, v147, v62
	v_cvt_pk_fp8_f32 v62, v66, v67
	v_lshlrev_b32_e32 v68, 16, v63
	v_and_b32_e32 v63, 0xffff0000, v63
	v_mul_f32_e32 v66, v147, v68
	v_mul_f32_e32 v63, v147, v63
	v_cvt_pk_fp8_f32 v62, v66, v63 op_sel:[0,0,1]
	v_lshlrev_b32_e32 v63, 16, v64
	v_mul_f32_e32 v66, v147, v63
	v_and_b32_e32 v63, 0xffff0000, v64
	v_mul_f32_e32 v64, v147, v63
	v_cvt_pk_fp8_f32 v63, v66, v64
	v_lshlrev_b32_e32 v67, 16, v65
	v_and_b32_e32 v65, 0xffff0000, v65
	v_mul_f32_e32 v64, v147, v67
	v_mul_f32_e32 v65, v147, v65
	v_cvt_pk_fp8_f32 v63, v64, v65 op_sel:[0,0,1]
	global_store_dwordx2 v[126:127], v[62:63], off offset:512
	s_nop 0
	v_lshlrev_b32_e32 v62, 16, v58
	v_and_b32_e32 v58, 0xffff0000, v58
	v_mul_f32_e32 v62, v147, v62
	v_mul_f32_e32 v63, v147, v58
	v_cvt_pk_fp8_f32 v58, v62, v63
	v_lshlrev_b32_e32 v64, 16, v59
	v_and_b32_e32 v59, 0xffff0000, v59
	v_mul_f32_e32 v62, v147, v64
	v_mul_f32_e32 v59, v147, v59
	v_cvt_pk_fp8_f32 v58, v62, v59 op_sel:[0,0,1]
	v_lshlrev_b32_e32 v59, 16, v60
	v_mul_f32_e32 v62, v147, v59
	v_and_b32_e32 v59, 0xffff0000, v60
	v_mul_f32_e32 v60, v147, v59
	v_cvt_pk_fp8_f32 v59, v62, v60
	v_lshlrev_b32_e32 v63, 16, v61
	v_and_b32_e32 v61, 0xffff0000, v61
	v_mul_f32_e32 v60, v147, v63
	v_mul_f32_e32 v61, v147, v61
	v_cvt_pk_fp8_f32 v59, v60, v61 op_sel:[0,0,1]
	global_store_dwordx2 v[126:127], v[58:59], off offset:544
	s_nop 0
	v_lshlrev_b32_e32 v58, 16, v54
	v_and_b32_e32 v54, 0xffff0000, v54
	v_mul_f32_e32 v58, v147, v58
	v_mul_f32_e32 v59, v147, v54
	v_cvt_pk_fp8_f32 v54, v58, v59
	v_lshlrev_b32_e32 v60, 16, v55
	v_and_b32_e32 v55, 0xffff0000, v55
	v_mul_f32_e32 v58, v147, v60
	v_mul_f32_e32 v55, v147, v55
	v_cvt_pk_fp8_f32 v54, v58, v55 op_sel:[0,0,1]
	v_lshlrev_b32_e32 v55, 16, v56
	v_mul_f32_e32 v58, v147, v55
	v_and_b32_e32 v55, 0xffff0000, v56
	v_mul_f32_e32 v56, v147, v55
	v_cvt_pk_fp8_f32 v55, v58, v56
	v_lshlrev_b32_e32 v59, 16, v57
	v_and_b32_e32 v57, 0xffff0000, v57
	v_mul_f32_e32 v56, v147, v59
	v_mul_f32_e32 v57, v147, v57
	v_cvt_pk_fp8_f32 v55, v56, v57 op_sel:[0,0,1]
	global_store_dwordx2 v[126:127], v[54:55], off offset:576
	s_nop 0
	v_lshlrev_b32_e32 v54, 16, v50
	v_and_b32_e32 v50, 0xffff0000, v50
	v_mul_f32_e32 v54, v147, v54
	v_mul_f32_e32 v55, v147, v50
	v_cvt_pk_fp8_f32 v50, v54, v55
	v_lshlrev_b32_e32 v56, 16, v51
	v_and_b32_e32 v51, 0xffff0000, v51
	v_mul_f32_e32 v54, v147, v56
	v_mul_f32_e32 v51, v147, v51
	v_cvt_pk_fp8_f32 v50, v54, v51 op_sel:[0,0,1]
	v_lshlrev_b32_e32 v51, 16, v52
	v_mul_f32_e32 v54, v147, v51
	v_and_b32_e32 v51, 0xffff0000, v52
	v_mul_f32_e32 v52, v147, v51
	v_cvt_pk_fp8_f32 v51, v54, v52
	v_lshlrev_b32_e32 v55, 16, v53
	v_and_b32_e32 v53, 0xffff0000, v53
	v_mul_f32_e32 v52, v147, v55
	v_mul_f32_e32 v53, v147, v53
	v_cvt_pk_fp8_f32 v51, v52, v53 op_sel:[0,0,1]
	global_store_dwordx2 v[126:127], v[50:51], off offset:608
	s_nop 0
	v_lshlrev_b32_e32 v50, 16, v46
	v_and_b32_e32 v46, 0xffff0000, v46
	v_mul_f32_e32 v50, v147, v50
	v_mul_f32_e32 v51, v147, v46
	v_cvt_pk_fp8_f32 v46, v50, v51
	v_lshlrev_b32_e32 v52, 16, v47
	v_and_b32_e32 v47, 0xffff0000, v47
	v_mul_f32_e32 v50, v147, v52
	v_mul_f32_e32 v47, v147, v47
	v_cvt_pk_fp8_f32 v46, v50, v47 op_sel:[0,0,1]
	v_lshlrev_b32_e32 v47, 16, v48
	v_mul_f32_e32 v50, v147, v47
	v_and_b32_e32 v47, 0xffff0000, v48
	v_mul_f32_e32 v48, v147, v47
	v_cvt_pk_fp8_f32 v47, v50, v48
	v_lshlrev_b32_e32 v51, 16, v49
	v_and_b32_e32 v49, 0xffff0000, v49
	v_mul_f32_e32 v48, v147, v51
	v_mul_f32_e32 v49, v147, v49
	v_cvt_pk_fp8_f32 v47, v48, v49 op_sel:[0,0,1]
	global_store_dwordx2 v[126:127], v[46:47], off offset:640
	s_nop 0
	v_lshlrev_b32_e32 v46, 16, v42
	v_and_b32_e32 v42, 0xffff0000, v42
	v_mul_f32_e32 v46, v147, v46
	v_mul_f32_e32 v47, v147, v42
	v_cvt_pk_fp8_f32 v42, v46, v47
	v_lshlrev_b32_e32 v48, 16, v43
	v_and_b32_e32 v43, 0xffff0000, v43
	v_mul_f32_e32 v46, v147, v48
	v_mul_f32_e32 v43, v147, v43
	v_cvt_pk_fp8_f32 v42, v46, v43 op_sel:[0,0,1]
	v_lshlrev_b32_e32 v43, 16, v44
	v_mul_f32_e32 v46, v147, v43
	v_and_b32_e32 v43, 0xffff0000, v44
	v_mul_f32_e32 v44, v147, v43
	v_cvt_pk_fp8_f32 v43, v46, v44
	v_lshlrev_b32_e32 v47, 16, v45
	v_and_b32_e32 v45, 0xffff0000, v45
	v_mul_f32_e32 v44, v147, v47
	v_mul_f32_e32 v45, v147, v45
	v_cvt_pk_fp8_f32 v43, v44, v45 op_sel:[0,0,1]
	global_store_dwordx2 v[126:127], v[42:43], off offset:672
	s_nop 0
	v_lshlrev_b32_e32 v42, 16, v38
	v_and_b32_e32 v38, 0xffff0000, v38
	v_mul_f32_e32 v42, v147, v42
	v_mul_f32_e32 v43, v147, v38
	v_cvt_pk_fp8_f32 v38, v42, v43
	v_lshlrev_b32_e32 v44, 16, v39
	v_and_b32_e32 v39, 0xffff0000, v39
	v_mul_f32_e32 v42, v147, v44
	v_mul_f32_e32 v39, v147, v39
	v_cvt_pk_fp8_f32 v38, v42, v39 op_sel:[0,0,1]
	v_lshlrev_b32_e32 v39, 16, v40
	v_mul_f32_e32 v42, v147, v39
	v_and_b32_e32 v39, 0xffff0000, v40
	v_mul_f32_e32 v40, v147, v39
	v_cvt_pk_fp8_f32 v39, v42, v40
	v_lshlrev_b32_e32 v43, 16, v41
	v_and_b32_e32 v41, 0xffff0000, v41
	v_mul_f32_e32 v40, v147, v43
	v_mul_f32_e32 v41, v147, v41
	v_cvt_pk_fp8_f32 v39, v40, v41 op_sel:[0,0,1]
	global_store_dwordx2 v[126:127], v[38:39], off offset:704
	s_nop 0
	v_lshlrev_b32_e32 v38, 16, v34
	v_and_b32_e32 v34, 0xffff0000, v34
	v_mul_f32_e32 v38, v147, v38
	v_mul_f32_e32 v39, v147, v34
	v_cvt_pk_fp8_f32 v34, v38, v39
	v_lshlrev_b32_e32 v40, 16, v35
	v_and_b32_e32 v35, 0xffff0000, v35
	v_mul_f32_e32 v38, v147, v40
	v_mul_f32_e32 v35, v147, v35
	v_cvt_pk_fp8_f32 v34, v38, v35 op_sel:[0,0,1]
	v_lshlrev_b32_e32 v35, 16, v36
	v_mul_f32_e32 v38, v147, v35
	v_and_b32_e32 v35, 0xffff0000, v36
	v_mul_f32_e32 v36, v147, v35
	v_cvt_pk_fp8_f32 v35, v38, v36
	v_lshlrev_b32_e32 v39, 16, v37
	v_and_b32_e32 v37, 0xffff0000, v37
	v_mul_f32_e32 v36, v147, v39
	v_mul_f32_e32 v37, v147, v37
	v_cvt_pk_fp8_f32 v35, v36, v37 op_sel:[0,0,1]
	global_store_dwordx2 v[126:127], v[34:35], off offset:736
	s_nop 0
	v_lshlrev_b32_e32 v34, 16, v30
	v_and_b32_e32 v30, 0xffff0000, v30
	v_mul_f32_e32 v34, v147, v34
	v_mul_f32_e32 v35, v147, v30
	v_cvt_pk_fp8_f32 v30, v34, v35
	v_lshlrev_b32_e32 v36, 16, v31
	v_and_b32_e32 v31, 0xffff0000, v31
	v_mul_f32_e32 v34, v147, v36
	v_mul_f32_e32 v31, v147, v31
	v_cvt_pk_fp8_f32 v30, v34, v31 op_sel:[0,0,1]
	v_lshlrev_b32_e32 v31, 16, v32
	v_mul_f32_e32 v34, v147, v31
	v_and_b32_e32 v31, 0xffff0000, v32
	v_mul_f32_e32 v32, v147, v31
	v_cvt_pk_fp8_f32 v31, v34, v32
	v_lshlrev_b32_e32 v35, 16, v33
	v_and_b32_e32 v33, 0xffff0000, v33
	v_mul_f32_e32 v32, v147, v35
	v_mul_f32_e32 v33, v147, v33
	v_cvt_pk_fp8_f32 v31, v32, v33 op_sel:[0,0,1]
	global_store_dwordx2 v[126:127], v[30:31], off offset:768
	s_nop 0
	v_lshlrev_b32_e32 v30, 16, v26
	v_and_b32_e32 v26, 0xffff0000, v26
	v_mul_f32_e32 v30, v147, v30
	v_mul_f32_e32 v31, v147, v26
	v_cvt_pk_fp8_f32 v26, v30, v31
	v_lshlrev_b32_e32 v32, 16, v27
	v_and_b32_e32 v27, 0xffff0000, v27
	v_mul_f32_e32 v30, v147, v32
	v_mul_f32_e32 v27, v147, v27
	v_cvt_pk_fp8_f32 v26, v30, v27 op_sel:[0,0,1]
	v_lshlrev_b32_e32 v27, 16, v28
	v_mul_f32_e32 v30, v147, v27
	v_and_b32_e32 v27, 0xffff0000, v28
	v_mul_f32_e32 v28, v147, v27
	v_cvt_pk_fp8_f32 v27, v30, v28
	v_lshlrev_b32_e32 v31, 16, v29
	v_and_b32_e32 v29, 0xffff0000, v29
	v_mul_f32_e32 v28, v147, v31
	v_mul_f32_e32 v29, v147, v29
	v_cvt_pk_fp8_f32 v27, v28, v29 op_sel:[0,0,1]
	global_store_dwordx2 v[126:127], v[26:27], off offset:800
	s_nop 0
	v_lshlrev_b32_e32 v26, 16, v22
	v_and_b32_e32 v22, 0xffff0000, v22
	v_mul_f32_e32 v26, v147, v26
	v_mul_f32_e32 v27, v147, v22
	v_cvt_pk_fp8_f32 v22, v26, v27
	v_lshlrev_b32_e32 v28, 16, v23
	v_and_b32_e32 v23, 0xffff0000, v23
	v_mul_f32_e32 v26, v147, v28
	v_mul_f32_e32 v23, v147, v23
	v_cvt_pk_fp8_f32 v22, v26, v23 op_sel:[0,0,1]
	v_lshlrev_b32_e32 v23, 16, v24
	v_mul_f32_e32 v26, v147, v23
	v_and_b32_e32 v23, 0xffff0000, v24
	v_mul_f32_e32 v24, v147, v23
	v_cvt_pk_fp8_f32 v23, v26, v24
	v_lshlrev_b32_e32 v27, 16, v25
	v_and_b32_e32 v25, 0xffff0000, v25
	v_mul_f32_e32 v24, v147, v27
	v_mul_f32_e32 v25, v147, v25
	v_cvt_pk_fp8_f32 v23, v24, v25 op_sel:[0,0,1]
	global_store_dwordx2 v[126:127], v[22:23], off offset:832
	s_nop 0
	v_lshlrev_b32_e32 v22, 16, v18
	v_and_b32_e32 v18, 0xffff0000, v18
	v_mul_f32_e32 v22, v147, v22
	v_mul_f32_e32 v23, v147, v18
	v_cvt_pk_fp8_f32 v18, v22, v23
	v_lshlrev_b32_e32 v24, 16, v19
	v_and_b32_e32 v19, 0xffff0000, v19
	v_mul_f32_e32 v22, v147, v24
	v_mul_f32_e32 v19, v147, v19
	v_cvt_pk_fp8_f32 v18, v22, v19 op_sel:[0,0,1]
	v_lshlrev_b32_e32 v19, 16, v20
	v_mul_f32_e32 v22, v147, v19
	v_and_b32_e32 v19, 0xffff0000, v20
	v_mul_f32_e32 v20, v147, v19
	v_cvt_pk_fp8_f32 v19, v22, v20
	v_lshlrev_b32_e32 v23, 16, v21
	v_and_b32_e32 v21, 0xffff0000, v21
	v_mul_f32_e32 v20, v147, v23
	v_mul_f32_e32 v21, v147, v21
	v_cvt_pk_fp8_f32 v19, v20, v21 op_sel:[0,0,1]
	global_store_dwordx2 v[126:127], v[18:19], off offset:864
	s_nop 0
	v_lshlrev_b32_e32 v18, 16, v14
	v_and_b32_e32 v14, 0xffff0000, v14
	v_mul_f32_e32 v18, v147, v18
	v_mul_f32_e32 v19, v147, v14
	v_cvt_pk_fp8_f32 v14, v18, v19
	v_lshlrev_b32_e32 v20, 16, v15
	v_and_b32_e32 v15, 0xffff0000, v15
	v_mul_f32_e32 v18, v147, v20
	v_mul_f32_e32 v15, v147, v15
	v_cvt_pk_fp8_f32 v14, v18, v15 op_sel:[0,0,1]
	v_lshlrev_b32_e32 v15, 16, v16
	v_mul_f32_e32 v18, v147, v15
	v_and_b32_e32 v15, 0xffff0000, v16
	v_mul_f32_e32 v16, v147, v15
	v_cvt_pk_fp8_f32 v15, v18, v16
	v_lshlrev_b32_e32 v19, 16, v17
	v_and_b32_e32 v17, 0xffff0000, v17
	v_mul_f32_e32 v16, v147, v19
	v_mul_f32_e32 v17, v147, v17
	v_cvt_pk_fp8_f32 v15, v16, v17 op_sel:[0,0,1]
	global_store_dwordx2 v[126:127], v[14:15], off offset:896
	s_nop 0
	v_lshlrev_b32_e32 v14, 16, v10
	v_and_b32_e32 v10, 0xffff0000, v10
	v_mul_f32_e32 v14, v147, v14
	v_mul_f32_e32 v15, v147, v10
	v_cvt_pk_fp8_f32 v10, v14, v15
	v_lshlrev_b32_e32 v16, 16, v11
	v_and_b32_e32 v11, 0xffff0000, v11
	v_mul_f32_e32 v14, v147, v16
	v_mul_f32_e32 v11, v147, v11
	v_cvt_pk_fp8_f32 v10, v14, v11 op_sel:[0,0,1]
	v_lshlrev_b32_e32 v11, 16, v12
	v_mul_f32_e32 v14, v147, v11
	v_and_b32_e32 v11, 0xffff0000, v12
	v_mul_f32_e32 v12, v147, v11
	v_cvt_pk_fp8_f32 v11, v14, v12
	v_lshlrev_b32_e32 v15, 16, v13
	v_and_b32_e32 v13, 0xffff0000, v13
	v_mul_f32_e32 v12, v147, v15
	v_mul_f32_e32 v13, v147, v13
	v_cvt_pk_fp8_f32 v11, v12, v13 op_sel:[0,0,1]
	global_store_dwordx2 v[126:127], v[10:11], off offset:928
	s_nop 0
	v_lshlrev_b32_e32 v10, 16, v6
	v_and_b32_e32 v6, 0xffff0000, v6
	v_mul_f32_e32 v10, v147, v10
	v_mul_f32_e32 v11, v147, v6
	v_cvt_pk_fp8_f32 v6, v10, v11
	v_lshlrev_b32_e32 v12, 16, v7
	v_and_b32_e32 v7, 0xffff0000, v7
	v_mul_f32_e32 v10, v147, v12
	v_mul_f32_e32 v7, v147, v7
	v_cvt_pk_fp8_f32 v6, v10, v7 op_sel:[0,0,1]
	v_lshlrev_b32_e32 v7, 16, v8
	v_mul_f32_e32 v10, v147, v7
	v_and_b32_e32 v7, 0xffff0000, v8
	v_mul_f32_e32 v8, v147, v7
	v_cvt_pk_fp8_f32 v7, v10, v8
	v_lshlrev_b32_e32 v11, 16, v9
	v_and_b32_e32 v9, 0xffff0000, v9
	v_mul_f32_e32 v8, v147, v11
	v_mul_f32_e32 v9, v147, v9
	v_cvt_pk_fp8_f32 v7, v8, v9 op_sel:[0,0,1]
	global_store_dwordx2 v[126:127], v[6:7], off offset:960
	s_nop 0
	v_lshlrev_b32_e32 v6, 16, v2
	v_and_b32_e32 v2, 0xffff0000, v2
	v_mul_f32_e32 v6, v147, v6
	v_mul_f32_e32 v7, v147, v2
	v_cvt_pk_fp8_f32 v2, v6, v7
	v_lshlrev_b32_e32 v8, 16, v3
	v_and_b32_e32 v3, 0xffff0000, v3
	v_mul_f32_e32 v6, v147, v8
	v_mul_f32_e32 v3, v147, v3
	v_cvt_pk_fp8_f32 v2, v6, v3 op_sel:[0,0,1]
	v_lshlrev_b32_e32 v3, 16, v4
	v_mul_f32_e32 v6, v147, v3
	v_and_b32_e32 v3, 0xffff0000, v4
	v_mul_f32_e32 v4, v147, v3
	v_cvt_pk_fp8_f32 v3, v6, v4
	v_lshlrev_b32_e32 v7, 16, v5
	v_and_b32_e32 v5, 0xffff0000, v5
	v_mul_f32_e32 v4, v147, v7
	v_mul_f32_e32 v5, v147, v5
	v_cvt_pk_fp8_f32 v3, v4, v5 op_sel:[0,0,1]
	ds_bpermute_b32 v4, v179, v145
	ds_bpermute_b32 v5, v185, v145
	global_store_dwordx2 v[126:127], v[2:3], off offset:992
	ds_bpermute_b32 v2, v181, v145
	s_waitcnt lgkmcnt(2)
	v_fma_f32 v3, v130, v4, v172
	v_fma_f32 v4, v134, v4, v173
	s_waitcnt lgkmcnt(0)
	ds_write2_b32 v180, v3, v4 offset1:16
	ds_bpermute_b32 v3, v183, v145
	s_waitcnt lgkmcnt(2)
	v_fma_f32 v4, v131, v2, v172
	v_fma_f32 v2, v135, v2, v173
	ds_write2_b32 v182, v4, v2 offset1:16
	s_waitcnt lgkmcnt(1)
	v_fma_f32 v2, v132, v3, v172
	v_fma_f32 v3, v136, v3, v173
	ds_write2_b32 v184, v2, v3 offset1:16
	v_fma_f32 v2, v133, v5, v172
	v_fma_f32 v3, v137, v5, v173
	ds_write2_b32 v186, v2, v3 offset1:16
	s_waitcnt lgkmcnt(0)
	s_and_saveexec_b64 s[20:21], s[6:7]
	s_cbranch_execz .LBB0_439
	v_add_u32_e32 v2, s0, v176
	ds_read2_b32 v[32:33], v2 offset1:1
	ds_read2_b32 v[30:31], v2 offset0:2 offset1:3
	ds_read2_b32 v[28:29], v2 offset0:4 offset1:5
	ds_read2_b32 v[26:27], v2 offset0:6 offset1:7
	ds_read2_b32 v[24:25], v2 offset0:8 offset1:9
	ds_read2_b32 v[22:23], v2 offset0:10 offset1:11
	ds_read2_b32 v[20:21], v2 offset0:12 offset1:13
	ds_read2_b32 v[18:19], v2 offset0:14 offset1:15
	ds_read2_b32 v[16:17], v2 offset0:16 offset1:17
	ds_read2_b32 v[14:15], v2 offset0:18 offset1:19
	ds_read2_b32 v[12:13], v2 offset0:20 offset1:21
	ds_read2_b32 v[10:11], v2 offset0:22 offset1:23
	ds_read2_b32 v[8:9], v2 offset0:24 offset1:25
	ds_read2_b32 v[6:7], v2 offset0:26 offset1:27
	ds_read2_b32 v[4:5], v2 offset0:28 offset1:29
	ds_read2_b32 v[2:3], v2 offset0:30 offset1:31
	s_waitcnt lgkmcnt(14)
	v_cmp_gt_f32_e32 vcc, v33, v32
	s_nop 1
	v_cndmask_b32_e32 v35, v32, v33, vcc
	v_cndmask_b32_e64 v34, 0, 1, vcc
	v_cmp_gt_f32_e32 vcc, v30, v35
	s_nop 1
	v_cndmask_b32_e32 v35, v35, v30, vcc
	v_cndmask_b32_e64 v34, v34, 2, vcc
	v_cmp_gt_f32_e32 vcc, v31, v35
	s_nop 1
	v_cndmask_b32_e32 v35, v35, v31, vcc
	v_cndmask_b32_e64 v34, v34, 3, vcc
	s_waitcnt lgkmcnt(13)
	v_cmp_gt_f32_e32 vcc, v28, v35
	s_nop 1
	v_cndmask_b32_e32 v35, v35, v28, vcc
	v_cndmask_b32_e64 v34, v34, 4, vcc
	v_cmp_gt_f32_e32 vcc, v29, v35
	s_nop 1
	v_cndmask_b32_e32 v35, v35, v29, vcc
	v_cndmask_b32_e64 v34, v34, 5, vcc
	s_waitcnt lgkmcnt(12)
	v_cmp_gt_f32_e32 vcc, v26, v35
	s_nop 1
	v_cndmask_b32_e32 v35, v35, v26, vcc
	v_cndmask_b32_e64 v34, v34, 6, vcc
	v_cmp_gt_f32_e32 vcc, v27, v35
	s_nop 1
	v_cndmask_b32_e32 v35, v35, v27, vcc
	v_cndmask_b32_e64 v34, v34, 7, vcc
	s_waitcnt lgkmcnt(11)
	v_cmp_gt_f32_e32 vcc, v24, v35
	s_nop 1
	v_cndmask_b32_e32 v35, v35, v24, vcc
	v_cndmask_b32_e64 v34, v34, 8, vcc
	v_cmp_gt_f32_e32 vcc, v25, v35
	s_nop 1
	v_cndmask_b32_e32 v35, v35, v25, vcc
	v_cndmask_b32_e64 v34, v34, 9, vcc
	s_waitcnt lgkmcnt(10)
	v_cmp_gt_f32_e32 vcc, v22, v35
	s_nop 1
	v_cndmask_b32_e32 v35, v35, v22, vcc
	v_cndmask_b32_e64 v34, v34, 10, vcc
	v_cmp_gt_f32_e32 vcc, v23, v35
	s_nop 1
	v_cndmask_b32_e32 v35, v35, v23, vcc
	v_cndmask_b32_e64 v34, v34, 11, vcc
	s_waitcnt lgkmcnt(9)
	v_cmp_gt_f32_e32 vcc, v20, v35
	s_nop 1
	v_cndmask_b32_e32 v35, v35, v20, vcc
	v_cndmask_b32_e64 v34, v34, 12, vcc
	v_cmp_gt_f32_e32 vcc, v21, v35
	s_nop 1
	v_cndmask_b32_e32 v35, v35, v21, vcc
	v_cndmask_b32_e64 v34, v34, 13, vcc
	s_waitcnt lgkmcnt(8)
	v_cmp_gt_f32_e32 vcc, v18, v35
	s_nop 1
	v_cndmask_b32_e32 v35, v35, v18, vcc
	v_cndmask_b32_e64 v34, v34, 14, vcc
	v_cmp_gt_f32_e32 vcc, v19, v35
	s_nop 1
	v_cndmask_b32_e32 v35, v35, v19, vcc
	v_cndmask_b32_e64 v34, v34, 15, vcc
	s_waitcnt lgkmcnt(7)
	v_cmp_gt_f32_e32 vcc, v16, v35
	s_nop 1
	v_cndmask_b32_e32 v35, v35, v16, vcc
	v_cndmask_b32_e64 v34, v34, 16, vcc
	v_cmp_gt_f32_e32 vcc, v17, v35
	s_nop 1
	v_cndmask_b32_e32 v35, v35, v17, vcc
	v_cndmask_b32_e64 v34, v34, 17, vcc
	s_waitcnt lgkmcnt(6)
	v_cmp_gt_f32_e32 vcc, v14, v35
	s_nop 1
	v_cndmask_b32_e32 v35, v35, v14, vcc
	v_cndmask_b32_e64 v34, v34, 18, vcc
	v_cmp_gt_f32_e32 vcc, v15, v35
	s_nop 1
	v_cndmask_b32_e32 v35, v35, v15, vcc
	v_cndmask_b32_e64 v34, v34, 19, vcc
	s_waitcnt lgkmcnt(5)
	v_cmp_gt_f32_e32 vcc, v12, v35
	s_nop 1
	v_cndmask_b32_e32 v35, v35, v12, vcc
	v_cndmask_b32_e64 v34, v34, 20, vcc
	v_cmp_gt_f32_e32 vcc, v13, v35
	s_nop 1
	v_cndmask_b32_e32 v35, v35, v13, vcc
	v_cndmask_b32_e64 v34, v34, 21, vcc
	s_waitcnt lgkmcnt(4)
	v_cmp_gt_f32_e32 vcc, v10, v35
	s_nop 1
	v_cndmask_b32_e32 v35, v35, v10, vcc
	v_cndmask_b32_e64 v34, v34, 22, vcc
	v_cmp_gt_f32_e32 vcc, v11, v35
	s_nop 1
	v_cndmask_b32_e32 v35, v35, v11, vcc
	v_cndmask_b32_e64 v34, v34, 23, vcc
	s_waitcnt lgkmcnt(3)
	v_cmp_gt_f32_e32 vcc, v8, v35
	s_nop 1
	v_cndmask_b32_e32 v35, v35, v8, vcc
	v_cndmask_b32_e64 v34, v34, 24, vcc
	v_cmp_gt_f32_e32 vcc, v9, v35
	s_nop 1
	v_cndmask_b32_e32 v35, v35, v9, vcc
	v_cndmask_b32_e64 v34, v34, 25, vcc
	s_waitcnt lgkmcnt(2)
	v_cmp_gt_f32_e32 vcc, v6, v35
	s_nop 1
	v_cndmask_b32_e32 v35, v35, v6, vcc
	v_cndmask_b32_e64 v34, v34, 26, vcc
	v_cmp_gt_f32_e32 vcc, v7, v35
	s_nop 1
	v_cndmask_b32_e32 v35, v35, v7, vcc
	v_cndmask_b32_e64 v34, v34, 27, vcc
	s_waitcnt lgkmcnt(1)
	v_cmp_gt_f32_e32 vcc, v4, v35
	s_nop 1
	v_cndmask_b32_e32 v35, v35, v4, vcc
	v_cndmask_b32_e64 v34, v34, 28, vcc
	v_cmp_gt_f32_e32 vcc, v5, v35
	s_nop 1
	v_cndmask_b32_e32 v35, v35, v5, vcc
	v_cndmask_b32_e64 v34, v34, 29, vcc
	s_waitcnt lgkmcnt(0)
	v_cmp_gt_f32_e32 vcc, v2, v35
	s_nop 1
	v_cndmask_b32_e32 v35, v35, v2, vcc
	v_cndmask_b32_e64 v34, v34, 30, vcc
	v_cmp_gt_f32_e32 vcc, v3, v35
	s_nop 1
	v_cndmask_b32_e64 v144, v34, 31, vcc
	v_cndmask_b32_e32 v34, v35, v3, vcc
	v_cmp_eq_u32_e32 vcc, 0, v144
	v_lshlrev_b32_e64 v36, v144, 1
	v_and_b32_e32 v38, 2, v36
	v_cndmask_b32_e32 v37, v32, v198, vcc
	v_cmp_gt_f32_e64 s[8:9], v33, v37
	v_cndmask_b32_e64 v35, 0, -1, vcc
	s_or_b64 vcc, vcc, s[8:9]
	v_cndmask_b32_e64 v39, 0, 1, vcc
	v_cndmask_b32_e32 v40, v32, v33, vcc
	v_cmp_eq_u32_e32 vcc, 0, v38
	v_and_b32_e32 v38, 4, v36
	s_nop 0
	v_cndmask_b32_e32 v37, v37, v40, vcc
	v_cndmask_b32_e32 v35, v35, v39, vcc
	v_cmp_eq_u32_e32 vcc, 0, v38
	v_cmp_gt_f32_e64 s[8:9], v30, v37
	s_and_b64 vcc, vcc, s[8:9]
	v_cndmask_b32_e64 v35, v35, 2, vcc
	v_cndmask_b32_e32 v37, v37, v30, vcc
	v_and_b32_e32 v38, 8, v36
	v_cmp_gt_i32_e64 s[8:9], 0, v35
	v_cmp_gt_f32_e64 s[10:11], v31, v37
	v_cmp_eq_u32_e32 vcc, 0, v38
	s_or_b64 s[8:9], s[8:9], s[10:11]
	s_and_b64 vcc, vcc, s[8:9]
	v_cndmask_b32_e64 v35, v35, 3, vcc
	v_cndmask_b32_e32 v37, v37, v31, vcc
	v_and_b32_e32 v38, 16, v36
	v_cmp_gt_i32_e64 s[8:9], 0, v35
	v_cmp_gt_f32_e64 s[10:11], v28, v37
	v_cmp_eq_u32_e32 vcc, 0, v38
	s_or_b64 s[8:9], s[8:9], s[10:11]
	s_and_b64 vcc, vcc, s[8:9]
	v_cndmask_b32_e64 v35, v35, 4, vcc
	v_cndmask_b32_e32 v37, v37, v28, vcc
	v_and_b32_e32 v38, 32, v36
	v_cmp_gt_i32_e64 s[8:9], 0, v35
	v_cmp_gt_f32_e64 s[10:11], v29, v37
	v_cmp_eq_u32_e32 vcc, 0, v38
	s_or_b64 s[8:9], s[8:9], s[10:11]
	s_and_b64 vcc, vcc, s[8:9]
	v_cndmask_b32_e64 v35, v35, 5, vcc
	v_cndmask_b32_e32 v37, v37, v29, vcc
	v_and_b32_e32 v38, 64, v36
	v_cmp_gt_i32_e64 s[8:9], 0, v35
	v_cmp_gt_f32_e64 s[10:11], v26, v37
	v_cmp_eq_u32_e32 vcc, 0, v38
	s_or_b64 s[8:9], s[8:9], s[10:11]
	s_and_b64 vcc, vcc, s[8:9]
	v_cndmask_b32_e64 v35, v35, 6, vcc
	v_cndmask_b32_e32 v37, v37, v26, vcc
	v_and_b32_e32 v38, 0x80, v36
	v_cmp_gt_i32_e64 s[8:9], 0, v35
	v_cmp_gt_f32_e64 s[10:11], v27, v37
	v_cmp_eq_u32_e32 vcc, 0, v38
	s_or_b64 s[8:9], s[8:9], s[10:11]
	s_and_b64 vcc, vcc, s[8:9]
	v_cndmask_b32_e64 v35, v35, 7, vcc
	v_cndmask_b32_e32 v37, v37, v27, vcc
	v_and_b32_e32 v38, 0x100, v36
	v_cmp_gt_i32_e64 s[8:9], 0, v35
	v_cmp_gt_f32_e64 s[10:11], v24, v37
	v_cmp_eq_u32_e32 vcc, 0, v38
	s_or_b64 s[8:9], s[8:9], s[10:11]
	s_and_b64 vcc, vcc, s[8:9]
	v_cndmask_b32_e64 v35, v35, 8, vcc
	v_cndmask_b32_e32 v37, v37, v24, vcc
	v_and_b32_e32 v38, 0x200, v36
	v_cmp_gt_i32_e64 s[8:9], 0, v35
	v_cmp_gt_f32_e64 s[10:11], v25, v37
	v_cmp_eq_u32_e32 vcc, 0, v38
	s_or_b64 s[8:9], s[8:9], s[10:11]
	s_and_b64 vcc, vcc, s[8:9]
	v_cndmask_b32_e64 v35, v35, 9, vcc
	v_cndmask_b32_e32 v37, v37, v25, vcc
	v_and_b32_e32 v38, 0x400, v36
	v_cmp_gt_i32_e64 s[8:9], 0, v35
	v_cmp_gt_f32_e64 s[10:11], v22, v37
	v_cmp_eq_u32_e32 vcc, 0, v38
	s_or_b64 s[8:9], s[8:9], s[10:11]
	s_and_b64 vcc, vcc, s[8:9]
	v_cndmask_b32_e64 v35, v35, 10, vcc
	v_cndmask_b32_e32 v37, v37, v22, vcc
	v_and_b32_e32 v38, 0x800, v36
	v_cmp_gt_i32_e64 s[8:9], 0, v35
	v_cmp_gt_f32_e64 s[10:11], v23, v37
	v_cmp_eq_u32_e32 vcc, 0, v38
	s_or_b64 s[8:9], s[8:9], s[10:11]
	s_and_b64 vcc, vcc, s[8:9]
	v_cndmask_b32_e64 v35, v35, 11, vcc
	v_cndmask_b32_e32 v37, v37, v23, vcc
	v_and_b32_e32 v38, 0x1000, v36
	v_cmp_gt_i32_e64 s[8:9], 0, v35
	v_cmp_gt_f32_e64 s[10:11], v20, v37
	v_cmp_eq_u32_e32 vcc, 0, v38
	s_or_b64 s[8:9], s[8:9], s[10:11]
	s_and_b64 vcc, vcc, s[8:9]
	v_cndmask_b32_e64 v35, v35, 12, vcc
	v_cndmask_b32_e32 v37, v37, v20, vcc
	v_and_b32_e32 v38, 0x2000, v36
	v_cmp_gt_i32_e64 s[8:9], 0, v35
	v_cmp_gt_f32_e64 s[10:11], v21, v37
	v_cmp_eq_u32_e32 vcc, 0, v38
	s_or_b64 s[8:9], s[8:9], s[10:11]
	s_and_b64 vcc, vcc, s[8:9]
	v_cndmask_b32_e64 v35, v35, 13, vcc
	v_cndmask_b32_e32 v37, v37, v21, vcc
	v_and_b32_e32 v38, 0x4000, v36
	v_cmp_gt_i32_e64 s[8:9], 0, v35
	v_cmp_gt_f32_e64 s[10:11], v18, v37
	v_cmp_eq_u32_e32 vcc, 0, v38
	s_or_b64 s[8:9], s[8:9], s[10:11]
	s_and_b64 vcc, vcc, s[8:9]
	v_cndmask_b32_e64 v35, v35, 14, vcc
	v_cndmask_b32_e32 v37, v37, v18, vcc
	v_and_b32_e32 v38, 0x8000, v36
	v_cmp_gt_i32_e64 s[8:9], 0, v35
	v_cmp_gt_f32_e64 s[10:11], v19, v37
	v_cmp_eq_u32_e32 vcc, 0, v38
	s_or_b64 s[8:9], s[8:9], s[10:11]
	s_and_b64 vcc, vcc, s[8:9]
	v_cndmask_b32_e64 v35, v35, 15, vcc
	v_cndmask_b32_e32 v37, v37, v19, vcc
	v_and_b32_e32 v38, 0x10000, v36
	v_cmp_gt_i32_e64 s[8:9], 0, v35
	v_cmp_gt_f32_e64 s[10:11], v16, v37
	v_cmp_eq_u32_e32 vcc, 0, v38
	s_or_b64 s[8:9], s[8:9], s[10:11]
	s_and_b64 vcc, vcc, s[8:9]
	v_cndmask_b32_e64 v35, v35, 16, vcc
	v_cndmask_b32_e32 v37, v37, v16, vcc
	v_and_b32_e32 v38, 0x20000, v36
	v_cmp_gt_i32_e64 s[8:9], 0, v35
	v_cmp_gt_f32_e64 s[10:11], v17, v37
	v_cmp_eq_u32_e32 vcc, 0, v38
	s_or_b64 s[8:9], s[8:9], s[10:11]
	s_and_b64 vcc, vcc, s[8:9]
	v_cndmask_b32_e64 v35, v35, 17, vcc
	v_cndmask_b32_e32 v37, v37, v17, vcc
	v_and_b32_e32 v38, 0x40000, v36
	v_cmp_gt_i32_e64 s[8:9], 0, v35
	v_cmp_gt_f32_e64 s[10:11], v14, v37
	v_cmp_eq_u32_e32 vcc, 0, v38
	s_or_b64 s[8:9], s[8:9], s[10:11]
	s_and_b64 vcc, vcc, s[8:9]
	v_cndmask_b32_e64 v35, v35, 18, vcc
	v_cndmask_b32_e32 v37, v37, v14, vcc
	v_and_b32_e32 v38, 0x80000, v36
	v_cmp_gt_i32_e64 s[8:9], 0, v35
	v_cmp_gt_f32_e64 s[10:11], v15, v37
	v_cmp_eq_u32_e32 vcc, 0, v38
	s_or_b64 s[8:9], s[8:9], s[10:11]
	s_and_b64 vcc, vcc, s[8:9]
	v_cndmask_b32_e64 v35, v35, 19, vcc
	v_cndmask_b32_e32 v37, v37, v15, vcc
	v_and_b32_e32 v38, 0x100000, v36
	v_cmp_gt_i32_e64 s[8:9], 0, v35
	v_cmp_gt_f32_e64 s[10:11], v12, v37
	v_cmp_eq_u32_e32 vcc, 0, v38
	s_or_b64 s[8:9], s[8:9], s[10:11]
	s_and_b64 vcc, vcc, s[8:9]
	v_cndmask_b32_e64 v35, v35, 20, vcc
	v_cndmask_b32_e32 v37, v37, v12, vcc
	v_and_b32_e32 v38, 0x200000, v36
	v_cmp_gt_i32_e64 s[8:9], 0, v35
	v_cmp_gt_f32_e64 s[10:11], v13, v37
	v_cmp_eq_u32_e32 vcc, 0, v38
	s_or_b64 s[8:9], s[8:9], s[10:11]
	s_and_b64 vcc, vcc, s[8:9]
	v_cndmask_b32_e64 v35, v35, 21, vcc
	v_cndmask_b32_e32 v37, v37, v13, vcc
	v_and_b32_e32 v38, 0x400000, v36
	v_cmp_gt_i32_e64 s[8:9], 0, v35
	v_cmp_gt_f32_e64 s[10:11], v10, v37
	v_cmp_eq_u32_e32 vcc, 0, v38
	s_or_b64 s[8:9], s[8:9], s[10:11]
	s_and_b64 vcc, vcc, s[8:9]
	v_cndmask_b32_e64 v35, v35, 22, vcc
	v_cndmask_b32_e32 v37, v37, v10, vcc
	v_and_b32_e32 v38, 0x800000, v36
	v_cmp_gt_i32_e64 s[8:9], 0, v35
	v_cmp_gt_f32_e64 s[10:11], v11, v37
	v_cmp_eq_u32_e32 vcc, 0, v38
	s_or_b64 s[8:9], s[8:9], s[10:11]
	s_and_b64 vcc, vcc, s[8:9]
	v_cndmask_b32_e64 v35, v35, 23, vcc
	v_cndmask_b32_e32 v37, v37, v11, vcc
	v_and_b32_e32 v38, 0x1000000, v36
	v_cmp_gt_i32_e64 s[8:9], 0, v35
	v_cmp_gt_f32_e64 s[10:11], v8, v37
	v_cmp_eq_u32_e32 vcc, 0, v38
	s_or_b64 s[8:9], s[8:9], s[10:11]
	s_and_b64 vcc, vcc, s[8:9]
	v_cndmask_b32_e64 v35, v35, 24, vcc
	v_cndmask_b32_e32 v37, v37, v8, vcc
	v_and_b32_e32 v38, 0x2000000, v36
	v_cmp_gt_i32_e64 s[8:9], 0, v35
	v_cmp_gt_f32_e64 s[10:11], v9, v37
	v_cmp_eq_u32_e32 vcc, 0, v38
	s_or_b64 s[8:9], s[8:9], s[10:11]
	s_and_b64 vcc, vcc, s[8:9]
	v_cndmask_b32_e64 v35, v35, 25, vcc
	v_cndmask_b32_e32 v37, v37, v9, vcc
	v_and_b32_e32 v38, 0x4000000, v36
	v_cmp_gt_i32_e64 s[8:9], 0, v35
	v_cmp_gt_f32_e64 s[10:11], v6, v37
	v_cmp_eq_u32_e32 vcc, 0, v38
	s_or_b64 s[8:9], s[8:9], s[10:11]
	s_and_b64 vcc, vcc, s[8:9]
	v_cndmask_b32_e64 v35, v35, 26, vcc
	v_cndmask_b32_e32 v37, v37, v6, vcc
	v_and_b32_e32 v38, 0x8000000, v36
	v_cmp_gt_i32_e64 s[8:9], 0, v35
	v_cmp_gt_f32_e64 s[10:11], v7, v37
	v_cmp_eq_u32_e32 vcc, 0, v38
	s_or_b64 s[8:9], s[8:9], s[10:11]
	s_and_b64 vcc, vcc, s[8:9]
	v_cndmask_b32_e64 v35, v35, 27, vcc
	v_cndmask_b32_e32 v37, v37, v7, vcc
	v_and_b32_e32 v38, 0x10000000, v36
	v_cmp_gt_i32_e64 s[8:9], 0, v35
	v_cmp_gt_f32_e64 s[10:11], v4, v37
	v_cmp_eq_u32_e32 vcc, 0, v38
	s_or_b64 s[8:9], s[8:9], s[10:11]
	s_and_b64 vcc, vcc, s[8:9]
	v_cndmask_b32_e64 v35, v35, 28, vcc
	v_cndmask_b32_e32 v37, v37, v4, vcc
	v_and_b32_e32 v38, 0x20000000, v36
	v_cmp_gt_i32_e64 s[8:9], 0, v35
	v_cmp_gt_f32_e64 s[10:11], v5, v37
	v_cmp_eq_u32_e32 vcc, 0, v38
	s_or_b64 s[8:9], s[8:9], s[10:11]
	s_and_b64 vcc, vcc, s[8:9]
	v_cndmask_b32_e64 v35, v35, 29, vcc
	v_cndmask_b32_e32 v37, v37, v5, vcc
	v_and_b32_e32 v38, 2.0, v36
	v_cmp_gt_i32_e64 s[8:9], 0, v35
	v_cmp_gt_f32_e64 s[10:11], v2, v37
	v_cmp_eq_u32_e32 vcc, 0, v38
	s_or_b64 s[8:9], s[8:9], s[10:11]
	s_and_b64 vcc, vcc, s[8:9]
	v_cndmask_b32_e64 v35, v35, 30, vcc
	v_cndmask_b32_e32 v37, v37, v2, vcc
	v_cmp_gt_i32_e32 vcc, 0, v35
	v_cmp_gt_f32_e64 s[8:9], v3, v37
	s_or_b64 vcc, vcc, s[8:9]
	v_cndmask_b32_e64 v38, v35, 31, vcc
	v_cndmask_b32_e32 v39, v37, v3, vcc
	v_cmp_eq_u32_e32 vcc, 31, v144
	s_nop 1
	v_cndmask_b32_e32 v148, v38, v35, vcc
	v_lshl_or_b32 v36, 1, v148, v36
	v_cndmask_b32_e32 v35, v39, v37, vcc
	v_and_b32_e32 v37, 1, v36
	v_cmp_eq_u32_e32 vcc, 1, v37
	v_and_b32_e32 v39, 2, v36
	v_bfe_i32 v38, v36, 0, 1
	v_cndmask_b32_e32 v37, v32, v198, vcc
	v_cmp_gt_f32_e64 s[8:9], v33, v37
	s_or_b64 vcc, vcc, s[8:9]
	v_cndmask_b32_e64 v40, 0, 1, vcc
	v_cndmask_b32_e32 v41, v32, v33, vcc
	v_cmp_eq_u32_e32 vcc, 0, v39
	v_and_b32_e32 v39, 4, v36
	s_nop 0
	v_cndmask_b32_e32 v38, v38, v40, vcc
	v_cndmask_b32_e32 v37, v37, v41, vcc
	v_cmp_eq_u32_e32 vcc, 0, v39
	v_and_b32_e32 v39, 3, v36
	v_cmp_eq_u32_e64 s[8:9], 3, v39
	v_cmp_gt_f32_e64 s[10:11], v30, v37
	s_or_b64 s[8:9], s[8:9], s[10:11]
	s_and_b64 vcc, vcc, s[8:9]
	v_cndmask_b32_e64 v38, v38, 2, vcc
	v_cndmask_b32_e32 v37, v37, v30, vcc
	v_and_b32_e32 v39, 8, v36
	v_cmp_gt_i32_e64 s[8:9], 0, v38
	v_cmp_gt_f32_e64 s[10:11], v31, v37
	v_cmp_eq_u32_e32 vcc, 0, v39
	s_or_b64 s[8:9], s[8:9], s[10:11]
	s_and_b64 vcc, vcc, s[8:9]
	v_cndmask_b32_e64 v38, v38, 3, vcc
	v_cndmask_b32_e32 v37, v37, v31, vcc
	v_and_b32_e32 v39, 16, v36
	v_cmp_gt_i32_e64 s[8:9], 0, v38
	v_cmp_gt_f32_e64 s[10:11], v28, v37
	v_cmp_eq_u32_e32 vcc, 0, v39
	s_or_b64 s[8:9], s[8:9], s[10:11]
	s_and_b64 vcc, vcc, s[8:9]
	v_cndmask_b32_e64 v38, v38, 4, vcc
	v_cndmask_b32_e32 v37, v37, v28, vcc
	v_and_b32_e32 v39, 32, v36
	v_cmp_gt_i32_e64 s[8:9], 0, v38
	v_cmp_gt_f32_e64 s[10:11], v29, v37
	v_cmp_eq_u32_e32 vcc, 0, v39
	s_or_b64 s[8:9], s[8:9], s[10:11]
	s_and_b64 vcc, vcc, s[8:9]
	v_cndmask_b32_e64 v38, v38, 5, vcc
	v_cndmask_b32_e32 v37, v37, v29, vcc
	v_and_b32_e32 v39, 64, v36
	v_cmp_gt_i32_e64 s[8:9], 0, v38
	v_cmp_gt_f32_e64 s[10:11], v26, v37
	v_cmp_eq_u32_e32 vcc, 0, v39
	s_or_b64 s[8:9], s[8:9], s[10:11]
	s_and_b64 vcc, vcc, s[8:9]
	v_cndmask_b32_e64 v38, v38, 6, vcc
	v_cndmask_b32_e32 v37, v37, v26, vcc
	v_and_b32_e32 v39, 0x80, v36
	v_cmp_gt_i32_e64 s[8:9], 0, v38
	v_cmp_gt_f32_e64 s[10:11], v27, v37
	v_cmp_eq_u32_e32 vcc, 0, v39
	s_or_b64 s[8:9], s[8:9], s[10:11]
	s_and_b64 vcc, vcc, s[8:9]
	v_cndmask_b32_e64 v38, v38, 7, vcc
	v_cndmask_b32_e32 v37, v37, v27, vcc
	v_and_b32_e32 v39, 0x100, v36
	v_cmp_gt_i32_e64 s[8:9], 0, v38
	v_cmp_gt_f32_e64 s[10:11], v24, v37
	v_cmp_eq_u32_e32 vcc, 0, v39
	s_or_b64 s[8:9], s[8:9], s[10:11]
	s_and_b64 vcc, vcc, s[8:9]
	v_cndmask_b32_e64 v38, v38, 8, vcc
	v_cndmask_b32_e32 v37, v37, v24, vcc
	v_and_b32_e32 v39, 0x200, v36
	v_cmp_gt_i32_e64 s[8:9], 0, v38
	v_cmp_gt_f32_e64 s[10:11], v25, v37
	v_cmp_eq_u32_e32 vcc, 0, v39
	s_or_b64 s[8:9], s[8:9], s[10:11]
	s_and_b64 vcc, vcc, s[8:9]
	v_cndmask_b32_e64 v38, v38, 9, vcc
	v_cndmask_b32_e32 v37, v37, v25, vcc
	v_and_b32_e32 v39, 0x400, v36
	v_cmp_gt_i32_e64 s[8:9], 0, v38
	v_cmp_gt_f32_e64 s[10:11], v22, v37
	v_cmp_eq_u32_e32 vcc, 0, v39
	s_or_b64 s[8:9], s[8:9], s[10:11]
	s_and_b64 vcc, vcc, s[8:9]
	v_cndmask_b32_e64 v38, v38, 10, vcc
	v_cndmask_b32_e32 v37, v37, v22, vcc
	v_and_b32_e32 v39, 0x800, v36
	v_cmp_gt_i32_e64 s[8:9], 0, v38
	v_cmp_gt_f32_e64 s[10:11], v23, v37
	v_cmp_eq_u32_e32 vcc, 0, v39
	s_or_b64 s[8:9], s[8:9], s[10:11]
	s_and_b64 vcc, vcc, s[8:9]
	v_cndmask_b32_e64 v38, v38, 11, vcc
	v_cndmask_b32_e32 v37, v37, v23, vcc
	v_and_b32_e32 v39, 0x1000, v36
	v_cmp_gt_i32_e64 s[8:9], 0, v38
	v_cmp_gt_f32_e64 s[10:11], v20, v37
	v_cmp_eq_u32_e32 vcc, 0, v39
	s_or_b64 s[8:9], s[8:9], s[10:11]
	s_and_b64 vcc, vcc, s[8:9]
	v_cndmask_b32_e64 v38, v38, 12, vcc
	v_cndmask_b32_e32 v37, v37, v20, vcc
	v_and_b32_e32 v39, 0x2000, v36
	v_cmp_gt_i32_e64 s[8:9], 0, v38
	v_cmp_gt_f32_e64 s[10:11], v21, v37
	v_cmp_eq_u32_e32 vcc, 0, v39
	s_or_b64 s[8:9], s[8:9], s[10:11]
	s_and_b64 vcc, vcc, s[8:9]
	v_cndmask_b32_e64 v38, v38, 13, vcc
	v_cndmask_b32_e32 v37, v37, v21, vcc
	v_and_b32_e32 v39, 0x4000, v36
	v_cmp_gt_i32_e64 s[8:9], 0, v38
	v_cmp_gt_f32_e64 s[10:11], v18, v37
	v_cmp_eq_u32_e32 vcc, 0, v39
	s_or_b64 s[8:9], s[8:9], s[10:11]
	s_and_b64 vcc, vcc, s[8:9]
	v_cndmask_b32_e64 v38, v38, 14, vcc
	v_cndmask_b32_e32 v37, v37, v18, vcc
	v_and_b32_e32 v39, 0x8000, v36
	v_cmp_gt_i32_e64 s[8:9], 0, v38
	v_cmp_gt_f32_e64 s[10:11], v19, v37
	v_cmp_eq_u32_e32 vcc, 0, v39
	s_or_b64 s[8:9], s[8:9], s[10:11]
	s_and_b64 vcc, vcc, s[8:9]
	v_cndmask_b32_e64 v38, v38, 15, vcc
	v_cndmask_b32_e32 v37, v37, v19, vcc
	v_and_b32_e32 v39, 0x10000, v36
	v_cmp_gt_i32_e64 s[8:9], 0, v38
	v_cmp_gt_f32_e64 s[10:11], v16, v37
	v_cmp_eq_u32_e32 vcc, 0, v39
	s_or_b64 s[8:9], s[8:9], s[10:11]
	s_and_b64 vcc, vcc, s[8:9]
	v_cndmask_b32_e64 v38, v38, 16, vcc
	v_cndmask_b32_e32 v37, v37, v16, vcc
	v_and_b32_e32 v39, 0x20000, v36
	v_cmp_gt_i32_e64 s[8:9], 0, v38
	v_cmp_gt_f32_e64 s[10:11], v17, v37
	v_cmp_eq_u32_e32 vcc, 0, v39
	s_or_b64 s[8:9], s[8:9], s[10:11]
	s_and_b64 vcc, vcc, s[8:9]
	v_cndmask_b32_e64 v38, v38, 17, vcc
	v_cndmask_b32_e32 v37, v37, v17, vcc
	v_and_b32_e32 v39, 0x40000, v36
	v_cmp_gt_i32_e64 s[8:9], 0, v38
	v_cmp_gt_f32_e64 s[10:11], v14, v37
	v_cmp_eq_u32_e32 vcc, 0, v39
	s_or_b64 s[8:9], s[8:9], s[10:11]
	s_and_b64 vcc, vcc, s[8:9]
	v_cndmask_b32_e64 v38, v38, 18, vcc
	v_cndmask_b32_e32 v37, v37, v14, vcc
	v_and_b32_e32 v39, 0x80000, v36
	v_cmp_gt_i32_e64 s[8:9], 0, v38
	v_cmp_gt_f32_e64 s[10:11], v15, v37
	v_cmp_eq_u32_e32 vcc, 0, v39
	s_or_b64 s[8:9], s[8:9], s[10:11]
	s_and_b64 vcc, vcc, s[8:9]
	v_cndmask_b32_e64 v38, v38, 19, vcc
	v_cndmask_b32_e32 v37, v37, v15, vcc
	v_and_b32_e32 v39, 0x100000, v36
	v_cmp_gt_i32_e64 s[8:9], 0, v38
	v_cmp_gt_f32_e64 s[10:11], v12, v37
	v_cmp_eq_u32_e32 vcc, 0, v39
	s_or_b64 s[8:9], s[8:9], s[10:11]
	s_and_b64 vcc, vcc, s[8:9]
	v_cndmask_b32_e64 v38, v38, 20, vcc
	v_cndmask_b32_e32 v37, v37, v12, vcc
	v_and_b32_e32 v39, 0x200000, v36
	v_cmp_gt_i32_e64 s[8:9], 0, v38
	v_cmp_gt_f32_e64 s[10:11], v13, v37
	v_cmp_eq_u32_e32 vcc, 0, v39
	s_or_b64 s[8:9], s[8:9], s[10:11]
	s_and_b64 vcc, vcc, s[8:9]
	v_cndmask_b32_e64 v38, v38, 21, vcc
	v_cndmask_b32_e32 v37, v37, v13, vcc
	v_and_b32_e32 v39, 0x400000, v36
	v_cmp_gt_i32_e64 s[8:9], 0, v38
	v_cmp_gt_f32_e64 s[10:11], v10, v37
	v_cmp_eq_u32_e32 vcc, 0, v39
	s_or_b64 s[8:9], s[8:9], s[10:11]
	s_and_b64 vcc, vcc, s[8:9]
	v_cndmask_b32_e64 v38, v38, 22, vcc
	v_cndmask_b32_e32 v37, v37, v10, vcc
	v_and_b32_e32 v39, 0x800000, v36
	v_cmp_gt_i32_e64 s[8:9], 0, v38
	v_cmp_gt_f32_e64 s[10:11], v11, v37
	v_cmp_eq_u32_e32 vcc, 0, v39
	s_or_b64 s[8:9], s[8:9], s[10:11]
	s_and_b64 vcc, vcc, s[8:9]
	v_cndmask_b32_e64 v38, v38, 23, vcc
	v_cndmask_b32_e32 v37, v37, v11, vcc
	v_and_b32_e32 v39, 0x1000000, v36
	v_cmp_gt_i32_e64 s[8:9], 0, v38
	v_cmp_gt_f32_e64 s[10:11], v8, v37
	v_cmp_eq_u32_e32 vcc, 0, v39
	s_or_b64 s[8:9], s[8:9], s[10:11]
	s_and_b64 vcc, vcc, s[8:9]
	v_cndmask_b32_e64 v38, v38, 24, vcc
	v_cndmask_b32_e32 v37, v37, v8, vcc
	v_and_b32_e32 v39, 0x2000000, v36
	v_cmp_gt_i32_e64 s[8:9], 0, v38
	v_cmp_gt_f32_e64 s[10:11], v9, v37
	v_cmp_eq_u32_e32 vcc, 0, v39
	s_or_b64 s[8:9], s[8:9], s[10:11]
	s_and_b64 vcc, vcc, s[8:9]
	v_cndmask_b32_e64 v38, v38, 25, vcc
	v_cndmask_b32_e32 v37, v37, v9, vcc
	v_and_b32_e32 v39, 0x4000000, v36
	v_cmp_gt_i32_e64 s[8:9], 0, v38
	v_cmp_gt_f32_e64 s[10:11], v6, v37
	v_cmp_eq_u32_e32 vcc, 0, v39
	s_or_b64 s[8:9], s[8:9], s[10:11]
	s_and_b64 vcc, vcc, s[8:9]
	v_cndmask_b32_e64 v38, v38, 26, vcc
	v_cndmask_b32_e32 v37, v37, v6, vcc
	v_and_b32_e32 v39, 0x8000000, v36
	v_cmp_gt_i32_e64 s[8:9], 0, v38
	v_cmp_gt_f32_e64 s[10:11], v7, v37
	v_cmp_eq_u32_e32 vcc, 0, v39
	s_or_b64 s[8:9], s[8:9], s[10:11]
	s_and_b64 vcc, vcc, s[8:9]
	v_cndmask_b32_e64 v38, v38, 27, vcc
	v_cndmask_b32_e32 v37, v37, v7, vcc
	v_and_b32_e32 v39, 0x10000000, v36
	v_cmp_gt_i32_e64 s[8:9], 0, v38
	v_cmp_gt_f32_e64 s[10:11], v4, v37
	v_cmp_eq_u32_e32 vcc, 0, v39
	s_or_b64 s[8:9], s[8:9], s[10:11]
	s_and_b64 vcc, vcc, s[8:9]
	v_cndmask_b32_e64 v38, v38, 28, vcc
	v_cndmask_b32_e32 v37, v37, v4, vcc
	v_and_b32_e32 v39, 0x20000000, v36
	v_cmp_gt_i32_e64 s[8:9], 0, v38
	v_cmp_gt_f32_e64 s[10:11], v5, v37
	v_cmp_eq_u32_e32 vcc, 0, v39
	s_or_b64 s[8:9], s[8:9], s[10:11]
	s_and_b64 vcc, vcc, s[8:9]
	v_cndmask_b32_e64 v38, v38, 29, vcc
	v_cndmask_b32_e32 v37, v37, v5, vcc
	v_and_b32_e32 v39, 2.0, v36
	v_cmp_gt_i32_e64 s[8:9], 0, v38
	v_cmp_gt_f32_e64 s[10:11], v2, v37
	v_cmp_eq_u32_e32 vcc, 0, v39
	s_or_b64 s[8:9], s[8:9], s[10:11]
	s_and_b64 vcc, vcc, s[8:9]
	v_cndmask_b32_e64 v38, v38, 30, vcc
	v_cndmask_b32_e32 v37, v37, v2, vcc
	v_cmp_gt_i32_e64 s[8:9], 0, v38
	v_cmp_gt_f32_e64 s[10:11], v3, v37
	v_cmp_lt_i32_e32 vcc, -1, v36
	s_or_b64 s[8:9], s[8:9], s[10:11]
	s_and_b64 vcc, vcc, s[8:9]
	v_cndmask_b32_e64 v152, v38, 31, vcc
	v_lshlrev_b32_e64 v38, v152, 1
	v_or_b32_e32 v39, v38, v36
	v_and_b32_e32 v40, 1, v39
	v_cndmask_b32_e32 v37, v37, v3, vcc
	v_cmp_eq_u32_e32 vcc, 1, v40
	v_bitop3_b32 v42, v38, 2, v36 bitop3:0xc8
	v_bfe_i32 v41, v39, 0, 1
	v_cndmask_b32_e32 v40, v32, v198, vcc
	v_cmp_gt_f32_e64 s[8:9], v33, v40
	s_or_b64 vcc, vcc, s[8:9]
	v_cndmask_b32_e64 v43, 0, 1, vcc
	v_cndmask_b32_e32 v32, v32, v33, vcc
	v_cmp_eq_u32_e32 vcc, 0, v42
	s_nop 1
	v_cndmask_b32_e32 v32, v40, v32, vcc
	v_bitop3_b32 v40, v38, 4, v36 bitop3:0xc8
	v_cndmask_b32_e32 v33, v41, v43, vcc
	v_cmp_eq_u32_e32 vcc, 0, v40
	v_bitop3_b32 v40, v38, 3, v36 bitop3:0xc8
	v_cmp_eq_u32_e64 s[8:9], 3, v40
	v_cmp_gt_f32_e64 s[10:11], v30, v32
	s_or_b64 s[8:9], s[8:9], s[10:11]
	s_and_b64 vcc, vcc, s[8:9]
	v_cndmask_b32_e64 v33, v33, 2, vcc
	v_cndmask_b32_e32 v30, v32, v30, vcc
	v_bitop3_b32 v32, v38, 8, v36 bitop3:0xc8
	v_cmp_gt_i32_e64 s[8:9], 0, v33
	v_cmp_gt_f32_e64 s[10:11], v31, v30
	v_cmp_eq_u32_e32 vcc, 0, v32
	s_or_b64 s[8:9], s[8:9], s[10:11]
	s_and_b64 vcc, vcc, s[8:9]
	v_cndmask_b32_e64 v32, v33, 3, vcc
	v_cndmask_b32_e32 v30, v30, v31, vcc
	v_bitop3_b32 v31, v38, 16, v36 bitop3:0xc8
	v_cmp_gt_i32_e64 s[8:9], 0, v32
	v_cmp_gt_f32_e64 s[10:11], v28, v30
	v_cmp_eq_u32_e32 vcc, 0, v31
	s_or_b64 s[8:9], s[8:9], s[10:11]
	s_and_b64 vcc, vcc, s[8:9]
	v_cndmask_b32_e64 v31, v32, 4, vcc
	v_cndmask_b32_e32 v28, v30, v28, vcc
	v_bitop3_b32 v30, v38, 32, v36 bitop3:0xc8
	v_cmp_gt_i32_e64 s[8:9], 0, v31
	v_cmp_gt_f32_e64 s[10:11], v29, v28
	v_cmp_eq_u32_e32 vcc, 0, v30
	s_or_b64 s[8:9], s[8:9], s[10:11]
	s_and_b64 vcc, vcc, s[8:9]
	v_cndmask_b32_e64 v30, v31, 5, vcc
	v_cndmask_b32_e32 v28, v28, v29, vcc
	v_bitop3_b32 v29, v38, 64, v36 bitop3:0xc8
	v_cmp_gt_i32_e64 s[8:9], 0, v30
	v_cmp_gt_f32_e64 s[10:11], v26, v28
	v_cmp_eq_u32_e32 vcc, 0, v29
	s_or_b64 s[8:9], s[8:9], s[10:11]
	s_and_b64 vcc, vcc, s[8:9]
	v_cndmask_b32_e64 v29, v30, 6, vcc
	v_cndmask_b32_e32 v26, v28, v26, vcc
	v_bitop3_b32 v28, v38, s26, v36 bitop3:0xc8
	v_cmp_gt_i32_e64 s[8:9], 0, v29
	v_cmp_gt_f32_e64 s[10:11], v27, v26
	v_cmp_eq_u32_e32 vcc, 0, v28
	s_or_b64 s[8:9], s[8:9], s[10:11]
	s_and_b64 vcc, vcc, s[8:9]
	v_cndmask_b32_e64 v28, v29, 7, vcc
	v_cndmask_b32_e32 v26, v26, v27, vcc
	v_bitop3_b32 v27, v38, s27, v36 bitop3:0xc8
	v_cmp_gt_i32_e64 s[8:9], 0, v28
	v_cmp_gt_f32_e64 s[10:11], v24, v26
	v_cmp_eq_u32_e32 vcc, 0, v27
	s_or_b64 s[8:9], s[8:9], s[10:11]
	s_and_b64 vcc, vcc, s[8:9]
	v_cndmask_b32_e64 v27, v28, 8, vcc
	v_cndmask_b32_e32 v24, v26, v24, vcc
	v_bitop3_b32 v26, v38, s28, v36 bitop3:0xc8
	v_cmp_gt_i32_e64 s[8:9], 0, v27
	v_cmp_gt_f32_e64 s[10:11], v25, v24
	v_cmp_eq_u32_e32 vcc, 0, v26
	s_or_b64 s[8:9], s[8:9], s[10:11]
	s_and_b64 vcc, vcc, s[8:9]
	v_cndmask_b32_e64 v26, v27, 9, vcc
	v_cndmask_b32_e32 v24, v24, v25, vcc
	v_bitop3_b32 v25, v38, s29, v36 bitop3:0xc8
	v_cmp_gt_i32_e64 s[8:9], 0, v26
	v_cmp_gt_f32_e64 s[10:11], v22, v24
	v_cmp_eq_u32_e32 vcc, 0, v25
	s_or_b64 s[8:9], s[8:9], s[10:11]
	s_and_b64 vcc, vcc, s[8:9]
	v_cndmask_b32_e64 v25, v26, 10, vcc
	v_cndmask_b32_e32 v22, v24, v22, vcc
	v_bitop3_b32 v24, v38, s30, v36 bitop3:0xc8
	v_cmp_gt_i32_e64 s[8:9], 0, v25
	v_cmp_gt_f32_e64 s[10:11], v23, v22
	v_cmp_eq_u32_e32 vcc, 0, v24
	s_or_b64 s[8:9], s[8:9], s[10:11]
	s_and_b64 vcc, vcc, s[8:9]
	v_cndmask_b32_e64 v24, v25, 11, vcc
	v_cndmask_b32_e32 v22, v22, v23, vcc
	v_bitop3_b32 v23, v38, s31, v36 bitop3:0xc8
	v_cmp_gt_i32_e64 s[8:9], 0, v24
	v_cmp_gt_f32_e64 s[10:11], v20, v22
	v_cmp_eq_u32_e32 vcc, 0, v23
	s_or_b64 s[8:9], s[8:9], s[10:11]
	s_and_b64 vcc, vcc, s[8:9]
	v_cndmask_b32_e64 v23, v24, 12, vcc
	v_cndmask_b32_e32 v20, v22, v20, vcc
	v_bitop3_b32 v22, v38, s33, v36 bitop3:0xc8
	v_cmp_gt_i32_e64 s[8:9], 0, v23
	v_cmp_gt_f32_e64 s[10:11], v21, v20
	v_cmp_eq_u32_e32 vcc, 0, v22
	s_or_b64 s[8:9], s[8:9], s[10:11]
	s_and_b64 vcc, vcc, s[8:9]
	v_cndmask_b32_e64 v22, v23, 13, vcc
	v_cndmask_b32_e32 v20, v20, v21, vcc
	v_bitop3_b32 v21, v38, s34, v36 bitop3:0xc8
	v_cmp_gt_i32_e64 s[8:9], 0, v22
	v_cmp_gt_f32_e64 s[10:11], v18, v20
	v_cmp_eq_u32_e32 vcc, 0, v21
	s_or_b64 s[8:9], s[8:9], s[10:11]
	s_and_b64 vcc, vcc, s[8:9]
	v_cndmask_b32_e64 v21, v22, 14, vcc
	v_cndmask_b32_e32 v18, v20, v18, vcc
	v_bitop3_b32 v20, v38, s35, v36 bitop3:0xc8
	v_cmp_gt_i32_e64 s[8:9], 0, v21
	v_cmp_gt_f32_e64 s[10:11], v19, v18
	v_cmp_eq_u32_e32 vcc, 0, v20
	s_or_b64 s[8:9], s[8:9], s[10:11]
	s_and_b64 vcc, vcc, s[8:9]
	v_cndmask_b32_e64 v20, v21, 15, vcc
	v_cndmask_b32_e32 v18, v18, v19, vcc
	v_bitop3_b32 v19, v38, s36, v36 bitop3:0xc8
	v_cmp_gt_i32_e64 s[8:9], 0, v20
	v_cmp_gt_f32_e64 s[10:11], v16, v18
	v_cmp_eq_u32_e32 vcc, 0, v19
	s_or_b64 s[8:9], s[8:9], s[10:11]
	s_and_b64 vcc, vcc, s[8:9]
	v_cndmask_b32_e64 v19, v20, 16, vcc
	v_cndmask_b32_e32 v16, v18, v16, vcc
	v_bitop3_b32 v18, v38, s37, v36 bitop3:0xc8
	v_cmp_gt_i32_e64 s[8:9], 0, v19
	v_cmp_gt_f32_e64 s[10:11], v17, v16
	v_cmp_eq_u32_e32 vcc, 0, v18
	s_or_b64 s[8:9], s[8:9], s[10:11]
	s_and_b64 vcc, vcc, s[8:9]
	v_cndmask_b32_e64 v18, v19, 17, vcc
	v_cndmask_b32_e32 v16, v16, v17, vcc
	v_bitop3_b32 v17, v38, s38, v36 bitop3:0xc8
	v_cmp_gt_i32_e64 s[8:9], 0, v18
	v_cmp_gt_f32_e64 s[10:11], v14, v16
	v_cmp_eq_u32_e32 vcc, 0, v17
	s_or_b64 s[8:9], s[8:9], s[10:11]
	s_and_b64 vcc, vcc, s[8:9]
	v_cndmask_b32_e64 v17, v18, 18, vcc
	v_cndmask_b32_e32 v14, v16, v14, vcc
	v_bitop3_b32 v16, v38, s39, v36 bitop3:0xc8
	v_cmp_gt_i32_e64 s[8:9], 0, v17
	v_cmp_gt_f32_e64 s[10:11], v15, v14
	v_cmp_eq_u32_e32 vcc, 0, v16
	s_or_b64 s[8:9], s[8:9], s[10:11]
	s_and_b64 vcc, vcc, s[8:9]
	v_cndmask_b32_e64 v16, v17, 19, vcc
	v_cndmask_b32_e32 v14, v14, v15, vcc
	v_bitop3_b32 v15, v38, s40, v36 bitop3:0xc8
	v_cmp_gt_i32_e64 s[8:9], 0, v16
	v_cmp_gt_f32_e64 s[10:11], v12, v14
	v_cmp_eq_u32_e32 vcc, 0, v15
	s_or_b64 s[8:9], s[8:9], s[10:11]
	s_and_b64 vcc, vcc, s[8:9]
	v_cndmask_b32_e64 v15, v16, 20, vcc
	v_cndmask_b32_e32 v12, v14, v12, vcc
	v_bitop3_b32 v14, v38, s41, v36 bitop3:0xc8
	v_cmp_gt_i32_e64 s[8:9], 0, v15
	v_cmp_gt_f32_e64 s[10:11], v13, v12
	v_cmp_eq_u32_e32 vcc, 0, v14
	s_or_b64 s[8:9], s[8:9], s[10:11]
	s_and_b64 vcc, vcc, s[8:9]
	v_cndmask_b32_e64 v14, v15, 21, vcc
	v_cndmask_b32_e32 v12, v12, v13, vcc
	v_bitop3_b32 v13, v38, s42, v36 bitop3:0xc8
	v_cmp_gt_i32_e64 s[8:9], 0, v14
	v_cmp_gt_f32_e64 s[10:11], v10, v12
	v_cmp_eq_u32_e32 vcc, 0, v13
	s_or_b64 s[8:9], s[8:9], s[10:11]
	s_and_b64 vcc, vcc, s[8:9]
	v_cndmask_b32_e64 v13, v14, 22, vcc
	v_cndmask_b32_e32 v10, v12, v10, vcc
	v_bitop3_b32 v12, v38, s43, v36 bitop3:0xc8
	v_cmp_gt_i32_e64 s[8:9], 0, v13
	v_cmp_gt_f32_e64 s[10:11], v11, v10
	v_cmp_eq_u32_e32 vcc, 0, v12
	s_or_b64 s[8:9], s[8:9], s[10:11]
	s_and_b64 vcc, vcc, s[8:9]
	v_cndmask_b32_e64 v12, v13, 23, vcc
	v_cndmask_b32_e32 v10, v10, v11, vcc
	v_bitop3_b32 v11, v38, s44, v36 bitop3:0xc8
	v_cmp_gt_i32_e64 s[8:9], 0, v12
	v_cmp_gt_f32_e64 s[10:11], v8, v10
	v_cmp_eq_u32_e32 vcc, 0, v11
	s_or_b64 s[8:9], s[8:9], s[10:11]
	s_and_b64 vcc, vcc, s[8:9]
	v_cndmask_b32_e64 v11, v12, 24, vcc
	v_cndmask_b32_e32 v8, v10, v8, vcc
	v_bitop3_b32 v10, v38, s45, v36 bitop3:0xc8
	v_cmp_gt_i32_e64 s[8:9], 0, v11
	v_cmp_gt_f32_e64 s[10:11], v9, v8
	v_cmp_eq_u32_e32 vcc, 0, v10
	s_or_b64 s[8:9], s[8:9], s[10:11]
	s_and_b64 vcc, vcc, s[8:9]
	v_cndmask_b32_e64 v10, v11, 25, vcc
	v_cndmask_b32_e32 v8, v8, v9, vcc
	v_bitop3_b32 v9, v38, s46, v36 bitop3:0xc8
	v_cmp_gt_i32_e64 s[8:9], 0, v10
	v_cmp_gt_f32_e64 s[10:11], v6, v8
	v_cmp_eq_u32_e32 vcc, 0, v9
	s_or_b64 s[8:9], s[8:9], s[10:11]
	s_and_b64 vcc, vcc, s[8:9]
	v_cndmask_b32_e64 v9, v10, 26, vcc
	v_cndmask_b32_e32 v6, v8, v6, vcc
	v_bitop3_b32 v8, v38, s47, v36 bitop3:0xc8
	v_cmp_gt_i32_e64 s[8:9], 0, v9
	v_cmp_gt_f32_e64 s[10:11], v7, v6
	v_cmp_eq_u32_e32 vcc, 0, v8
	s_or_b64 s[8:9], s[8:9], s[10:11]
	s_and_b64 vcc, vcc, s[8:9]
	v_cndmask_b32_e64 v8, v9, 27, vcc
	v_cndmask_b32_e32 v6, v6, v7, vcc
	v_bitop3_b32 v7, v38, s48, v36 bitop3:0xc8
	v_cmp_gt_i32_e64 s[8:9], 0, v8
	v_cmp_gt_f32_e64 s[10:11], v4, v6
	v_cmp_eq_u32_e32 vcc, 0, v7
	s_or_b64 s[8:9], s[8:9], s[10:11]
	s_and_b64 vcc, vcc, s[8:9]
	v_cndmask_b32_e64 v7, v8, 28, vcc
	v_cndmask_b32_e32 v4, v6, v4, vcc
	v_bitop3_b32 v6, v38, s49, v36 bitop3:0xc8
	v_cmp_gt_i32_e64 s[8:9], 0, v7
	v_cmp_gt_f32_e64 s[10:11], v5, v4
	v_cmp_eq_u32_e32 vcc, 0, v6
	s_or_b64 s[8:9], s[8:9], s[10:11]
	s_and_b64 vcc, vcc, s[8:9]
	v_cndmask_b32_e64 v6, v7, 29, vcc
	v_cndmask_b32_e32 v4, v4, v5, vcc
	v_bitop3_b32 v5, v38, 2.0, v36 bitop3:0xc8
	v_cmp_gt_i32_e64 s[8:9], 0, v6
	v_cmp_gt_f32_e64 s[10:11], v2, v4
	v_cmp_eq_u32_e32 vcc, 0, v5
	s_or_b64 s[8:9], s[8:9], s[10:11]
	s_and_b64 vcc, vcc, s[8:9]
	v_cndmask_b32_e32 v2, v4, v2, vcc
	v_sub_f32_e32 v4, v35, v34
	v_cndmask_b32_e64 v5, v6, 30, vcc
	v_mul_f32_e32 v6, 0x3fb8aa3b, v4
	v_fma_f32 v7, v4, s50, -v6
	v_rndne_f32_e32 v8, v6
	v_fmac_f32_e32 v7, 0x32a5705f, v4
	v_sub_f32_e32 v6, v6, v8
	v_add_f32_e32 v6, v6, v7
	v_cmp_gt_i32_e64 s[8:9], 0, v5
	v_cmp_gt_f32_e64 s[10:11], v3, v2
	v_exp_f32_e32 v6, v6
	v_cvt_i32_f32_e32 v7, v8
	v_cmp_lt_i32_e32 vcc, -1, v39
	s_or_b64 s[8:9], s[8:9], s[10:11]
	s_and_b64 vcc, vcc, s[8:9]
	v_cndmask_b32_e64 v156, v5, 31, vcc
	v_sub_f32_e32 v5, v37, v34
	v_cndmask_b32_e32 v2, v2, v3, vcc
	v_ldexp_f32 v3, v6, v7
	v_mul_f32_e32 v6, 0x3fb8aa3b, v5
	v_fma_f32 v7, v5, s50, -v6
	v_rndne_f32_e32 v8, v6
	v_fmac_f32_e32 v7, 0x32a5705f, v5
	v_sub_f32_e32 v6, v6, v8
	v_add_f32_e32 v6, v6, v7
	v_exp_f32_e32 v6, v6
	v_cvt_i32_f32_e32 v7, v8
	v_cmp_ngt_f32_e32 vcc, s51, v4
	v_sub_f32_e32 v2, v2, v34
	s_nop 0
	v_cndmask_b32_e32 v3, 0, v3, vcc
	v_cmp_nlt_f32_e32 vcc, s52, v4
	s_nop 1
	v_cndmask_b32_e32 v4, v199, v3, vcc
	v_ldexp_f32 v3, v6, v7
	v_mul_f32_e32 v6, 0x3fb8aa3b, v2
	v_fma_f32 v7, v2, s50, -v6
	v_rndne_f32_e32 v8, v6
	v_fmac_f32_e32 v7, 0x32a5705f, v2
	v_sub_f32_e32 v6, v6, v8
	v_add_f32_e32 v6, v6, v7
	v_exp_f32_e32 v6, v6
	v_cvt_i32_f32_e32 v7, v8
	v_cmp_ngt_f32_e32 vcc, s51, v5
	s_nop 1
	v_cndmask_b32_e32 v3, 0, v3, vcc
	v_cmp_nlt_f32_e32 vcc, s52, v5
	v_ldexp_f32 v5, v6, v7
	s_nop 0
	v_cndmask_b32_e32 v3, v199, v3, vcc
	v_cmp_ngt_f32_e32 vcc, s51, v2
	s_nop 1
	v_cndmask_b32_e32 v5, 0, v5, vcc
	v_cmp_nlt_f32_e32 vcc, s52, v2
	s_nop 1
	v_cndmask_b32_e32 v2, v199, v5, vcc
	v_add_f32_e32 v5, 1.0, v4
	v_add_f32_e32 v5, v5, v3
	v_add_f32_e32 v5, v5, v2
	v_div_scale_f32 v6, s[8:9], v5, v5, 1.0
	v_rcp_f32_e32 v7, v6
	s_nop 0
	v_fma_f32 v8, -v6, v7, 1.0
	v_fmac_f32_e32 v7, v8, v7
	v_div_scale_f32 v8, vcc, 1.0, v5, 1.0
	v_mul_f32_e32 v9, v8, v7
	v_fma_f32 v10, -v6, v9, v8
	v_fmac_f32_e32 v9, v10, v7
	v_fma_f32 v6, -v6, v9, v8
	v_lshl_add_u32 v8, v144, 2, s1
	ds_add_rtn_u32 v200, v8, v197
	v_lshl_add_u32 v8, v148, 2, s1
	ds_add_rtn_u32 v201, v8, v197
	v_lshl_add_u32 v8, v152, 2, s1
	ds_add_rtn_u32 v202, v8, v197
	v_lshl_add_u32 v8, v156, 2, s1
	ds_add_rtn_u32 v204, v8, v197
	v_div_fmas_f32 v6, v6, v7, v9
	v_div_fixup_f32 v138, v6, v5, 1.0
	v_mul_f32_e32 v203, v4, v138
	v_pk_mul_f32 v[162:163], v[2:3], v[138:139] op_sel_hi:[1,0]

.LBB0_655:
	s_lshl_b32 s35, s63, 10
	s_and_b32 s35, s35, 0x400
	v_mov_b32_e32 v28, v0
	s_add_i32 s35, s35, 0
	s_add_i32 s35, s35, 0x24cc0
	v_and_b32_e32 v29, 0xc0, v28
	v_and_b32_e32 v30, 48, v28
	v_lshlrev_b32_e32 v2, 2, v29
	v_lshlrev_b32_e32 v3, 2, v30
	v_add3_u32 v6, s35, v2, v3
	ds_read_b128 v[2:5], v6
	ds_read_b128 v[10:13], v6 offset:16
	ds_read_b128 v[20:23], v6 offset:32
	ds_read_b128 v[24:27], v6 offset:48
	s_lshl_b32 s40, s40, 10
	s_lshl_b32 s38, s38, 8
	s_waitcnt lgkmcnt(2)
	v_pk_mul_f32 v[18:19], v[10:11], s[28:29] op_sel_hi:[1,0]
	v_pk_mul_f32 v[16:17], v[2:3], s[28:29] op_sel_hi:[1,0]
	v_pk_mul_f32 v[8:9], v[4:5], s[28:29] op_sel_hi:[1,0]
	v_pk_mul_f32 v[14:15], v[12:13], s[28:29] op_sel_hi:[1,0]
	s_waitcnt lgkmcnt(1)
	v_pk_mul_f32 v[4:5], v[22:23], s[28:29] op_sel_hi:[1,0]
	s_waitcnt lgkmcnt(0)
	v_pk_mul_f32 v[6:7], v[26:27], s[28:29] op_sel_hi:[1,0]
	v_pk_mul_f32 v[12:13], v[24:25], s[28:29] op_sel_hi:[1,0]
	v_pk_fma_f32 v[24:25], v[158:159], s[30:31], v[16:17] op_sel_hi:[1,0,1]
	v_pk_fma_f32 v[26:27], v[154:155], s[30:31], v[18:19] op_sel_hi:[1,0,1]
	v_cvt_pk_fp8_f32 v22, v24, v25
	v_cvt_pk_fp8_f32 v23, v26, v27
	s_sub_i32 s38, s38, s40
	v_pk_mul_f32 v[10:11], v[20:21], s[28:29] op_sel_hi:[1,0]
	v_pk_fma_f32 v[24:25], v[160:161], s[30:31], v[8:9] op_sel_hi:[1,0,1]
	v_pk_fma_f32 v[26:27], v[156:157], s[30:31], v[14:15] op_sel_hi:[1,0,1]
	v_ashrrev_i32_e32 v31, 2, v28
	v_and_b32_e32 v3, 15, v28
	v_or3_b32 v2, v29, s38, v30
	v_cvt_pk_fp8_f32 v22, v24, v25 op_sel:[0,0,1]
	v_cvt_pk_fp8_f32 v23, v26, v27 op_sel:[0,0,1]
	v_pk_fma_f32 v[26:27], v[150:151], s[30:31], v[10:11] op_sel_hi:[1,0,1]
	v_pk_fma_f32 v[28:29], v[146:147], s[30:31], v[12:13] op_sel_hi:[1,0,1]
	v_cvt_pk_fp8_f32 v24, v26, v27
	v_cvt_pk_fp8_f32 v25, v28, v29
	v_and_or_b32 v20, v31, s60, v3
	v_lshl_add_u32 v20, s37, 8, v20
	v_pk_fma_f32 v[26:27], v[152:153], s[30:31], v[4:5] op_sel_hi:[1,0,1]
	v_pk_fma_f32 v[28:29], v[148:149], s[30:31], v[6:7] op_sel_hi:[1,0,1]
	v_ashrrev_i32_e32 v21, 31, v20
	v_cvt_pk_fp8_f32 v24, v26, v27 op_sel:[0,0,1]
	v_cvt_pk_fp8_f32 v25, v28, v29 op_sel:[0,0,1]
	v_lshlrev_b64 v[26:27], 10, v[20:21]
	v_ashrrev_i32_e32 v3, 31, v2
	v_lshl_add_u64 v[26:27], s[14:15], 0, v[26:27]
	v_lshl_add_u64 v[26:27], v[26:27], 0, v[2:3]
	global_store_dwordx4 v[26:27], v[22:25], off
	v_pk_fma_f32 v[28:29], v[138:139], s[30:31], v[18:19] op_sel_hi:[1,0,1]
	v_pk_fma_f32 v[30:31], v[130:131], s[30:31], v[12:13] op_sel_hi:[1,0,1]
	v_pk_fma_f32 v[24:25], v[142:143], s[30:31], v[16:17] op_sel_hi:[1,0,1]
	v_cvt_pk_fp8_f32 v22, v24, v25
	v_cvt_pk_fp8_f32 v23, v28, v29
	v_pk_fma_f32 v[24:25], v[144:145], s[30:31], v[8:9] op_sel_hi:[1,0,1]
	v_pk_fma_f32 v[28:29], v[140:141], s[30:31], v[14:15] op_sel_hi:[1,0,1]
	v_cvt_pk_fp8_f32 v22, v24, v25 op_sel:[0,0,1]
	v_cvt_pk_fp8_f32 v23, v28, v29 op_sel:[0,0,1]
	v_pk_fma_f32 v[28:29], v[134:135], s[30:31], v[10:11] op_sel_hi:[1,0,1]
	v_cvt_pk_fp8_f32 v24, v28, v29
	v_cvt_pk_fp8_f32 v25, v30, v31
	v_or_b32_e32 v26, 16, v20
	v_pk_fma_f32 v[28:29], v[136:137], s[30:31], v[4:5] op_sel_hi:[1,0,1]
	v_pk_fma_f32 v[30:31], v[132:133], s[30:31], v[6:7] op_sel_hi:[1,0,1]
	v_ashrrev_i32_e32 v27, 31, v26
	v_cvt_pk_fp8_f32 v24, v28, v29 op_sel:[0,0,1]
	v_cvt_pk_fp8_f32 v25, v30, v31 op_sel:[0,0,1]
	v_lshlrev_b64 v[26:27], 10, v[26:27]
	v_lshl_add_u64 v[26:27], s[14:15], 0, v[26:27]
	v_lshl_add_u64 v[26:27], v[26:27], 0, v[2:3]
	global_store_dwordx4 v[26:27], v[22:25], off
	v_pk_fma_f32 v[28:29], v[122:123], s[30:31], v[18:19] op_sel_hi:[1,0,1]
	v_pk_fma_f32 v[30:31], v[114:115], s[30:31], v[12:13] op_sel_hi:[1,0,1]
	v_pk_fma_f32 v[24:25], v[126:127], s[30:31], v[16:17] op_sel_hi:[1,0,1]
	v_cvt_pk_fp8_f32 v22, v24, v25
	v_cvt_pk_fp8_f32 v23, v28, v29
	v_pk_fma_f32 v[24:25], v[128:129], s[30:31], v[8:9] op_sel_hi:[1,0,1]
	v_pk_fma_f32 v[28:29], v[124:125], s[30:31], v[14:15] op_sel_hi:[1,0,1]
	v_cvt_pk_fp8_f32 v22, v24, v25 op_sel:[0,0,1]
	v_cvt_pk_fp8_f32 v23, v28, v29 op_sel:[0,0,1]
	v_pk_fma_f32 v[28:29], v[118:119], s[30:31], v[10:11] op_sel_hi:[1,0,1]
	v_cvt_pk_fp8_f32 v24, v28, v29
	v_cvt_pk_fp8_f32 v25, v30, v31
	v_or_b32_e32 v26, 32, v20
	v_pk_fma_f32 v[28:29], v[120:121], s[30:31], v[4:5] op_sel_hi:[1,0,1]
	v_pk_fma_f32 v[30:31], v[116:117], s[30:31], v[6:7] op_sel_hi:[1,0,1]
	v_ashrrev_i32_e32 v27, 31, v26
	v_cvt_pk_fp8_f32 v24, v28, v29 op_sel:[0,0,1]
	v_cvt_pk_fp8_f32 v25, v30, v31 op_sel:[0,0,1]
	v_lshlrev_b64 v[26:27], 10, v[26:27]
	v_lshl_add_u64 v[26:27], s[14:15], 0, v[26:27]
	v_lshl_add_u64 v[26:27], v[26:27], 0, v[2:3]
	global_store_dwordx4 v[26:27], v[22:25], off
	v_pk_fma_f32 v[28:29], v[106:107], s[30:31], v[18:19] op_sel_hi:[1,0,1]
	v_pk_fma_f32 v[30:31], v[98:99], s[30:31], v[12:13] op_sel_hi:[1,0,1]
	v_pk_fma_f32 v[24:25], v[110:111], s[30:31], v[16:17] op_sel_hi:[1,0,1]
	v_cvt_pk_fp8_f32 v22, v24, v25
	v_cvt_pk_fp8_f32 v23, v28, v29
	v_pk_fma_f32 v[24:25], v[112:113], s[30:31], v[8:9] op_sel_hi:[1,0,1]
	v_pk_fma_f32 v[28:29], v[108:109], s[30:31], v[14:15] op_sel_hi:[1,0,1]
	v_cvt_pk_fp8_f32 v22, v24, v25 op_sel:[0,0,1]
	v_cvt_pk_fp8_f32 v23, v28, v29 op_sel:[0,0,1]
	v_pk_fma_f32 v[28:29], v[102:103], s[30:31], v[10:11] op_sel_hi:[1,0,1]
	v_cvt_pk_fp8_f32 v24, v28, v29
	v_cvt_pk_fp8_f32 v25, v30, v31
	v_or_b32_e32 v26, 48, v20
	v_pk_fma_f32 v[28:29], v[104:105], s[30:31], v[4:5] op_sel_hi:[1,0,1]
	v_pk_fma_f32 v[30:31], v[100:101], s[30:31], v[6:7] op_sel_hi:[1,0,1]
	v_ashrrev_i32_e32 v27, 31, v26
	v_cvt_pk_fp8_f32 v24, v28, v29 op_sel:[0,0,1]
	v_cvt_pk_fp8_f32 v25, v30, v31 op_sel:[0,0,1]
	v_lshlrev_b64 v[26:27], 10, v[26:27]
	v_lshl_add_u64 v[26:27], s[14:15], 0, v[26:27]
	v_lshl_add_u64 v[26:27], v[26:27], 0, v[2:3]
	global_store_dwordx4 v[26:27], v[22:25], off
	v_pk_fma_f32 v[28:29], v[90:91], s[30:31], v[18:19] op_sel_hi:[1,0,1]
	v_pk_fma_f32 v[30:31], v[82:83], s[30:31], v[12:13] op_sel_hi:[1,0,1]
	v_pk_fma_f32 v[24:25], v[94:95], s[30:31], v[16:17] op_sel_hi:[1,0,1]
	v_cvt_pk_fp8_f32 v22, v24, v25
	v_cvt_pk_fp8_f32 v23, v28, v29
	v_pk_fma_f32 v[24:25], v[96:97], s[30:31], v[8:9] op_sel_hi:[1,0,1]
	v_pk_fma_f32 v[28:29], v[92:93], s[30:31], v[14:15] op_sel_hi:[1,0,1]
	v_cvt_pk_fp8_f32 v22, v24, v25 op_sel:[0,0,1]
	v_cvt_pk_fp8_f32 v23, v28, v29 op_sel:[0,0,1]
	v_pk_fma_f32 v[28:29], v[86:87], s[30:31], v[10:11] op_sel_hi:[1,0,1]
	v_cvt_pk_fp8_f32 v24, v28, v29
	v_cvt_pk_fp8_f32 v25, v30, v31
	v_add_u32_e32 v26, 0x80, v20
	v_pk_fma_f32 v[28:29], v[88:89], s[30:31], v[4:5] op_sel_hi:[1,0,1]
	v_pk_fma_f32 v[30:31], v[84:85], s[30:31], v[6:7] op_sel_hi:[1,0,1]
	v_ashrrev_i32_e32 v27, 31, v26
	v_cvt_pk_fp8_f32 v24, v28, v29 op_sel:[0,0,1]
	v_cvt_pk_fp8_f32 v25, v30, v31 op_sel:[0,0,1]
	v_lshlrev_b64 v[26:27], 10, v[26:27]
	v_lshl_add_u64 v[26:27], s[14:15], 0, v[26:27]
	v_lshl_add_u64 v[26:27], v[26:27], 0, v[2:3]
	global_store_dwordx4 v[26:27], v[22:25], off
	v_pk_fma_f32 v[28:29], v[74:75], s[30:31], v[18:19] op_sel_hi:[1,0,1]
	v_pk_fma_f32 v[30:31], v[66:67], s[30:31], v[12:13] op_sel_hi:[1,0,1]
	v_pk_fma_f32 v[24:25], v[78:79], s[30:31], v[16:17] op_sel_hi:[1,0,1]
	v_cvt_pk_fp8_f32 v22, v24, v25
	v_cvt_pk_fp8_f32 v23, v28, v29
	v_pk_fma_f32 v[24:25], v[80:81], s[30:31], v[8:9] op_sel_hi:[1,0,1]
	v_pk_fma_f32 v[28:29], v[76:77], s[30:31], v[14:15] op_sel_hi:[1,0,1]
	v_cvt_pk_fp8_f32 v22, v24, v25 op_sel:[0,0,1]
	v_cvt_pk_fp8_f32 v23, v28, v29 op_sel:[0,0,1]
	v_pk_fma_f32 v[28:29], v[70:71], s[30:31], v[10:11] op_sel_hi:[1,0,1]
	v_cvt_pk_fp8_f32 v24, v28, v29
	v_cvt_pk_fp8_f32 v25, v30, v31
	v_add_u32_e32 v26, 0x90, v20
	v_pk_fma_f32 v[28:29], v[72:73], s[30:31], v[4:5] op_sel_hi:[1,0,1]
	v_pk_fma_f32 v[30:31], v[68:69], s[30:31], v[6:7] op_sel_hi:[1,0,1]
	v_ashrrev_i32_e32 v27, 31, v26
	v_cvt_pk_fp8_f32 v24, v28, v29 op_sel:[0,0,1]
	v_cvt_pk_fp8_f32 v25, v30, v31 op_sel:[0,0,1]
	v_lshlrev_b64 v[26:27], 10, v[26:27]
	v_lshl_add_u64 v[26:27], s[14:15], 0, v[26:27]
	v_lshl_add_u64 v[26:27], v[26:27], 0, v[2:3]
	global_store_dwordx4 v[26:27], v[22:25], off
	v_pk_fma_f32 v[28:29], v[58:59], s[30:31], v[18:19] op_sel_hi:[1,0,1]
	v_pk_fma_f32 v[30:31], v[50:51], s[30:31], v[12:13] op_sel_hi:[1,0,1]
	v_pk_fma_f32 v[24:25], v[62:63], s[30:31], v[16:17] op_sel_hi:[1,0,1]
	v_cvt_pk_fp8_f32 v22, v24, v25
	v_cvt_pk_fp8_f32 v23, v28, v29
	v_pk_fma_f32 v[24:25], v[64:65], s[30:31], v[8:9] op_sel_hi:[1,0,1]
	v_pk_fma_f32 v[28:29], v[60:61], s[30:31], v[14:15] op_sel_hi:[1,0,1]
	v_cvt_pk_fp8_f32 v22, v24, v25 op_sel:[0,0,1]
	v_cvt_pk_fp8_f32 v23, v28, v29 op_sel:[0,0,1]
	v_pk_fma_f32 v[28:29], v[54:55], s[30:31], v[10:11] op_sel_hi:[1,0,1]
	v_cvt_pk_fp8_f32 v24, v28, v29
	v_cvt_pk_fp8_f32 v25, v30, v31
	v_add_u32_e32 v26, 0xa0, v20
	v_pk_fma_f32 v[28:29], v[56:57], s[30:31], v[4:5] op_sel_hi:[1,0,1]
	v_pk_fma_f32 v[30:31], v[52:53], s[30:31], v[6:7] op_sel_hi:[1,0,1]
	v_ashrrev_i32_e32 v27, 31, v26
	v_cvt_pk_fp8_f32 v24, v28, v29 op_sel:[0,0,1]
	v_cvt_pk_fp8_f32 v25, v30, v31 op_sel:[0,0,1]
	v_lshlrev_b64 v[26:27], 10, v[26:27]
	v_lshl_add_u64 v[26:27], s[14:15], 0, v[26:27]
	v_lshl_add_u64 v[26:27], v[26:27], 0, v[2:3]
	global_store_dwordx4 v[26:27], v[22:25], off
	v_pk_fma_f32 v[18:19], v[42:43], s[30:31], v[18:19] op_sel_hi:[1,0,1]
	v_pk_fma_f32 v[8:9], v[48:49], s[30:31], v[8:9] op_sel_hi:[1,0,1]
	v_pk_fma_f32 v[22:23], v[46:47], s[30:31], v[16:17] op_sel_hi:[1,0,1]
	v_cvt_pk_fp8_f32 v16, v22, v23
	v_cvt_pk_fp8_f32 v17, v18, v19
	v_cvt_pk_fp8_f32 v16, v8, v9 op_sel:[0,0,1]
	v_pk_fma_f32 v[8:9], v[38:39], s[30:31], v[10:11] op_sel_hi:[1,0,1]
	v_pk_fma_f32 v[10:11], v[34:35], s[30:31], v[12:13] op_sel_hi:[1,0,1]
	v_cvt_pk_fp8_f32 v18, v8, v9
	v_cvt_pk_fp8_f32 v19, v10, v11
	v_add_u32_e32 v20, 0xb0, v20
	v_pk_fma_f32 v[14:15], v[44:45], s[30:31], v[14:15] op_sel_hi:[1,0,1]
	v_pk_fma_f32 v[4:5], v[40:41], s[30:31], v[4:5] op_sel_hi:[1,0,1]
	v_pk_fma_f32 v[6:7], v[36:37], s[30:31], v[6:7] op_sel_hi:[1,0,1]
	v_ashrrev_i32_e32 v21, 31, v20
	v_cvt_pk_fp8_f32 v17, v14, v15 op_sel:[0,0,1]
	v_cvt_pk_fp8_f32 v18, v4, v5 op_sel:[0,0,1]
	v_cvt_pk_fp8_f32 v19, v6, v7 op_sel:[0,0,1]
	v_lshlrev_b64 v[4:5], 10, v[20:21]
	v_lshl_add_u64 v[4:5], s[14:15], 0, v[4:5]
	v_lshl_add_u64 v[2:3], v[4:5], 0, v[2:3]
	s_and_b64 vcc, exec, s[4:5]
	s_mov_b64 s[4:5], -1
	global_store_dwordx4 v[2:3], v[16:19], off
	s_cbranch_vccnz .LBB0_646
	s_andn2_b64 vcc, exec, s[18:19]
	s_cbranch_vccnz .LBB0_658
	s_lshl_b32 s4, s62, 10
	s_and_b32 s4, s4, 0x400
	s_add_i32 s4, s4, 0
	s_ashr_i32 s37, s36, 31
	s_add_i32 s35, s4, 0x24cc0
	s_lshl_b64 s[4:5], s[36:37], 12
	s_add_u32 s37, s16, s4
	s_addc_u32 s38, s17, s5
	s_lshl_b32 s4, s36, 10
	s_lshl_b32 s5, s34, 8
	s_sub_i32 s4, s5, s4
	s_ashr_i32 s5, s4, 31
	s_lshl_b64 s[4:5], s[4:5], 2
	s_add_u32 s4, s37, s4
	s_addc_u32 s5, s38, s5
	s_mov_b32 m0, s35
	s_nop 0
	global_load_lds_dwordx4 v1, s[4:5] offset:0
